# adds: importance-loop Q prefetch, top-k bit loop with one scalar compare per token, write-through (sc1) 16-byte stores in the GEMM epilogues
# speedup vs baseline: 1.0014x; 1.0014x over previous
;     __device__ __forceinline__ static u32x4 pack8(const f32x4 a, const f32x4 b) { u32x4 w; w.x = cvt_pk_bf16(a[0], a[1]); w.y = cvt_pk_bf16(a[2], a[3]); w.z = cvt_pk_bf16(b[0], b[1]); w.w = cvt_pk_bf16(b[2], b[3]); return w; }
;     __device__ __forceinline__ void operator()(const f32x4 (&acc)[2][2][4][2], const Unit& u, int wr, int wc, int fr, int fq) const {
;         const int pn = u.pn, row0 = u.pm * BM + wr * 64 + fr, cl = wc * 32 + 8 * fq;
; #pragma unroll
;         for (int ai = 0; ai < 2; ++ai)
; #pragma unroll
;             for (int m = 0; m < 4; ++m) { const size_t row = (size_t)(row0 + ai * HALF + m * 16);
; #pragma unroll
;                 for (int bj = 0; bj < 2; ++bj) { const int c256 = bj * HALF + cl; f32x4 v0 = acc[ai][bj][m][0], v1 = acc[ai][bj][m][1];
;                     if (pn < 4) { *(u32x4*)(QH + row * 1024 + pn * 256 + c256) = pack8(silu4(v0), silu4(v1)); }
;                     else if (pn < 8) { const int col = (pn - 4) * 256 + c256; const f32x4 l0 = *(const f32x4*)(LB + col), l1 = *(const f32x4*)(LB + col + 4); f32x4 o0, o1;
;                         for (int i = 0; i < 4; ++i) { o0[i] = __logf(l0[i] + (1.f - l0[i]) * __builtin_amdgcn_rcpf(1.f + __expf(-v0[i]))); o1[i] = __logf(l1[i] + (1.f - l1[i]) * __builtin_amdgcn_rcpf(1.f + __expf(-v1[i]))); }
;                         *(u32x4*)(LOGF + row * 1024 + col) = pack8(o0, o1); }
;                     else if (pn < 12) { *(u32x4*)(VH + row * 1024 + (pn - 8) * 256 + c256) = pack8(v0, v1); }
;                     else if (pn < 16) { *(u32x4*)(GH + row * 1024 + (pn - 12) * 256 + c256) = pack8(silu4(v0), silu4(v1)); }
;                     else if (pn < 20) { const float sc = 0.125f * 1.4426950408889634f; *(u32x4*)(QN + row * 1024 + (pn - 16) * 256 + c256) = pack8(v0 * sc, v1 * sc); }
;                     else if (pn < 26) { *(u32x4*)(KV6 + (size_t)(pn - 20) * ((size_t)16384 * 256) + row * 256 + c256) = pack8(v0, v1); }
;                     else if (c256 < 64) { f32x4 o0, o1; for (int i = 0; i < 4; ++i) { o0[i] = __builtin_amdgcn_rcpf(1.f + __expf(-v0[i])); o1[i] = __builtin_amdgcn_rcpf(1.f + __expf(-v1[i])); }
;                         *(f32x4*)(GATE + row * 64 + c256) = o0; *(f32x4*)(GATE + row * 64 + c256 + 4) = o1; } } }
.LBB0_135:
	s_cmp_gt_i32 s0, 3
	s_cselect_b64 s[18:19], -1, 0
	s_cmp_gt_u32 s0, 7
	s_cselect_b64 s[20:21], -1, 0
	s_cmp_gt_u32 s0, 11
	v_lshl_add_u32 v152, s2, 8, v162
	s_cselect_b64 s[62:63], -1, 0
	s_cmp_gt_u32 s0, 15
	v_sub_co_u32_e64 v153, s[2:3], s0, 20
	s_cselect_b64 s[60:61], -1, 0
	s_xor_b64 s[58:59], s[2:3], -1
	s_cmp_gt_u32 s0, 25
	v_readfirstlane_b32 s24, v153
	s_cselect_b64 s[56:57], -1, 0
	s_lshl_b64 s[2:3], s[24:25], 23
	s_lshl_b32 s24, s0, 8
	v_ashrrev_i32_e32 v153, 31, v152
	s_mov_b64 s[10:11], -1
	s_add_i32 s33, s24, 0xfffffc00
	s_ashr_i32 s1, s24, 31
	s_mov_b32 s0, s24
	v_lshlrev_b64 v[158:159], 6, v[152:153]
	v_lshlrev_b64 v[156:157], 9, v[152:153]
	v_lshlrev_b64 v[154:155], 11, v[152:153]
	s_and_b64 vcc, exec, s[18:19]
	s_cbranch_vccz .LBB0_159
	s_and_b64 vcc, exec, s[20:21]
	s_cbranch_vccz .LBB0_156
	s_and_b64 vcc, exec, s[62:63]
	s_cbranch_vccz .LBB0_153
	s_and_b64 vcc, exec, s[60:61]
	s_cbranch_vccz .LBB0_150
	s_and_b64 vcc, exec, s[58:59]
	s_cbranch_vccz .LBB0_147
	s_and_b64 vcc, exec, s[56:57]
	s_cbranch_vccz .LBB0_144
	s_and_saveexec_b64 s[10:11], s[4:5]
	s_cbranch_execz .LBB0_143
	v_mul_f32_e32 v153, 0xbfb8aa3b, v124
	v_exp_f32_e32 v153, v153
	v_mul_f32_e32 v160, 0xbfb8aa3b, v120
	v_exp_f32_e32 v160, v160
	v_mul_f32_e32 v161, 0xbfb8aa3b, v121
	v_add_f32_e32 v153, 1.0, v153
	v_rcp_f32_e32 v168, v153
	v_mul_f32_e32 v153, 0xbfb8aa3b, v125
	v_exp_f32_e32 v153, v153
	v_exp_f32_e32 v161, v161
	v_add_f32_e32 v160, 1.0, v160
	v_rcp_f32_e32 v172, v160
	v_add_f32_e32 v153, 1.0, v153
	v_mul_f32_e32 v160, 0xbfb8aa3b, v126
	v_rcp_f32_e32 v169, v153
	v_add_f32_e32 v153, 1.0, v161
	v_exp_f32_e32 v160, v160
	v_mul_f32_e32 v161, 0xbfb8aa3b, v122
	v_exp_f32_e32 v161, v161
	v_rcp_f32_e32 v173, v153
	v_add_f32_e32 v153, 1.0, v160
	v_mul_f32_e32 v160, 0xbfb8aa3b, v127
	v_rcp_f32_e32 v170, v153
	v_add_f32_e32 v153, 1.0, v161
	v_exp_f32_e32 v160, v160
	v_mul_f32_e32 v161, 0xbfb8aa3b, v123
	v_exp_f32_e32 v161, v161
	v_rcp_f32_e32 v174, v153
	v_add_f32_e32 v153, 1.0, v160
	v_rcp_f32_e32 v171, v153
	v_add_f32_e32 v153, 1.0, v161
	v_rcp_f32_e32 v175, v153
	v_lshl_add_u64 v[160:161], v[158:159], 2, v[140:141]
	global_store_dwordx4 v[160:161], v[168:171], off sc1
	global_store_dwordx4 v[160:161], v[172:175], off offset:16 sc1

;     __device__ __forceinline__ static u32x4 pack8(const f32x4 a, const f32x4 b) { u32x4 w; w.x = cvt_pk_bf16(a[0], a[1]); w.y = cvt_pk_bf16(a[2], a[3]); w.z = cvt_pk_bf16(b[0], b[1]); w.w = cvt_pk_bf16(b[2], b[3]); return w; }
;     __device__ __forceinline__ void operator()(const f32x4 (&acc)[2][2][4][2], const Unit& u, int wr, int wc, int fr, int fq) const {
;     ...
;                     else if (pn < 26) { *(u32x4*)(KV6 + (size_t)(pn - 20) * ((size_t)16384 * 256) + row * 256 + c256) = pack8(v0, v1); }
.LBB0_144:
	s_andn2_b64 vcc, exec, s[10:11]
	s_cbranch_vccnz .LBB0_146
	s_add_u32 s10, s73, s2
	s_addc_u32 s11, s74, s3
	v_lshl_add_u64 v[160:161], s[10:11], 0, v[156:157]
	v_lshl_add_u64 v[160:161], v[136:137], 1, v[160:161]
	v_cvt_pk_bf16_f32 v168, v124, v125
	v_cvt_pk_bf16_f32 v169, v126, v127
	v_cvt_pk_bf16_f32 v170, v120, v121
	v_cvt_pk_bf16_f32 v171, v122, v123
	global_store_dwordx4 v[160:161], v[168:171], off sc1

;     __device__ __forceinline__ static u32x4 pack8(const f32x4 a, const f32x4 b) { u32x4 w; w.x = cvt_pk_bf16(a[0], a[1]); w.y = cvt_pk_bf16(a[2], a[3]); w.z = cvt_pk_bf16(b[0], b[1]); w.w = cvt_pk_bf16(b[2], b[3]); return w; }
;     __device__ __forceinline__ void operator()(const f32x4 (&acc)[2][2][4][2], const Unit& u, int wr, int wc, int fr, int fq) const {
;     ...
;                     else if (pn < 20) { const float sc = 0.125f * 1.4426950408889634f; *(u32x4*)(QN + row * 1024 + (pn - 16) * 256 + c256) = pack8(v0 * sc, v1 * sc); }
.LBB0_147:
	s_andn2_b64 vcc, exec, s[10:11]
	s_cbranch_vccnz .LBB0_149
	v_pk_mul_f32 v[160:161], v[126:127], s[46:47] op_sel_hi:[1,0]
	v_pk_mul_f32 v[168:169], v[124:125], s[46:47] op_sel_hi:[1,0]
	v_pk_mul_f32 v[170:171], v[120:121], s[46:47] op_sel_hi:[1,0]
	v_cvt_pk_bf16_f32 v168, v168, v169
	v_cvt_pk_bf16_f32 v169, v160, v161
	v_lshl_add_u64 v[160:161], s[36:37], 0, v[154:155]
	v_lshl_add_u64 v[160:161], s[24:25], 1, v[160:161]
	v_lshl_add_u64 v[160:161], v[136:137], 1, v[160:161]
	v_add_co_u32_e32 v160, vcc, 0xffffe000, v160
	v_pk_mul_f32 v[172:173], v[122:123], s[46:47] op_sel_hi:[1,0]
	s_nop 0
	v_addc_co_u32_e32 v161, vcc, -1, v161, vcc
	v_cvt_pk_bf16_f32 v170, v170, v171
	v_cvt_pk_bf16_f32 v171, v172, v173
	global_store_dwordx4 v[160:161], v[168:171], off sc1

;     __device__ __forceinline__ static u32x4 pack8(const f32x4 a, const f32x4 b) { u32x4 w; w.x = cvt_pk_bf16(a[0], a[1]); w.y = cvt_pk_bf16(a[2], a[3]); w.z = cvt_pk_bf16(b[0], b[1]); w.w = cvt_pk_bf16(b[2], b[3]); return w; }
;     __device__ __forceinline__ static f32x4 silu4(const f32x4 v) { f32x4 o; for (int i = 0; i < 4; ++i) o[i] = v[i] * __builtin_amdgcn_rcpf(1.f + __expf(-v[i])); return o; }
;     __device__ __forceinline__ void operator()(const f32x4 (&acc)[2][2][4][2], const Unit& u, int wr, int wc, int fr, int fq) const {
;     ...
;                     else if (pn < 16) { *(u32x4*)(GH + row * 1024 + (pn - 12) * 256 + c256) = pack8(silu4(v0), silu4(v1)); }
.LBB0_150:
	s_andn2_b64 vcc, exec, s[10:11]
	s_cbranch_vccnz .LBB0_152
	v_mul_f32_e32 v168, 0xbfb8aa3b, v127
	v_exp_f32_e32 v168, v168
	v_mul_f32_e32 v160, 0xbfb8aa3b, v125
	v_mul_f32_e32 v161, 0xbfb8aa3b, v126
	v_mul_f32_e32 v153, 0xbfb8aa3b, v124
	v_exp_f32_e32 v160, v160
	v_exp_f32_e32 v161, v161
	v_add_f32_e32 v168, 1.0, v168
	v_mul_f32_e32 v169, 0xbfb8aa3b, v120
	v_mul_f32_e32 v170, 0xbfb8aa3b, v121
	v_exp_f32_e32 v153, v153
	v_rcp_f32_e32 v168, v168
	v_exp_f32_e32 v169, v169
	v_exp_f32_e32 v170, v170
	v_add_f32_e32 v160, 1.0, v160
	v_add_f32_e32 v161, 1.0, v161
	v_add_f32_e32 v153, 1.0, v153
	v_rcp_f32_e32 v160, v160
	v_rcp_f32_e32 v161, v161
	v_mul_f32_e32 v171, v127, v168
	v_add_f32_e32 v168, 1.0, v169
	v_add_f32_e32 v169, 1.0, v170
	v_mul_f32_e32 v170, 0xbfb8aa3b, v122
	v_mul_f32_e32 v172, 0xbfb8aa3b, v123
	v_rcp_f32_e32 v153, v153
	v_rcp_f32_e32 v168, v168
	v_exp_f32_e32 v170, v170
	v_exp_f32_e32 v172, v172
	v_rcp_f32_e32 v169, v169
	v_mul_f32_e32 v160, v125, v160
	v_mul_f32_e32 v161, v126, v161
	v_mul_f32_e32 v153, v124, v153
	v_add_f32_e32 v170, 1.0, v170
	v_add_f32_e32 v172, 1.0, v172
	v_mul_f32_e32 v173, v120, v168
	v_mul_f32_e32 v174, v121, v169
	v_cvt_pk_bf16_f32 v168, v153, v160
	v_cvt_pk_bf16_f32 v169, v161, v171
	v_lshl_add_u64 v[160:161], s[34:35], 0, v[154:155]
	v_rcp_f32_e32 v170, v170
	v_rcp_f32_e32 v172, v172
	v_lshl_add_u64 v[160:161], s[24:25], 1, v[160:161]
	v_lshl_add_u64 v[160:161], v[136:137], 1, v[160:161]
	v_add_co_u32_e32 v160, vcc, 0xfffff000, v160
	v_mul_f32_e32 v175, v122, v170
	s_nop 0
	v_addc_co_u32_e32 v161, vcc, -1, v161, vcc
	v_mul_f32_e32 v172, v123, v172
	v_cvt_pk_bf16_f32 v170, v173, v174
	v_cvt_pk_bf16_f32 v171, v175, v172
	global_store_dwordx4 v[160:161], v[168:171], off offset:-2048 sc1

;     __device__ __forceinline__ static u32x4 pack8(const f32x4 a, const f32x4 b) { u32x4 w; w.x = cvt_pk_bf16(a[0], a[1]); w.y = cvt_pk_bf16(a[2], a[3]); w.z = cvt_pk_bf16(b[0], b[1]); w.w = cvt_pk_bf16(b[2], b[3]); return w; }
;     __device__ __forceinline__ void operator()(const f32x4 (&acc)[2][2][4][2], const Unit& u, int wr, int wc, int fr, int fq) const {
;     ...
;                     else if (pn < 12) { *(u32x4*)(VH + row * 1024 + (pn - 8) * 256 + c256) = pack8(v0, v1); }
.LBB0_153:
	s_andn2_b64 vcc, exec, s[10:11]
	s_cbranch_vccnz .LBB0_155
	v_lshl_add_u64 v[160:161], s[30:31], 0, v[154:155]
	v_lshl_add_u64 v[160:161], s[24:25], 1, v[160:161]
	v_lshl_add_u64 v[160:161], v[136:137], 1, v[160:161]
	v_cvt_pk_bf16_f32 v168, v124, v125
	v_cvt_pk_bf16_f32 v169, v126, v127
	v_cvt_pk_bf16_f32 v170, v120, v121
	v_cvt_pk_bf16_f32 v171, v122, v123
	global_store_dwordx4 v[160:161], v[168:171], off offset:-4096 sc1

;     __device__ __forceinline__ static u32x4 pack8(const f32x4 a, const f32x4 b) { u32x4 w; w.x = cvt_pk_bf16(a[0], a[1]); w.y = cvt_pk_bf16(a[2], a[3]); w.z = cvt_pk_bf16(b[0], b[1]); w.w = cvt_pk_bf16(b[2], b[3]); return w; }
;     __device__ __forceinline__ void operator()(const f32x4 (&acc)[2][2][4][2], const Unit& u, int wr, int wc, int fr, int fq) const {
;     ...
;                     else if (pn < 8) { const int col = (pn - 4) * 256 + c256; const f32x4 l0 = *(const f32x4*)(LB + col), l1 = *(const f32x4*)(LB + col + 4); f32x4 o0, o1;
;                         for (int i = 0; i < 4; ++i) { o0[i] = __logf(l0[i] + (1.f - l0[i]) * __builtin_amdgcn_rcpf(1.f + __expf(-v0[i]))); o1[i] = __logf(l1[i] + (1.f - l1[i]) * __builtin_amdgcn_rcpf(1.f + __expf(-v1[i]))); }
;                         *(u32x4*)(LOGF + row * 1024 + col) = pack8(o0, o1); }
.LBB0_156:
	s_andn2_b64 vcc, exec, s[10:11]
	s_cbranch_vccnz .LBB0_158
	v_add_u32_e32 v160, s33, v136
	v_ashrrev_i32_e32 v161, 31, v160
	v_lshl_add_u64 v[160:161], v[160:161], 2, s[40:41]
	global_load_dwordx4 v[168:171], v[160:161], off
	global_load_dwordx4 v[172:175], v[160:161], off offset:16
	v_mul_f32_e32 v153, 0xbfb8aa3b, v124
	v_mul_f32_e32 v160, 0xbfb8aa3b, v120
	v_exp_f32_e32 v153, v153
	v_mul_f32_e32 v161, 0xbfb8aa3b, v125
	v_exp_f32_e32 v160, v160
	v_mul_f32_e32 v176, 0xbfb8aa3b, v121
	v_exp_f32_e32 v161, v161
	v_mul_f32_e32 v177, 0xbfb8aa3b, v126
	v_mul_f32_e32 v178, 0xbfb8aa3b, v122
	v_exp_f32_e32 v176, v176
	v_exp_f32_e32 v177, v177
	v_exp_f32_e32 v178, v178
	v_add_f32_e32 v153, 1.0, v153
	v_add_f32_e32 v160, 1.0, v160
	v_rcp_f32_e32 v153, v153
	v_add_f32_e32 v161, 1.0, v161
	v_rcp_f32_e32 v160, v160
	v_add_f32_e32 v176, 1.0, v176
	v_rcp_f32_e32 v161, v161
	v_add_f32_e32 v177, 1.0, v177
	v_add_f32_e32 v178, 1.0, v178
	v_rcp_f32_e32 v176, v176
	v_rcp_f32_e32 v177, v177
	v_rcp_f32_e32 v178, v178
	s_waitcnt vmcnt(0)
	v_sub_f32_e32 v179, 1.0, v168
	v_sub_f32_e32 v180, 1.0, v172
	v_fma_f32 v153, v153, v179, v168
	v_sub_f32_e32 v181, 1.0, v169
	v_fma_f32 v160, v160, v180, v172
	v_cmp_gt_f32_e32 vcc, s82, v153
	v_sub_f32_e32 v182, 1.0, v173
	v_fma_f32 v161, v161, v181, v169
	v_cndmask_b32_e64 v172, 0, 32, vcc
	v_cmp_gt_f32_e64 s[10:11], s82, v160
	v_sub_f32_e32 v183, 1.0, v170
	v_sub_f32_e32 v184, 1.0, v174
	v_fma_f32 v168, v176, v182, v173
	v_cndmask_b32_e64 v173, 0, 32, s[10:11]
	v_cmp_gt_f32_e64 s[12:13], s82, v161
	v_ldexp_f32 v153, v153, v172
	v_fma_f32 v169, v177, v183, v170
	v_fma_f32 v170, v178, v184, v174
	v_cndmask_b32_e64 v174, 0, 32, s[12:13]
	v_cmp_gt_f32_e64 s[14:15], s82, v168
	v_ldexp_f32 v160, v160, v173
	v_log_f32_e32 v153, v153
	v_cndmask_b32_e64 v176, 0, 32, s[14:15]
	v_ldexp_f32 v161, v161, v174
	v_log_f32_e32 v160, v160
	v_cmp_gt_f32_e64 s[16:17], s82, v169
	v_ldexp_f32 v168, v168, v176
	v_log_f32_e32 v161, v161
	v_cndmask_b32_e64 v177, 0, 32, s[16:17]
	v_log_f32_e32 v168, v168
	v_ldexp_f32 v169, v169, v177
	v_mul_f32_e32 v177, 0x3f317217, v153
	v_mul_f32_e32 v178, 0x3f317217, v160
	v_fma_f32 v177, v153, s83, -v177
	v_mul_f32_e32 v179, 0x3f317217, v161
	v_fma_f32 v178, v160, s83, -v178
	v_fmac_f32_e32 v177, 0x3377d1cf, v153
	v_cndmask_b32_e32 v172, 0, v167, vcc
	v_mul_f32_e32 v180, 0x3f317217, v168
	v_fma_f32 v179, v161, s83, -v179
	v_fmac_f32_e32 v178, 0x3377d1cf, v160
	v_fmac_f32_e32 v177, 0x3f317217, v153
	v_cmp_lt_f32_e64 vcc, |v153|, s84
	v_fma_f32 v180, v168, s83, -v180
	v_fmac_f32_e32 v179, 0x3377d1cf, v161
	v_fmac_f32_e32 v178, 0x3f317217, v160
	v_cndmask_b32_e32 v153, v153, v177, vcc
	v_cmp_lt_f32_e64 vcc, |v160|, s84
	v_log_f32_e32 v169, v169
	v_fmac_f32_e32 v180, 0x3377d1cf, v168
	v_fmac_f32_e32 v179, 0x3f317217, v161
	v_cndmask_b32_e32 v160, v160, v178, vcc
	v_cmp_lt_f32_e64 vcc, |v161|, s84
	v_cndmask_b32_e64 v173, 0, v167, s[10:11]
	v_fmac_f32_e32 v180, 0x3f317217, v168
	v_cndmask_b32_e32 v161, v161, v179, vcc
	v_cmp_lt_f32_e64 vcc, |v168|, s84
	v_cndmask_b32_e64 v176, 0, v167, s[14:15]
	v_sub_f32_e32 v160, v160, v173
	v_cndmask_b32_e32 v168, v168, v180, vcc
	v_cmp_gt_f32_e32 vcc, s82, v170
	v_mul_f32_e32 v173, 0xbfb8aa3b, v127
	v_sub_f32_e32 v153, v153, v172
	v_sub_f32_e32 v172, v168, v176
	v_cndmask_b32_e64 v168, 0, 32, vcc
	v_exp_f32_e32 v173, v173
	v_mul_f32_e32 v181, 0x3f317217, v169
	v_ldexp_f32 v168, v170, v168
	v_fma_f32 v181, v169, s83, -v181
	v_log_f32_e32 v168, v168
	v_fmac_f32_e32 v181, 0x3377d1cf, v169
	v_fmac_f32_e32 v181, 0x3f317217, v169
	v_cmp_lt_f32_e64 s[10:11], |v169|, s84
	v_add_f32_e32 v173, 1.0, v173
	v_cndmask_b32_e64 v170, 0, v167, s[16:17]
	v_cndmask_b32_e64 v169, v169, v181, s[10:11]
	v_rcp_f32_e32 v173, v173
	v_sub_f32_e32 v169, v169, v170
	v_mul_f32_e32 v170, 0x3f317217, v168
	v_cndmask_b32_e64 v174, 0, v167, s[12:13]
	v_fma_f32 v170, v168, s83, -v170
	v_sub_f32_e32 v161, v161, v174
	v_fmac_f32_e32 v170, 0x3377d1cf, v168
	v_sub_f32_e32 v174, 1.0, v171
	v_fmac_f32_e32 v170, 0x3f317217, v168
	v_cmp_lt_f32_e64 s[10:11], |v168|, s84
	v_fmac_f32_e32 v171, v173, v174
	s_nop 0
	v_cndmask_b32_e64 v168, v168, v170, s[10:11]
	v_cndmask_b32_e32 v170, 0, v167, vcc
	v_cmp_gt_f32_e32 vcc, s82, v171
	v_sub_f32_e32 v174, v168, v170
	s_nop 0
	v_cndmask_b32_e64 v173, 0, 32, vcc
	v_ldexp_f32 v171, v171, v173
	v_mul_f32_e32 v173, 0xbfb8aa3b, v123
	v_exp_f32_e32 v173, v173
	v_log_f32_e32 v171, v171
	v_add_f32_e32 v170, 1.0, v173
	v_rcp_f32_e32 v170, v170
	v_sub_f32_e32 v173, 1.0, v175
	v_mul_f32_e32 v168, 0x3f317217, v171
	v_fma_f32 v168, v171, s83, -v168
	v_fmac_f32_e32 v175, v170, v173
	v_cmp_gt_f32_e64 s[10:11], s82, v175
	v_fmac_f32_e32 v168, 0x3377d1cf, v171
	v_fmac_f32_e32 v168, 0x3f317217, v171
	v_cndmask_b32_e64 v170, 0, 32, s[10:11]
	v_ldexp_f32 v170, v175, v170
	v_log_f32_e32 v170, v170
	v_cmp_lt_f32_e64 s[12:13], |v171|, s84
	s_nop 1
	v_cndmask_b32_e64 v168, v171, v168, s[12:13]
	v_cndmask_b32_e32 v171, 0, v167, vcc
	v_sub_f32_e32 v171, v168, v171
	v_mul_f32_e32 v168, 0x3f317217, v170
	v_fma_f32 v168, v170, s83, -v168
	v_fmac_f32_e32 v168, 0x3377d1cf, v170
	v_fmac_f32_e32 v168, 0x3f317217, v170
	v_cmp_lt_f32_e64 vcc, |v170|, s84
	s_nop 1
	v_cndmask_b32_e32 v168, v170, v168, vcc
	v_cndmask_b32_e64 v170, 0, v167, s[10:11]
	v_sub_f32_e32 v173, v168, v170
	v_cvt_pk_bf16_f32 v168, v153, v161
	v_cvt_pk_bf16_f32 v169, v169, v171
	v_cvt_pk_bf16_f32 v170, v160, v172
	v_cvt_pk_bf16_f32 v171, v174, v173
	v_lshl_add_u64 v[160:161], s[38:39], 0, v[154:155]
	v_lshl_add_u64 v[172:173], s[0:1], 0, v[136:137]
	v_lshl_add_u64 v[160:161], v[172:173], 1, v[160:161]
	global_store_dwordx4 v[160:161], v[168:171], off offset:-2048 sc1

;     __device__ __forceinline__ static u32x4 pack8(const f32x4 a, const f32x4 b) { u32x4 w; w.x = cvt_pk_bf16(a[0], a[1]); w.y = cvt_pk_bf16(a[2], a[3]); w.z = cvt_pk_bf16(b[0], b[1]); w.w = cvt_pk_bf16(b[2], b[3]); return w; }
;     __device__ __forceinline__ static f32x4 silu4(const f32x4 v) { f32x4 o; for (int i = 0; i < 4; ++i) o[i] = v[i] * __builtin_amdgcn_rcpf(1.f + __expf(-v[i])); return o; }
;     __device__ __forceinline__ void operator()(const f32x4 (&acc)[2][2][4][2], const Unit& u, int wr, int wc, int fr, int fq) const {
;     ...
;                 for (int bj = 0; bj < 2; ++bj) { const int c256 = bj * HALF + cl; f32x4 v0 = acc[ai][bj][m][0], v1 = acc[ai][bj][m][1];
;                     if (pn < 4) { *(u32x4*)(QH + row * 1024 + pn * 256 + c256) = pack8(silu4(v0), silu4(v1)); }
;                     else if (pn < 8) { const int col = (pn - 4) * 256 + c256; const f32x4 l0 = *(const f32x4*)(LB + col), l1 = *(const f32x4*)(LB + col + 4); f32x4 o0, o1;
;                         for (int i = 0; i < 4; ++i) { o0[i] = __logf(l0[i] + (1.f - l0[i]) * __builtin_amdgcn_rcpf(1.f + __expf(-v0[i]))); o1[i] = __logf(l1[i] + (1.f - l1[i]) * __builtin_amdgcn_rcpf(1.f + __expf(-v1[i]))); }
;                         *(u32x4*)(LOGF + row * 1024 + col) = pack8(o0, o1); }
;                     else if (pn < 12) { *(u32x4*)(VH + row * 1024 + (pn - 8) * 256 + c256) = pack8(v0, v1); }
;                     else if (pn < 16) { *(u32x4*)(GH + row * 1024 + (pn - 12) * 256 + c256) = pack8(silu4(v0), silu4(v1)); }
;                     else if (pn < 20) { const float sc = 0.125f * 1.4426950408889634f; *(u32x4*)(QN + row * 1024 + (pn - 16) * 256 + c256) = pack8(v0 * sc, v1 * sc); }
;                     else if (pn < 26) { *(u32x4*)(KV6 + (size_t)(pn - 20) * ((size_t)16384 * 256) + row * 256 + c256) = pack8(v0, v1); }
;                     else if (c256 < 64) { f32x4 o0, o1; for (int i = 0; i < 4; ++i) { o0[i] = __builtin_amdgcn_rcpf(1.f + __expf(-v0[i])); o1[i] = __builtin_amdgcn_rcpf(1.f + __expf(-v1[i])); }
;                         *(f32x4*)(GATE + row * 64 + c256) = o0; *(f32x4*)(GATE + row * 64 + c256 + 4) = o1; } } }
.LBB0_159:
	v_lshl_add_u64 v[160:161], s[28:29], 0, v[154:155]
	s_andn2_b64 vcc, exec, s[10:11]
	v_lshl_add_u64 v[160:161], s[0:1], 1, v[160:161]
	s_cbranch_vccnz .LBB0_161
	v_mul_f32_e32 v153, 0xbfb8aa3b, v124
	v_mul_f32_e32 v168, 0xbfb8aa3b, v125
	v_mul_f32_e32 v169, 0xbfb8aa3b, v126
	v_exp_f32_e32 v153, v153
	v_exp_f32_e32 v168, v168
	v_exp_f32_e32 v169, v169
	v_mul_f32_e32 v170, 0xbfb8aa3b, v127
	v_add_f32_e32 v153, 1.0, v153
	v_add_f32_e32 v168, 1.0, v168
	v_add_f32_e32 v169, 1.0, v169
	v_rcp_f32_e32 v153, v153
	v_rcp_f32_e32 v168, v168
	v_rcp_f32_e32 v169, v169
	v_exp_f32_e32 v170, v170
	v_mul_f32_e32 v124, v124, v153
	v_mul_f32_e32 v125, v125, v168
	v_mul_f32_e32 v126, v126, v169
	v_add_f32_e32 v153, 1.0, v170
	v_mul_f32_e32 v168, 0xbfb8aa3b, v120
	v_mul_f32_e32 v169, 0xbfb8aa3b, v121
	v_rcp_f32_e32 v153, v153
	v_exp_f32_e32 v168, v168
	v_exp_f32_e32 v169, v169
	v_mul_f32_e32 v170, 0xbfb8aa3b, v123
	v_mul_f32_e32 v127, v127, v153
	v_add_f32_e32 v153, 1.0, v168
	v_add_f32_e32 v168, 1.0, v169
	v_mul_f32_e32 v169, 0xbfb8aa3b, v122
	v_exp_f32_e32 v170, v170
	v_exp_f32_e32 v169, v169
	v_rcp_f32_e32 v153, v153
	v_rcp_f32_e32 v168, v168
	v_add_f32_e32 v170, 1.0, v170
	v_add_f32_e32 v169, 1.0, v169
	v_rcp_f32_e32 v170, v170
	v_rcp_f32_e32 v169, v169
	v_mul_f32_e32 v153, v120, v153
	v_cvt_pk_bf16_f32 v120, v124, v125
	v_mul_f32_e32 v123, v123, v170
	v_lshl_add_u64 v[124:125], v[136:137], 1, v[160:161]
	v_mul_f32_e32 v168, v121, v168
	v_mul_f32_e32 v169, v122, v169
	v_cvt_pk_bf16_f32 v121, v126, v127
	v_cvt_pk_bf16_f32 v122, v153, v168
	v_cvt_pk_bf16_f32 v123, v169, v123
	global_store_dwordx4 v[124:125], v[120:123], off sc1
.LBB0_161:
	s_nop 1
	v_cndmask_b32_e64 v120, 0, 1, s[18:19]
	v_cmp_ne_u32_e64 s[12:13], 1, v120
	v_cndmask_b32_e64 v120, 0, 1, s[20:21]
	s_mov_b64 s[14:15], -1
	s_andn2_b64 vcc, exec, s[18:19]
	v_cmp_ne_u32_e64 s[10:11], 1, v120
	s_cbranch_vccnz .LBB0_185
	s_and_b64 vcc, exec, s[10:11]
	s_cbranch_vccnz .LBB0_182
	s_andn2_b64 vcc, exec, s[62:63]
	s_cbranch_vccnz .LBB0_179
	s_andn2_b64 vcc, exec, s[60:61]
	s_cbranch_vccnz .LBB0_176
	s_andn2_b64 vcc, exec, s[58:59]
	s_cbranch_vccnz .LBB0_173
	s_andn2_b64 vcc, exec, s[56:57]
	s_cbranch_vccnz .LBB0_170
	s_and_saveexec_b64 s[14:15], s[6:7]
	s_cbranch_execz .LBB0_169
	v_mul_f32_e32 v121, 0xbfb8aa3b, v112
	v_exp_f32_e32 v121, v121
	v_mul_f32_e32 v122, 0xbfb8aa3b, v117
	v_mul_f32_e32 v123, 0xbfb8aa3b, v113
	v_exp_f32_e32 v122, v122
	v_exp_f32_e32 v123, v123
	v_add_f32_e32 v121, 1.0, v121
	v_rcp_f32_e32 v124, v121
	v_add_f32_e32 v121, 1.0, v122
	v_add_f32_e32 v122, 1.0, v123
	v_mul_f32_e32 v123, 0xbfb8aa3b, v118
	v_mul_f32_e32 v125, 0xbfb8aa3b, v114
	v_exp_f32_e32 v123, v123
	v_exp_f32_e32 v126, v125
	v_mul_f32_e32 v120, 0xbfb8aa3b, v116
	v_rcp_f32_e32 v125, v122
	v_add_f32_e32 v122, 1.0, v123
	v_add_f32_e32 v123, 1.0, v126
	v_mul_f32_e32 v126, 0xbfb8aa3b, v119
	v_exp_f32_e32 v120, v120
	v_exp_f32_e32 v127, v126
	v_mul_f32_e32 v126, 0xbfb8aa3b, v115
	v_exp_f32_e32 v153, v126
	v_add_f32_e32 v120, 1.0, v120
	v_rcp_f32_e32 v126, v123
	v_add_f32_e32 v123, 1.0, v127
	v_rcp_f32_e32 v120, v120
	v_rcp_f32_e32 v121, v121
	v_rcp_f32_e32 v122, v122
	v_rcp_f32_e32 v123, v123
	v_add_f32_e32 v127, 1.0, v153
	v_rcp_f32_e32 v127, v127
	v_lshl_add_u64 v[158:159], v[158:159], 2, v[142:143]
	global_store_dwordx4 v[158:159], v[120:123], off sc1
	global_store_dwordx4 v[158:159], v[124:127], off offset:16 sc1

;     __device__ __forceinline__ static u32x4 pack8(const f32x4 a, const f32x4 b) { u32x4 w; w.x = cvt_pk_bf16(a[0], a[1]); w.y = cvt_pk_bf16(a[2], a[3]); w.z = cvt_pk_bf16(b[0], b[1]); w.w = cvt_pk_bf16(b[2], b[3]); return w; }
;     __device__ __forceinline__ void operator()(const f32x4 (&acc)[2][2][4][2], const Unit& u, int wr, int wc, int fr, int fq) const {
;     ...
;                     else if (pn < 26) { *(u32x4*)(KV6 + (size_t)(pn - 20) * ((size_t)16384 * 256) + row * 256 + c256) = pack8(v0, v1); }
.LBB0_170:
	s_andn2_b64 vcc, exec, s[14:15]
	s_cbranch_vccnz .LBB0_172
	s_add_u32 s14, s73, s2
	s_addc_u32 s15, s74, s3
	v_lshl_add_u64 v[124:125], s[14:15], 0, v[156:157]
	v_lshl_add_u64 v[124:125], v[136:137], 1, v[124:125]
	v_cvt_pk_bf16_f32 v120, v116, v117
	v_cvt_pk_bf16_f32 v121, v118, v119
	v_cvt_pk_bf16_f32 v122, v112, v113
	v_cvt_pk_bf16_f32 v123, v114, v115
	global_store_dwordx4 v[124:125], v[120:123], off offset:256 sc1

;     __device__ __forceinline__ static u32x4 pack8(const f32x4 a, const f32x4 b) { u32x4 w; w.x = cvt_pk_bf16(a[0], a[1]); w.y = cvt_pk_bf16(a[2], a[3]); w.z = cvt_pk_bf16(b[0], b[1]); w.w = cvt_pk_bf16(b[2], b[3]); return w; }
;     __device__ __forceinline__ void operator()(const f32x4 (&acc)[2][2][4][2], const Unit& u, int wr, int wc, int fr, int fq) const {
;     ...
;                     else if (pn < 20) { const float sc = 0.125f * 1.4426950408889634f; *(u32x4*)(QN + row * 1024 + (pn - 16) * 256 + c256) = pack8(v0 * sc, v1 * sc); }
.LBB0_173:
	s_andn2_b64 vcc, exec, s[14:15]
	s_cbranch_vccnz .LBB0_175
	v_pk_mul_f32 v[122:123], v[118:119], s[46:47] op_sel_hi:[1,0]
	v_pk_mul_f32 v[120:121], v[116:117], s[46:47] op_sel_hi:[1,0]
	v_pk_mul_f32 v[124:125], v[114:115], s[46:47] op_sel_hi:[1,0]
	v_pk_mul_f32 v[126:127], v[112:113], s[46:47] op_sel_hi:[1,0]
	v_cvt_pk_bf16_f32 v120, v120, v121
	v_cvt_pk_bf16_f32 v121, v122, v123
	s_nop 0
	v_cvt_pk_bf16_f32 v122, v126, v127
	v_cvt_pk_bf16_f32 v123, v124, v125
	v_lshl_add_u64 v[124:125], s[36:37], 0, v[154:155]
	v_lshl_add_u64 v[124:125], s[24:25], 1, v[124:125]
	v_lshl_add_u64 v[124:125], v[138:139], 1, v[124:125]
	v_add_co_u32_e32 v124, vcc, 0xffffe000, v124
	s_nop 1
	v_addc_co_u32_e32 v125, vcc, -1, v125, vcc
	global_store_dwordx4 v[124:125], v[120:123], off sc1

;     __device__ __forceinline__ static u32x4 pack8(const f32x4 a, const f32x4 b) { u32x4 w; w.x = cvt_pk_bf16(a[0], a[1]); w.y = cvt_pk_bf16(a[2], a[3]); w.z = cvt_pk_bf16(b[0], b[1]); w.w = cvt_pk_bf16(b[2], b[3]); return w; }
;     __device__ __forceinline__ static f32x4 silu4(const f32x4 v) { f32x4 o; for (int i = 0; i < 4; ++i) o[i] = v[i] * __builtin_amdgcn_rcpf(1.f + __expf(-v[i])); return o; }
;     __device__ __forceinline__ void operator()(const f32x4 (&acc)[2][2][4][2], const Unit& u, int wr, int wc, int fr, int fq) const {
;     ...
;                     else if (pn < 16) { *(u32x4*)(GH + row * 1024 + (pn - 12) * 256 + c256) = pack8(silu4(v0), silu4(v1)); }
.LBB0_176:
	s_andn2_b64 vcc, exec, s[14:15]
	s_cbranch_vccnz .LBB0_178
	v_mul_f32_e32 v120, 0xbfb8aa3b, v116
	v_mul_f32_e32 v121, 0xbfb8aa3b, v117
	v_mul_f32_e32 v122, 0xbfb8aa3b, v118
	v_mul_f32_e32 v124, 0xbfb8aa3b, v112
	v_mul_f32_e32 v125, 0xbfb8aa3b, v113
	v_exp_f32_e32 v120, v120
	v_exp_f32_e32 v121, v121
	v_exp_f32_e32 v122, v122
	v_mul_f32_e32 v123, 0xbfb8aa3b, v119
	v_exp_f32_e32 v124, v124
	v_exp_f32_e32 v125, v125
	v_exp_f32_e32 v123, v123
	v_add_f32_e32 v120, 1.0, v120
	v_add_f32_e32 v121, 1.0, v121
	v_add_f32_e32 v122, 1.0, v122
	v_add_f32_e32 v124, 1.0, v124
	v_add_f32_e32 v125, 1.0, v125
	v_rcp_f32_e32 v120, v120
	v_rcp_f32_e32 v121, v121
	v_rcp_f32_e32 v122, v122
	v_add_f32_e32 v123, 1.0, v123
	v_rcp_f32_e32 v124, v124
	v_mul_f32_e32 v126, 0xbfb8aa3b, v114
	v_mul_f32_e32 v127, 0xbfb8aa3b, v115
	v_rcp_f32_e32 v125, v125
	v_rcp_f32_e32 v123, v123
	v_exp_f32_e32 v126, v126
	v_exp_f32_e32 v127, v127
	v_mul_f32_e32 v120, v116, v120
	v_mul_f32_e32 v121, v117, v121
	v_mul_f32_e32 v122, v118, v122
	v_mul_f32_e32 v124, v112, v124
	v_mul_f32_e32 v125, v113, v125
	v_mul_f32_e32 v123, v119, v123
	v_add_f32_e32 v126, 1.0, v126
	v_add_f32_e32 v127, 1.0, v127
	v_cvt_pk_bf16_f32 v120, v120, v121
	v_cvt_pk_bf16_f32 v121, v122, v123
	v_cvt_pk_bf16_f32 v122, v124, v125
	v_lshl_add_u64 v[124:125], s[34:35], 0, v[154:155]
	v_rcp_f32_e32 v126, v126
	v_rcp_f32_e32 v127, v127
	v_lshl_add_u64 v[124:125], s[24:25], 1, v[124:125]
	v_lshl_add_u64 v[124:125], v[138:139], 1, v[124:125]
	v_add_co_u32_e32 v124, vcc, 0xfffff000, v124
	v_mul_f32_e32 v126, v114, v126
	s_nop 0
	v_addc_co_u32_e32 v125, vcc, -1, v125, vcc
	v_mul_f32_e32 v127, v115, v127
	v_cvt_pk_bf16_f32 v123, v126, v127
	global_store_dwordx4 v[124:125], v[120:123], off offset:-2048 sc1

;     __device__ __forceinline__ static u32x4 pack8(const f32x4 a, const f32x4 b) { u32x4 w; w.x = cvt_pk_bf16(a[0], a[1]); w.y = cvt_pk_bf16(a[2], a[3]); w.z = cvt_pk_bf16(b[0], b[1]); w.w = cvt_pk_bf16(b[2], b[3]); return w; }
;     __device__ __forceinline__ void operator()(const f32x4 (&acc)[2][2][4][2], const Unit& u, int wr, int wc, int fr, int fq) const {
;     ...
;                     else if (pn < 12) { *(u32x4*)(VH + row * 1024 + (pn - 8) * 256 + c256) = pack8(v0, v1); }
.LBB0_179:
	s_andn2_b64 vcc, exec, s[14:15]
	s_cbranch_vccnz .LBB0_181
	v_lshl_add_u64 v[124:125], s[30:31], 0, v[154:155]
	v_lshl_add_u64 v[124:125], s[24:25], 1, v[124:125]
	v_lshl_add_u64 v[124:125], v[136:137], 1, v[124:125]
	v_cvt_pk_bf16_f32 v120, v116, v117
	v_cvt_pk_bf16_f32 v121, v118, v119
	v_cvt_pk_bf16_f32 v122, v112, v113
	v_cvt_pk_bf16_f32 v123, v114, v115
	global_store_dwordx4 v[124:125], v[120:123], off offset:-3840 sc1

;     __device__ __forceinline__ static u32x4 pack8(const f32x4 a, const f32x4 b) { u32x4 w; w.x = cvt_pk_bf16(a[0], a[1]); w.y = cvt_pk_bf16(a[2], a[3]); w.z = cvt_pk_bf16(b[0], b[1]); w.w = cvt_pk_bf16(b[2], b[3]); return w; }
;     __device__ __forceinline__ void operator()(const f32x4 (&acc)[2][2][4][2], const Unit& u, int wr, int wc, int fr, int fq) const {
;     ...
;                     else if (pn < 8) { const int col = (pn - 4) * 256 + c256; const f32x4 l0 = *(const f32x4*)(LB + col), l1 = *(const f32x4*)(LB + col + 4); f32x4 o0, o1;
;                         for (int i = 0; i < 4; ++i) { o0[i] = __logf(l0[i] + (1.f - l0[i]) * __builtin_amdgcn_rcpf(1.f + __expf(-v0[i]))); o1[i] = __logf(l1[i] + (1.f - l1[i]) * __builtin_amdgcn_rcpf(1.f + __expf(-v1[i]))); }
;                         *(u32x4*)(LOGF + row * 1024 + col) = pack8(o0, o1); }
.LBB0_182:
	s_andn2_b64 vcc, exec, s[14:15]
	s_cbranch_vccnz .LBB0_184
	v_add_u32_e32 v120, s33, v138
	v_ashrrev_i32_e32 v121, 31, v120
	v_lshl_add_u64 v[124:125], v[120:121], 2, s[40:41]
	global_load_dwordx4 v[120:123], v[124:125], off
	s_nop 0
	global_load_dwordx4 v[124:127], v[124:125], off offset:16
	v_mul_f32_e32 v153, 0xbfb8aa3b, v116
	v_mul_f32_e32 v156, 0xbfb8aa3b, v112
	v_exp_f32_e32 v153, v153
	v_mul_f32_e32 v157, 0xbfb8aa3b, v117
	v_exp_f32_e32 v156, v156
	v_mul_f32_e32 v158, 0xbfb8aa3b, v113
	v_exp_f32_e32 v157, v157
	v_exp_f32_e32 v158, v158
	v_mul_f32_e32 v159, 0xbfb8aa3b, v118
	v_add_f32_e32 v153, 1.0, v153
	v_exp_f32_e32 v159, v159
	v_add_f32_e32 v156, 1.0, v156
	v_rcp_f32_e32 v153, v153
	v_add_f32_e32 v157, 1.0, v157
	v_rcp_f32_e32 v156, v156
	v_add_f32_e32 v158, 1.0, v158
	v_rcp_f32_e32 v157, v157
	v_mul_f32_e32 v168, 0xbfb8aa3b, v114
	v_rcp_f32_e32 v158, v158
	v_exp_f32_e32 v168, v168
	v_add_f32_e32 v159, 1.0, v159
	v_rcp_f32_e32 v159, v159
	v_add_f32_e32 v168, 1.0, v168
	v_rcp_f32_e32 v168, v168
	s_waitcnt vmcnt(0)
	v_sub_f32_e32 v169, 1.0, v120
	v_sub_f32_e32 v170, 1.0, v124
	v_fma_f32 v120, v153, v169, v120
	v_sub_f32_e32 v171, 1.0, v121
	v_fma_f32 v124, v156, v170, v124
	v_cmp_gt_f32_e32 vcc, s82, v120
	v_sub_f32_e32 v172, 1.0, v125
	v_fma_f32 v121, v157, v171, v121
	v_cndmask_b32_e64 v153, 0, 32, vcc
	v_cmp_gt_f32_e64 s[14:15], s82, v124
	v_fma_f32 v125, v158, v172, v125
	v_cmp_gt_f32_e64 s[16:17], s82, v121
	v_cndmask_b32_e64 v156, 0, 32, s[14:15]
	v_ldexp_f32 v120, v120, v153
	v_sub_f32_e32 v173, 1.0, v122
	v_cndmask_b32_e64 v157, 0, 32, s[16:17]
	v_cmp_gt_f32_e64 s[18:19], s82, v125
	v_ldexp_f32 v124, v124, v156
	v_log_f32_e32 v120, v120
	v_fma_f32 v122, v159, v173, v122
	v_cndmask_b32_e64 v158, 0, 32, s[18:19]
	v_ldexp_f32 v121, v121, v157
	v_log_f32_e32 v124, v124
	v_cmp_gt_f32_e64 s[20:21], s82, v122
	v_ldexp_f32 v125, v125, v158
	v_log_f32_e32 v121, v121
	v_cndmask_b32_e64 v159, 0, 32, s[20:21]
	v_log_f32_e32 v125, v125
	v_sub_f32_e32 v174, 1.0, v126
	v_ldexp_f32 v122, v122, v159
	v_mul_f32_e32 v159, 0x3f317217, v120
	v_fma_f32 v126, v168, v174, v126
	v_mul_f32_e32 v168, 0x3f317217, v124
	v_fma_f32 v159, v120, s83, -v159
	v_mul_f32_e32 v169, 0x3f317217, v121
	v_fma_f32 v168, v124, s83, -v168
	v_fmac_f32_e32 v159, 0x3377d1cf, v120
	v_cndmask_b32_e32 v153, 0, v167, vcc
	v_mul_f32_e32 v170, 0x3f317217, v125
	v_fma_f32 v169, v121, s83, -v169
	v_fmac_f32_e32 v168, 0x3377d1cf, v124
	v_fmac_f32_e32 v159, 0x3f317217, v120
	v_cmp_lt_f32_e64 vcc, |v120|, s84
	v_fma_f32 v170, v125, s83, -v170
	v_fmac_f32_e32 v169, 0x3377d1cf, v121
	v_fmac_f32_e32 v168, 0x3f317217, v124
	v_cndmask_b32_e32 v120, v120, v159, vcc
	v_cmp_lt_f32_e64 vcc, |v124|, s84
	v_log_f32_e32 v122, v122
	v_fmac_f32_e32 v170, 0x3377d1cf, v125
	v_fmac_f32_e32 v169, 0x3f317217, v121
	v_cndmask_b32_e32 v124, v124, v168, vcc
	v_cmp_lt_f32_e64 vcc, |v121|, s84
	v_cndmask_b32_e64 v156, 0, v167, s[14:15]
	v_fmac_f32_e32 v170, 0x3f317217, v125
	v_cndmask_b32_e32 v121, v121, v169, vcc
	v_cmp_lt_f32_e64 vcc, |v125|, s84
	v_sub_f32_e32 v124, v124, v156
	v_mul_f32_e32 v156, 0xbfb8aa3b, v119
	v_cndmask_b32_e32 v125, v125, v170, vcc
	v_cmp_gt_f32_e32 vcc, s82, v126
	v_sub_f32_e32 v120, v120, v153
	v_exp_f32_e32 v156, v156
	v_cndmask_b32_e64 v153, 0, 32, vcc
	v_mul_f32_e32 v171, 0x3f317217, v122
	v_ldexp_f32 v126, v126, v153
	v_fma_f32 v171, v122, s83, -v171
	v_log_f32_e32 v126, v126
	v_fmac_f32_e32 v171, 0x3377d1cf, v122
	v_fmac_f32_e32 v171, 0x3f317217, v122
	v_cmp_lt_f32_e64 s[14:15], |v122|, s84
	v_add_f32_e32 v156, 1.0, v156
	v_cndmask_b32_e64 v153, 0, v167, s[20:21]
	v_cndmask_b32_e64 v122, v122, v171, s[14:15]
	v_rcp_f32_e32 v156, v156
	v_sub_f32_e32 v122, v122, v153
	v_mul_f32_e32 v153, 0x3f317217, v126
	v_cndmask_b32_e64 v157, 0, v167, s[16:17]
	v_fma_f32 v153, v126, s83, -v153
	v_sub_f32_e32 v121, v121, v157
	v_fmac_f32_e32 v153, 0x3377d1cf, v126
	v_sub_f32_e32 v157, 1.0, v123
	v_fmac_f32_e32 v153, 0x3f317217, v126
	v_cmp_lt_f32_e64 s[14:15], |v126|, s84
	v_fmac_f32_e32 v123, v156, v157
	v_sub_f32_e32 v157, 1.0, v127
	v_cndmask_b32_e64 v126, v126, v153, s[14:15]
	v_cndmask_b32_e32 v153, 0, v167, vcc
	v_cmp_gt_f32_e32 vcc, s82, v123
	v_sub_f32_e32 v126, v126, v153
	v_cndmask_b32_e64 v158, 0, v167, s[18:19]
	v_cndmask_b32_e64 v156, 0, 32, vcc
	v_ldexp_f32 v123, v123, v156
	v_mul_f32_e32 v156, 0xbfb8aa3b, v115
	v_exp_f32_e32 v156, v156
	v_log_f32_e32 v123, v123
	v_sub_f32_e32 v125, v125, v158
	v_cvt_pk_bf16_f32 v120, v120, v121
	v_add_f32_e32 v156, 1.0, v156
	v_rcp_f32_e32 v156, v156
	v_mul_f32_e32 v153, 0x3f317217, v123
	v_fma_f32 v153, v123, s83, -v153
	v_fmac_f32_e32 v153, 0x3377d1cf, v123
	v_fmac_f32_e32 v127, v156, v157
	v_cmp_gt_f32_e64 s[14:15], s82, v127
	v_fmac_f32_e32 v153, 0x3f317217, v123
	v_cmp_lt_f32_e64 s[16:17], |v123|, s84
	v_cndmask_b32_e64 v156, 0, 32, s[14:15]
	v_ldexp_f32 v127, v127, v156
	v_log_f32_e32 v127, v127
	v_cndmask_b32_e64 v123, v123, v153, s[16:17]
	v_cndmask_b32_e32 v153, 0, v167, vcc
	v_sub_f32_e32 v123, v123, v153
	v_mul_f32_e32 v153, 0x3f317217, v127
	v_fma_f32 v153, v127, s83, -v153
	v_fmac_f32_e32 v153, 0x3377d1cf, v127
	v_fmac_f32_e32 v153, 0x3f317217, v127
	v_cmp_lt_f32_e64 vcc, |v127|, s84
	v_cvt_pk_bf16_f32 v121, v122, v123
	v_cvt_pk_bf16_f32 v122, v124, v125
	v_lshl_add_u64 v[124:125], s[38:39], 0, v[154:155]
	s_nop 0
	v_cndmask_b32_e32 v127, v127, v153, vcc
	v_cndmask_b32_e64 v153, 0, v167, s[14:15]
	v_sub_f32_e32 v127, v127, v153
	v_cvt_pk_bf16_f32 v123, v126, v127
	v_lshl_add_u64 v[126:127], s[0:1], 0, v[138:139]
	v_lshl_add_u64 v[124:125], v[126:127], 1, v[124:125]
	global_store_dwordx4 v[124:125], v[120:123], off offset:-2048 sc1

;     __device__ __forceinline__ static u32x4 pack8(const f32x4 a, const f32x4 b) { u32x4 w; w.x = cvt_pk_bf16(a[0], a[1]); w.y = cvt_pk_bf16(a[2], a[3]); w.z = cvt_pk_bf16(b[0], b[1]); w.w = cvt_pk_bf16(b[2], b[3]); return w; }
;     __device__ __forceinline__ static f32x4 silu4(const f32x4 v) { f32x4 o; for (int i = 0; i < 4; ++i) o[i] = v[i] * __builtin_amdgcn_rcpf(1.f + __expf(-v[i])); return o; }
;     __device__ __forceinline__ void operator()(const f32x4 (&acc)[2][2][4][2], const Unit& u, int wr, int wc, int fr, int fq) const {
;     ...
;                     if (pn < 4) { *(u32x4*)(QH + row * 1024 + pn * 256 + c256) = pack8(silu4(v0), silu4(v1)); }
.LBB0_185:
	s_andn2_b64 vcc, exec, s[14:15]
	s_cbranch_vccnz .LBB0_187
	v_mul_f32_e32 v120, 0xbfb8aa3b, v116
	v_mul_f32_e32 v121, 0xbfb8aa3b, v117
	v_mul_f32_e32 v122, 0xbfb8aa3b, v118
	v_exp_f32_e32 v120, v120
	v_exp_f32_e32 v121, v121
	v_exp_f32_e32 v122, v122
	v_mul_f32_e32 v123, 0xbfb8aa3b, v119
	v_add_f32_e32 v120, 1.0, v120
	v_add_f32_e32 v121, 1.0, v121
	v_add_f32_e32 v122, 1.0, v122
	v_rcp_f32_e32 v120, v120
	v_rcp_f32_e32 v121, v121
	v_rcp_f32_e32 v122, v122
	v_exp_f32_e32 v123, v123
	v_mul_f32_e32 v116, v116, v120
	v_mul_f32_e32 v117, v117, v121
	v_mul_f32_e32 v118, v118, v122
	v_add_f32_e32 v120, 1.0, v123
	v_mul_f32_e32 v121, 0xbfb8aa3b, v112
	v_mul_f32_e32 v122, 0xbfb8aa3b, v113
	v_rcp_f32_e32 v120, v120
	v_exp_f32_e32 v121, v121
	v_exp_f32_e32 v122, v122
	v_mul_f32_e32 v123, 0xbfb8aa3b, v115
	v_mul_f32_e32 v119, v119, v120
	v_add_f32_e32 v120, 1.0, v121
	v_add_f32_e32 v121, 1.0, v122
	v_mul_f32_e32 v122, 0xbfb8aa3b, v114
	v_exp_f32_e32 v123, v123
	v_exp_f32_e32 v122, v122
	v_rcp_f32_e32 v120, v120
	v_rcp_f32_e32 v121, v121
	v_add_f32_e32 v123, 1.0, v123
	v_add_f32_e32 v122, 1.0, v122
	v_rcp_f32_e32 v123, v123
	v_rcp_f32_e32 v122, v122
	v_mul_f32_e32 v120, v112, v120
	v_cvt_pk_bf16_f32 v112, v116, v117
	v_mul_f32_e32 v115, v115, v123
	v_lshl_add_u64 v[116:117], v[136:137], 1, v[160:161]
	v_mul_f32_e32 v121, v113, v121
	v_mul_f32_e32 v122, v114, v122
	v_cvt_pk_bf16_f32 v113, v118, v119
	v_cvt_pk_bf16_f32 v114, v120, v121
	v_cvt_pk_bf16_f32 v115, v122, v115
	global_store_dwordx4 v[116:117], v[112:115], off offset:256 sc1

;     __device__ __forceinline__ static u32x4 pack8(const f32x4 a, const f32x4 b) { u32x4 w; w.x = cvt_pk_bf16(a[0], a[1]); w.y = cvt_pk_bf16(a[2], a[3]); w.z = cvt_pk_bf16(b[0], b[1]); w.w = cvt_pk_bf16(b[2], b[3]); return w; }
;     __device__ __forceinline__ static f32x4 silu4(const f32x4 v) { f32x4 o; for (int i = 0; i < 4; ++i) o[i] = v[i] * __builtin_amdgcn_rcpf(1.f + __expf(-v[i])); return o; }
;     __device__ __forceinline__ void operator()(const f32x4 (&acc)[2][2][4][2], const Unit& u, int wr, int wc, int fr, int fq) const {
;     ...
;                     if (pn < 4) { *(u32x4*)(QH + row * 1024 + pn * 256 + c256) = pack8(silu4(v0), silu4(v1)); }
.LBB0_191:
	v_mul_f32_e32 v104, 0xbfb8aa3b, v100
	v_mul_f32_e32 v105, 0xbfb8aa3b, v101
	v_mul_f32_e32 v106, 0xbfb8aa3b, v102
	v_exp_f32_e32 v104, v104
	v_exp_f32_e32 v105, v105
	v_exp_f32_e32 v106, v106
	v_mul_f32_e32 v107, 0xbfb8aa3b, v103
	v_add_f32_e32 v104, 1.0, v104
	v_add_f32_e32 v105, 1.0, v105
	v_add_f32_e32 v106, 1.0, v106
	v_rcp_f32_e32 v104, v104
	v_rcp_f32_e32 v105, v105
	v_rcp_f32_e32 v106, v106
	v_exp_f32_e32 v107, v107
	v_mul_f32_e32 v100, v100, v104
	v_mul_f32_e32 v101, v101, v105
	v_mul_f32_e32 v102, v102, v106
	v_add_f32_e32 v104, 1.0, v107
	v_mul_f32_e32 v105, 0xbfb8aa3b, v96
	v_mul_f32_e32 v106, 0xbfb8aa3b, v97
	v_rcp_f32_e32 v104, v104
	v_exp_f32_e32 v105, v105
	v_exp_f32_e32 v106, v106
	v_mul_f32_e32 v107, 0xbfb8aa3b, v99
	v_mul_f32_e32 v103, v103, v104
	v_add_f32_e32 v104, 1.0, v105
	v_add_f32_e32 v105, 1.0, v106
	v_mul_f32_e32 v106, 0xbfb8aa3b, v98
	v_exp_f32_e32 v107, v107
	v_exp_f32_e32 v106, v106
	v_rcp_f32_e32 v104, v104
	v_rcp_f32_e32 v105, v105
	v_add_f32_e32 v107, 1.0, v107
	v_add_f32_e32 v106, 1.0, v106
	v_rcp_f32_e32 v107, v107
	v_rcp_f32_e32 v106, v106
	v_mul_f32_e32 v104, v96, v104
	v_cvt_pk_bf16_f32 v96, v100, v101
	v_mul_f32_e32 v99, v99, v107
	v_lshl_add_u64 v[100:101], v[136:137], 1, v[118:119]
	v_mul_f32_e32 v105, v97, v105
	v_mul_f32_e32 v106, v98, v106
	v_cvt_pk_bf16_f32 v97, v102, v103
	v_cvt_pk_bf16_f32 v98, v104, v105
	v_cvt_pk_bf16_f32 v99, v106, v99
	global_store_dwordx4 v[100:101], v[96:99], off offset:256 sc1

;     __device__ __forceinline__ static u32x4 pack8(const f32x4 a, const f32x4 b) { u32x4 w; w.x = cvt_pk_bf16(a[0], a[1]); w.y = cvt_pk_bf16(a[2], a[3]); w.z = cvt_pk_bf16(b[0], b[1]); w.w = cvt_pk_bf16(b[2], b[3]); return w; }
;     __device__ __forceinline__ static f32x4 silu4(const f32x4 v) { f32x4 o; for (int i = 0; i < 4; ++i) o[i] = v[i] * __builtin_amdgcn_rcpf(1.f + __expf(-v[i])); return o; }
;     __device__ __forceinline__ void operator()(const f32x4 (&acc)[2][2][4][2], const Unit& u, int wr, int wc, int fr, int fq) const {
;     ...
;                     if (pn < 4) { *(u32x4*)(QH + row * 1024 + pn * 256 + c256) = pack8(silu4(v0), silu4(v1)); }
.LBB0_196:
	v_mul_f32_e32 v88, 0xbfb8aa3b, v84
	v_mul_f32_e32 v89, 0xbfb8aa3b, v85
	v_mul_f32_e32 v90, 0xbfb8aa3b, v86
	v_exp_f32_e32 v88, v88
	v_exp_f32_e32 v89, v89
	v_exp_f32_e32 v90, v90
	v_mul_f32_e32 v91, 0xbfb8aa3b, v87
	v_add_f32_e32 v88, 1.0, v88
	v_add_f32_e32 v89, 1.0, v89
	v_add_f32_e32 v90, 1.0, v90
	v_rcp_f32_e32 v88, v88
	v_rcp_f32_e32 v89, v89
	v_rcp_f32_e32 v90, v90
	v_exp_f32_e32 v91, v91
	v_mul_f32_e32 v84, v84, v88
	v_mul_f32_e32 v85, v85, v89
	v_mul_f32_e32 v86, v86, v90
	v_add_f32_e32 v88, 1.0, v91
	v_mul_f32_e32 v89, 0xbfb8aa3b, v80
	v_mul_f32_e32 v90, 0xbfb8aa3b, v81
	v_rcp_f32_e32 v88, v88
	v_exp_f32_e32 v89, v89
	v_exp_f32_e32 v90, v90
	v_mul_f32_e32 v91, 0xbfb8aa3b, v83
	v_mul_f32_e32 v87, v87, v88
	v_add_f32_e32 v88, 1.0, v89
	v_add_f32_e32 v89, 1.0, v90
	v_mul_f32_e32 v90, 0xbfb8aa3b, v82
	v_exp_f32_e32 v91, v91
	v_exp_f32_e32 v90, v90
	v_rcp_f32_e32 v88, v88
	v_rcp_f32_e32 v89, v89
	v_add_f32_e32 v91, 1.0, v91
	v_add_f32_e32 v90, 1.0, v90
	v_rcp_f32_e32 v91, v91
	v_rcp_f32_e32 v90, v90
	v_mul_f32_e32 v88, v80, v88
	v_cvt_pk_bf16_f32 v80, v84, v85
	v_mul_f32_e32 v83, v83, v91
	v_lshl_add_u64 v[84:85], v[136:137], 1, v[102:103]
	v_mul_f32_e32 v89, v81, v89
	v_mul_f32_e32 v90, v82, v90
	v_cvt_pk_bf16_f32 v81, v86, v87
	v_cvt_pk_bf16_f32 v82, v88, v89
	v_cvt_pk_bf16_f32 v83, v90, v83
	global_store_dwordx4 v[84:85], v[80:83], off offset:256 sc1

;     __device__ __forceinline__ static u32x4 pack8(const f32x4 a, const f32x4 b) { u32x4 w; w.x = cvt_pk_bf16(a[0], a[1]); w.y = cvt_pk_bf16(a[2], a[3]); w.z = cvt_pk_bf16(b[0], b[1]); w.w = cvt_pk_bf16(b[2], b[3]); return w; }
;     __device__ __forceinline__ static f32x4 silu4(const f32x4 v) { f32x4 o; for (int i = 0; i < 4; ++i) o[i] = v[i] * __builtin_amdgcn_rcpf(1.f + __expf(-v[i])); return o; }
;     __device__ __forceinline__ void operator()(const f32x4 (&acc)[2][2][4][2], const Unit& u, int wr, int wc, int fr, int fq) const {
;     ...
;                     if (pn < 4) { *(u32x4*)(QH + row * 1024 + pn * 256 + c256) = pack8(silu4(v0), silu4(v1)); }
.LBB0_201:
	v_mul_f32_e32 v72, 0xbfb8aa3b, v68
	v_mul_f32_e32 v73, 0xbfb8aa3b, v69
	v_mul_f32_e32 v74, 0xbfb8aa3b, v70
	v_exp_f32_e32 v72, v72
	v_exp_f32_e32 v73, v73
	v_exp_f32_e32 v74, v74
	v_mul_f32_e32 v75, 0xbfb8aa3b, v71
	v_add_f32_e32 v72, 1.0, v72
	v_add_f32_e32 v73, 1.0, v73
	v_add_f32_e32 v74, 1.0, v74
	v_rcp_f32_e32 v72, v72
	v_rcp_f32_e32 v73, v73
	v_rcp_f32_e32 v74, v74
	v_exp_f32_e32 v75, v75
	v_mul_f32_e32 v68, v68, v72
	v_mul_f32_e32 v69, v69, v73
	v_mul_f32_e32 v70, v70, v74
	v_add_f32_e32 v72, 1.0, v75
	v_mul_f32_e32 v73, 0xbfb8aa3b, v64
	v_mul_f32_e32 v74, 0xbfb8aa3b, v65
	v_rcp_f32_e32 v72, v72
	v_exp_f32_e32 v73, v73
	v_exp_f32_e32 v74, v74
	v_mul_f32_e32 v75, 0xbfb8aa3b, v67
	v_mul_f32_e32 v71, v71, v72
	v_add_f32_e32 v72, 1.0, v73
	v_add_f32_e32 v73, 1.0, v74
	v_mul_f32_e32 v74, 0xbfb8aa3b, v66
	v_exp_f32_e32 v75, v75
	v_exp_f32_e32 v74, v74
	v_rcp_f32_e32 v72, v72
	v_rcp_f32_e32 v73, v73
	v_add_f32_e32 v75, 1.0, v75
	v_add_f32_e32 v74, 1.0, v74
	v_rcp_f32_e32 v75, v75
	v_rcp_f32_e32 v74, v74
	v_mul_f32_e32 v72, v64, v72
	v_cvt_pk_bf16_f32 v64, v68, v69
	v_mul_f32_e32 v67, v67, v75
	v_lshl_add_u64 v[68:69], v[136:137], 1, v[86:87]
	v_mul_f32_e32 v73, v65, v73
	v_mul_f32_e32 v74, v66, v74
	v_cvt_pk_bf16_f32 v65, v70, v71
	v_cvt_pk_bf16_f32 v66, v72, v73
	v_cvt_pk_bf16_f32 v67, v74, v67
	global_store_dwordx4 v[68:69], v[64:67], off offset:256 sc1

;     __device__ __forceinline__ static u32x4 pack8(const f32x4 a, const f32x4 b) { u32x4 w; w.x = cvt_pk_bf16(a[0], a[1]); w.y = cvt_pk_bf16(a[2], a[3]); w.z = cvt_pk_bf16(b[0], b[1]); w.w = cvt_pk_bf16(b[2], b[3]); return w; }
;     __device__ __forceinline__ static f32x4 silu4(const f32x4 v) { f32x4 o; for (int i = 0; i < 4; ++i) o[i] = v[i] * __builtin_amdgcn_rcpf(1.f + __expf(-v[i])); return o; }
;     __device__ __forceinline__ void operator()(const f32x4 (&acc)[2][2][4][2], const Unit& u, int wr, int wc, int fr, int fq) const {
;     ...
;                     if (pn < 4) { *(u32x4*)(QH + row * 1024 + pn * 256 + c256) = pack8(silu4(v0), silu4(v1)); }
.LBB0_206:
	v_mul_f32_e32 v56, 0xbfb8aa3b, v52
	v_mul_f32_e32 v57, 0xbfb8aa3b, v53
	v_mul_f32_e32 v58, 0xbfb8aa3b, v54
	v_exp_f32_e32 v56, v56
	v_exp_f32_e32 v57, v57
	v_exp_f32_e32 v58, v58
	v_mul_f32_e32 v59, 0xbfb8aa3b, v55
	v_add_f32_e32 v56, 1.0, v56
	v_add_f32_e32 v57, 1.0, v57
	v_add_f32_e32 v58, 1.0, v58
	v_rcp_f32_e32 v56, v56
	v_rcp_f32_e32 v57, v57
	v_rcp_f32_e32 v58, v58
	v_exp_f32_e32 v59, v59
	v_mul_f32_e32 v52, v52, v56
	v_mul_f32_e32 v53, v53, v57
	v_mul_f32_e32 v54, v54, v58
	v_add_f32_e32 v56, 1.0, v59
	v_mul_f32_e32 v57, 0xbfb8aa3b, v48
	v_mul_f32_e32 v58, 0xbfb8aa3b, v49
	v_rcp_f32_e32 v56, v56
	v_exp_f32_e32 v57, v57
	v_exp_f32_e32 v58, v58
	v_mul_f32_e32 v59, 0xbfb8aa3b, v51
	v_mul_f32_e32 v55, v55, v56
	v_add_f32_e32 v56, 1.0, v57
	v_add_f32_e32 v57, 1.0, v58
	v_mul_f32_e32 v58, 0xbfb8aa3b, v50
	v_exp_f32_e32 v59, v59
	v_exp_f32_e32 v58, v58
	v_rcp_f32_e32 v56, v56
	v_rcp_f32_e32 v57, v57
	v_add_f32_e32 v59, 1.0, v59
	v_add_f32_e32 v58, 1.0, v58
	v_rcp_f32_e32 v59, v59
	v_rcp_f32_e32 v58, v58
	v_mul_f32_e32 v56, v48, v56
	v_cvt_pk_bf16_f32 v48, v52, v53
	v_mul_f32_e32 v51, v51, v59
	v_lshl_add_u64 v[52:53], v[136:137], 1, v[70:71]
	v_mul_f32_e32 v57, v49, v57
	v_mul_f32_e32 v58, v50, v58
	v_cvt_pk_bf16_f32 v49, v54, v55
	v_cvt_pk_bf16_f32 v50, v56, v57
	v_cvt_pk_bf16_f32 v51, v58, v51
	global_store_dwordx4 v[52:53], v[48:51], off offset:256 sc1

;     __device__ __forceinline__ static u32x4 pack8(const f32x4 a, const f32x4 b) { u32x4 w; w.x = cvt_pk_bf16(a[0], a[1]); w.y = cvt_pk_bf16(a[2], a[3]); w.z = cvt_pk_bf16(b[0], b[1]); w.w = cvt_pk_bf16(b[2], b[3]); return w; }
;     __device__ __forceinline__ static f32x4 silu4(const f32x4 v) { f32x4 o; for (int i = 0; i < 4; ++i) o[i] = v[i] * __builtin_amdgcn_rcpf(1.f + __expf(-v[i])); return o; }
;     __device__ __forceinline__ void operator()(const f32x4 (&acc)[2][2][4][2], const Unit& u, int wr, int wc, int fr, int fq) const {
;     ...
;                     if (pn < 4) { *(u32x4*)(QH + row * 1024 + pn * 256 + c256) = pack8(silu4(v0), silu4(v1)); }
.LBB0_211:
	v_mul_f32_e32 v40, 0xbfb8aa3b, v36
	v_mul_f32_e32 v41, 0xbfb8aa3b, v37
	v_mul_f32_e32 v42, 0xbfb8aa3b, v38
	v_exp_f32_e32 v40, v40
	v_exp_f32_e32 v41, v41
	v_exp_f32_e32 v42, v42
	v_mul_f32_e32 v43, 0xbfb8aa3b, v39
	v_add_f32_e32 v40, 1.0, v40
	v_add_f32_e32 v41, 1.0, v41
	v_add_f32_e32 v42, 1.0, v42
	v_rcp_f32_e32 v40, v40
	v_rcp_f32_e32 v41, v41
	v_rcp_f32_e32 v42, v42
	v_exp_f32_e32 v43, v43
	v_mul_f32_e32 v36, v36, v40
	v_mul_f32_e32 v37, v37, v41
	v_mul_f32_e32 v38, v38, v42
	v_add_f32_e32 v40, 1.0, v43
	v_mul_f32_e32 v41, 0xbfb8aa3b, v32
	v_mul_f32_e32 v42, 0xbfb8aa3b, v33
	v_rcp_f32_e32 v40, v40
	v_exp_f32_e32 v41, v41
	v_exp_f32_e32 v42, v42
	v_mul_f32_e32 v43, 0xbfb8aa3b, v35
	v_mul_f32_e32 v39, v39, v40
	v_add_f32_e32 v40, 1.0, v41
	v_add_f32_e32 v41, 1.0, v42
	v_mul_f32_e32 v42, 0xbfb8aa3b, v34
	v_exp_f32_e32 v43, v43
	v_exp_f32_e32 v42, v42
	v_rcp_f32_e32 v40, v40
	v_rcp_f32_e32 v41, v41
	v_add_f32_e32 v43, 1.0, v43
	v_add_f32_e32 v42, 1.0, v42
	v_rcp_f32_e32 v43, v43
	v_rcp_f32_e32 v42, v42
	v_mul_f32_e32 v40, v32, v40
	v_cvt_pk_bf16_f32 v32, v36, v37
	v_mul_f32_e32 v35, v35, v43
	v_lshl_add_u64 v[36:37], v[136:137], 1, v[54:55]
	v_mul_f32_e32 v41, v33, v41
	v_mul_f32_e32 v42, v34, v42
	v_cvt_pk_bf16_f32 v33, v38, v39
	v_cvt_pk_bf16_f32 v34, v40, v41
	v_cvt_pk_bf16_f32 v35, v42, v35
	global_store_dwordx4 v[36:37], v[32:35], off offset:256 sc1

;     __device__ __forceinline__ static u32x4 pack8(const f32x4 a, const f32x4 b) { u32x4 w; w.x = cvt_pk_bf16(a[0], a[1]); w.y = cvt_pk_bf16(a[2], a[3]); w.z = cvt_pk_bf16(b[0], b[1]); w.w = cvt_pk_bf16(b[2], b[3]); return w; }
;     __device__ __forceinline__ static f32x4 silu4(const f32x4 v) { f32x4 o; for (int i = 0; i < 4; ++i) o[i] = v[i] * __builtin_amdgcn_rcpf(1.f + __expf(-v[i])); return o; }
;     __device__ __forceinline__ void operator()(const f32x4 (&acc)[2][2][4][2], const Unit& u, int wr, int wc, int fr, int fq) const {
;     ...
;                     if (pn < 4) { *(u32x4*)(QH + row * 1024 + pn * 256 + c256) = pack8(silu4(v0), silu4(v1)); }
.LBB0_216:
	v_mul_f32_e32 v24, 0xbfb8aa3b, v20
	v_mul_f32_e32 v25, 0xbfb8aa3b, v21
	v_mul_f32_e32 v26, 0xbfb8aa3b, v22
	v_exp_f32_e32 v24, v24
	v_exp_f32_e32 v25, v25
	v_exp_f32_e32 v26, v26
	v_mul_f32_e32 v27, 0xbfb8aa3b, v23
	v_add_f32_e32 v24, 1.0, v24
	v_add_f32_e32 v25, 1.0, v25
	v_add_f32_e32 v26, 1.0, v26
	v_rcp_f32_e32 v24, v24
	v_rcp_f32_e32 v25, v25
	v_rcp_f32_e32 v26, v26
	v_exp_f32_e32 v27, v27
	v_mul_f32_e32 v20, v20, v24
	v_mul_f32_e32 v21, v21, v25
	v_mul_f32_e32 v22, v22, v26
	v_add_f32_e32 v24, 1.0, v27
	v_mul_f32_e32 v25, 0xbfb8aa3b, v16
	v_mul_f32_e32 v26, 0xbfb8aa3b, v17
	v_rcp_f32_e32 v24, v24
	v_exp_f32_e32 v25, v25
	v_exp_f32_e32 v26, v26
	v_mul_f32_e32 v27, 0xbfb8aa3b, v19
	v_mul_f32_e32 v23, v23, v24
	v_add_f32_e32 v24, 1.0, v25
	v_add_f32_e32 v25, 1.0, v26
	v_mul_f32_e32 v26, 0xbfb8aa3b, v18
	v_exp_f32_e32 v27, v27
	v_exp_f32_e32 v26, v26
	v_rcp_f32_e32 v24, v24
	v_rcp_f32_e32 v25, v25
	v_add_f32_e32 v27, 1.0, v27
	v_add_f32_e32 v26, 1.0, v26
	v_rcp_f32_e32 v27, v27
	v_rcp_f32_e32 v26, v26
	v_mul_f32_e32 v24, v16, v24
	v_cvt_pk_bf16_f32 v16, v20, v21
	v_mul_f32_e32 v19, v19, v27
	v_lshl_add_u64 v[20:21], v[136:137], 1, v[38:39]
	v_mul_f32_e32 v25, v17, v25
	v_mul_f32_e32 v26, v18, v26
	v_cvt_pk_bf16_f32 v17, v22, v23
	v_cvt_pk_bf16_f32 v18, v24, v25
	v_cvt_pk_bf16_f32 v19, v26, v19
	global_store_dwordx4 v[20:21], v[16:19], off offset:256 sc1

;     __device__ __forceinline__ static u32x4 pack8(const f32x4 a, const f32x4 b) { u32x4 w; w.x = cvt_pk_bf16(a[0], a[1]); w.y = cvt_pk_bf16(a[2], a[3]); w.z = cvt_pk_bf16(b[0], b[1]); w.w = cvt_pk_bf16(b[2], b[3]); return w; }
;     __device__ __forceinline__ static f32x4 silu4(const f32x4 v) { f32x4 o; for (int i = 0; i < 4; ++i) o[i] = v[i] * __builtin_amdgcn_rcpf(1.f + __expf(-v[i])); return o; }
;     __device__ __forceinline__ void operator()(const f32x4 (&acc)[2][2][4][2], const Unit& u, int wr, int wc, int fr, int fq) const {
;     ...
;                 for (int bj = 0; bj < 2; ++bj) { const int c256 = bj * HALF + cl; f32x4 v0 = acc[ai][bj][m][0], v1 = acc[ai][bj][m][1];
;                     if (pn < 4) { *(u32x4*)(QH + row * 1024 + pn * 256 + c256) = pack8(silu4(v0), silu4(v1)); }
;                     else if (pn < 8) { const int col = (pn - 4) * 256 + c256; const f32x4 l0 = *(const f32x4*)(LB + col), l1 = *(const f32x4*)(LB + col + 4); f32x4 o0, o1;
;                         for (int i = 0; i < 4; ++i) { o0[i] = __logf(l0[i] + (1.f - l0[i]) * __builtin_amdgcn_rcpf(1.f + __expf(-v0[i]))); o1[i] = __logf(l1[i] + (1.f - l1[i]) * __builtin_amdgcn_rcpf(1.f + __expf(-v1[i]))); }
;                         *(u32x4*)(LOGF + row * 1024 + col) = pack8(o0, o1); }
;                     else if (pn < 12) { *(u32x4*)(VH + row * 1024 + (pn - 8) * 256 + c256) = pack8(v0, v1); }
;                     else if (pn < 16) { *(u32x4*)(GH + row * 1024 + (pn - 12) * 256 + c256) = pack8(silu4(v0), silu4(v1)); }
;                     else if (pn < 20) { const float sc = 0.125f * 1.4426950408889634f; *(u32x4*)(QN + row * 1024 + (pn - 16) * 256 + c256) = pack8(v0 * sc, v1 * sc); }
;                     else if (pn < 26) { *(u32x4*)(KV6 + (size_t)(pn - 20) * ((size_t)16384 * 256) + row * 256 + c256) = pack8(v0, v1); }
;                     else if (c256 < 64) { f32x4 o0, o1; for (int i = 0; i < 4; ++i) { o0[i] = __builtin_amdgcn_rcpf(1.f + __expf(-v0[i])); o1[i] = __builtin_amdgcn_rcpf(1.f + __expf(-v1[i])); }
;                         *(f32x4*)(GATE + row * 64 + c256) = o0; *(f32x4*)(GATE + row * 64 + c256 + 4) = o1; } } }
.LBB0_222:
	s_and_b64 vcc, exec, s[10:11]
	s_cbranch_vccnz .LBB0_242
	s_andn2_b64 vcc, exec, s[62:63]
	s_cbranch_vccnz .LBB0_239
	s_andn2_b64 vcc, exec, s[60:61]
	s_cbranch_vccnz .LBB0_236
	s_andn2_b64 vcc, exec, s[58:59]
	s_cbranch_vccnz .LBB0_233
	s_andn2_b64 vcc, exec, s[56:57]
	s_cbranch_vccnz .LBB0_230
	s_and_saveexec_b64 s[14:15], s[4:5]
	s_cbranch_execz .LBB0_229
	v_mul_f32_e32 v119, 0xbfb8aa3b, v104
	v_exp_f32_e32 v119, v119
	v_mul_f32_e32 v120, 0xbfb8aa3b, v109
	v_mul_f32_e32 v121, 0xbfb8aa3b, v105
	v_exp_f32_e32 v120, v120
	v_exp_f32_e32 v121, v121
	v_add_f32_e32 v119, 1.0, v119
	v_rcp_f32_e32 v122, v119
	v_add_f32_e32 v119, 1.0, v120
	v_add_f32_e32 v120, 1.0, v121
	v_mul_f32_e32 v121, 0xbfb8aa3b, v110
	v_mul_f32_e32 v123, 0xbfb8aa3b, v106
	v_exp_f32_e32 v121, v121
	v_exp_f32_e32 v124, v123
	v_mul_f32_e32 v118, 0xbfb8aa3b, v108
	v_rcp_f32_e32 v123, v120
	v_add_f32_e32 v120, 1.0, v121
	v_add_f32_e32 v121, 1.0, v124
	v_mul_f32_e32 v124, 0xbfb8aa3b, v111
	v_exp_f32_e32 v118, v118
	v_exp_f32_e32 v125, v124
	v_mul_f32_e32 v124, 0xbfb8aa3b, v107
	v_exp_f32_e32 v126, v124
	v_add_f32_e32 v118, 1.0, v118
	v_rcp_f32_e32 v124, v121
	v_add_f32_e32 v121, 1.0, v125
	v_rcp_f32_e32 v118, v118
	v_rcp_f32_e32 v119, v119
	v_rcp_f32_e32 v120, v120
	v_rcp_f32_e32 v121, v121
	v_add_f32_e32 v125, 1.0, v126
	v_rcp_f32_e32 v125, v125
	v_lshl_add_u64 v[126:127], v[116:117], 2, v[140:141]
	global_store_dwordx4 v[126:127], v[118:121], off sc1
	global_store_dwordx4 v[126:127], v[122:125], off offset:16 sc1

;     __device__ __forceinline__ static u32x4 pack8(const f32x4 a, const f32x4 b) { u32x4 w; w.x = cvt_pk_bf16(a[0], a[1]); w.y = cvt_pk_bf16(a[2], a[3]); w.z = cvt_pk_bf16(b[0], b[1]); w.w = cvt_pk_bf16(b[2], b[3]); return w; }
;     __device__ __forceinline__ void operator()(const f32x4 (&acc)[2][2][4][2], const Unit& u, int wr, int wc, int fr, int fq) const {
;     ...
;                     else if (pn < 26) { *(u32x4*)(KV6 + (size_t)(pn - 20) * ((size_t)16384 * 256) + row * 256 + c256) = pack8(v0, v1); }
.LBB0_230:
	s_andn2_b64 vcc, exec, s[14:15]
	s_cbranch_vccnz .LBB0_232
	s_add_u32 s14, s73, s2
	s_addc_u32 s15, s74, s3
	v_lshl_add_u64 v[122:123], s[14:15], 0, v[114:115]
	v_lshl_add_u64 v[122:123], v[136:137], 1, v[122:123]
	v_cvt_pk_bf16_f32 v118, v108, v109
	v_cvt_pk_bf16_f32 v119, v110, v111
	v_cvt_pk_bf16_f32 v120, v104, v105
	v_cvt_pk_bf16_f32 v121, v106, v107
	global_store_dwordx4 v[122:123], v[118:121], off sc1

;     __device__ __forceinline__ static u32x4 pack8(const f32x4 a, const f32x4 b) { u32x4 w; w.x = cvt_pk_bf16(a[0], a[1]); w.y = cvt_pk_bf16(a[2], a[3]); w.z = cvt_pk_bf16(b[0], b[1]); w.w = cvt_pk_bf16(b[2], b[3]); return w; }
;     __device__ __forceinline__ void operator()(const f32x4 (&acc)[2][2][4][2], const Unit& u, int wr, int wc, int fr, int fq) const {
;     ...
;                     else if (pn < 20) { const float sc = 0.125f * 1.4426950408889634f; *(u32x4*)(QN + row * 1024 + (pn - 16) * 256 + c256) = pack8(v0 * sc, v1 * sc); }
.LBB0_233:
	s_andn2_b64 vcc, exec, s[14:15]
	s_cbranch_vccnz .LBB0_235
	v_pk_mul_f32 v[120:121], v[110:111], s[46:47] op_sel_hi:[1,0]
	v_pk_mul_f32 v[118:119], v[108:109], s[46:47] op_sel_hi:[1,0]
	v_pk_mul_f32 v[122:123], v[106:107], s[46:47] op_sel_hi:[1,0]
	v_pk_mul_f32 v[124:125], v[104:105], s[46:47] op_sel_hi:[1,0]
	v_cvt_pk_bf16_f32 v118, v118, v119
	v_cvt_pk_bf16_f32 v119, v120, v121
	s_nop 0
	v_cvt_pk_bf16_f32 v120, v124, v125
	v_cvt_pk_bf16_f32 v121, v122, v123
	v_lshl_add_u64 v[122:123], s[36:37], 0, v[112:113]
	v_lshl_add_u64 v[122:123], s[24:25], 1, v[122:123]
	v_lshl_add_u64 v[122:123], v[136:137], 1, v[122:123]
	v_add_co_u32_e32 v122, vcc, 0xffffe000, v122
	s_nop 1
	v_addc_co_u32_e32 v123, vcc, -1, v123, vcc
	global_store_dwordx4 v[122:123], v[118:121], off sc1

;     __device__ __forceinline__ static u32x4 pack8(const f32x4 a, const f32x4 b) { u32x4 w; w.x = cvt_pk_bf16(a[0], a[1]); w.y = cvt_pk_bf16(a[2], a[3]); w.z = cvt_pk_bf16(b[0], b[1]); w.w = cvt_pk_bf16(b[2], b[3]); return w; }
;     __device__ __forceinline__ static f32x4 silu4(const f32x4 v) { f32x4 o; for (int i = 0; i < 4; ++i) o[i] = v[i] * __builtin_amdgcn_rcpf(1.f + __expf(-v[i])); return o; }
;     __device__ __forceinline__ void operator()(const f32x4 (&acc)[2][2][4][2], const Unit& u, int wr, int wc, int fr, int fq) const {
;     ...
;                     else if (pn < 16) { *(u32x4*)(GH + row * 1024 + (pn - 12) * 256 + c256) = pack8(silu4(v0), silu4(v1)); }
.LBB0_236:
	s_andn2_b64 vcc, exec, s[14:15]
	s_cbranch_vccnz .LBB0_238
	v_mul_f32_e32 v118, 0xbfb8aa3b, v108
	v_mul_f32_e32 v119, 0xbfb8aa3b, v109
	v_mul_f32_e32 v120, 0xbfb8aa3b, v110
	v_mul_f32_e32 v122, 0xbfb8aa3b, v104
	v_mul_f32_e32 v123, 0xbfb8aa3b, v105
	v_exp_f32_e32 v118, v118
	v_exp_f32_e32 v119, v119
	v_exp_f32_e32 v120, v120
	v_mul_f32_e32 v121, 0xbfb8aa3b, v111
	v_exp_f32_e32 v122, v122
	v_exp_f32_e32 v123, v123
	v_exp_f32_e32 v121, v121
	v_add_f32_e32 v118, 1.0, v118
	v_add_f32_e32 v119, 1.0, v119
	v_add_f32_e32 v120, 1.0, v120
	v_add_f32_e32 v122, 1.0, v122
	v_add_f32_e32 v123, 1.0, v123
	v_rcp_f32_e32 v118, v118
	v_rcp_f32_e32 v119, v119
	v_rcp_f32_e32 v120, v120
	v_add_f32_e32 v121, 1.0, v121
	v_rcp_f32_e32 v122, v122
	v_mul_f32_e32 v124, 0xbfb8aa3b, v106
	v_mul_f32_e32 v125, 0xbfb8aa3b, v107
	v_rcp_f32_e32 v123, v123
	v_rcp_f32_e32 v121, v121
	v_exp_f32_e32 v124, v124
	v_exp_f32_e32 v125, v125
	v_mul_f32_e32 v118, v108, v118
	v_mul_f32_e32 v119, v109, v119
	v_mul_f32_e32 v120, v110, v120
	v_mul_f32_e32 v122, v104, v122
	v_mul_f32_e32 v123, v105, v123
	v_mul_f32_e32 v121, v111, v121
	v_add_f32_e32 v124, 1.0, v124
	v_add_f32_e32 v125, 1.0, v125
	v_cvt_pk_bf16_f32 v118, v118, v119
	v_cvt_pk_bf16_f32 v119, v120, v121
	v_cvt_pk_bf16_f32 v120, v122, v123
	v_lshl_add_u64 v[122:123], s[34:35], 0, v[112:113]
	v_rcp_f32_e32 v124, v124
	v_rcp_f32_e32 v125, v125
	v_lshl_add_u64 v[122:123], s[24:25], 1, v[122:123]
	v_lshl_add_u64 v[122:123], v[136:137], 1, v[122:123]
	v_add_co_u32_e32 v122, vcc, 0xfffff000, v122
	v_mul_f32_e32 v124, v106, v124
	s_nop 0
	v_addc_co_u32_e32 v123, vcc, -1, v123, vcc
	v_mul_f32_e32 v125, v107, v125
	v_cvt_pk_bf16_f32 v121, v124, v125
	global_store_dwordx4 v[122:123], v[118:121], off offset:-2048 sc1

;     __device__ __forceinline__ static u32x4 pack8(const f32x4 a, const f32x4 b) { u32x4 w; w.x = cvt_pk_bf16(a[0], a[1]); w.y = cvt_pk_bf16(a[2], a[3]); w.z = cvt_pk_bf16(b[0], b[1]); w.w = cvt_pk_bf16(b[2], b[3]); return w; }
;     __device__ __forceinline__ void operator()(const f32x4 (&acc)[2][2][4][2], const Unit& u, int wr, int wc, int fr, int fq) const {
;     ...
;                     else if (pn < 12) { *(u32x4*)(VH + row * 1024 + (pn - 8) * 256 + c256) = pack8(v0, v1); }
.LBB0_239:
	s_andn2_b64 vcc, exec, s[14:15]
	s_cbranch_vccnz .LBB0_241
	v_lshl_add_u64 v[122:123], s[30:31], 0, v[112:113]
	v_lshl_add_u64 v[122:123], s[24:25], 1, v[122:123]
	v_lshl_add_u64 v[122:123], v[136:137], 1, v[122:123]
	v_cvt_pk_bf16_f32 v118, v108, v109
	v_cvt_pk_bf16_f32 v119, v110, v111
	v_cvt_pk_bf16_f32 v120, v104, v105
	v_cvt_pk_bf16_f32 v121, v106, v107
	global_store_dwordx4 v[122:123], v[118:121], off offset:-4096 sc1

;     __device__ __forceinline__ static u32x4 pack8(const f32x4 a, const f32x4 b) { u32x4 w; w.x = cvt_pk_bf16(a[0], a[1]); w.y = cvt_pk_bf16(a[2], a[3]); w.z = cvt_pk_bf16(b[0], b[1]); w.w = cvt_pk_bf16(b[2], b[3]); return w; }
;     __device__ __forceinline__ void operator()(const f32x4 (&acc)[2][2][4][2], const Unit& u, int wr, int wc, int fr, int fq) const {
;     ...
;                     else if (pn < 8) { const int col = (pn - 4) * 256 + c256; const f32x4 l0 = *(const f32x4*)(LB + col), l1 = *(const f32x4*)(LB + col + 4); f32x4 o0, o1;
;                         for (int i = 0; i < 4; ++i) { o0[i] = __logf(l0[i] + (1.f - l0[i]) * __builtin_amdgcn_rcpf(1.f + __expf(-v0[i]))); o1[i] = __logf(l1[i] + (1.f - l1[i]) * __builtin_amdgcn_rcpf(1.f + __expf(-v1[i]))); }
;                         *(u32x4*)(LOGF + row * 1024 + col) = pack8(o0, o1); }
.LBB0_242:
	s_andn2_b64 vcc, exec, s[14:15]
	s_cbranch_vccnz .LBB0_244
	v_add_u32_e32 v118, s33, v136
	v_ashrrev_i32_e32 v119, 31, v118
	v_lshl_add_u64 v[122:123], v[118:119], 2, s[40:41]
	global_load_dwordx4 v[118:121], v[122:123], off
	s_nop 0
	global_load_dwordx4 v[122:125], v[122:123], off offset:16
	v_mul_f32_e32 v126, 0xbfb8aa3b, v108
	v_mul_f32_e32 v127, 0xbfb8aa3b, v104
	v_exp_f32_e32 v126, v126
	v_mul_f32_e32 v153, 0xbfb8aa3b, v109
	v_exp_f32_e32 v127, v127
	v_mul_f32_e32 v154, 0xbfb8aa3b, v105
	v_exp_f32_e32 v153, v153
	v_exp_f32_e32 v154, v154
	v_mul_f32_e32 v155, 0xbfb8aa3b, v110
	v_add_f32_e32 v126, 1.0, v126
	v_exp_f32_e32 v155, v155
	v_add_f32_e32 v127, 1.0, v127
	v_rcp_f32_e32 v126, v126
	v_add_f32_e32 v153, 1.0, v153
	v_rcp_f32_e32 v127, v127
	v_add_f32_e32 v154, 1.0, v154
	v_rcp_f32_e32 v153, v153
	v_mul_f32_e32 v156, 0xbfb8aa3b, v106
	v_rcp_f32_e32 v154, v154
	v_exp_f32_e32 v156, v156
	v_add_f32_e32 v155, 1.0, v155
	v_rcp_f32_e32 v155, v155
	v_add_f32_e32 v156, 1.0, v156
	v_rcp_f32_e32 v156, v156
	s_waitcnt vmcnt(0)
	v_sub_f32_e32 v157, 1.0, v118
	v_sub_f32_e32 v158, 1.0, v122
	v_fma_f32 v118, v126, v157, v118
	v_sub_f32_e32 v159, 1.0, v119
	v_fma_f32 v122, v127, v158, v122
	v_cmp_gt_f32_e32 vcc, s82, v118
	v_sub_f32_e32 v160, 1.0, v123
	v_fma_f32 v119, v153, v159, v119
	v_cndmask_b32_e64 v126, 0, 32, vcc
	v_cmp_gt_f32_e64 s[14:15], s82, v122
	v_fma_f32 v123, v154, v160, v123
	v_cmp_gt_f32_e64 s[16:17], s82, v119
	v_cndmask_b32_e64 v127, 0, 32, s[14:15]
	v_ldexp_f32 v118, v118, v126
	v_sub_f32_e32 v161, 1.0, v120
	v_cndmask_b32_e64 v153, 0, 32, s[16:17]
	v_cmp_gt_f32_e64 s[18:19], s82, v123
	v_ldexp_f32 v122, v122, v127
	v_log_f32_e32 v118, v118
	v_fma_f32 v120, v155, v161, v120
	v_cndmask_b32_e64 v154, 0, 32, s[18:19]
	v_ldexp_f32 v119, v119, v153
	v_log_f32_e32 v122, v122
	v_cmp_gt_f32_e64 s[20:21], s82, v120
	v_ldexp_f32 v123, v123, v154
	v_log_f32_e32 v119, v119
	v_cndmask_b32_e64 v155, 0, 32, s[20:21]
	v_log_f32_e32 v123, v123
	v_sub_f32_e32 v168, 1.0, v124
	v_ldexp_f32 v120, v120, v155
	v_mul_f32_e32 v155, 0x3f317217, v118
	v_fma_f32 v124, v156, v168, v124
	v_mul_f32_e32 v156, 0x3f317217, v122
	v_fma_f32 v155, v118, s83, -v155
	v_mul_f32_e32 v157, 0x3f317217, v119
	v_fma_f32 v156, v122, s83, -v156
	v_fmac_f32_e32 v155, 0x3377d1cf, v118
	v_cndmask_b32_e32 v126, 0, v167, vcc
	v_mul_f32_e32 v158, 0x3f317217, v123
	v_fma_f32 v157, v119, s83, -v157
	v_fmac_f32_e32 v156, 0x3377d1cf, v122
	v_fmac_f32_e32 v155, 0x3f317217, v118
	v_cmp_lt_f32_e64 vcc, |v118|, s84
	v_fma_f32 v158, v123, s83, -v158
	v_fmac_f32_e32 v157, 0x3377d1cf, v119
	v_fmac_f32_e32 v156, 0x3f317217, v122
	v_cndmask_b32_e32 v118, v118, v155, vcc
	v_cmp_lt_f32_e64 vcc, |v122|, s84
	v_log_f32_e32 v120, v120
	v_fmac_f32_e32 v158, 0x3377d1cf, v123
	v_fmac_f32_e32 v157, 0x3f317217, v119
	v_cndmask_b32_e32 v122, v122, v156, vcc
	v_cmp_lt_f32_e64 vcc, |v119|, s84
	v_cndmask_b32_e64 v127, 0, v167, s[14:15]
	v_fmac_f32_e32 v158, 0x3f317217, v123
	v_cndmask_b32_e32 v119, v119, v157, vcc
	v_cmp_lt_f32_e64 vcc, |v123|, s84
	v_sub_f32_e32 v122, v122, v127
	v_mul_f32_e32 v127, 0xbfb8aa3b, v111
	v_cndmask_b32_e32 v123, v123, v158, vcc
	v_cmp_gt_f32_e32 vcc, s82, v124
	v_sub_f32_e32 v118, v118, v126
	v_exp_f32_e32 v127, v127
	v_cndmask_b32_e64 v126, 0, 32, vcc
	v_mul_f32_e32 v159, 0x3f317217, v120
	v_ldexp_f32 v124, v124, v126
	v_fma_f32 v159, v120, s83, -v159
	v_log_f32_e32 v124, v124
	v_fmac_f32_e32 v159, 0x3377d1cf, v120
	v_fmac_f32_e32 v159, 0x3f317217, v120
	v_cmp_lt_f32_e64 s[14:15], |v120|, s84
	v_add_f32_e32 v127, 1.0, v127
	v_cndmask_b32_e64 v126, 0, v167, s[20:21]
	v_cndmask_b32_e64 v120, v120, v159, s[14:15]
	v_rcp_f32_e32 v127, v127
	v_sub_f32_e32 v120, v120, v126
	v_mul_f32_e32 v126, 0x3f317217, v124
	v_cndmask_b32_e64 v153, 0, v167, s[16:17]
	v_fma_f32 v126, v124, s83, -v126
	v_sub_f32_e32 v119, v119, v153
	v_fmac_f32_e32 v126, 0x3377d1cf, v124
	v_sub_f32_e32 v153, 1.0, v121
	v_fmac_f32_e32 v126, 0x3f317217, v124
	v_cmp_lt_f32_e64 s[14:15], |v124|, s84
	v_fmac_f32_e32 v121, v127, v153
	v_sub_f32_e32 v153, 1.0, v125
	v_cndmask_b32_e64 v124, v124, v126, s[14:15]
	v_cndmask_b32_e32 v126, 0, v167, vcc
	v_cmp_gt_f32_e32 vcc, s82, v121
	v_sub_f32_e32 v124, v124, v126
	v_cndmask_b32_e64 v154, 0, v167, s[18:19]
	v_cndmask_b32_e64 v127, 0, 32, vcc
	v_ldexp_f32 v121, v121, v127
	v_mul_f32_e32 v127, 0xbfb8aa3b, v107
	v_exp_f32_e32 v127, v127
	v_log_f32_e32 v121, v121
	v_sub_f32_e32 v123, v123, v154
	v_cvt_pk_bf16_f32 v118, v118, v119
	v_add_f32_e32 v127, 1.0, v127
	v_rcp_f32_e32 v127, v127
	v_mul_f32_e32 v126, 0x3f317217, v121
	v_fma_f32 v126, v121, s83, -v126
	v_fmac_f32_e32 v126, 0x3377d1cf, v121
	v_fmac_f32_e32 v125, v127, v153
	v_cmp_gt_f32_e64 s[14:15], s82, v125
	v_fmac_f32_e32 v126, 0x3f317217, v121
	v_cmp_lt_f32_e64 s[16:17], |v121|, s84
	v_cndmask_b32_e64 v127, 0, 32, s[14:15]
	v_ldexp_f32 v125, v125, v127
	v_log_f32_e32 v125, v125
	v_cndmask_b32_e64 v121, v121, v126, s[16:17]
	v_cndmask_b32_e32 v126, 0, v167, vcc
	v_sub_f32_e32 v121, v121, v126
	v_mul_f32_e32 v126, 0x3f317217, v125
	v_fma_f32 v126, v125, s83, -v126
	v_fmac_f32_e32 v126, 0x3377d1cf, v125
	v_fmac_f32_e32 v126, 0x3f317217, v125
	v_cmp_lt_f32_e64 vcc, |v125|, s84
	v_cvt_pk_bf16_f32 v119, v120, v121
	v_cvt_pk_bf16_f32 v120, v122, v123
	v_lshl_add_u64 v[122:123], s[38:39], 0, v[112:113]
	s_nop 0
	v_cndmask_b32_e32 v125, v125, v126, vcc
	v_cndmask_b32_e64 v126, 0, v167, s[14:15]
	v_sub_f32_e32 v125, v125, v126
	v_cvt_pk_bf16_f32 v121, v124, v125
	v_lshl_add_u64 v[124:125], s[0:1], 0, v[136:137]
	v_lshl_add_u64 v[122:123], v[124:125], 1, v[122:123]
	global_store_dwordx4 v[122:123], v[118:121], off offset:-2048 sc1

;     __device__ __forceinline__ static u32x4 pack8(const f32x4 a, const f32x4 b) { u32x4 w; w.x = cvt_pk_bf16(a[0], a[1]); w.y = cvt_pk_bf16(a[2], a[3]); w.z = cvt_pk_bf16(b[0], b[1]); w.w = cvt_pk_bf16(b[2], b[3]); return w; }
;     __device__ __forceinline__ static f32x4 silu4(const f32x4 v) { f32x4 o; for (int i = 0; i < 4; ++i) o[i] = v[i] * __builtin_amdgcn_rcpf(1.f + __expf(-v[i])); return o; }
;     __device__ __forceinline__ void operator()(const f32x4 (&acc)[2][2][4][2], const Unit& u, int wr, int wc, int fr, int fq) const {
;     ...
;                 for (int bj = 0; bj < 2; ++bj) { const int c256 = bj * HALF + cl; f32x4 v0 = acc[ai][bj][m][0], v1 = acc[ai][bj][m][1];
;                     if (pn < 4) { *(u32x4*)(QH + row * 1024 + pn * 256 + c256) = pack8(silu4(v0), silu4(v1)); }
;                     else if (pn < 8) { const int col = (pn - 4) * 256 + c256; const f32x4 l0 = *(const f32x4*)(LB + col), l1 = *(const f32x4*)(LB + col + 4); f32x4 o0, o1;
;                         for (int i = 0; i < 4; ++i) { o0[i] = __logf(l0[i] + (1.f - l0[i]) * __builtin_amdgcn_rcpf(1.f + __expf(-v0[i]))); o1[i] = __logf(l1[i] + (1.f - l1[i]) * __builtin_amdgcn_rcpf(1.f + __expf(-v1[i]))); }
;                         *(u32x4*)(LOGF + row * 1024 + col) = pack8(o0, o1); }
;                     else if (pn < 12) { *(u32x4*)(VH + row * 1024 + (pn - 8) * 256 + c256) = pack8(v0, v1); }
;                     else if (pn < 16) { *(u32x4*)(GH + row * 1024 + (pn - 12) * 256 + c256) = pack8(silu4(v0), silu4(v1)); }
;                     else if (pn < 20) { const float sc = 0.125f * 1.4426950408889634f; *(u32x4*)(QN + row * 1024 + (pn - 16) * 256 + c256) = pack8(v0 * sc, v1 * sc); }
;                     else if (pn < 26) { *(u32x4*)(KV6 + (size_t)(pn - 20) * ((size_t)16384 * 256) + row * 256 + c256) = pack8(v0, v1); }
;                     else if (c256 < 64) { f32x4 o0, o1; for (int i = 0; i < 4; ++i) { o0[i] = __builtin_amdgcn_rcpf(1.f + __expf(-v0[i])); o1[i] = __builtin_amdgcn_rcpf(1.f + __expf(-v1[i])); }
;                         *(f32x4*)(GATE + row * 64 + c256) = o0; *(f32x4*)(GATE + row * 64 + c256 + 4) = o1; } } }
.LBB0_245:
	v_mul_f32_e32 v120, 0xbfb8aa3b, v108
	v_mul_f32_e32 v121, 0xbfb8aa3b, v109
	v_mul_f32_e32 v122, 0xbfb8aa3b, v110
	v_exp_f32_e32 v120, v120
	v_exp_f32_e32 v121, v121
	v_exp_f32_e32 v122, v122
	v_mul_f32_e32 v123, 0xbfb8aa3b, v111
	v_add_f32_e32 v120, 1.0, v120
	v_add_f32_e32 v121, 1.0, v121
	v_add_f32_e32 v122, 1.0, v122
	v_rcp_f32_e32 v120, v120
	v_rcp_f32_e32 v121, v121
	v_rcp_f32_e32 v122, v122
	v_exp_f32_e32 v123, v123
	v_mul_f32_e32 v108, v108, v120
	v_mul_f32_e32 v109, v109, v121
	v_mul_f32_e32 v110, v110, v122
	v_add_f32_e32 v120, 1.0, v123
	v_mul_f32_e32 v121, 0xbfb8aa3b, v104
	v_mul_f32_e32 v122, 0xbfb8aa3b, v105
	v_rcp_f32_e32 v120, v120
	v_exp_f32_e32 v121, v121
	v_exp_f32_e32 v122, v122
	v_mul_f32_e32 v123, 0xbfb8aa3b, v107
	v_mul_f32_e32 v111, v111, v120
	v_add_f32_e32 v120, 1.0, v121
	v_add_f32_e32 v121, 1.0, v122
	v_mul_f32_e32 v122, 0xbfb8aa3b, v106
	v_exp_f32_e32 v123, v123
	v_exp_f32_e32 v122, v122
	v_rcp_f32_e32 v120, v120
	v_rcp_f32_e32 v121, v121
	v_add_f32_e32 v123, 1.0, v123
	v_add_f32_e32 v122, 1.0, v122
	v_rcp_f32_e32 v123, v123
	v_rcp_f32_e32 v122, v122
	v_mul_f32_e32 v120, v104, v120
	v_cvt_pk_bf16_f32 v104, v108, v109
	v_mul_f32_e32 v107, v107, v123
	v_lshl_add_u64 v[108:109], v[136:137], 1, v[118:119]
	v_mul_f32_e32 v121, v105, v121
	v_mul_f32_e32 v122, v106, v122
	v_cvt_pk_bf16_f32 v105, v110, v111
	v_cvt_pk_bf16_f32 v106, v120, v121
	v_cvt_pk_bf16_f32 v107, v122, v107
	global_store_dwordx4 v[108:109], v[104:107], off sc1
	s_and_b64 vcc, exec, s[12:13]
	s_mov_b64 s[14:15], -1
	s_cbranch_vccnz .LBB0_190
.LBB0_246:
	s_and_b64 vcc, exec, s[10:11]
	s_cbranch_vccnz .LBB0_266
	s_andn2_b64 vcc, exec, s[62:63]
	s_cbranch_vccnz .LBB0_263
	s_andn2_b64 vcc, exec, s[60:61]
	s_cbranch_vccnz .LBB0_260
	s_andn2_b64 vcc, exec, s[58:59]
	s_cbranch_vccnz .LBB0_257
	s_andn2_b64 vcc, exec, s[56:57]
	s_cbranch_vccnz .LBB0_254
	s_and_saveexec_b64 s[14:15], s[6:7]
	s_cbranch_execz .LBB0_253
	v_mul_f32_e32 v105, 0xbfb8aa3b, v96
	v_exp_f32_e32 v105, v105
	v_mul_f32_e32 v106, 0xbfb8aa3b, v101
	v_mul_f32_e32 v107, 0xbfb8aa3b, v97
	v_exp_f32_e32 v106, v106
	v_exp_f32_e32 v107, v107
	v_add_f32_e32 v105, 1.0, v105
	v_rcp_f32_e32 v108, v105
	v_add_f32_e32 v105, 1.0, v106
	v_add_f32_e32 v106, 1.0, v107
	v_mul_f32_e32 v107, 0xbfb8aa3b, v102
	v_mul_f32_e32 v109, 0xbfb8aa3b, v98
	v_exp_f32_e32 v107, v107
	v_exp_f32_e32 v110, v109
	v_mul_f32_e32 v104, 0xbfb8aa3b, v100
	v_rcp_f32_e32 v109, v106
	v_add_f32_e32 v106, 1.0, v107
	v_add_f32_e32 v107, 1.0, v110
	v_mul_f32_e32 v110, 0xbfb8aa3b, v103
	v_exp_f32_e32 v104, v104
	v_exp_f32_e32 v111, v110
	v_mul_f32_e32 v110, 0xbfb8aa3b, v99
	v_exp_f32_e32 v120, v110
	v_add_f32_e32 v104, 1.0, v104
	v_rcp_f32_e32 v110, v107
	v_add_f32_e32 v107, 1.0, v111
	v_rcp_f32_e32 v104, v104
	v_rcp_f32_e32 v105, v105
	v_rcp_f32_e32 v106, v106
	v_rcp_f32_e32 v107, v107
	v_add_f32_e32 v111, 1.0, v120
	v_rcp_f32_e32 v111, v111
	v_lshl_add_u64 v[116:117], v[116:117], 2, v[142:143]
	global_store_dwordx4 v[116:117], v[104:107], off sc1
	global_store_dwordx4 v[116:117], v[108:111], off offset:16 sc1

;     __device__ __forceinline__ static u32x4 pack8(const f32x4 a, const f32x4 b) { u32x4 w; w.x = cvt_pk_bf16(a[0], a[1]); w.y = cvt_pk_bf16(a[2], a[3]); w.z = cvt_pk_bf16(b[0], b[1]); w.w = cvt_pk_bf16(b[2], b[3]); return w; }
;     __device__ __forceinline__ void operator()(const f32x4 (&acc)[2][2][4][2], const Unit& u, int wr, int wc, int fr, int fq) const {
;     ...
;                     else if (pn < 26) { *(u32x4*)(KV6 + (size_t)(pn - 20) * ((size_t)16384 * 256) + row * 256 + c256) = pack8(v0, v1); }
.LBB0_254:
	s_andn2_b64 vcc, exec, s[14:15]
	s_cbranch_vccnz .LBB0_256
	s_add_u32 s14, s73, s2
	s_addc_u32 s15, s74, s3
	v_lshl_add_u64 v[108:109], s[14:15], 0, v[114:115]
	v_lshl_add_u64 v[108:109], v[136:137], 1, v[108:109]
	v_cvt_pk_bf16_f32 v104, v100, v101
	v_cvt_pk_bf16_f32 v105, v102, v103
	v_cvt_pk_bf16_f32 v106, v96, v97
	v_cvt_pk_bf16_f32 v107, v98, v99
	global_store_dwordx4 v[108:109], v[104:107], off offset:256 sc1

;     __device__ __forceinline__ static u32x4 pack8(const f32x4 a, const f32x4 b) { u32x4 w; w.x = cvt_pk_bf16(a[0], a[1]); w.y = cvt_pk_bf16(a[2], a[3]); w.z = cvt_pk_bf16(b[0], b[1]); w.w = cvt_pk_bf16(b[2], b[3]); return w; }
;     __device__ __forceinline__ void operator()(const f32x4 (&acc)[2][2][4][2], const Unit& u, int wr, int wc, int fr, int fq) const {
;     ...
;                     else if (pn < 20) { const float sc = 0.125f * 1.4426950408889634f; *(u32x4*)(QN + row * 1024 + (pn - 16) * 256 + c256) = pack8(v0 * sc, v1 * sc); }
.LBB0_257:
	s_andn2_b64 vcc, exec, s[14:15]
	s_cbranch_vccnz .LBB0_259
	v_pk_mul_f32 v[106:107], v[102:103], s[46:47] op_sel_hi:[1,0]
	v_pk_mul_f32 v[104:105], v[100:101], s[46:47] op_sel_hi:[1,0]
	v_pk_mul_f32 v[108:109], v[98:99], s[46:47] op_sel_hi:[1,0]
	v_pk_mul_f32 v[110:111], v[96:97], s[46:47] op_sel_hi:[1,0]
	v_cvt_pk_bf16_f32 v104, v104, v105
	v_cvt_pk_bf16_f32 v105, v106, v107
	s_nop 0
	v_cvt_pk_bf16_f32 v106, v110, v111
	v_cvt_pk_bf16_f32 v107, v108, v109
	v_lshl_add_u64 v[108:109], s[36:37], 0, v[112:113]
	v_lshl_add_u64 v[108:109], s[24:25], 1, v[108:109]
	v_lshl_add_u64 v[108:109], v[138:139], 1, v[108:109]
	v_add_co_u32_e32 v108, vcc, 0xffffe000, v108
	s_nop 1
	v_addc_co_u32_e32 v109, vcc, -1, v109, vcc
	global_store_dwordx4 v[108:109], v[104:107], off sc1

;     __device__ __forceinline__ static u32x4 pack8(const f32x4 a, const f32x4 b) { u32x4 w; w.x = cvt_pk_bf16(a[0], a[1]); w.y = cvt_pk_bf16(a[2], a[3]); w.z = cvt_pk_bf16(b[0], b[1]); w.w = cvt_pk_bf16(b[2], b[3]); return w; }
;     __device__ __forceinline__ static f32x4 silu4(const f32x4 v) { f32x4 o; for (int i = 0; i < 4; ++i) o[i] = v[i] * __builtin_amdgcn_rcpf(1.f + __expf(-v[i])); return o; }
;     __device__ __forceinline__ void operator()(const f32x4 (&acc)[2][2][4][2], const Unit& u, int wr, int wc, int fr, int fq) const {
;     ...
;                     else if (pn < 16) { *(u32x4*)(GH + row * 1024 + (pn - 12) * 256 + c256) = pack8(silu4(v0), silu4(v1)); }
.LBB0_260:
	s_andn2_b64 vcc, exec, s[14:15]
	s_cbranch_vccnz .LBB0_262
	v_mul_f32_e32 v104, 0xbfb8aa3b, v100
	v_mul_f32_e32 v105, 0xbfb8aa3b, v101
	v_mul_f32_e32 v106, 0xbfb8aa3b, v102
	v_mul_f32_e32 v108, 0xbfb8aa3b, v96
	v_mul_f32_e32 v109, 0xbfb8aa3b, v97
	v_exp_f32_e32 v104, v104
	v_exp_f32_e32 v105, v105
	v_exp_f32_e32 v106, v106
	v_mul_f32_e32 v107, 0xbfb8aa3b, v103
	v_exp_f32_e32 v108, v108
	v_exp_f32_e32 v109, v109
	v_exp_f32_e32 v107, v107
	v_add_f32_e32 v104, 1.0, v104
	v_add_f32_e32 v105, 1.0, v105
	v_add_f32_e32 v106, 1.0, v106
	v_add_f32_e32 v108, 1.0, v108
	v_add_f32_e32 v109, 1.0, v109
	v_rcp_f32_e32 v104, v104
	v_rcp_f32_e32 v105, v105
	v_rcp_f32_e32 v106, v106
	v_add_f32_e32 v107, 1.0, v107
	v_rcp_f32_e32 v108, v108
	v_mul_f32_e32 v110, 0xbfb8aa3b, v98
	v_mul_f32_e32 v111, 0xbfb8aa3b, v99
	v_rcp_f32_e32 v109, v109
	v_rcp_f32_e32 v107, v107
	v_exp_f32_e32 v110, v110
	v_exp_f32_e32 v111, v111
	v_mul_f32_e32 v104, v100, v104
	v_mul_f32_e32 v105, v101, v105
	v_mul_f32_e32 v106, v102, v106
	v_mul_f32_e32 v108, v96, v108
	v_mul_f32_e32 v109, v97, v109
	v_mul_f32_e32 v107, v103, v107
	v_add_f32_e32 v110, 1.0, v110
	v_add_f32_e32 v111, 1.0, v111
	v_cvt_pk_bf16_f32 v104, v104, v105
	v_cvt_pk_bf16_f32 v105, v106, v107
	v_cvt_pk_bf16_f32 v106, v108, v109
	v_lshl_add_u64 v[108:109], s[34:35], 0, v[112:113]
	v_rcp_f32_e32 v110, v110
	v_rcp_f32_e32 v111, v111
	v_lshl_add_u64 v[108:109], s[24:25], 1, v[108:109]
	v_lshl_add_u64 v[108:109], v[138:139], 1, v[108:109]
	v_add_co_u32_e32 v108, vcc, 0xfffff000, v108
	v_mul_f32_e32 v110, v98, v110
	s_nop 0
	v_addc_co_u32_e32 v109, vcc, -1, v109, vcc
	v_mul_f32_e32 v111, v99, v111
	v_cvt_pk_bf16_f32 v107, v110, v111
	global_store_dwordx4 v[108:109], v[104:107], off offset:-2048 sc1

;     __device__ __forceinline__ static u32x4 pack8(const f32x4 a, const f32x4 b) { u32x4 w; w.x = cvt_pk_bf16(a[0], a[1]); w.y = cvt_pk_bf16(a[2], a[3]); w.z = cvt_pk_bf16(b[0], b[1]); w.w = cvt_pk_bf16(b[2], b[3]); return w; }
;     __device__ __forceinline__ void operator()(const f32x4 (&acc)[2][2][4][2], const Unit& u, int wr, int wc, int fr, int fq) const {
;     ...
;                     else if (pn < 12) { *(u32x4*)(VH + row * 1024 + (pn - 8) * 256 + c256) = pack8(v0, v1); }
.LBB0_263:
	s_andn2_b64 vcc, exec, s[14:15]
	s_cbranch_vccnz .LBB0_265
	v_lshl_add_u64 v[108:109], s[30:31], 0, v[112:113]
	v_lshl_add_u64 v[108:109], s[24:25], 1, v[108:109]
	v_lshl_add_u64 v[108:109], v[136:137], 1, v[108:109]
	v_cvt_pk_bf16_f32 v104, v100, v101
	v_cvt_pk_bf16_f32 v105, v102, v103
	v_cvt_pk_bf16_f32 v106, v96, v97
	v_cvt_pk_bf16_f32 v107, v98, v99
	global_store_dwordx4 v[108:109], v[104:107], off offset:-3840 sc1

;     __device__ __forceinline__ static u32x4 pack8(const f32x4 a, const f32x4 b) { u32x4 w; w.x = cvt_pk_bf16(a[0], a[1]); w.y = cvt_pk_bf16(a[2], a[3]); w.z = cvt_pk_bf16(b[0], b[1]); w.w = cvt_pk_bf16(b[2], b[3]); return w; }
;     __device__ __forceinline__ void operator()(const f32x4 (&acc)[2][2][4][2], const Unit& u, int wr, int wc, int fr, int fq) const {
;     ...
;                     else if (pn < 8) { const int col = (pn - 4) * 256 + c256; const f32x4 l0 = *(const f32x4*)(LB + col), l1 = *(const f32x4*)(LB + col + 4); f32x4 o0, o1;
;                         for (int i = 0; i < 4; ++i) { o0[i] = __logf(l0[i] + (1.f - l0[i]) * __builtin_amdgcn_rcpf(1.f + __expf(-v0[i]))); o1[i] = __logf(l1[i] + (1.f - l1[i]) * __builtin_amdgcn_rcpf(1.f + __expf(-v1[i]))); }
;                         *(u32x4*)(LOGF + row * 1024 + col) = pack8(o0, o1); }
.LBB0_266:
	s_andn2_b64 vcc, exec, s[14:15]
	s_cbranch_vccnz .LBB0_268
	v_add_u32_e32 v104, s33, v138
	v_ashrrev_i32_e32 v105, 31, v104
	v_lshl_add_u64 v[108:109], v[104:105], 2, s[40:41]
	global_load_dwordx4 v[104:107], v[108:109], off
	s_nop 0
	global_load_dwordx4 v[108:111], v[108:109], off offset:16
	v_mul_f32_e32 v114, 0xbfb8aa3b, v100
	v_mul_f32_e32 v115, 0xbfb8aa3b, v96
	v_exp_f32_e32 v114, v114
	v_mul_f32_e32 v116, 0xbfb8aa3b, v101
	v_exp_f32_e32 v115, v115
	v_mul_f32_e32 v117, 0xbfb8aa3b, v97
	v_exp_f32_e32 v116, v116
	v_exp_f32_e32 v117, v117
	v_mul_f32_e32 v120, 0xbfb8aa3b, v102
	v_add_f32_e32 v114, 1.0, v114
	v_exp_f32_e32 v120, v120
	v_add_f32_e32 v115, 1.0, v115
	v_rcp_f32_e32 v114, v114
	v_add_f32_e32 v116, 1.0, v116
	v_rcp_f32_e32 v115, v115
	v_add_f32_e32 v117, 1.0, v117
	v_rcp_f32_e32 v116, v116
	v_mul_f32_e32 v121, 0xbfb8aa3b, v98
	v_rcp_f32_e32 v117, v117
	v_exp_f32_e32 v121, v121
	v_add_f32_e32 v120, 1.0, v120
	v_rcp_f32_e32 v120, v120
	v_add_f32_e32 v121, 1.0, v121
	v_rcp_f32_e32 v121, v121
	s_waitcnt vmcnt(0)
	v_sub_f32_e32 v122, 1.0, v104
	v_sub_f32_e32 v123, 1.0, v108
	v_fma_f32 v104, v114, v122, v104
	v_sub_f32_e32 v124, 1.0, v105
	v_fma_f32 v108, v115, v123, v108
	v_cmp_gt_f32_e32 vcc, s82, v104
	v_sub_f32_e32 v125, 1.0, v109
	v_fma_f32 v105, v116, v124, v105
	v_cndmask_b32_e64 v114, 0, 32, vcc
	v_cmp_gt_f32_e64 s[14:15], s82, v108
	v_fma_f32 v109, v117, v125, v109
	v_cmp_gt_f32_e64 s[16:17], s82, v105
	v_cndmask_b32_e64 v115, 0, 32, s[14:15]
	v_ldexp_f32 v104, v104, v114
	v_sub_f32_e32 v126, 1.0, v106
	v_cndmask_b32_e64 v116, 0, 32, s[16:17]
	v_cmp_gt_f32_e64 s[18:19], s82, v109
	v_ldexp_f32 v108, v108, v115
	v_log_f32_e32 v104, v104
	v_fma_f32 v106, v120, v126, v106
	v_cndmask_b32_e64 v117, 0, 32, s[18:19]
	v_ldexp_f32 v105, v105, v116
	v_log_f32_e32 v108, v108
	v_cmp_gt_f32_e64 s[20:21], s82, v106
	v_ldexp_f32 v109, v109, v117
	v_log_f32_e32 v105, v105
	v_cndmask_b32_e64 v120, 0, 32, s[20:21]
	v_log_f32_e32 v109, v109
	v_sub_f32_e32 v127, 1.0, v110
	v_ldexp_f32 v106, v106, v120
	v_mul_f32_e32 v120, 0x3f317217, v104
	v_fma_f32 v110, v121, v127, v110
	v_mul_f32_e32 v121, 0x3f317217, v108
	v_fma_f32 v120, v104, s83, -v120
	v_mul_f32_e32 v122, 0x3f317217, v105
	v_fma_f32 v121, v108, s83, -v121
	v_fmac_f32_e32 v120, 0x3377d1cf, v104
	v_cndmask_b32_e32 v114, 0, v167, vcc
	v_mul_f32_e32 v123, 0x3f317217, v109
	v_fma_f32 v122, v105, s83, -v122
	v_fmac_f32_e32 v121, 0x3377d1cf, v108
	v_fmac_f32_e32 v120, 0x3f317217, v104
	v_cmp_lt_f32_e64 vcc, |v104|, s84
	v_fma_f32 v123, v109, s83, -v123
	v_fmac_f32_e32 v122, 0x3377d1cf, v105
	v_fmac_f32_e32 v121, 0x3f317217, v108
	v_cndmask_b32_e32 v104, v104, v120, vcc
	v_cmp_lt_f32_e64 vcc, |v108|, s84
	v_log_f32_e32 v106, v106
	v_fmac_f32_e32 v123, 0x3377d1cf, v109
	v_fmac_f32_e32 v122, 0x3f317217, v105
	v_cndmask_b32_e32 v108, v108, v121, vcc
	v_cmp_lt_f32_e64 vcc, |v105|, s84
	v_cndmask_b32_e64 v115, 0, v167, s[14:15]
	v_fmac_f32_e32 v123, 0x3f317217, v109
	v_cndmask_b32_e32 v105, v105, v122, vcc
	v_cmp_lt_f32_e64 vcc, |v109|, s84
	v_sub_f32_e32 v108, v108, v115
	v_mul_f32_e32 v115, 0xbfb8aa3b, v103
	v_cndmask_b32_e32 v109, v109, v123, vcc
	v_cmp_gt_f32_e32 vcc, s82, v110
	v_sub_f32_e32 v104, v104, v114
	v_exp_f32_e32 v115, v115
	v_cndmask_b32_e64 v114, 0, 32, vcc
	v_mul_f32_e32 v124, 0x3f317217, v106
	v_ldexp_f32 v110, v110, v114
	v_fma_f32 v124, v106, s83, -v124
	v_log_f32_e32 v110, v110
	v_fmac_f32_e32 v124, 0x3377d1cf, v106
	v_fmac_f32_e32 v124, 0x3f317217, v106
	v_cmp_lt_f32_e64 s[14:15], |v106|, s84
	v_add_f32_e32 v115, 1.0, v115
	v_cndmask_b32_e64 v114, 0, v167, s[20:21]
	v_cndmask_b32_e64 v106, v106, v124, s[14:15]
	v_rcp_f32_e32 v115, v115
	v_sub_f32_e32 v106, v106, v114
	v_mul_f32_e32 v114, 0x3f317217, v110
	v_cndmask_b32_e64 v116, 0, v167, s[16:17]
	v_fma_f32 v114, v110, s83, -v114
	v_sub_f32_e32 v105, v105, v116
	v_fmac_f32_e32 v114, 0x3377d1cf, v110
	v_sub_f32_e32 v116, 1.0, v107
	v_fmac_f32_e32 v114, 0x3f317217, v110
	v_cmp_lt_f32_e64 s[14:15], |v110|, s84
	v_fmac_f32_e32 v107, v115, v116
	v_sub_f32_e32 v116, 1.0, v111
	v_cndmask_b32_e64 v110, v110, v114, s[14:15]
	v_cndmask_b32_e32 v114, 0, v167, vcc
	v_cmp_gt_f32_e32 vcc, s82, v107
	v_sub_f32_e32 v110, v110, v114
	v_cndmask_b32_e64 v117, 0, v167, s[18:19]
	v_cndmask_b32_e64 v115, 0, 32, vcc
	v_ldexp_f32 v107, v107, v115
	v_mul_f32_e32 v115, 0xbfb8aa3b, v99
	v_exp_f32_e32 v115, v115
	v_log_f32_e32 v107, v107
	v_sub_f32_e32 v109, v109, v117
	v_cvt_pk_bf16_f32 v104, v104, v105
	v_add_f32_e32 v115, 1.0, v115
	v_rcp_f32_e32 v115, v115
	v_mul_f32_e32 v114, 0x3f317217, v107
	v_fma_f32 v114, v107, s83, -v114
	v_fmac_f32_e32 v114, 0x3377d1cf, v107
	v_fmac_f32_e32 v111, v115, v116
	v_cmp_gt_f32_e64 s[14:15], s82, v111
	v_fmac_f32_e32 v114, 0x3f317217, v107
	v_cmp_lt_f32_e64 s[16:17], |v107|, s84
	v_cndmask_b32_e64 v115, 0, 32, s[14:15]
	v_ldexp_f32 v111, v111, v115
	v_log_f32_e32 v111, v111
	v_cndmask_b32_e64 v107, v107, v114, s[16:17]
	v_cndmask_b32_e32 v114, 0, v167, vcc
	v_sub_f32_e32 v107, v107, v114
	v_mul_f32_e32 v114, 0x3f317217, v111
	v_fma_f32 v114, v111, s83, -v114
	v_fmac_f32_e32 v114, 0x3377d1cf, v111
	v_fmac_f32_e32 v114, 0x3f317217, v111
	v_cmp_lt_f32_e64 vcc, |v111|, s84
	v_cvt_pk_bf16_f32 v105, v106, v107
	v_cvt_pk_bf16_f32 v106, v108, v109
	v_lshl_add_u64 v[108:109], s[38:39], 0, v[112:113]
	s_nop 0
	v_cndmask_b32_e32 v111, v111, v114, vcc
	v_cndmask_b32_e64 v114, 0, v167, s[14:15]
	v_sub_f32_e32 v111, v111, v114
	v_cvt_pk_bf16_f32 v107, v110, v111
	v_lshl_add_u64 v[110:111], s[0:1], 0, v[138:139]
	v_lshl_add_u64 v[108:109], v[110:111], 1, v[108:109]
	global_store_dwordx4 v[108:109], v[104:107], off offset:-2048 sc1

;     __device__ __forceinline__ static u32x4 pack8(const f32x4 a, const f32x4 b) { u32x4 w; w.x = cvt_pk_bf16(a[0], a[1]); w.y = cvt_pk_bf16(a[2], a[3]); w.z = cvt_pk_bf16(b[0], b[1]); w.w = cvt_pk_bf16(b[2], b[3]); return w; }
;     __device__ __forceinline__ static f32x4 silu4(const f32x4 v) { f32x4 o; for (int i = 0; i < 4; ++i) o[i] = v[i] * __builtin_amdgcn_rcpf(1.f + __expf(-v[i])); return o; }
;     __device__ __forceinline__ void operator()(const f32x4 (&acc)[2][2][4][2], const Unit& u, int wr, int wc, int fr, int fq) const {
;     ...
;                 for (int bj = 0; bj < 2; ++bj) { const int c256 = bj * HALF + cl; f32x4 v0 = acc[ai][bj][m][0], v1 = acc[ai][bj][m][1];
;                     if (pn < 4) { *(u32x4*)(QH + row * 1024 + pn * 256 + c256) = pack8(silu4(v0), silu4(v1)); }
;                     else if (pn < 8) { const int col = (pn - 4) * 256 + c256; const f32x4 l0 = *(const f32x4*)(LB + col), l1 = *(const f32x4*)(LB + col + 4); f32x4 o0, o1;
;                         for (int i = 0; i < 4; ++i) { o0[i] = __logf(l0[i] + (1.f - l0[i]) * __builtin_amdgcn_rcpf(1.f + __expf(-v0[i]))); o1[i] = __logf(l1[i] + (1.f - l1[i]) * __builtin_amdgcn_rcpf(1.f + __expf(-v1[i]))); }
;                         *(u32x4*)(LOGF + row * 1024 + col) = pack8(o0, o1); }
;                     else if (pn < 12) { *(u32x4*)(VH + row * 1024 + (pn - 8) * 256 + c256) = pack8(v0, v1); }
;                     else if (pn < 16) { *(u32x4*)(GH + row * 1024 + (pn - 12) * 256 + c256) = pack8(silu4(v0), silu4(v1)); }
;                     else if (pn < 20) { const float sc = 0.125f * 1.4426950408889634f; *(u32x4*)(QN + row * 1024 + (pn - 16) * 256 + c256) = pack8(v0 * sc, v1 * sc); }
;                     else if (pn < 26) { *(u32x4*)(KV6 + (size_t)(pn - 20) * ((size_t)16384 * 256) + row * 256 + c256) = pack8(v0, v1); }
;                     else if (c256 < 64) { f32x4 o0, o1; for (int i = 0; i < 4; ++i) { o0[i] = __builtin_amdgcn_rcpf(1.f + __expf(-v0[i])); o1[i] = __builtin_amdgcn_rcpf(1.f + __expf(-v1[i])); }
;                         *(f32x4*)(GATE + row * 64 + c256) = o0; *(f32x4*)(GATE + row * 64 + c256 + 4) = o1; } } }
.LBB0_269:
	s_and_b64 vcc, exec, s[10:11]
	s_cbranch_vccnz .LBB0_289
	s_andn2_b64 vcc, exec, s[62:63]
	s_cbranch_vccnz .LBB0_286
	s_andn2_b64 vcc, exec, s[60:61]
	s_cbranch_vccnz .LBB0_283
	s_andn2_b64 vcc, exec, s[58:59]
	s_cbranch_vccnz .LBB0_280
	s_andn2_b64 vcc, exec, s[56:57]
	s_cbranch_vccnz .LBB0_277
	s_and_saveexec_b64 s[14:15], s[4:5]
	s_cbranch_execz .LBB0_276
	v_mul_f32_e32 v103, 0xbfb8aa3b, v88
	v_exp_f32_e32 v103, v103
	v_mul_f32_e32 v104, 0xbfb8aa3b, v93
	v_mul_f32_e32 v105, 0xbfb8aa3b, v89
	v_exp_f32_e32 v104, v104
	v_exp_f32_e32 v105, v105
	v_add_f32_e32 v103, 1.0, v103
	v_rcp_f32_e32 v106, v103
	v_add_f32_e32 v103, 1.0, v104
	v_add_f32_e32 v104, 1.0, v105
	v_mul_f32_e32 v105, 0xbfb8aa3b, v94
	v_mul_f32_e32 v107, 0xbfb8aa3b, v90
	v_exp_f32_e32 v105, v105
	v_exp_f32_e32 v108, v107
	v_mul_f32_e32 v102, 0xbfb8aa3b, v92
	v_rcp_f32_e32 v107, v104
	v_add_f32_e32 v104, 1.0, v105
	v_add_f32_e32 v105, 1.0, v108
	v_mul_f32_e32 v108, 0xbfb8aa3b, v95
	v_exp_f32_e32 v102, v102
	v_exp_f32_e32 v109, v108
	v_mul_f32_e32 v108, 0xbfb8aa3b, v91
	v_exp_f32_e32 v110, v108
	v_add_f32_e32 v102, 1.0, v102
	v_rcp_f32_e32 v108, v105
	v_add_f32_e32 v105, 1.0, v109
	v_rcp_f32_e32 v102, v102
	v_rcp_f32_e32 v103, v103
	v_rcp_f32_e32 v104, v104
	v_rcp_f32_e32 v105, v105
	v_add_f32_e32 v109, 1.0, v110
	v_rcp_f32_e32 v109, v109
	v_lshl_add_u64 v[110:111], v[100:101], 2, v[140:141]
	global_store_dwordx4 v[110:111], v[102:105], off sc1
	global_store_dwordx4 v[110:111], v[106:109], off offset:16 sc1

;     __device__ __forceinline__ static u32x4 pack8(const f32x4 a, const f32x4 b) { u32x4 w; w.x = cvt_pk_bf16(a[0], a[1]); w.y = cvt_pk_bf16(a[2], a[3]); w.z = cvt_pk_bf16(b[0], b[1]); w.w = cvt_pk_bf16(b[2], b[3]); return w; }
;     __device__ __forceinline__ void operator()(const f32x4 (&acc)[2][2][4][2], const Unit& u, int wr, int wc, int fr, int fq) const {
;     ...
;                     else if (pn < 26) { *(u32x4*)(KV6 + (size_t)(pn - 20) * ((size_t)16384 * 256) + row * 256 + c256) = pack8(v0, v1); }
.LBB0_277:
	s_andn2_b64 vcc, exec, s[14:15]
	s_cbranch_vccnz .LBB0_279
	s_add_u32 s14, s73, s2
	s_addc_u32 s15, s74, s3
	v_lshl_add_u64 v[106:107], s[14:15], 0, v[98:99]
	v_lshl_add_u64 v[106:107], v[136:137], 1, v[106:107]
	v_cvt_pk_bf16_f32 v102, v92, v93
	v_cvt_pk_bf16_f32 v103, v94, v95
	v_cvt_pk_bf16_f32 v104, v88, v89
	v_cvt_pk_bf16_f32 v105, v90, v91
	global_store_dwordx4 v[106:107], v[102:105], off sc1

;     __device__ __forceinline__ static u32x4 pack8(const f32x4 a, const f32x4 b) { u32x4 w; w.x = cvt_pk_bf16(a[0], a[1]); w.y = cvt_pk_bf16(a[2], a[3]); w.z = cvt_pk_bf16(b[0], b[1]); w.w = cvt_pk_bf16(b[2], b[3]); return w; }
;     __device__ __forceinline__ void operator()(const f32x4 (&acc)[2][2][4][2], const Unit& u, int wr, int wc, int fr, int fq) const {
;     ...
;                     else if (pn < 20) { const float sc = 0.125f * 1.4426950408889634f; *(u32x4*)(QN + row * 1024 + (pn - 16) * 256 + c256) = pack8(v0 * sc, v1 * sc); }
.LBB0_280:
	s_andn2_b64 vcc, exec, s[14:15]
	s_cbranch_vccnz .LBB0_282
	v_pk_mul_f32 v[104:105], v[94:95], s[46:47] op_sel_hi:[1,0]
	v_pk_mul_f32 v[102:103], v[92:93], s[46:47] op_sel_hi:[1,0]
	v_pk_mul_f32 v[106:107], v[90:91], s[46:47] op_sel_hi:[1,0]
	v_pk_mul_f32 v[108:109], v[88:89], s[46:47] op_sel_hi:[1,0]
	v_cvt_pk_bf16_f32 v102, v102, v103
	v_cvt_pk_bf16_f32 v103, v104, v105
	s_nop 0
	v_cvt_pk_bf16_f32 v104, v108, v109
	v_cvt_pk_bf16_f32 v105, v106, v107
	v_lshl_add_u64 v[106:107], s[36:37], 0, v[96:97]
	v_lshl_add_u64 v[106:107], s[24:25], 1, v[106:107]
	v_lshl_add_u64 v[106:107], v[136:137], 1, v[106:107]
	v_add_co_u32_e32 v106, vcc, 0xffffe000, v106
	s_nop 1
	v_addc_co_u32_e32 v107, vcc, -1, v107, vcc
	global_store_dwordx4 v[106:107], v[102:105], off sc1

;     __device__ __forceinline__ static u32x4 pack8(const f32x4 a, const f32x4 b) { u32x4 w; w.x = cvt_pk_bf16(a[0], a[1]); w.y = cvt_pk_bf16(a[2], a[3]); w.z = cvt_pk_bf16(b[0], b[1]); w.w = cvt_pk_bf16(b[2], b[3]); return w; }
;     __device__ __forceinline__ static f32x4 silu4(const f32x4 v) { f32x4 o; for (int i = 0; i < 4; ++i) o[i] = v[i] * __builtin_amdgcn_rcpf(1.f + __expf(-v[i])); return o; }
;     __device__ __forceinline__ void operator()(const f32x4 (&acc)[2][2][4][2], const Unit& u, int wr, int wc, int fr, int fq) const {
;     ...
;                     else if (pn < 16) { *(u32x4*)(GH + row * 1024 + (pn - 12) * 256 + c256) = pack8(silu4(v0), silu4(v1)); }
.LBB0_283:
	s_andn2_b64 vcc, exec, s[14:15]
	s_cbranch_vccnz .LBB0_285
	v_mul_f32_e32 v102, 0xbfb8aa3b, v92
	v_mul_f32_e32 v103, 0xbfb8aa3b, v93
	v_mul_f32_e32 v104, 0xbfb8aa3b, v94
	v_mul_f32_e32 v106, 0xbfb8aa3b, v88
	v_mul_f32_e32 v107, 0xbfb8aa3b, v89
	v_exp_f32_e32 v102, v102
	v_exp_f32_e32 v103, v103
	v_exp_f32_e32 v104, v104
	v_mul_f32_e32 v105, 0xbfb8aa3b, v95
	v_exp_f32_e32 v106, v106
	v_exp_f32_e32 v107, v107
	v_exp_f32_e32 v105, v105
	v_add_f32_e32 v102, 1.0, v102
	v_add_f32_e32 v103, 1.0, v103
	v_add_f32_e32 v104, 1.0, v104
	v_add_f32_e32 v106, 1.0, v106
	v_add_f32_e32 v107, 1.0, v107
	v_rcp_f32_e32 v102, v102
	v_rcp_f32_e32 v103, v103
	v_rcp_f32_e32 v104, v104
	v_add_f32_e32 v105, 1.0, v105
	v_rcp_f32_e32 v106, v106
	v_mul_f32_e32 v108, 0xbfb8aa3b, v90
	v_mul_f32_e32 v109, 0xbfb8aa3b, v91
	v_rcp_f32_e32 v107, v107
	v_rcp_f32_e32 v105, v105
	v_exp_f32_e32 v108, v108
	v_exp_f32_e32 v109, v109
	v_mul_f32_e32 v102, v92, v102
	v_mul_f32_e32 v103, v93, v103
	v_mul_f32_e32 v104, v94, v104
	v_mul_f32_e32 v106, v88, v106
	v_mul_f32_e32 v107, v89, v107
	v_mul_f32_e32 v105, v95, v105
	v_add_f32_e32 v108, 1.0, v108
	v_add_f32_e32 v109, 1.0, v109
	v_cvt_pk_bf16_f32 v102, v102, v103
	v_cvt_pk_bf16_f32 v103, v104, v105
	v_cvt_pk_bf16_f32 v104, v106, v107
	v_lshl_add_u64 v[106:107], s[34:35], 0, v[96:97]
	v_rcp_f32_e32 v108, v108
	v_rcp_f32_e32 v109, v109
	v_lshl_add_u64 v[106:107], s[24:25], 1, v[106:107]
	v_lshl_add_u64 v[106:107], v[136:137], 1, v[106:107]
	v_add_co_u32_e32 v106, vcc, 0xfffff000, v106
	v_mul_f32_e32 v108, v90, v108
	s_nop 0
	v_addc_co_u32_e32 v107, vcc, -1, v107, vcc
	v_mul_f32_e32 v109, v91, v109
	v_cvt_pk_bf16_f32 v105, v108, v109
	global_store_dwordx4 v[106:107], v[102:105], off offset:-2048 sc1

;     __device__ __forceinline__ static u32x4 pack8(const f32x4 a, const f32x4 b) { u32x4 w; w.x = cvt_pk_bf16(a[0], a[1]); w.y = cvt_pk_bf16(a[2], a[3]); w.z = cvt_pk_bf16(b[0], b[1]); w.w = cvt_pk_bf16(b[2], b[3]); return w; }
;     __device__ __forceinline__ void operator()(const f32x4 (&acc)[2][2][4][2], const Unit& u, int wr, int wc, int fr, int fq) const {
;     ...
;                     else if (pn < 12) { *(u32x4*)(VH + row * 1024 + (pn - 8) * 256 + c256) = pack8(v0, v1); }
.LBB0_286:
	s_andn2_b64 vcc, exec, s[14:15]
	s_cbranch_vccnz .LBB0_288
	v_lshl_add_u64 v[106:107], s[30:31], 0, v[96:97]
	v_lshl_add_u64 v[106:107], s[24:25], 1, v[106:107]
	v_lshl_add_u64 v[106:107], v[136:137], 1, v[106:107]
	v_cvt_pk_bf16_f32 v102, v92, v93
	v_cvt_pk_bf16_f32 v103, v94, v95
	v_cvt_pk_bf16_f32 v104, v88, v89
	v_cvt_pk_bf16_f32 v105, v90, v91
	global_store_dwordx4 v[106:107], v[102:105], off offset:-4096 sc1

;     __device__ __forceinline__ static u32x4 pack8(const f32x4 a, const f32x4 b) { u32x4 w; w.x = cvt_pk_bf16(a[0], a[1]); w.y = cvt_pk_bf16(a[2], a[3]); w.z = cvt_pk_bf16(b[0], b[1]); w.w = cvt_pk_bf16(b[2], b[3]); return w; }
;     __device__ __forceinline__ void operator()(const f32x4 (&acc)[2][2][4][2], const Unit& u, int wr, int wc, int fr, int fq) const {
;     ...
;                     else if (pn < 8) { const int col = (pn - 4) * 256 + c256; const f32x4 l0 = *(const f32x4*)(LB + col), l1 = *(const f32x4*)(LB + col + 4); f32x4 o0, o1;
;                         for (int i = 0; i < 4; ++i) { o0[i] = __logf(l0[i] + (1.f - l0[i]) * __builtin_amdgcn_rcpf(1.f + __expf(-v0[i]))); o1[i] = __logf(l1[i] + (1.f - l1[i]) * __builtin_amdgcn_rcpf(1.f + __expf(-v1[i]))); }
;                         *(u32x4*)(LOGF + row * 1024 + col) = pack8(o0, o1); }
.LBB0_289:
	s_andn2_b64 vcc, exec, s[14:15]
	s_cbranch_vccnz .LBB0_291
	v_add_u32_e32 v102, s33, v136
	v_ashrrev_i32_e32 v103, 31, v102
	v_lshl_add_u64 v[106:107], v[102:103], 2, s[40:41]
	global_load_dwordx4 v[102:105], v[106:107], off
	s_nop 0
	global_load_dwordx4 v[106:109], v[106:107], off offset:16
	v_mul_f32_e32 v110, 0xbfb8aa3b, v92
	v_mul_f32_e32 v111, 0xbfb8aa3b, v88
	v_exp_f32_e32 v110, v110
	v_mul_f32_e32 v112, 0xbfb8aa3b, v93
	v_exp_f32_e32 v111, v111
	v_mul_f32_e32 v113, 0xbfb8aa3b, v89
	v_exp_f32_e32 v112, v112
	v_exp_f32_e32 v113, v113
	v_mul_f32_e32 v114, 0xbfb8aa3b, v94
	v_add_f32_e32 v110, 1.0, v110
	v_exp_f32_e32 v114, v114
	v_add_f32_e32 v111, 1.0, v111
	v_rcp_f32_e32 v110, v110
	v_add_f32_e32 v112, 1.0, v112
	v_rcp_f32_e32 v111, v111
	v_add_f32_e32 v113, 1.0, v113
	v_rcp_f32_e32 v112, v112
	v_mul_f32_e32 v115, 0xbfb8aa3b, v90
	v_rcp_f32_e32 v113, v113
	v_exp_f32_e32 v115, v115
	v_add_f32_e32 v114, 1.0, v114
	v_rcp_f32_e32 v114, v114
	v_add_f32_e32 v115, 1.0, v115
	v_rcp_f32_e32 v115, v115
	s_waitcnt vmcnt(0)
	v_sub_f32_e32 v116, 1.0, v102
	v_sub_f32_e32 v117, 1.0, v106
	v_fma_f32 v102, v110, v116, v102
	v_sub_f32_e32 v118, 1.0, v103
	v_fma_f32 v106, v111, v117, v106
	v_cmp_gt_f32_e32 vcc, s82, v102
	v_sub_f32_e32 v119, 1.0, v107
	v_fma_f32 v103, v112, v118, v103
	v_cndmask_b32_e64 v110, 0, 32, vcc
	v_cmp_gt_f32_e64 s[14:15], s82, v106
	v_fma_f32 v107, v113, v119, v107
	v_cmp_gt_f32_e64 s[16:17], s82, v103
	v_cndmask_b32_e64 v111, 0, 32, s[14:15]
	v_ldexp_f32 v102, v102, v110
	v_sub_f32_e32 v120, 1.0, v104
	v_cndmask_b32_e64 v112, 0, 32, s[16:17]
	v_cmp_gt_f32_e64 s[18:19], s82, v107
	v_ldexp_f32 v106, v106, v111
	v_log_f32_e32 v102, v102
	v_fma_f32 v104, v114, v120, v104
	v_cndmask_b32_e64 v113, 0, 32, s[18:19]
	v_ldexp_f32 v103, v103, v112
	v_log_f32_e32 v106, v106
	v_cmp_gt_f32_e64 s[20:21], s82, v104
	v_ldexp_f32 v107, v107, v113
	v_log_f32_e32 v103, v103
	v_cndmask_b32_e64 v114, 0, 32, s[20:21]
	v_log_f32_e32 v107, v107
	v_sub_f32_e32 v121, 1.0, v108
	v_ldexp_f32 v104, v104, v114
	v_mul_f32_e32 v114, 0x3f317217, v102
	v_fma_f32 v108, v115, v121, v108
	v_mul_f32_e32 v115, 0x3f317217, v106
	v_fma_f32 v114, v102, s83, -v114
	v_mul_f32_e32 v116, 0x3f317217, v103
	v_fma_f32 v115, v106, s83, -v115
	v_fmac_f32_e32 v114, 0x3377d1cf, v102
	v_cndmask_b32_e32 v110, 0, v167, vcc
	v_mul_f32_e32 v117, 0x3f317217, v107
	v_fma_f32 v116, v103, s83, -v116
	v_fmac_f32_e32 v115, 0x3377d1cf, v106
	v_fmac_f32_e32 v114, 0x3f317217, v102
	v_cmp_lt_f32_e64 vcc, |v102|, s84
	v_fma_f32 v117, v107, s83, -v117
	v_fmac_f32_e32 v116, 0x3377d1cf, v103
	v_fmac_f32_e32 v115, 0x3f317217, v106
	v_cndmask_b32_e32 v102, v102, v114, vcc
	v_cmp_lt_f32_e64 vcc, |v106|, s84
	v_log_f32_e32 v104, v104
	v_fmac_f32_e32 v117, 0x3377d1cf, v107
	v_fmac_f32_e32 v116, 0x3f317217, v103
	v_cndmask_b32_e32 v106, v106, v115, vcc
	v_cmp_lt_f32_e64 vcc, |v103|, s84
	v_cndmask_b32_e64 v111, 0, v167, s[14:15]
	v_fmac_f32_e32 v117, 0x3f317217, v107
	v_cndmask_b32_e32 v103, v103, v116, vcc
	v_cmp_lt_f32_e64 vcc, |v107|, s84
	v_sub_f32_e32 v106, v106, v111
	v_mul_f32_e32 v111, 0xbfb8aa3b, v95
	v_cndmask_b32_e32 v107, v107, v117, vcc
	v_cmp_gt_f32_e32 vcc, s82, v108
	v_sub_f32_e32 v102, v102, v110
	v_exp_f32_e32 v111, v111
	v_cndmask_b32_e64 v110, 0, 32, vcc
	v_mul_f32_e32 v118, 0x3f317217, v104
	v_ldexp_f32 v108, v108, v110
	v_fma_f32 v118, v104, s83, -v118
	v_log_f32_e32 v108, v108
	v_fmac_f32_e32 v118, 0x3377d1cf, v104
	v_fmac_f32_e32 v118, 0x3f317217, v104
	v_cmp_lt_f32_e64 s[14:15], |v104|, s84
	v_add_f32_e32 v111, 1.0, v111
	v_cndmask_b32_e64 v110, 0, v167, s[20:21]
	v_cndmask_b32_e64 v104, v104, v118, s[14:15]
	v_rcp_f32_e32 v111, v111
	v_sub_f32_e32 v104, v104, v110
	v_mul_f32_e32 v110, 0x3f317217, v108
	v_cndmask_b32_e64 v112, 0, v167, s[16:17]
	v_fma_f32 v110, v108, s83, -v110
	v_sub_f32_e32 v103, v103, v112
	v_fmac_f32_e32 v110, 0x3377d1cf, v108
	v_sub_f32_e32 v112, 1.0, v105
	v_fmac_f32_e32 v110, 0x3f317217, v108
	v_cmp_lt_f32_e64 s[14:15], |v108|, s84
	v_fmac_f32_e32 v105, v111, v112
	v_sub_f32_e32 v112, 1.0, v109
	v_cndmask_b32_e64 v108, v108, v110, s[14:15]
	v_cndmask_b32_e32 v110, 0, v167, vcc
	v_cmp_gt_f32_e32 vcc, s82, v105
	v_sub_f32_e32 v108, v108, v110
	v_cndmask_b32_e64 v113, 0, v167, s[18:19]
	v_cndmask_b32_e64 v111, 0, 32, vcc
	v_ldexp_f32 v105, v105, v111
	v_mul_f32_e32 v111, 0xbfb8aa3b, v91
	v_exp_f32_e32 v111, v111
	v_log_f32_e32 v105, v105
	v_sub_f32_e32 v107, v107, v113
	v_cvt_pk_bf16_f32 v102, v102, v103
	v_add_f32_e32 v111, 1.0, v111
	v_rcp_f32_e32 v111, v111
	v_mul_f32_e32 v110, 0x3f317217, v105
	v_fma_f32 v110, v105, s83, -v110
	v_fmac_f32_e32 v110, 0x3377d1cf, v105
	v_fmac_f32_e32 v109, v111, v112
	v_cmp_gt_f32_e64 s[14:15], s82, v109
	v_fmac_f32_e32 v110, 0x3f317217, v105
	v_cmp_lt_f32_e64 s[16:17], |v105|, s84
	v_cndmask_b32_e64 v111, 0, 32, s[14:15]
	v_ldexp_f32 v109, v109, v111
	v_log_f32_e32 v109, v109
	v_cndmask_b32_e64 v105, v105, v110, s[16:17]
	v_cndmask_b32_e32 v110, 0, v167, vcc
	v_sub_f32_e32 v105, v105, v110
	v_mul_f32_e32 v110, 0x3f317217, v109
	v_fma_f32 v110, v109, s83, -v110
	v_fmac_f32_e32 v110, 0x3377d1cf, v109
	v_fmac_f32_e32 v110, 0x3f317217, v109
	v_cmp_lt_f32_e64 vcc, |v109|, s84
	v_cvt_pk_bf16_f32 v103, v104, v105
	v_cvt_pk_bf16_f32 v104, v106, v107
	v_lshl_add_u64 v[106:107], s[38:39], 0, v[96:97]
	s_nop 0
	v_cndmask_b32_e32 v109, v109, v110, vcc
	v_cndmask_b32_e64 v110, 0, v167, s[14:15]
	v_sub_f32_e32 v109, v109, v110
	v_cvt_pk_bf16_f32 v105, v108, v109
	v_lshl_add_u64 v[108:109], s[0:1], 0, v[136:137]
	v_lshl_add_u64 v[106:107], v[108:109], 1, v[106:107]
	global_store_dwordx4 v[106:107], v[102:105], off offset:-2048 sc1

;     __device__ __forceinline__ static u32x4 pack8(const f32x4 a, const f32x4 b) { u32x4 w; w.x = cvt_pk_bf16(a[0], a[1]); w.y = cvt_pk_bf16(a[2], a[3]); w.z = cvt_pk_bf16(b[0], b[1]); w.w = cvt_pk_bf16(b[2], b[3]); return w; }
;     __device__ __forceinline__ static f32x4 silu4(const f32x4 v) { f32x4 o; for (int i = 0; i < 4; ++i) o[i] = v[i] * __builtin_amdgcn_rcpf(1.f + __expf(-v[i])); return o; }
;     __device__ __forceinline__ void operator()(const f32x4 (&acc)[2][2][4][2], const Unit& u, int wr, int wc, int fr, int fq) const {
;     ...
;                 for (int bj = 0; bj < 2; ++bj) { const int c256 = bj * HALF + cl; f32x4 v0 = acc[ai][bj][m][0], v1 = acc[ai][bj][m][1];
;                     if (pn < 4) { *(u32x4*)(QH + row * 1024 + pn * 256 + c256) = pack8(silu4(v0), silu4(v1)); }
;                     else if (pn < 8) { const int col = (pn - 4) * 256 + c256; const f32x4 l0 = *(const f32x4*)(LB + col), l1 = *(const f32x4*)(LB + col + 4); f32x4 o0, o1;
;                         for (int i = 0; i < 4; ++i) { o0[i] = __logf(l0[i] + (1.f - l0[i]) * __builtin_amdgcn_rcpf(1.f + __expf(-v0[i]))); o1[i] = __logf(l1[i] + (1.f - l1[i]) * __builtin_amdgcn_rcpf(1.f + __expf(-v1[i]))); }
;                         *(u32x4*)(LOGF + row * 1024 + col) = pack8(o0, o1); }
;                     else if (pn < 12) { *(u32x4*)(VH + row * 1024 + (pn - 8) * 256 + c256) = pack8(v0, v1); }
;                     else if (pn < 16) { *(u32x4*)(GH + row * 1024 + (pn - 12) * 256 + c256) = pack8(silu4(v0), silu4(v1)); }
;                     else if (pn < 20) { const float sc = 0.125f * 1.4426950408889634f; *(u32x4*)(QN + row * 1024 + (pn - 16) * 256 + c256) = pack8(v0 * sc, v1 * sc); }
;                     else if (pn < 26) { *(u32x4*)(KV6 + (size_t)(pn - 20) * ((size_t)16384 * 256) + row * 256 + c256) = pack8(v0, v1); }
;                     else if (c256 < 64) { f32x4 o0, o1; for (int i = 0; i < 4; ++i) { o0[i] = __builtin_amdgcn_rcpf(1.f + __expf(-v0[i])); o1[i] = __builtin_amdgcn_rcpf(1.f + __expf(-v1[i])); }
;                         *(f32x4*)(GATE + row * 64 + c256) = o0; *(f32x4*)(GATE + row * 64 + c256 + 4) = o1; } } }
.LBB0_292:
	v_mul_f32_e32 v104, 0xbfb8aa3b, v92
	v_mul_f32_e32 v105, 0xbfb8aa3b, v93
	v_mul_f32_e32 v106, 0xbfb8aa3b, v94
	v_exp_f32_e32 v104, v104
	v_exp_f32_e32 v105, v105
	v_exp_f32_e32 v106, v106
	v_mul_f32_e32 v107, 0xbfb8aa3b, v95
	v_add_f32_e32 v104, 1.0, v104
	v_add_f32_e32 v105, 1.0, v105
	v_add_f32_e32 v106, 1.0, v106
	v_rcp_f32_e32 v104, v104
	v_rcp_f32_e32 v105, v105
	v_rcp_f32_e32 v106, v106
	v_exp_f32_e32 v107, v107
	v_mul_f32_e32 v92, v92, v104
	v_mul_f32_e32 v93, v93, v105
	v_mul_f32_e32 v94, v94, v106
	v_add_f32_e32 v104, 1.0, v107
	v_mul_f32_e32 v105, 0xbfb8aa3b, v88
	v_mul_f32_e32 v106, 0xbfb8aa3b, v89
	v_rcp_f32_e32 v104, v104
	v_exp_f32_e32 v105, v105
	v_exp_f32_e32 v106, v106
	v_mul_f32_e32 v107, 0xbfb8aa3b, v91
	v_mul_f32_e32 v95, v95, v104
	v_add_f32_e32 v104, 1.0, v105
	v_add_f32_e32 v105, 1.0, v106
	v_mul_f32_e32 v106, 0xbfb8aa3b, v90
	v_exp_f32_e32 v107, v107
	v_exp_f32_e32 v106, v106
	v_rcp_f32_e32 v104, v104
	v_rcp_f32_e32 v105, v105
	v_add_f32_e32 v107, 1.0, v107
	v_add_f32_e32 v106, 1.0, v106
	v_rcp_f32_e32 v107, v107
	v_rcp_f32_e32 v106, v106
	v_mul_f32_e32 v104, v88, v104
	v_cvt_pk_bf16_f32 v88, v92, v93
	v_mul_f32_e32 v91, v91, v107
	v_lshl_add_u64 v[92:93], v[136:137], 1, v[102:103]
	v_mul_f32_e32 v105, v89, v105
	v_mul_f32_e32 v106, v90, v106
	v_cvt_pk_bf16_f32 v89, v94, v95
	v_cvt_pk_bf16_f32 v90, v104, v105
	v_cvt_pk_bf16_f32 v91, v106, v91
	global_store_dwordx4 v[92:93], v[88:91], off sc1
	s_and_b64 vcc, exec, s[12:13]
	s_mov_b64 s[14:15], -1
	s_cbranch_vccnz .LBB0_195
.LBB0_293:
	s_and_b64 vcc, exec, s[10:11]
	s_cbranch_vccnz .LBB0_313
	s_andn2_b64 vcc, exec, s[62:63]
	s_cbranch_vccnz .LBB0_310
	s_andn2_b64 vcc, exec, s[60:61]
	s_cbranch_vccnz .LBB0_307
	s_andn2_b64 vcc, exec, s[58:59]
	s_cbranch_vccnz .LBB0_304
	s_andn2_b64 vcc, exec, s[56:57]
	s_cbranch_vccnz .LBB0_301
	s_and_saveexec_b64 s[14:15], s[6:7]
	s_cbranch_execz .LBB0_300
	v_mul_f32_e32 v89, 0xbfb8aa3b, v80
	v_exp_f32_e32 v89, v89
	v_mul_f32_e32 v90, 0xbfb8aa3b, v85
	v_mul_f32_e32 v91, 0xbfb8aa3b, v81
	v_exp_f32_e32 v90, v90
	v_exp_f32_e32 v91, v91
	v_add_f32_e32 v89, 1.0, v89
	v_rcp_f32_e32 v92, v89
	v_add_f32_e32 v89, 1.0, v90
	v_add_f32_e32 v90, 1.0, v91
	v_mul_f32_e32 v91, 0xbfb8aa3b, v86
	v_mul_f32_e32 v93, 0xbfb8aa3b, v82
	v_exp_f32_e32 v91, v91
	v_exp_f32_e32 v94, v93
	v_mul_f32_e32 v88, 0xbfb8aa3b, v84
	v_rcp_f32_e32 v93, v90
	v_add_f32_e32 v90, 1.0, v91
	v_add_f32_e32 v91, 1.0, v94
	v_mul_f32_e32 v94, 0xbfb8aa3b, v87
	v_exp_f32_e32 v88, v88
	v_exp_f32_e32 v95, v94
	v_mul_f32_e32 v94, 0xbfb8aa3b, v83
	v_exp_f32_e32 v104, v94
	v_add_f32_e32 v88, 1.0, v88
	v_rcp_f32_e32 v94, v91
	v_add_f32_e32 v91, 1.0, v95
	v_rcp_f32_e32 v88, v88
	v_rcp_f32_e32 v89, v89
	v_rcp_f32_e32 v90, v90
	v_rcp_f32_e32 v91, v91
	v_add_f32_e32 v95, 1.0, v104
	v_rcp_f32_e32 v95, v95
	v_lshl_add_u64 v[100:101], v[100:101], 2, v[142:143]
	global_store_dwordx4 v[100:101], v[88:91], off sc1
	global_store_dwordx4 v[100:101], v[92:95], off offset:16 sc1

;     __device__ __forceinline__ static u32x4 pack8(const f32x4 a, const f32x4 b) { u32x4 w; w.x = cvt_pk_bf16(a[0], a[1]); w.y = cvt_pk_bf16(a[2], a[3]); w.z = cvt_pk_bf16(b[0], b[1]); w.w = cvt_pk_bf16(b[2], b[3]); return w; }
;     __device__ __forceinline__ void operator()(const f32x4 (&acc)[2][2][4][2], const Unit& u, int wr, int wc, int fr, int fq) const {
;     ...
;                     else if (pn < 26) { *(u32x4*)(KV6 + (size_t)(pn - 20) * ((size_t)16384 * 256) + row * 256 + c256) = pack8(v0, v1); }
.LBB0_301:
	s_andn2_b64 vcc, exec, s[14:15]
	s_cbranch_vccnz .LBB0_303
	s_add_u32 s14, s73, s2
	s_addc_u32 s15, s74, s3
	v_lshl_add_u64 v[92:93], s[14:15], 0, v[98:99]
	v_lshl_add_u64 v[92:93], v[136:137], 1, v[92:93]
	v_cvt_pk_bf16_f32 v88, v84, v85
	v_cvt_pk_bf16_f32 v89, v86, v87
	v_cvt_pk_bf16_f32 v90, v80, v81
	v_cvt_pk_bf16_f32 v91, v82, v83
	global_store_dwordx4 v[92:93], v[88:91], off offset:256 sc1

;     __device__ __forceinline__ static u32x4 pack8(const f32x4 a, const f32x4 b) { u32x4 w; w.x = cvt_pk_bf16(a[0], a[1]); w.y = cvt_pk_bf16(a[2], a[3]); w.z = cvt_pk_bf16(b[0], b[1]); w.w = cvt_pk_bf16(b[2], b[3]); return w; }
;     __device__ __forceinline__ void operator()(const f32x4 (&acc)[2][2][4][2], const Unit& u, int wr, int wc, int fr, int fq) const {
;     ...
;                     else if (pn < 20) { const float sc = 0.125f * 1.4426950408889634f; *(u32x4*)(QN + row * 1024 + (pn - 16) * 256 + c256) = pack8(v0 * sc, v1 * sc); }
.LBB0_304:
	s_andn2_b64 vcc, exec, s[14:15]
	s_cbranch_vccnz .LBB0_306
	v_pk_mul_f32 v[90:91], v[86:87], s[46:47] op_sel_hi:[1,0]
	v_pk_mul_f32 v[88:89], v[84:85], s[46:47] op_sel_hi:[1,0]
	v_pk_mul_f32 v[92:93], v[82:83], s[46:47] op_sel_hi:[1,0]
	v_pk_mul_f32 v[94:95], v[80:81], s[46:47] op_sel_hi:[1,0]
	v_cvt_pk_bf16_f32 v88, v88, v89
	v_cvt_pk_bf16_f32 v89, v90, v91
	s_nop 0
	v_cvt_pk_bf16_f32 v90, v94, v95
	v_cvt_pk_bf16_f32 v91, v92, v93
	v_lshl_add_u64 v[92:93], s[36:37], 0, v[96:97]
	v_lshl_add_u64 v[92:93], s[24:25], 1, v[92:93]
	v_lshl_add_u64 v[92:93], v[138:139], 1, v[92:93]
	v_add_co_u32_e32 v92, vcc, 0xffffe000, v92
	s_nop 1
	v_addc_co_u32_e32 v93, vcc, -1, v93, vcc
	global_store_dwordx4 v[92:93], v[88:91], off sc1

;     __device__ __forceinline__ static u32x4 pack8(const f32x4 a, const f32x4 b) { u32x4 w; w.x = cvt_pk_bf16(a[0], a[1]); w.y = cvt_pk_bf16(a[2], a[3]); w.z = cvt_pk_bf16(b[0], b[1]); w.w = cvt_pk_bf16(b[2], b[3]); return w; }
;     __device__ __forceinline__ static f32x4 silu4(const f32x4 v) { f32x4 o; for (int i = 0; i < 4; ++i) o[i] = v[i] * __builtin_amdgcn_rcpf(1.f + __expf(-v[i])); return o; }
;     __device__ __forceinline__ void operator()(const f32x4 (&acc)[2][2][4][2], const Unit& u, int wr, int wc, int fr, int fq) const {
;     ...
;                     else if (pn < 16) { *(u32x4*)(GH + row * 1024 + (pn - 12) * 256 + c256) = pack8(silu4(v0), silu4(v1)); }
.LBB0_307:
	s_andn2_b64 vcc, exec, s[14:15]
	s_cbranch_vccnz .LBB0_309
	v_mul_f32_e32 v88, 0xbfb8aa3b, v84
	v_mul_f32_e32 v89, 0xbfb8aa3b, v85
	v_mul_f32_e32 v90, 0xbfb8aa3b, v86
	v_mul_f32_e32 v92, 0xbfb8aa3b, v80
	v_mul_f32_e32 v93, 0xbfb8aa3b, v81
	v_exp_f32_e32 v88, v88
	v_exp_f32_e32 v89, v89
	v_exp_f32_e32 v90, v90
	v_mul_f32_e32 v91, 0xbfb8aa3b, v87
	v_exp_f32_e32 v92, v92
	v_exp_f32_e32 v93, v93
	v_exp_f32_e32 v91, v91
	v_add_f32_e32 v88, 1.0, v88
	v_add_f32_e32 v89, 1.0, v89
	v_add_f32_e32 v90, 1.0, v90
	v_add_f32_e32 v92, 1.0, v92
	v_add_f32_e32 v93, 1.0, v93
	v_rcp_f32_e32 v88, v88
	v_rcp_f32_e32 v89, v89
	v_rcp_f32_e32 v90, v90
	v_add_f32_e32 v91, 1.0, v91
	v_rcp_f32_e32 v92, v92
	v_mul_f32_e32 v94, 0xbfb8aa3b, v82
	v_mul_f32_e32 v95, 0xbfb8aa3b, v83
	v_rcp_f32_e32 v93, v93
	v_rcp_f32_e32 v91, v91
	v_exp_f32_e32 v94, v94
	v_exp_f32_e32 v95, v95
	v_mul_f32_e32 v88, v84, v88
	v_mul_f32_e32 v89, v85, v89
	v_mul_f32_e32 v90, v86, v90
	v_mul_f32_e32 v92, v80, v92
	v_mul_f32_e32 v93, v81, v93
	v_mul_f32_e32 v91, v87, v91
	v_add_f32_e32 v94, 1.0, v94
	v_add_f32_e32 v95, 1.0, v95
	v_cvt_pk_bf16_f32 v88, v88, v89
	v_cvt_pk_bf16_f32 v89, v90, v91
	v_cvt_pk_bf16_f32 v90, v92, v93
	v_lshl_add_u64 v[92:93], s[34:35], 0, v[96:97]
	v_rcp_f32_e32 v94, v94
	v_rcp_f32_e32 v95, v95
	v_lshl_add_u64 v[92:93], s[24:25], 1, v[92:93]
	v_lshl_add_u64 v[92:93], v[138:139], 1, v[92:93]
	v_add_co_u32_e32 v92, vcc, 0xfffff000, v92
	v_mul_f32_e32 v94, v82, v94
	s_nop 0
	v_addc_co_u32_e32 v93, vcc, -1, v93, vcc
	v_mul_f32_e32 v95, v83, v95
	v_cvt_pk_bf16_f32 v91, v94, v95
	global_store_dwordx4 v[92:93], v[88:91], off offset:-2048 sc1

;     __device__ __forceinline__ static u32x4 pack8(const f32x4 a, const f32x4 b) { u32x4 w; w.x = cvt_pk_bf16(a[0], a[1]); w.y = cvt_pk_bf16(a[2], a[3]); w.z = cvt_pk_bf16(b[0], b[1]); w.w = cvt_pk_bf16(b[2], b[3]); return w; }
;     __device__ __forceinline__ void operator()(const f32x4 (&acc)[2][2][4][2], const Unit& u, int wr, int wc, int fr, int fq) const {
;     ...
;                     else if (pn < 12) { *(u32x4*)(VH + row * 1024 + (pn - 8) * 256 + c256) = pack8(v0, v1); }
.LBB0_310:
	s_andn2_b64 vcc, exec, s[14:15]
	s_cbranch_vccnz .LBB0_312
	v_lshl_add_u64 v[92:93], s[30:31], 0, v[96:97]
	v_lshl_add_u64 v[92:93], s[24:25], 1, v[92:93]
	v_lshl_add_u64 v[92:93], v[136:137], 1, v[92:93]
	v_cvt_pk_bf16_f32 v88, v84, v85
	v_cvt_pk_bf16_f32 v89, v86, v87
	v_cvt_pk_bf16_f32 v90, v80, v81
	v_cvt_pk_bf16_f32 v91, v82, v83
	global_store_dwordx4 v[92:93], v[88:91], off offset:-3840 sc1

;     __device__ __forceinline__ static u32x4 pack8(const f32x4 a, const f32x4 b) { u32x4 w; w.x = cvt_pk_bf16(a[0], a[1]); w.y = cvt_pk_bf16(a[2], a[3]); w.z = cvt_pk_bf16(b[0], b[1]); w.w = cvt_pk_bf16(b[2], b[3]); return w; }
;     __device__ __forceinline__ void operator()(const f32x4 (&acc)[2][2][4][2], const Unit& u, int wr, int wc, int fr, int fq) const {
;     ...
;                     else if (pn < 8) { const int col = (pn - 4) * 256 + c256; const f32x4 l0 = *(const f32x4*)(LB + col), l1 = *(const f32x4*)(LB + col + 4); f32x4 o0, o1;
;                         for (int i = 0; i < 4; ++i) { o0[i] = __logf(l0[i] + (1.f - l0[i]) * __builtin_amdgcn_rcpf(1.f + __expf(-v0[i]))); o1[i] = __logf(l1[i] + (1.f - l1[i]) * __builtin_amdgcn_rcpf(1.f + __expf(-v1[i]))); }
;                         *(u32x4*)(LOGF + row * 1024 + col) = pack8(o0, o1); }
.LBB0_313:
	s_andn2_b64 vcc, exec, s[14:15]
	s_cbranch_vccnz .LBB0_315
	v_add_u32_e32 v88, s33, v138
	v_ashrrev_i32_e32 v89, 31, v88
	v_lshl_add_u64 v[92:93], v[88:89], 2, s[40:41]
	global_load_dwordx4 v[88:91], v[92:93], off
	s_nop 0
	global_load_dwordx4 v[92:95], v[92:93], off offset:16
	v_mul_f32_e32 v98, 0xbfb8aa3b, v84
	v_mul_f32_e32 v99, 0xbfb8aa3b, v80
	v_exp_f32_e32 v98, v98
	v_mul_f32_e32 v100, 0xbfb8aa3b, v85
	v_exp_f32_e32 v99, v99
	v_mul_f32_e32 v101, 0xbfb8aa3b, v81
	v_exp_f32_e32 v100, v100
	v_exp_f32_e32 v101, v101
	v_mul_f32_e32 v104, 0xbfb8aa3b, v86
	v_add_f32_e32 v98, 1.0, v98
	v_exp_f32_e32 v104, v104
	v_add_f32_e32 v99, 1.0, v99
	v_rcp_f32_e32 v98, v98
	v_add_f32_e32 v100, 1.0, v100
	v_rcp_f32_e32 v99, v99
	v_add_f32_e32 v101, 1.0, v101
	v_rcp_f32_e32 v100, v100
	v_mul_f32_e32 v105, 0xbfb8aa3b, v82
	v_rcp_f32_e32 v101, v101
	v_exp_f32_e32 v105, v105
	v_add_f32_e32 v104, 1.0, v104
	v_rcp_f32_e32 v104, v104
	v_add_f32_e32 v105, 1.0, v105
	v_rcp_f32_e32 v105, v105
	s_waitcnt vmcnt(0)
	v_sub_f32_e32 v106, 1.0, v88
	v_sub_f32_e32 v107, 1.0, v92
	v_fma_f32 v88, v98, v106, v88
	v_sub_f32_e32 v108, 1.0, v89
	v_fma_f32 v92, v99, v107, v92
	v_cmp_gt_f32_e32 vcc, s82, v88
	v_sub_f32_e32 v109, 1.0, v93
	v_fma_f32 v89, v100, v108, v89
	v_cndmask_b32_e64 v98, 0, 32, vcc
	v_cmp_gt_f32_e64 s[14:15], s82, v92
	v_fma_f32 v93, v101, v109, v93
	v_cmp_gt_f32_e64 s[16:17], s82, v89
	v_cndmask_b32_e64 v99, 0, 32, s[14:15]
	v_ldexp_f32 v88, v88, v98
	v_sub_f32_e32 v110, 1.0, v90
	v_cndmask_b32_e64 v100, 0, 32, s[16:17]
	v_cmp_gt_f32_e64 s[18:19], s82, v93
	v_ldexp_f32 v92, v92, v99
	v_log_f32_e32 v88, v88
	v_fma_f32 v90, v104, v110, v90
	v_cndmask_b32_e64 v101, 0, 32, s[18:19]
	v_ldexp_f32 v89, v89, v100
	v_log_f32_e32 v92, v92
	v_cmp_gt_f32_e64 s[20:21], s82, v90
	v_ldexp_f32 v93, v93, v101
	v_log_f32_e32 v89, v89
	v_cndmask_b32_e64 v104, 0, 32, s[20:21]
	v_log_f32_e32 v93, v93
	v_sub_f32_e32 v111, 1.0, v94
	v_ldexp_f32 v90, v90, v104
	v_mul_f32_e32 v104, 0x3f317217, v88
	v_fma_f32 v94, v105, v111, v94
	v_mul_f32_e32 v105, 0x3f317217, v92
	v_fma_f32 v104, v88, s83, -v104
	v_mul_f32_e32 v106, 0x3f317217, v89
	v_fma_f32 v105, v92, s83, -v105
	v_fmac_f32_e32 v104, 0x3377d1cf, v88
	v_cndmask_b32_e32 v98, 0, v167, vcc
	v_mul_f32_e32 v107, 0x3f317217, v93
	v_fma_f32 v106, v89, s83, -v106
	v_fmac_f32_e32 v105, 0x3377d1cf, v92
	v_fmac_f32_e32 v104, 0x3f317217, v88
	v_cmp_lt_f32_e64 vcc, |v88|, s84
	v_fma_f32 v107, v93, s83, -v107
	v_fmac_f32_e32 v106, 0x3377d1cf, v89
	v_fmac_f32_e32 v105, 0x3f317217, v92
	v_cndmask_b32_e32 v88, v88, v104, vcc
	v_cmp_lt_f32_e64 vcc, |v92|, s84
	v_log_f32_e32 v90, v90
	v_fmac_f32_e32 v107, 0x3377d1cf, v93
	v_fmac_f32_e32 v106, 0x3f317217, v89
	v_cndmask_b32_e32 v92, v92, v105, vcc
	v_cmp_lt_f32_e64 vcc, |v89|, s84
	v_cndmask_b32_e64 v99, 0, v167, s[14:15]
	v_fmac_f32_e32 v107, 0x3f317217, v93
	v_cndmask_b32_e32 v89, v89, v106, vcc
	v_cmp_lt_f32_e64 vcc, |v93|, s84
	v_sub_f32_e32 v92, v92, v99
	v_mul_f32_e32 v99, 0xbfb8aa3b, v87
	v_cndmask_b32_e32 v93, v93, v107, vcc
	v_cmp_gt_f32_e32 vcc, s82, v94
	v_sub_f32_e32 v88, v88, v98
	v_exp_f32_e32 v99, v99
	v_cndmask_b32_e64 v98, 0, 32, vcc
	v_mul_f32_e32 v108, 0x3f317217, v90
	v_ldexp_f32 v94, v94, v98
	v_fma_f32 v108, v90, s83, -v108
	v_log_f32_e32 v94, v94
	v_fmac_f32_e32 v108, 0x3377d1cf, v90
	v_fmac_f32_e32 v108, 0x3f317217, v90
	v_cmp_lt_f32_e64 s[14:15], |v90|, s84
	v_add_f32_e32 v99, 1.0, v99
	v_cndmask_b32_e64 v98, 0, v167, s[20:21]
	v_cndmask_b32_e64 v90, v90, v108, s[14:15]
	v_rcp_f32_e32 v99, v99
	v_sub_f32_e32 v90, v90, v98
	v_mul_f32_e32 v98, 0x3f317217, v94
	v_cndmask_b32_e64 v100, 0, v167, s[16:17]
	v_fma_f32 v98, v94, s83, -v98
	v_sub_f32_e32 v89, v89, v100
	v_fmac_f32_e32 v98, 0x3377d1cf, v94
	v_sub_f32_e32 v100, 1.0, v91
	v_fmac_f32_e32 v98, 0x3f317217, v94
	v_cmp_lt_f32_e64 s[14:15], |v94|, s84
	v_fmac_f32_e32 v91, v99, v100
	v_sub_f32_e32 v100, 1.0, v95
	v_cndmask_b32_e64 v94, v94, v98, s[14:15]
	v_cndmask_b32_e32 v98, 0, v167, vcc
	v_cmp_gt_f32_e32 vcc, s82, v91
	v_sub_f32_e32 v94, v94, v98
	v_cndmask_b32_e64 v101, 0, v167, s[18:19]
	v_cndmask_b32_e64 v99, 0, 32, vcc
	v_ldexp_f32 v91, v91, v99
	v_mul_f32_e32 v99, 0xbfb8aa3b, v83
	v_exp_f32_e32 v99, v99
	v_log_f32_e32 v91, v91
	v_sub_f32_e32 v93, v93, v101
	v_cvt_pk_bf16_f32 v88, v88, v89
	v_add_f32_e32 v99, 1.0, v99
	v_rcp_f32_e32 v99, v99
	v_mul_f32_e32 v98, 0x3f317217, v91
	v_fma_f32 v98, v91, s83, -v98
	v_fmac_f32_e32 v98, 0x3377d1cf, v91
	v_fmac_f32_e32 v95, v99, v100
	v_cmp_gt_f32_e64 s[14:15], s82, v95
	v_fmac_f32_e32 v98, 0x3f317217, v91
	v_cmp_lt_f32_e64 s[16:17], |v91|, s84
	v_cndmask_b32_e64 v99, 0, 32, s[14:15]
	v_ldexp_f32 v95, v95, v99
	v_log_f32_e32 v95, v95
	v_cndmask_b32_e64 v91, v91, v98, s[16:17]
	v_cndmask_b32_e32 v98, 0, v167, vcc
	v_sub_f32_e32 v91, v91, v98
	v_mul_f32_e32 v98, 0x3f317217, v95
	v_fma_f32 v98, v95, s83, -v98
	v_fmac_f32_e32 v98, 0x3377d1cf, v95
	v_fmac_f32_e32 v98, 0x3f317217, v95
	v_cmp_lt_f32_e64 vcc, |v95|, s84
	v_cvt_pk_bf16_f32 v89, v90, v91
	v_cvt_pk_bf16_f32 v90, v92, v93
	v_lshl_add_u64 v[92:93], s[38:39], 0, v[96:97]
	s_nop 0
	v_cndmask_b32_e32 v95, v95, v98, vcc
	v_cndmask_b32_e64 v98, 0, v167, s[14:15]
	v_sub_f32_e32 v95, v95, v98
	v_cvt_pk_bf16_f32 v91, v94, v95
	v_lshl_add_u64 v[94:95], s[0:1], 0, v[138:139]
	v_lshl_add_u64 v[92:93], v[94:95], 1, v[92:93]
	global_store_dwordx4 v[92:93], v[88:91], off offset:-2048 sc1

;     __device__ __forceinline__ static u32x4 pack8(const f32x4 a, const f32x4 b) { u32x4 w; w.x = cvt_pk_bf16(a[0], a[1]); w.y = cvt_pk_bf16(a[2], a[3]); w.z = cvt_pk_bf16(b[0], b[1]); w.w = cvt_pk_bf16(b[2], b[3]); return w; }
;     __device__ __forceinline__ static f32x4 silu4(const f32x4 v) { f32x4 o; for (int i = 0; i < 4; ++i) o[i] = v[i] * __builtin_amdgcn_rcpf(1.f + __expf(-v[i])); return o; }
;     __device__ __forceinline__ void operator()(const f32x4 (&acc)[2][2][4][2], const Unit& u, int wr, int wc, int fr, int fq) const {
;     ...
;                 for (int bj = 0; bj < 2; ++bj) { const int c256 = bj * HALF + cl; f32x4 v0 = acc[ai][bj][m][0], v1 = acc[ai][bj][m][1];
;                     if (pn < 4) { *(u32x4*)(QH + row * 1024 + pn * 256 + c256) = pack8(silu4(v0), silu4(v1)); }
;                     else if (pn < 8) { const int col = (pn - 4) * 256 + c256; const f32x4 l0 = *(const f32x4*)(LB + col), l1 = *(const f32x4*)(LB + col + 4); f32x4 o0, o1;
;                         for (int i = 0; i < 4; ++i) { o0[i] = __logf(l0[i] + (1.f - l0[i]) * __builtin_amdgcn_rcpf(1.f + __expf(-v0[i]))); o1[i] = __logf(l1[i] + (1.f - l1[i]) * __builtin_amdgcn_rcpf(1.f + __expf(-v1[i]))); }
;                         *(u32x4*)(LOGF + row * 1024 + col) = pack8(o0, o1); }
;                     else if (pn < 12) { *(u32x4*)(VH + row * 1024 + (pn - 8) * 256 + c256) = pack8(v0, v1); }
;                     else if (pn < 16) { *(u32x4*)(GH + row * 1024 + (pn - 12) * 256 + c256) = pack8(silu4(v0), silu4(v1)); }
;                     else if (pn < 20) { const float sc = 0.125f * 1.4426950408889634f; *(u32x4*)(QN + row * 1024 + (pn - 16) * 256 + c256) = pack8(v0 * sc, v1 * sc); }
;                     else if (pn < 26) { *(u32x4*)(KV6 + (size_t)(pn - 20) * ((size_t)16384 * 256) + row * 256 + c256) = pack8(v0, v1); }
;                     else if (c256 < 64) { f32x4 o0, o1; for (int i = 0; i < 4; ++i) { o0[i] = __builtin_amdgcn_rcpf(1.f + __expf(-v0[i])); o1[i] = __builtin_amdgcn_rcpf(1.f + __expf(-v1[i])); }
;                         *(f32x4*)(GATE + row * 64 + c256) = o0; *(f32x4*)(GATE + row * 64 + c256 + 4) = o1; } } }
.LBB0_316:
	s_and_b64 vcc, exec, s[10:11]
	s_cbranch_vccnz .LBB0_336
	s_andn2_b64 vcc, exec, s[62:63]
	s_cbranch_vccnz .LBB0_333
	s_andn2_b64 vcc, exec, s[60:61]
	s_cbranch_vccnz .LBB0_330
	s_andn2_b64 vcc, exec, s[58:59]
	s_cbranch_vccnz .LBB0_327
	s_andn2_b64 vcc, exec, s[56:57]
	s_cbranch_vccnz .LBB0_324
	s_and_saveexec_b64 s[14:15], s[4:5]
	s_cbranch_execz .LBB0_323
	v_mul_f32_e32 v87, 0xbfb8aa3b, v72
	v_exp_f32_e32 v87, v87
	v_mul_f32_e32 v88, 0xbfb8aa3b, v77
	v_mul_f32_e32 v89, 0xbfb8aa3b, v73
	v_exp_f32_e32 v88, v88
	v_exp_f32_e32 v89, v89
	v_add_f32_e32 v87, 1.0, v87
	v_rcp_f32_e32 v90, v87
	v_add_f32_e32 v87, 1.0, v88
	v_add_f32_e32 v88, 1.0, v89
	v_mul_f32_e32 v89, 0xbfb8aa3b, v78
	v_mul_f32_e32 v91, 0xbfb8aa3b, v74
	v_exp_f32_e32 v89, v89
	v_exp_f32_e32 v92, v91
	v_mul_f32_e32 v86, 0xbfb8aa3b, v76
	v_rcp_f32_e32 v91, v88
	v_add_f32_e32 v88, 1.0, v89
	v_add_f32_e32 v89, 1.0, v92
	v_mul_f32_e32 v92, 0xbfb8aa3b, v79
	v_exp_f32_e32 v86, v86
	v_exp_f32_e32 v93, v92
	v_mul_f32_e32 v92, 0xbfb8aa3b, v75
	v_exp_f32_e32 v94, v92
	v_add_f32_e32 v86, 1.0, v86
	v_rcp_f32_e32 v92, v89
	v_add_f32_e32 v89, 1.0, v93
	v_rcp_f32_e32 v86, v86
	v_rcp_f32_e32 v87, v87
	v_rcp_f32_e32 v88, v88
	v_rcp_f32_e32 v89, v89
	v_add_f32_e32 v93, 1.0, v94
	v_rcp_f32_e32 v93, v93
	v_lshl_add_u64 v[94:95], v[84:85], 2, v[140:141]
	global_store_dwordx4 v[94:95], v[86:89], off sc1
	global_store_dwordx4 v[94:95], v[90:93], off offset:16 sc1

;     __device__ __forceinline__ static u32x4 pack8(const f32x4 a, const f32x4 b) { u32x4 w; w.x = cvt_pk_bf16(a[0], a[1]); w.y = cvt_pk_bf16(a[2], a[3]); w.z = cvt_pk_bf16(b[0], b[1]); w.w = cvt_pk_bf16(b[2], b[3]); return w; }
;     __device__ __forceinline__ void operator()(const f32x4 (&acc)[2][2][4][2], const Unit& u, int wr, int wc, int fr, int fq) const {
;     ...
;                     else if (pn < 26) { *(u32x4*)(KV6 + (size_t)(pn - 20) * ((size_t)16384 * 256) + row * 256 + c256) = pack8(v0, v1); }
.LBB0_324:
	s_andn2_b64 vcc, exec, s[14:15]
	s_cbranch_vccnz .LBB0_326
	s_add_u32 s14, s73, s2
	s_addc_u32 s15, s74, s3
	v_lshl_add_u64 v[90:91], s[14:15], 0, v[82:83]
	v_lshl_add_u64 v[90:91], v[136:137], 1, v[90:91]
	v_cvt_pk_bf16_f32 v86, v76, v77
	v_cvt_pk_bf16_f32 v87, v78, v79
	v_cvt_pk_bf16_f32 v88, v72, v73
	v_cvt_pk_bf16_f32 v89, v74, v75
	global_store_dwordx4 v[90:91], v[86:89], off sc1

;     __device__ __forceinline__ static u32x4 pack8(const f32x4 a, const f32x4 b) { u32x4 w; w.x = cvt_pk_bf16(a[0], a[1]); w.y = cvt_pk_bf16(a[2], a[3]); w.z = cvt_pk_bf16(b[0], b[1]); w.w = cvt_pk_bf16(b[2], b[3]); return w; }
;     __device__ __forceinline__ void operator()(const f32x4 (&acc)[2][2][4][2], const Unit& u, int wr, int wc, int fr, int fq) const {
;     ...
;                     else if (pn < 20) { const float sc = 0.125f * 1.4426950408889634f; *(u32x4*)(QN + row * 1024 + (pn - 16) * 256 + c256) = pack8(v0 * sc, v1 * sc); }
.LBB0_327:
	s_andn2_b64 vcc, exec, s[14:15]
	s_cbranch_vccnz .LBB0_329
	v_pk_mul_f32 v[88:89], v[78:79], s[46:47] op_sel_hi:[1,0]
	v_pk_mul_f32 v[86:87], v[76:77], s[46:47] op_sel_hi:[1,0]
	v_pk_mul_f32 v[90:91], v[74:75], s[46:47] op_sel_hi:[1,0]
	v_pk_mul_f32 v[92:93], v[72:73], s[46:47] op_sel_hi:[1,0]
	v_cvt_pk_bf16_f32 v86, v86, v87
	v_cvt_pk_bf16_f32 v87, v88, v89
	s_nop 0
	v_cvt_pk_bf16_f32 v88, v92, v93
	v_cvt_pk_bf16_f32 v89, v90, v91
	v_lshl_add_u64 v[90:91], s[36:37], 0, v[80:81]
	v_lshl_add_u64 v[90:91], s[24:25], 1, v[90:91]
	v_lshl_add_u64 v[90:91], v[136:137], 1, v[90:91]
	v_add_co_u32_e32 v90, vcc, 0xffffe000, v90
	s_nop 1
	v_addc_co_u32_e32 v91, vcc, -1, v91, vcc
	global_store_dwordx4 v[90:91], v[86:89], off sc1

;     __device__ __forceinline__ static u32x4 pack8(const f32x4 a, const f32x4 b) { u32x4 w; w.x = cvt_pk_bf16(a[0], a[1]); w.y = cvt_pk_bf16(a[2], a[3]); w.z = cvt_pk_bf16(b[0], b[1]); w.w = cvt_pk_bf16(b[2], b[3]); return w; }
;     __device__ __forceinline__ static f32x4 silu4(const f32x4 v) { f32x4 o; for (int i = 0; i < 4; ++i) o[i] = v[i] * __builtin_amdgcn_rcpf(1.f + __expf(-v[i])); return o; }
;     __device__ __forceinline__ void operator()(const f32x4 (&acc)[2][2][4][2], const Unit& u, int wr, int wc, int fr, int fq) const {
;     ...
;                     else if (pn < 16) { *(u32x4*)(GH + row * 1024 + (pn - 12) * 256 + c256) = pack8(silu4(v0), silu4(v1)); }
.LBB0_330:
	s_andn2_b64 vcc, exec, s[14:15]
	s_cbranch_vccnz .LBB0_332
	v_mul_f32_e32 v86, 0xbfb8aa3b, v76
	v_mul_f32_e32 v87, 0xbfb8aa3b, v77
	v_mul_f32_e32 v88, 0xbfb8aa3b, v78
	v_mul_f32_e32 v90, 0xbfb8aa3b, v72
	v_mul_f32_e32 v91, 0xbfb8aa3b, v73
	v_exp_f32_e32 v86, v86
	v_exp_f32_e32 v87, v87
	v_exp_f32_e32 v88, v88
	v_mul_f32_e32 v89, 0xbfb8aa3b, v79
	v_exp_f32_e32 v90, v90
	v_exp_f32_e32 v91, v91
	v_exp_f32_e32 v89, v89
	v_add_f32_e32 v86, 1.0, v86
	v_add_f32_e32 v87, 1.0, v87
	v_add_f32_e32 v88, 1.0, v88
	v_add_f32_e32 v90, 1.0, v90
	v_add_f32_e32 v91, 1.0, v91
	v_rcp_f32_e32 v86, v86
	v_rcp_f32_e32 v87, v87
	v_rcp_f32_e32 v88, v88
	v_add_f32_e32 v89, 1.0, v89
	v_rcp_f32_e32 v90, v90
	v_mul_f32_e32 v92, 0xbfb8aa3b, v74
	v_mul_f32_e32 v93, 0xbfb8aa3b, v75
	v_rcp_f32_e32 v91, v91
	v_rcp_f32_e32 v89, v89
	v_exp_f32_e32 v92, v92
	v_exp_f32_e32 v93, v93
	v_mul_f32_e32 v86, v76, v86
	v_mul_f32_e32 v87, v77, v87
	v_mul_f32_e32 v88, v78, v88
	v_mul_f32_e32 v90, v72, v90
	v_mul_f32_e32 v91, v73, v91
	v_mul_f32_e32 v89, v79, v89
	v_add_f32_e32 v92, 1.0, v92
	v_add_f32_e32 v93, 1.0, v93
	v_cvt_pk_bf16_f32 v86, v86, v87
	v_cvt_pk_bf16_f32 v87, v88, v89
	v_cvt_pk_bf16_f32 v88, v90, v91
	v_lshl_add_u64 v[90:91], s[34:35], 0, v[80:81]
	v_rcp_f32_e32 v92, v92
	v_rcp_f32_e32 v93, v93
	v_lshl_add_u64 v[90:91], s[24:25], 1, v[90:91]
	v_lshl_add_u64 v[90:91], v[136:137], 1, v[90:91]
	v_add_co_u32_e32 v90, vcc, 0xfffff000, v90
	v_mul_f32_e32 v92, v74, v92
	s_nop 0
	v_addc_co_u32_e32 v91, vcc, -1, v91, vcc
	v_mul_f32_e32 v93, v75, v93
	v_cvt_pk_bf16_f32 v89, v92, v93
	global_store_dwordx4 v[90:91], v[86:89], off offset:-2048 sc1

;     __device__ __forceinline__ static u32x4 pack8(const f32x4 a, const f32x4 b) { u32x4 w; w.x = cvt_pk_bf16(a[0], a[1]); w.y = cvt_pk_bf16(a[2], a[3]); w.z = cvt_pk_bf16(b[0], b[1]); w.w = cvt_pk_bf16(b[2], b[3]); return w; }
;     __device__ __forceinline__ void operator()(const f32x4 (&acc)[2][2][4][2], const Unit& u, int wr, int wc, int fr, int fq) const {
;     ...
;                     else if (pn < 12) { *(u32x4*)(VH + row * 1024 + (pn - 8) * 256 + c256) = pack8(v0, v1); }
.LBB0_333:
	s_andn2_b64 vcc, exec, s[14:15]
	s_cbranch_vccnz .LBB0_335
	v_lshl_add_u64 v[90:91], s[30:31], 0, v[80:81]
	v_lshl_add_u64 v[90:91], s[24:25], 1, v[90:91]
	v_lshl_add_u64 v[90:91], v[136:137], 1, v[90:91]
	v_cvt_pk_bf16_f32 v86, v76, v77
	v_cvt_pk_bf16_f32 v87, v78, v79
	v_cvt_pk_bf16_f32 v88, v72, v73
	v_cvt_pk_bf16_f32 v89, v74, v75
	global_store_dwordx4 v[90:91], v[86:89], off offset:-4096 sc1

;     __device__ __forceinline__ static u32x4 pack8(const f32x4 a, const f32x4 b) { u32x4 w; w.x = cvt_pk_bf16(a[0], a[1]); w.y = cvt_pk_bf16(a[2], a[3]); w.z = cvt_pk_bf16(b[0], b[1]); w.w = cvt_pk_bf16(b[2], b[3]); return w; }
;     __device__ __forceinline__ void operator()(const f32x4 (&acc)[2][2][4][2], const Unit& u, int wr, int wc, int fr, int fq) const {
;     ...
;                     else if (pn < 8) { const int col = (pn - 4) * 256 + c256; const f32x4 l0 = *(const f32x4*)(LB + col), l1 = *(const f32x4*)(LB + col + 4); f32x4 o0, o1;
;                         for (int i = 0; i < 4; ++i) { o0[i] = __logf(l0[i] + (1.f - l0[i]) * __builtin_amdgcn_rcpf(1.f + __expf(-v0[i]))); o1[i] = __logf(l1[i] + (1.f - l1[i]) * __builtin_amdgcn_rcpf(1.f + __expf(-v1[i]))); }
;                         *(u32x4*)(LOGF + row * 1024 + col) = pack8(o0, o1); }
.LBB0_336:
	s_andn2_b64 vcc, exec, s[14:15]
	s_cbranch_vccnz .LBB0_338
	v_add_u32_e32 v86, s33, v136
	v_ashrrev_i32_e32 v87, 31, v86
	v_lshl_add_u64 v[90:91], v[86:87], 2, s[40:41]
	global_load_dwordx4 v[86:89], v[90:91], off
	s_nop 0
	global_load_dwordx4 v[90:93], v[90:91], off offset:16
	v_mul_f32_e32 v94, 0xbfb8aa3b, v76
	v_mul_f32_e32 v95, 0xbfb8aa3b, v72
	v_exp_f32_e32 v94, v94
	v_mul_f32_e32 v96, 0xbfb8aa3b, v77
	v_exp_f32_e32 v95, v95
	v_mul_f32_e32 v97, 0xbfb8aa3b, v73
	v_exp_f32_e32 v96, v96
	v_exp_f32_e32 v97, v97
	v_mul_f32_e32 v98, 0xbfb8aa3b, v78
	v_add_f32_e32 v94, 1.0, v94
	v_exp_f32_e32 v98, v98
	v_add_f32_e32 v95, 1.0, v95
	v_rcp_f32_e32 v94, v94
	v_add_f32_e32 v96, 1.0, v96
	v_rcp_f32_e32 v95, v95
	v_add_f32_e32 v97, 1.0, v97
	v_rcp_f32_e32 v96, v96
	v_mul_f32_e32 v99, 0xbfb8aa3b, v74
	v_rcp_f32_e32 v97, v97
	v_exp_f32_e32 v99, v99
	v_add_f32_e32 v98, 1.0, v98
	v_rcp_f32_e32 v98, v98
	v_add_f32_e32 v99, 1.0, v99
	v_rcp_f32_e32 v99, v99
	s_waitcnt vmcnt(0)
	v_sub_f32_e32 v100, 1.0, v86
	v_sub_f32_e32 v101, 1.0, v90
	v_fma_f32 v86, v94, v100, v86
	v_sub_f32_e32 v102, 1.0, v87
	v_fma_f32 v90, v95, v101, v90
	v_cmp_gt_f32_e32 vcc, s82, v86
	v_sub_f32_e32 v103, 1.0, v91
	v_fma_f32 v87, v96, v102, v87
	v_cndmask_b32_e64 v94, 0, 32, vcc
	v_cmp_gt_f32_e64 s[14:15], s82, v90
	v_fma_f32 v91, v97, v103, v91
	v_cmp_gt_f32_e64 s[16:17], s82, v87
	v_cndmask_b32_e64 v95, 0, 32, s[14:15]
	v_ldexp_f32 v86, v86, v94
	v_sub_f32_e32 v104, 1.0, v88
	v_cndmask_b32_e64 v96, 0, 32, s[16:17]
	v_cmp_gt_f32_e64 s[18:19], s82, v91
	v_ldexp_f32 v90, v90, v95
	v_log_f32_e32 v86, v86
	v_fma_f32 v88, v98, v104, v88
	v_cndmask_b32_e64 v97, 0, 32, s[18:19]
	v_ldexp_f32 v87, v87, v96
	v_log_f32_e32 v90, v90
	v_cmp_gt_f32_e64 s[20:21], s82, v88
	v_ldexp_f32 v91, v91, v97
	v_log_f32_e32 v87, v87
	v_cndmask_b32_e64 v98, 0, 32, s[20:21]
	v_log_f32_e32 v91, v91
	v_sub_f32_e32 v105, 1.0, v92
	v_ldexp_f32 v88, v88, v98
	v_mul_f32_e32 v98, 0x3f317217, v86
	v_fma_f32 v92, v99, v105, v92
	v_mul_f32_e32 v99, 0x3f317217, v90
	v_fma_f32 v98, v86, s83, -v98
	v_mul_f32_e32 v100, 0x3f317217, v87
	v_fma_f32 v99, v90, s83, -v99
	v_fmac_f32_e32 v98, 0x3377d1cf, v86
	v_cndmask_b32_e32 v94, 0, v167, vcc
	v_mul_f32_e32 v101, 0x3f317217, v91
	v_fma_f32 v100, v87, s83, -v100
	v_fmac_f32_e32 v99, 0x3377d1cf, v90
	v_fmac_f32_e32 v98, 0x3f317217, v86
	v_cmp_lt_f32_e64 vcc, |v86|, s84
	v_fma_f32 v101, v91, s83, -v101
	v_fmac_f32_e32 v100, 0x3377d1cf, v87
	v_fmac_f32_e32 v99, 0x3f317217, v90
	v_cndmask_b32_e32 v86, v86, v98, vcc
	v_cmp_lt_f32_e64 vcc, |v90|, s84
	v_log_f32_e32 v88, v88
	v_fmac_f32_e32 v101, 0x3377d1cf, v91
	v_fmac_f32_e32 v100, 0x3f317217, v87
	v_cndmask_b32_e32 v90, v90, v99, vcc
	v_cmp_lt_f32_e64 vcc, |v87|, s84
	v_cndmask_b32_e64 v95, 0, v167, s[14:15]
	v_fmac_f32_e32 v101, 0x3f317217, v91
	v_cndmask_b32_e32 v87, v87, v100, vcc
	v_cmp_lt_f32_e64 vcc, |v91|, s84
	v_sub_f32_e32 v90, v90, v95
	v_mul_f32_e32 v95, 0xbfb8aa3b, v79
	v_cndmask_b32_e32 v91, v91, v101, vcc
	v_cmp_gt_f32_e32 vcc, s82, v92
	v_sub_f32_e32 v86, v86, v94
	v_exp_f32_e32 v95, v95
	v_cndmask_b32_e64 v94, 0, 32, vcc
	v_mul_f32_e32 v102, 0x3f317217, v88
	v_ldexp_f32 v92, v92, v94
	v_fma_f32 v102, v88, s83, -v102
	v_log_f32_e32 v92, v92
	v_fmac_f32_e32 v102, 0x3377d1cf, v88
	v_fmac_f32_e32 v102, 0x3f317217, v88
	v_cmp_lt_f32_e64 s[14:15], |v88|, s84
	v_add_f32_e32 v95, 1.0, v95
	v_cndmask_b32_e64 v94, 0, v167, s[20:21]
	v_cndmask_b32_e64 v88, v88, v102, s[14:15]
	v_rcp_f32_e32 v95, v95
	v_sub_f32_e32 v88, v88, v94
	v_mul_f32_e32 v94, 0x3f317217, v92
	v_cndmask_b32_e64 v96, 0, v167, s[16:17]
	v_fma_f32 v94, v92, s83, -v94
	v_sub_f32_e32 v87, v87, v96
	v_fmac_f32_e32 v94, 0x3377d1cf, v92
	v_sub_f32_e32 v96, 1.0, v89
	v_fmac_f32_e32 v94, 0x3f317217, v92
	v_cmp_lt_f32_e64 s[14:15], |v92|, s84
	v_fmac_f32_e32 v89, v95, v96
	v_sub_f32_e32 v96, 1.0, v93
	v_cndmask_b32_e64 v92, v92, v94, s[14:15]
	v_cndmask_b32_e32 v94, 0, v167, vcc
	v_cmp_gt_f32_e32 vcc, s82, v89
	v_sub_f32_e32 v92, v92, v94
	v_cndmask_b32_e64 v97, 0, v167, s[18:19]
	v_cndmask_b32_e64 v95, 0, 32, vcc
	v_ldexp_f32 v89, v89, v95
	v_mul_f32_e32 v95, 0xbfb8aa3b, v75
	v_exp_f32_e32 v95, v95
	v_log_f32_e32 v89, v89
	v_sub_f32_e32 v91, v91, v97
	v_cvt_pk_bf16_f32 v86, v86, v87
	v_add_f32_e32 v95, 1.0, v95
	v_rcp_f32_e32 v95, v95
	v_mul_f32_e32 v94, 0x3f317217, v89
	v_fma_f32 v94, v89, s83, -v94
	v_fmac_f32_e32 v94, 0x3377d1cf, v89
	v_fmac_f32_e32 v93, v95, v96
	v_cmp_gt_f32_e64 s[14:15], s82, v93
	v_fmac_f32_e32 v94, 0x3f317217, v89
	v_cmp_lt_f32_e64 s[16:17], |v89|, s84
	v_cndmask_b32_e64 v95, 0, 32, s[14:15]
	v_ldexp_f32 v93, v93, v95
	v_log_f32_e32 v93, v93
	v_cndmask_b32_e64 v89, v89, v94, s[16:17]
	v_cndmask_b32_e32 v94, 0, v167, vcc
	v_sub_f32_e32 v89, v89, v94
	v_mul_f32_e32 v94, 0x3f317217, v93
	v_fma_f32 v94, v93, s83, -v94
	v_fmac_f32_e32 v94, 0x3377d1cf, v93
	v_fmac_f32_e32 v94, 0x3f317217, v93
	v_cmp_lt_f32_e64 vcc, |v93|, s84
	v_cvt_pk_bf16_f32 v87, v88, v89
	v_cvt_pk_bf16_f32 v88, v90, v91
	v_lshl_add_u64 v[90:91], s[38:39], 0, v[80:81]
	s_nop 0
	v_cndmask_b32_e32 v93, v93, v94, vcc
	v_cndmask_b32_e64 v94, 0, v167, s[14:15]
	v_sub_f32_e32 v93, v93, v94
	v_cvt_pk_bf16_f32 v89, v92, v93
	v_lshl_add_u64 v[92:93], s[0:1], 0, v[136:137]
	v_lshl_add_u64 v[90:91], v[92:93], 1, v[90:91]
	global_store_dwordx4 v[90:91], v[86:89], off offset:-2048 sc1

;     __device__ __forceinline__ static u32x4 pack8(const f32x4 a, const f32x4 b) { u32x4 w; w.x = cvt_pk_bf16(a[0], a[1]); w.y = cvt_pk_bf16(a[2], a[3]); w.z = cvt_pk_bf16(b[0], b[1]); w.w = cvt_pk_bf16(b[2], b[3]); return w; }
;     __device__ __forceinline__ static f32x4 silu4(const f32x4 v) { f32x4 o; for (int i = 0; i < 4; ++i) o[i] = v[i] * __builtin_amdgcn_rcpf(1.f + __expf(-v[i])); return o; }
;     __device__ __forceinline__ void operator()(const f32x4 (&acc)[2][2][4][2], const Unit& u, int wr, int wc, int fr, int fq) const {
;     ...
;                 for (int bj = 0; bj < 2; ++bj) { const int c256 = bj * HALF + cl; f32x4 v0 = acc[ai][bj][m][0], v1 = acc[ai][bj][m][1];
;                     if (pn < 4) { *(u32x4*)(QH + row * 1024 + pn * 256 + c256) = pack8(silu4(v0), silu4(v1)); }
;                     else if (pn < 8) { const int col = (pn - 4) * 256 + c256; const f32x4 l0 = *(const f32x4*)(LB + col), l1 = *(const f32x4*)(LB + col + 4); f32x4 o0, o1;
;                         for (int i = 0; i < 4; ++i) { o0[i] = __logf(l0[i] + (1.f - l0[i]) * __builtin_amdgcn_rcpf(1.f + __expf(-v0[i]))); o1[i] = __logf(l1[i] + (1.f - l1[i]) * __builtin_amdgcn_rcpf(1.f + __expf(-v1[i]))); }
;                         *(u32x4*)(LOGF + row * 1024 + col) = pack8(o0, o1); }
;                     else if (pn < 12) { *(u32x4*)(VH + row * 1024 + (pn - 8) * 256 + c256) = pack8(v0, v1); }
;                     else if (pn < 16) { *(u32x4*)(GH + row * 1024 + (pn - 12) * 256 + c256) = pack8(silu4(v0), silu4(v1)); }
;                     else if (pn < 20) { const float sc = 0.125f * 1.4426950408889634f; *(u32x4*)(QN + row * 1024 + (pn - 16) * 256 + c256) = pack8(v0 * sc, v1 * sc); }
;                     else if (pn < 26) { *(u32x4*)(KV6 + (size_t)(pn - 20) * ((size_t)16384 * 256) + row * 256 + c256) = pack8(v0, v1); }
;                     else if (c256 < 64) { f32x4 o0, o1; for (int i = 0; i < 4; ++i) { o0[i] = __builtin_amdgcn_rcpf(1.f + __expf(-v0[i])); o1[i] = __builtin_amdgcn_rcpf(1.f + __expf(-v1[i])); }
;                         *(f32x4*)(GATE + row * 64 + c256) = o0; *(f32x4*)(GATE + row * 64 + c256 + 4) = o1; } } }
.LBB0_339:
	v_mul_f32_e32 v88, 0xbfb8aa3b, v76
	v_mul_f32_e32 v89, 0xbfb8aa3b, v77
	v_mul_f32_e32 v90, 0xbfb8aa3b, v78
	v_exp_f32_e32 v88, v88
	v_exp_f32_e32 v89, v89
	v_exp_f32_e32 v90, v90
	v_mul_f32_e32 v91, 0xbfb8aa3b, v79
	v_add_f32_e32 v88, 1.0, v88
	v_add_f32_e32 v89, 1.0, v89
	v_add_f32_e32 v90, 1.0, v90
	v_rcp_f32_e32 v88, v88
	v_rcp_f32_e32 v89, v89
	v_rcp_f32_e32 v90, v90
	v_exp_f32_e32 v91, v91
	v_mul_f32_e32 v76, v76, v88
	v_mul_f32_e32 v77, v77, v89
	v_mul_f32_e32 v78, v78, v90
	v_add_f32_e32 v88, 1.0, v91
	v_mul_f32_e32 v89, 0xbfb8aa3b, v72
	v_mul_f32_e32 v90, 0xbfb8aa3b, v73
	v_rcp_f32_e32 v88, v88
	v_exp_f32_e32 v89, v89
	v_exp_f32_e32 v90, v90
	v_mul_f32_e32 v91, 0xbfb8aa3b, v75
	v_mul_f32_e32 v79, v79, v88
	v_add_f32_e32 v88, 1.0, v89
	v_add_f32_e32 v89, 1.0, v90
	v_mul_f32_e32 v90, 0xbfb8aa3b, v74
	v_exp_f32_e32 v91, v91
	v_exp_f32_e32 v90, v90
	v_rcp_f32_e32 v88, v88
	v_rcp_f32_e32 v89, v89
	v_add_f32_e32 v91, 1.0, v91
	v_add_f32_e32 v90, 1.0, v90
	v_rcp_f32_e32 v91, v91
	v_rcp_f32_e32 v90, v90
	v_mul_f32_e32 v88, v72, v88
	v_cvt_pk_bf16_f32 v72, v76, v77
	v_mul_f32_e32 v75, v75, v91
	v_lshl_add_u64 v[76:77], v[136:137], 1, v[86:87]
	v_mul_f32_e32 v89, v73, v89
	v_mul_f32_e32 v90, v74, v90
	v_cvt_pk_bf16_f32 v73, v78, v79
	v_cvt_pk_bf16_f32 v74, v88, v89
	v_cvt_pk_bf16_f32 v75, v90, v75
	global_store_dwordx4 v[76:77], v[72:75], off sc1
	s_and_b64 vcc, exec, s[12:13]
	s_mov_b64 s[14:15], -1
	s_cbranch_vccnz .LBB0_200
.LBB0_340:
	s_and_b64 vcc, exec, s[10:11]
	s_cbranch_vccnz .LBB0_360
	s_andn2_b64 vcc, exec, s[62:63]
	s_cbranch_vccnz .LBB0_357
	s_andn2_b64 vcc, exec, s[60:61]
	s_cbranch_vccnz .LBB0_354
	s_andn2_b64 vcc, exec, s[58:59]
	s_cbranch_vccnz .LBB0_351
	s_andn2_b64 vcc, exec, s[56:57]
	s_cbranch_vccnz .LBB0_348
	s_and_saveexec_b64 s[14:15], s[6:7]
	s_cbranch_execz .LBB0_347
	v_mul_f32_e32 v73, 0xbfb8aa3b, v64
	v_exp_f32_e32 v73, v73
	v_mul_f32_e32 v74, 0xbfb8aa3b, v69
	v_mul_f32_e32 v75, 0xbfb8aa3b, v65
	v_exp_f32_e32 v74, v74
	v_exp_f32_e32 v75, v75
	v_add_f32_e32 v73, 1.0, v73
	v_rcp_f32_e32 v76, v73
	v_add_f32_e32 v73, 1.0, v74
	v_add_f32_e32 v74, 1.0, v75
	v_mul_f32_e32 v75, 0xbfb8aa3b, v70
	v_mul_f32_e32 v77, 0xbfb8aa3b, v66
	v_exp_f32_e32 v75, v75
	v_exp_f32_e32 v78, v77
	v_mul_f32_e32 v72, 0xbfb8aa3b, v68
	v_rcp_f32_e32 v77, v74
	v_add_f32_e32 v74, 1.0, v75
	v_add_f32_e32 v75, 1.0, v78
	v_mul_f32_e32 v78, 0xbfb8aa3b, v71
	v_exp_f32_e32 v72, v72
	v_exp_f32_e32 v79, v78
	v_mul_f32_e32 v78, 0xbfb8aa3b, v67
	v_exp_f32_e32 v88, v78
	v_add_f32_e32 v72, 1.0, v72
	v_rcp_f32_e32 v78, v75
	v_add_f32_e32 v75, 1.0, v79
	v_rcp_f32_e32 v72, v72
	v_rcp_f32_e32 v73, v73
	v_rcp_f32_e32 v74, v74
	v_rcp_f32_e32 v75, v75
	v_add_f32_e32 v79, 1.0, v88
	v_rcp_f32_e32 v79, v79
	v_lshl_add_u64 v[84:85], v[84:85], 2, v[142:143]
	global_store_dwordx4 v[84:85], v[72:75], off sc1
	global_store_dwordx4 v[84:85], v[76:79], off offset:16 sc1

;     __device__ __forceinline__ static u32x4 pack8(const f32x4 a, const f32x4 b) { u32x4 w; w.x = cvt_pk_bf16(a[0], a[1]); w.y = cvt_pk_bf16(a[2], a[3]); w.z = cvt_pk_bf16(b[0], b[1]); w.w = cvt_pk_bf16(b[2], b[3]); return w; }
;     __device__ __forceinline__ void operator()(const f32x4 (&acc)[2][2][4][2], const Unit& u, int wr, int wc, int fr, int fq) const {
;     ...
;                     else if (pn < 26) { *(u32x4*)(KV6 + (size_t)(pn - 20) * ((size_t)16384 * 256) + row * 256 + c256) = pack8(v0, v1); }
.LBB0_348:
	s_andn2_b64 vcc, exec, s[14:15]
	s_cbranch_vccnz .LBB0_350
	s_add_u32 s14, s73, s2
	s_addc_u32 s15, s74, s3
	v_lshl_add_u64 v[76:77], s[14:15], 0, v[82:83]
	v_lshl_add_u64 v[76:77], v[136:137], 1, v[76:77]
	v_cvt_pk_bf16_f32 v72, v68, v69
	v_cvt_pk_bf16_f32 v73, v70, v71
	v_cvt_pk_bf16_f32 v74, v64, v65
	v_cvt_pk_bf16_f32 v75, v66, v67
	global_store_dwordx4 v[76:77], v[72:75], off offset:256 sc1

;     __device__ __forceinline__ static u32x4 pack8(const f32x4 a, const f32x4 b) { u32x4 w; w.x = cvt_pk_bf16(a[0], a[1]); w.y = cvt_pk_bf16(a[2], a[3]); w.z = cvt_pk_bf16(b[0], b[1]); w.w = cvt_pk_bf16(b[2], b[3]); return w; }
;     __device__ __forceinline__ void operator()(const f32x4 (&acc)[2][2][4][2], const Unit& u, int wr, int wc, int fr, int fq) const {
;     ...
;                     else if (pn < 20) { const float sc = 0.125f * 1.4426950408889634f; *(u32x4*)(QN + row * 1024 + (pn - 16) * 256 + c256) = pack8(v0 * sc, v1 * sc); }
.LBB0_351:
	s_andn2_b64 vcc, exec, s[14:15]
	s_cbranch_vccnz .LBB0_353
	v_pk_mul_f32 v[74:75], v[70:71], s[46:47] op_sel_hi:[1,0]
	v_pk_mul_f32 v[72:73], v[68:69], s[46:47] op_sel_hi:[1,0]
	v_pk_mul_f32 v[76:77], v[66:67], s[46:47] op_sel_hi:[1,0]
	v_pk_mul_f32 v[78:79], v[64:65], s[46:47] op_sel_hi:[1,0]
	v_cvt_pk_bf16_f32 v72, v72, v73
	v_cvt_pk_bf16_f32 v73, v74, v75
	s_nop 0
	v_cvt_pk_bf16_f32 v74, v78, v79
	v_cvt_pk_bf16_f32 v75, v76, v77
	v_lshl_add_u64 v[76:77], s[36:37], 0, v[80:81]
	v_lshl_add_u64 v[76:77], s[24:25], 1, v[76:77]
	v_lshl_add_u64 v[76:77], v[138:139], 1, v[76:77]
	v_add_co_u32_e32 v76, vcc, 0xffffe000, v76
	s_nop 1
	v_addc_co_u32_e32 v77, vcc, -1, v77, vcc
	global_store_dwordx4 v[76:77], v[72:75], off sc1

;     __device__ __forceinline__ static u32x4 pack8(const f32x4 a, const f32x4 b) { u32x4 w; w.x = cvt_pk_bf16(a[0], a[1]); w.y = cvt_pk_bf16(a[2], a[3]); w.z = cvt_pk_bf16(b[0], b[1]); w.w = cvt_pk_bf16(b[2], b[3]); return w; }
;     __device__ __forceinline__ static f32x4 silu4(const f32x4 v) { f32x4 o; for (int i = 0; i < 4; ++i) o[i] = v[i] * __builtin_amdgcn_rcpf(1.f + __expf(-v[i])); return o; }
;     __device__ __forceinline__ void operator()(const f32x4 (&acc)[2][2][4][2], const Unit& u, int wr, int wc, int fr, int fq) const {
;     ...
;                     else if (pn < 16) { *(u32x4*)(GH + row * 1024 + (pn - 12) * 256 + c256) = pack8(silu4(v0), silu4(v1)); }
.LBB0_354:
	s_andn2_b64 vcc, exec, s[14:15]
	s_cbranch_vccnz .LBB0_356
	v_mul_f32_e32 v72, 0xbfb8aa3b, v68
	v_mul_f32_e32 v73, 0xbfb8aa3b, v69
	v_mul_f32_e32 v74, 0xbfb8aa3b, v70
	v_mul_f32_e32 v76, 0xbfb8aa3b, v64
	v_mul_f32_e32 v77, 0xbfb8aa3b, v65
	v_exp_f32_e32 v72, v72
	v_exp_f32_e32 v73, v73
	v_exp_f32_e32 v74, v74
	v_mul_f32_e32 v75, 0xbfb8aa3b, v71
	v_exp_f32_e32 v76, v76
	v_exp_f32_e32 v77, v77
	v_exp_f32_e32 v75, v75
	v_add_f32_e32 v72, 1.0, v72
	v_add_f32_e32 v73, 1.0, v73
	v_add_f32_e32 v74, 1.0, v74
	v_add_f32_e32 v76, 1.0, v76
	v_add_f32_e32 v77, 1.0, v77
	v_rcp_f32_e32 v72, v72
	v_rcp_f32_e32 v73, v73
	v_rcp_f32_e32 v74, v74
	v_add_f32_e32 v75, 1.0, v75
	v_rcp_f32_e32 v76, v76
	v_mul_f32_e32 v78, 0xbfb8aa3b, v66
	v_mul_f32_e32 v79, 0xbfb8aa3b, v67
	v_rcp_f32_e32 v77, v77
	v_rcp_f32_e32 v75, v75
	v_exp_f32_e32 v78, v78
	v_exp_f32_e32 v79, v79
	v_mul_f32_e32 v72, v68, v72
	v_mul_f32_e32 v73, v69, v73
	v_mul_f32_e32 v74, v70, v74
	v_mul_f32_e32 v76, v64, v76
	v_mul_f32_e32 v77, v65, v77
	v_mul_f32_e32 v75, v71, v75
	v_add_f32_e32 v78, 1.0, v78
	v_add_f32_e32 v79, 1.0, v79
	v_cvt_pk_bf16_f32 v72, v72, v73
	v_cvt_pk_bf16_f32 v73, v74, v75
	v_cvt_pk_bf16_f32 v74, v76, v77
	v_lshl_add_u64 v[76:77], s[34:35], 0, v[80:81]
	v_rcp_f32_e32 v78, v78
	v_rcp_f32_e32 v79, v79
	v_lshl_add_u64 v[76:77], s[24:25], 1, v[76:77]
	v_lshl_add_u64 v[76:77], v[138:139], 1, v[76:77]
	v_add_co_u32_e32 v76, vcc, 0xfffff000, v76
	v_mul_f32_e32 v78, v66, v78
	s_nop 0
	v_addc_co_u32_e32 v77, vcc, -1, v77, vcc
	v_mul_f32_e32 v79, v67, v79
	v_cvt_pk_bf16_f32 v75, v78, v79
	global_store_dwordx4 v[76:77], v[72:75], off offset:-2048 sc1

;     __device__ __forceinline__ static u32x4 pack8(const f32x4 a, const f32x4 b) { u32x4 w; w.x = cvt_pk_bf16(a[0], a[1]); w.y = cvt_pk_bf16(a[2], a[3]); w.z = cvt_pk_bf16(b[0], b[1]); w.w = cvt_pk_bf16(b[2], b[3]); return w; }
;     __device__ __forceinline__ void operator()(const f32x4 (&acc)[2][2][4][2], const Unit& u, int wr, int wc, int fr, int fq) const {
;     ...
;                     else if (pn < 12) { *(u32x4*)(VH + row * 1024 + (pn - 8) * 256 + c256) = pack8(v0, v1); }
.LBB0_357:
	s_andn2_b64 vcc, exec, s[14:15]
	s_cbranch_vccnz .LBB0_359
	v_lshl_add_u64 v[76:77], s[30:31], 0, v[80:81]
	v_lshl_add_u64 v[76:77], s[24:25], 1, v[76:77]
	v_lshl_add_u64 v[76:77], v[136:137], 1, v[76:77]
	v_cvt_pk_bf16_f32 v72, v68, v69
	v_cvt_pk_bf16_f32 v73, v70, v71
	v_cvt_pk_bf16_f32 v74, v64, v65
	v_cvt_pk_bf16_f32 v75, v66, v67
	global_store_dwordx4 v[76:77], v[72:75], off offset:-3840 sc1

;     __device__ __forceinline__ static u32x4 pack8(const f32x4 a, const f32x4 b) { u32x4 w; w.x = cvt_pk_bf16(a[0], a[1]); w.y = cvt_pk_bf16(a[2], a[3]); w.z = cvt_pk_bf16(b[0], b[1]); w.w = cvt_pk_bf16(b[2], b[3]); return w; }
;     __device__ __forceinline__ void operator()(const f32x4 (&acc)[2][2][4][2], const Unit& u, int wr, int wc, int fr, int fq) const {
;     ...
;                     else if (pn < 8) { const int col = (pn - 4) * 256 + c256; const f32x4 l0 = *(const f32x4*)(LB + col), l1 = *(const f32x4*)(LB + col + 4); f32x4 o0, o1;
;                         for (int i = 0; i < 4; ++i) { o0[i] = __logf(l0[i] + (1.f - l0[i]) * __builtin_amdgcn_rcpf(1.f + __expf(-v0[i]))); o1[i] = __logf(l1[i] + (1.f - l1[i]) * __builtin_amdgcn_rcpf(1.f + __expf(-v1[i]))); }
;                         *(u32x4*)(LOGF + row * 1024 + col) = pack8(o0, o1); }
.LBB0_360:
	s_andn2_b64 vcc, exec, s[14:15]
	s_cbranch_vccnz .LBB0_362
	v_add_u32_e32 v72, s33, v138
	v_ashrrev_i32_e32 v73, 31, v72
	v_lshl_add_u64 v[76:77], v[72:73], 2, s[40:41]
	global_load_dwordx4 v[72:75], v[76:77], off
	s_nop 0
	global_load_dwordx4 v[76:79], v[76:77], off offset:16
	v_mul_f32_e32 v82, 0xbfb8aa3b, v68
	v_mul_f32_e32 v83, 0xbfb8aa3b, v64
	v_exp_f32_e32 v82, v82
	v_mul_f32_e32 v84, 0xbfb8aa3b, v69
	v_exp_f32_e32 v83, v83
	v_mul_f32_e32 v85, 0xbfb8aa3b, v65
	v_exp_f32_e32 v84, v84
	v_exp_f32_e32 v85, v85
	v_mul_f32_e32 v88, 0xbfb8aa3b, v70
	v_add_f32_e32 v82, 1.0, v82
	v_exp_f32_e32 v88, v88
	v_add_f32_e32 v83, 1.0, v83
	v_rcp_f32_e32 v82, v82
	v_add_f32_e32 v84, 1.0, v84
	v_rcp_f32_e32 v83, v83
	v_add_f32_e32 v85, 1.0, v85
	v_rcp_f32_e32 v84, v84
	v_mul_f32_e32 v89, 0xbfb8aa3b, v66
	v_rcp_f32_e32 v85, v85
	v_exp_f32_e32 v89, v89
	v_add_f32_e32 v88, 1.0, v88
	v_rcp_f32_e32 v88, v88
	v_add_f32_e32 v89, 1.0, v89
	v_rcp_f32_e32 v89, v89
	s_waitcnt vmcnt(0)
	v_sub_f32_e32 v90, 1.0, v72
	v_sub_f32_e32 v91, 1.0, v76
	v_fma_f32 v72, v82, v90, v72
	v_sub_f32_e32 v92, 1.0, v73
	v_fma_f32 v76, v83, v91, v76
	v_cmp_gt_f32_e32 vcc, s82, v72
	v_sub_f32_e32 v93, 1.0, v77
	v_fma_f32 v73, v84, v92, v73
	v_cndmask_b32_e64 v82, 0, 32, vcc
	v_cmp_gt_f32_e64 s[14:15], s82, v76
	v_fma_f32 v77, v85, v93, v77
	v_cmp_gt_f32_e64 s[16:17], s82, v73
	v_cndmask_b32_e64 v83, 0, 32, s[14:15]
	v_ldexp_f32 v72, v72, v82
	v_sub_f32_e32 v94, 1.0, v74
	v_cndmask_b32_e64 v84, 0, 32, s[16:17]
	v_cmp_gt_f32_e64 s[18:19], s82, v77
	v_ldexp_f32 v76, v76, v83
	v_log_f32_e32 v72, v72
	v_fma_f32 v74, v88, v94, v74
	v_cndmask_b32_e64 v85, 0, 32, s[18:19]
	v_ldexp_f32 v73, v73, v84
	v_log_f32_e32 v76, v76
	v_cmp_gt_f32_e64 s[20:21], s82, v74
	v_ldexp_f32 v77, v77, v85
	v_log_f32_e32 v73, v73
	v_cndmask_b32_e64 v88, 0, 32, s[20:21]
	v_log_f32_e32 v77, v77
	v_sub_f32_e32 v95, 1.0, v78
	v_ldexp_f32 v74, v74, v88
	v_mul_f32_e32 v88, 0x3f317217, v72
	v_fma_f32 v78, v89, v95, v78
	v_mul_f32_e32 v89, 0x3f317217, v76
	v_fma_f32 v88, v72, s83, -v88
	v_mul_f32_e32 v90, 0x3f317217, v73
	v_fma_f32 v89, v76, s83, -v89
	v_fmac_f32_e32 v88, 0x3377d1cf, v72
	v_cndmask_b32_e32 v82, 0, v167, vcc
	v_mul_f32_e32 v91, 0x3f317217, v77
	v_fma_f32 v90, v73, s83, -v90
	v_fmac_f32_e32 v89, 0x3377d1cf, v76
	v_fmac_f32_e32 v88, 0x3f317217, v72
	v_cmp_lt_f32_e64 vcc, |v72|, s84
	v_fma_f32 v91, v77, s83, -v91
	v_fmac_f32_e32 v90, 0x3377d1cf, v73
	v_fmac_f32_e32 v89, 0x3f317217, v76
	v_cndmask_b32_e32 v72, v72, v88, vcc
	v_cmp_lt_f32_e64 vcc, |v76|, s84
	v_log_f32_e32 v74, v74
	v_fmac_f32_e32 v91, 0x3377d1cf, v77
	v_fmac_f32_e32 v90, 0x3f317217, v73
	v_cndmask_b32_e32 v76, v76, v89, vcc
	v_cmp_lt_f32_e64 vcc, |v73|, s84
	v_cndmask_b32_e64 v83, 0, v167, s[14:15]
	v_fmac_f32_e32 v91, 0x3f317217, v77
	v_cndmask_b32_e32 v73, v73, v90, vcc
	v_cmp_lt_f32_e64 vcc, |v77|, s84
	v_sub_f32_e32 v76, v76, v83
	v_mul_f32_e32 v83, 0xbfb8aa3b, v71
	v_cndmask_b32_e32 v77, v77, v91, vcc
	v_cmp_gt_f32_e32 vcc, s82, v78
	v_sub_f32_e32 v72, v72, v82
	v_exp_f32_e32 v83, v83
	v_cndmask_b32_e64 v82, 0, 32, vcc
	v_mul_f32_e32 v92, 0x3f317217, v74
	v_ldexp_f32 v78, v78, v82
	v_fma_f32 v92, v74, s83, -v92
	v_log_f32_e32 v78, v78
	v_fmac_f32_e32 v92, 0x3377d1cf, v74
	v_fmac_f32_e32 v92, 0x3f317217, v74
	v_cmp_lt_f32_e64 s[14:15], |v74|, s84
	v_add_f32_e32 v83, 1.0, v83
	v_cndmask_b32_e64 v82, 0, v167, s[20:21]
	v_cndmask_b32_e64 v74, v74, v92, s[14:15]
	v_rcp_f32_e32 v83, v83
	v_sub_f32_e32 v74, v74, v82
	v_mul_f32_e32 v82, 0x3f317217, v78
	v_cndmask_b32_e64 v84, 0, v167, s[16:17]
	v_fma_f32 v82, v78, s83, -v82
	v_sub_f32_e32 v73, v73, v84
	v_fmac_f32_e32 v82, 0x3377d1cf, v78
	v_sub_f32_e32 v84, 1.0, v75
	v_fmac_f32_e32 v82, 0x3f317217, v78
	v_cmp_lt_f32_e64 s[14:15], |v78|, s84
	v_fmac_f32_e32 v75, v83, v84
	v_sub_f32_e32 v84, 1.0, v79
	v_cndmask_b32_e64 v78, v78, v82, s[14:15]
	v_cndmask_b32_e32 v82, 0, v167, vcc
	v_cmp_gt_f32_e32 vcc, s82, v75
	v_sub_f32_e32 v78, v78, v82
	v_cndmask_b32_e64 v85, 0, v167, s[18:19]
	v_cndmask_b32_e64 v83, 0, 32, vcc
	v_ldexp_f32 v75, v75, v83
	v_mul_f32_e32 v83, 0xbfb8aa3b, v67
	v_exp_f32_e32 v83, v83
	v_log_f32_e32 v75, v75
	v_sub_f32_e32 v77, v77, v85
	v_cvt_pk_bf16_f32 v72, v72, v73
	v_add_f32_e32 v83, 1.0, v83
	v_rcp_f32_e32 v83, v83
	v_mul_f32_e32 v82, 0x3f317217, v75
	v_fma_f32 v82, v75, s83, -v82
	v_fmac_f32_e32 v82, 0x3377d1cf, v75
	v_fmac_f32_e32 v79, v83, v84
	v_cmp_gt_f32_e64 s[14:15], s82, v79
	v_fmac_f32_e32 v82, 0x3f317217, v75
	v_cmp_lt_f32_e64 s[16:17], |v75|, s84
	v_cndmask_b32_e64 v83, 0, 32, s[14:15]
	v_ldexp_f32 v79, v79, v83
	v_log_f32_e32 v79, v79
	v_cndmask_b32_e64 v75, v75, v82, s[16:17]
	v_cndmask_b32_e32 v82, 0, v167, vcc
	v_sub_f32_e32 v75, v75, v82
	v_mul_f32_e32 v82, 0x3f317217, v79
	v_fma_f32 v82, v79, s83, -v82
	v_fmac_f32_e32 v82, 0x3377d1cf, v79
	v_fmac_f32_e32 v82, 0x3f317217, v79
	v_cmp_lt_f32_e64 vcc, |v79|, s84
	v_cvt_pk_bf16_f32 v73, v74, v75
	v_cvt_pk_bf16_f32 v74, v76, v77
	v_lshl_add_u64 v[76:77], s[38:39], 0, v[80:81]
	s_nop 0
	v_cndmask_b32_e32 v79, v79, v82, vcc
	v_cndmask_b32_e64 v82, 0, v167, s[14:15]
	v_sub_f32_e32 v79, v79, v82
	v_cvt_pk_bf16_f32 v75, v78, v79
	v_lshl_add_u64 v[78:79], s[0:1], 0, v[138:139]
	v_lshl_add_u64 v[76:77], v[78:79], 1, v[76:77]
	global_store_dwordx4 v[76:77], v[72:75], off offset:-2048 sc1

;     __device__ __forceinline__ static u32x4 pack8(const f32x4 a, const f32x4 b) { u32x4 w; w.x = cvt_pk_bf16(a[0], a[1]); w.y = cvt_pk_bf16(a[2], a[3]); w.z = cvt_pk_bf16(b[0], b[1]); w.w = cvt_pk_bf16(b[2], b[3]); return w; }
;     __device__ __forceinline__ static f32x4 silu4(const f32x4 v) { f32x4 o; for (int i = 0; i < 4; ++i) o[i] = v[i] * __builtin_amdgcn_rcpf(1.f + __expf(-v[i])); return o; }
;     __device__ __forceinline__ void operator()(const f32x4 (&acc)[2][2][4][2], const Unit& u, int wr, int wc, int fr, int fq) const {
;     ...
;                 for (int bj = 0; bj < 2; ++bj) { const int c256 = bj * HALF + cl; f32x4 v0 = acc[ai][bj][m][0], v1 = acc[ai][bj][m][1];
;                     if (pn < 4) { *(u32x4*)(QH + row * 1024 + pn * 256 + c256) = pack8(silu4(v0), silu4(v1)); }
;                     else if (pn < 8) { const int col = (pn - 4) * 256 + c256; const f32x4 l0 = *(const f32x4*)(LB + col), l1 = *(const f32x4*)(LB + col + 4); f32x4 o0, o1;
;                         for (int i = 0; i < 4; ++i) { o0[i] = __logf(l0[i] + (1.f - l0[i]) * __builtin_amdgcn_rcpf(1.f + __expf(-v0[i]))); o1[i] = __logf(l1[i] + (1.f - l1[i]) * __builtin_amdgcn_rcpf(1.f + __expf(-v1[i]))); }
;                         *(u32x4*)(LOGF + row * 1024 + col) = pack8(o0, o1); }
;                     else if (pn < 12) { *(u32x4*)(VH + row * 1024 + (pn - 8) * 256 + c256) = pack8(v0, v1); }
;                     else if (pn < 16) { *(u32x4*)(GH + row * 1024 + (pn - 12) * 256 + c256) = pack8(silu4(v0), silu4(v1)); }
;                     else if (pn < 20) { const float sc = 0.125f * 1.4426950408889634f; *(u32x4*)(QN + row * 1024 + (pn - 16) * 256 + c256) = pack8(v0 * sc, v1 * sc); }
;                     else if (pn < 26) { *(u32x4*)(KV6 + (size_t)(pn - 20) * ((size_t)16384 * 256) + row * 256 + c256) = pack8(v0, v1); }
;                     else if (c256 < 64) { f32x4 o0, o1; for (int i = 0; i < 4; ++i) { o0[i] = __builtin_amdgcn_rcpf(1.f + __expf(-v0[i])); o1[i] = __builtin_amdgcn_rcpf(1.f + __expf(-v1[i])); }
;                         *(f32x4*)(GATE + row * 64 + c256) = o0; *(f32x4*)(GATE + row * 64 + c256 + 4) = o1; } } }
.LBB0_363:
	s_and_b64 vcc, exec, s[10:11]
	s_cbranch_vccnz .LBB0_383
	s_andn2_b64 vcc, exec, s[62:63]
	s_cbranch_vccnz .LBB0_380
	s_andn2_b64 vcc, exec, s[60:61]
	s_cbranch_vccnz .LBB0_377
	s_andn2_b64 vcc, exec, s[58:59]
	s_cbranch_vccnz .LBB0_374
	s_andn2_b64 vcc, exec, s[56:57]
	s_cbranch_vccnz .LBB0_371
	s_and_saveexec_b64 s[14:15], s[4:5]
	s_cbranch_execz .LBB0_370
	v_mul_f32_e32 v71, 0xbfb8aa3b, v56
	v_exp_f32_e32 v71, v71
	v_mul_f32_e32 v72, 0xbfb8aa3b, v61
	v_mul_f32_e32 v73, 0xbfb8aa3b, v57
	v_exp_f32_e32 v72, v72
	v_exp_f32_e32 v73, v73
	v_add_f32_e32 v71, 1.0, v71
	v_rcp_f32_e32 v74, v71
	v_add_f32_e32 v71, 1.0, v72
	v_add_f32_e32 v72, 1.0, v73
	v_mul_f32_e32 v73, 0xbfb8aa3b, v62
	v_mul_f32_e32 v75, 0xbfb8aa3b, v58
	v_exp_f32_e32 v73, v73
	v_exp_f32_e32 v76, v75
	v_mul_f32_e32 v70, 0xbfb8aa3b, v60
	v_rcp_f32_e32 v75, v72
	v_add_f32_e32 v72, 1.0, v73
	v_add_f32_e32 v73, 1.0, v76
	v_mul_f32_e32 v76, 0xbfb8aa3b, v63
	v_exp_f32_e32 v70, v70
	v_exp_f32_e32 v77, v76
	v_mul_f32_e32 v76, 0xbfb8aa3b, v59
	v_exp_f32_e32 v78, v76
	v_add_f32_e32 v70, 1.0, v70
	v_rcp_f32_e32 v76, v73
	v_add_f32_e32 v73, 1.0, v77
	v_rcp_f32_e32 v70, v70
	v_rcp_f32_e32 v71, v71
	v_rcp_f32_e32 v72, v72
	v_rcp_f32_e32 v73, v73
	v_add_f32_e32 v77, 1.0, v78
	v_rcp_f32_e32 v77, v77
	v_lshl_add_u64 v[78:79], v[68:69], 2, v[140:141]
	global_store_dwordx4 v[78:79], v[70:73], off sc1
	global_store_dwordx4 v[78:79], v[74:77], off offset:16 sc1

;     __device__ __forceinline__ static u32x4 pack8(const f32x4 a, const f32x4 b) { u32x4 w; w.x = cvt_pk_bf16(a[0], a[1]); w.y = cvt_pk_bf16(a[2], a[3]); w.z = cvt_pk_bf16(b[0], b[1]); w.w = cvt_pk_bf16(b[2], b[3]); return w; }
;     __device__ __forceinline__ void operator()(const f32x4 (&acc)[2][2][4][2], const Unit& u, int wr, int wc, int fr, int fq) const {
;     ...
;                     else if (pn < 26) { *(u32x4*)(KV6 + (size_t)(pn - 20) * ((size_t)16384 * 256) + row * 256 + c256) = pack8(v0, v1); }
.LBB0_371:
	s_andn2_b64 vcc, exec, s[14:15]
	s_cbranch_vccnz .LBB0_373
	s_add_u32 s14, s73, s2
	s_addc_u32 s15, s74, s3
	v_lshl_add_u64 v[74:75], s[14:15], 0, v[66:67]
	v_lshl_add_u64 v[74:75], v[136:137], 1, v[74:75]
	v_cvt_pk_bf16_f32 v70, v60, v61
	v_cvt_pk_bf16_f32 v71, v62, v63
	v_cvt_pk_bf16_f32 v72, v56, v57
	v_cvt_pk_bf16_f32 v73, v58, v59
	global_store_dwordx4 v[74:75], v[70:73], off sc1

;     __device__ __forceinline__ static u32x4 pack8(const f32x4 a, const f32x4 b) { u32x4 w; w.x = cvt_pk_bf16(a[0], a[1]); w.y = cvt_pk_bf16(a[2], a[3]); w.z = cvt_pk_bf16(b[0], b[1]); w.w = cvt_pk_bf16(b[2], b[3]); return w; }
;     __device__ __forceinline__ void operator()(const f32x4 (&acc)[2][2][4][2], const Unit& u, int wr, int wc, int fr, int fq) const {
;     ...
;                     else if (pn < 20) { const float sc = 0.125f * 1.4426950408889634f; *(u32x4*)(QN + row * 1024 + (pn - 16) * 256 + c256) = pack8(v0 * sc, v1 * sc); }
.LBB0_374:
	s_andn2_b64 vcc, exec, s[14:15]
	s_cbranch_vccnz .LBB0_376
	v_pk_mul_f32 v[72:73], v[62:63], s[46:47] op_sel_hi:[1,0]
	v_pk_mul_f32 v[70:71], v[60:61], s[46:47] op_sel_hi:[1,0]
	v_pk_mul_f32 v[74:75], v[58:59], s[46:47] op_sel_hi:[1,0]
	v_pk_mul_f32 v[76:77], v[56:57], s[46:47] op_sel_hi:[1,0]
	v_cvt_pk_bf16_f32 v70, v70, v71
	v_cvt_pk_bf16_f32 v71, v72, v73
	s_nop 0
	v_cvt_pk_bf16_f32 v72, v76, v77
	v_cvt_pk_bf16_f32 v73, v74, v75
	v_lshl_add_u64 v[74:75], s[36:37], 0, v[64:65]
	v_lshl_add_u64 v[74:75], s[24:25], 1, v[74:75]
	v_lshl_add_u64 v[74:75], v[136:137], 1, v[74:75]
	v_add_co_u32_e32 v74, vcc, 0xffffe000, v74
	s_nop 1
	v_addc_co_u32_e32 v75, vcc, -1, v75, vcc
	global_store_dwordx4 v[74:75], v[70:73], off sc1

;     __device__ __forceinline__ static u32x4 pack8(const f32x4 a, const f32x4 b) { u32x4 w; w.x = cvt_pk_bf16(a[0], a[1]); w.y = cvt_pk_bf16(a[2], a[3]); w.z = cvt_pk_bf16(b[0], b[1]); w.w = cvt_pk_bf16(b[2], b[3]); return w; }
;     __device__ __forceinline__ static f32x4 silu4(const f32x4 v) { f32x4 o; for (int i = 0; i < 4; ++i) o[i] = v[i] * __builtin_amdgcn_rcpf(1.f + __expf(-v[i])); return o; }
;     __device__ __forceinline__ void operator()(const f32x4 (&acc)[2][2][4][2], const Unit& u, int wr, int wc, int fr, int fq) const {
;     ...
;                     else if (pn < 16) { *(u32x4*)(GH + row * 1024 + (pn - 12) * 256 + c256) = pack8(silu4(v0), silu4(v1)); }
.LBB0_377:
	s_andn2_b64 vcc, exec, s[14:15]
	s_cbranch_vccnz .LBB0_379
	v_mul_f32_e32 v70, 0xbfb8aa3b, v60
	v_mul_f32_e32 v71, 0xbfb8aa3b, v61
	v_mul_f32_e32 v72, 0xbfb8aa3b, v62
	v_mul_f32_e32 v74, 0xbfb8aa3b, v56
	v_mul_f32_e32 v75, 0xbfb8aa3b, v57
	v_exp_f32_e32 v70, v70
	v_exp_f32_e32 v71, v71
	v_exp_f32_e32 v72, v72
	v_mul_f32_e32 v73, 0xbfb8aa3b, v63
	v_exp_f32_e32 v74, v74
	v_exp_f32_e32 v75, v75
	v_exp_f32_e32 v73, v73
	v_add_f32_e32 v70, 1.0, v70
	v_add_f32_e32 v71, 1.0, v71
	v_add_f32_e32 v72, 1.0, v72
	v_add_f32_e32 v74, 1.0, v74
	v_add_f32_e32 v75, 1.0, v75
	v_rcp_f32_e32 v70, v70
	v_rcp_f32_e32 v71, v71
	v_rcp_f32_e32 v72, v72
	v_add_f32_e32 v73, 1.0, v73
	v_rcp_f32_e32 v74, v74
	v_mul_f32_e32 v76, 0xbfb8aa3b, v58
	v_mul_f32_e32 v77, 0xbfb8aa3b, v59
	v_rcp_f32_e32 v75, v75
	v_rcp_f32_e32 v73, v73
	v_exp_f32_e32 v76, v76
	v_exp_f32_e32 v77, v77
	v_mul_f32_e32 v70, v60, v70
	v_mul_f32_e32 v71, v61, v71
	v_mul_f32_e32 v72, v62, v72
	v_mul_f32_e32 v74, v56, v74
	v_mul_f32_e32 v75, v57, v75
	v_mul_f32_e32 v73, v63, v73
	v_add_f32_e32 v76, 1.0, v76
	v_add_f32_e32 v77, 1.0, v77
	v_cvt_pk_bf16_f32 v70, v70, v71
	v_cvt_pk_bf16_f32 v71, v72, v73
	v_cvt_pk_bf16_f32 v72, v74, v75
	v_lshl_add_u64 v[74:75], s[34:35], 0, v[64:65]
	v_rcp_f32_e32 v76, v76
	v_rcp_f32_e32 v77, v77
	v_lshl_add_u64 v[74:75], s[24:25], 1, v[74:75]
	v_lshl_add_u64 v[74:75], v[136:137], 1, v[74:75]
	v_add_co_u32_e32 v74, vcc, 0xfffff000, v74
	v_mul_f32_e32 v76, v58, v76
	s_nop 0
	v_addc_co_u32_e32 v75, vcc, -1, v75, vcc
	v_mul_f32_e32 v77, v59, v77
	v_cvt_pk_bf16_f32 v73, v76, v77
	global_store_dwordx4 v[74:75], v[70:73], off offset:-2048 sc1

;     __device__ __forceinline__ static u32x4 pack8(const f32x4 a, const f32x4 b) { u32x4 w; w.x = cvt_pk_bf16(a[0], a[1]); w.y = cvt_pk_bf16(a[2], a[3]); w.z = cvt_pk_bf16(b[0], b[1]); w.w = cvt_pk_bf16(b[2], b[3]); return w; }
;     __device__ __forceinline__ void operator()(const f32x4 (&acc)[2][2][4][2], const Unit& u, int wr, int wc, int fr, int fq) const {
;     ...
;                     else if (pn < 12) { *(u32x4*)(VH + row * 1024 + (pn - 8) * 256 + c256) = pack8(v0, v1); }
.LBB0_380:
	s_andn2_b64 vcc, exec, s[14:15]
	s_cbranch_vccnz .LBB0_382
	v_lshl_add_u64 v[74:75], s[30:31], 0, v[64:65]
	v_lshl_add_u64 v[74:75], s[24:25], 1, v[74:75]
	v_lshl_add_u64 v[74:75], v[136:137], 1, v[74:75]
	v_cvt_pk_bf16_f32 v70, v60, v61
	v_cvt_pk_bf16_f32 v71, v62, v63
	v_cvt_pk_bf16_f32 v72, v56, v57
	v_cvt_pk_bf16_f32 v73, v58, v59
	global_store_dwordx4 v[74:75], v[70:73], off offset:-4096 sc1

;     __device__ __forceinline__ static u32x4 pack8(const f32x4 a, const f32x4 b) { u32x4 w; w.x = cvt_pk_bf16(a[0], a[1]); w.y = cvt_pk_bf16(a[2], a[3]); w.z = cvt_pk_bf16(b[0], b[1]); w.w = cvt_pk_bf16(b[2], b[3]); return w; }
;     __device__ __forceinline__ void operator()(const f32x4 (&acc)[2][2][4][2], const Unit& u, int wr, int wc, int fr, int fq) const {
;     ...
;                     else if (pn < 8) { const int col = (pn - 4) * 256 + c256; const f32x4 l0 = *(const f32x4*)(LB + col), l1 = *(const f32x4*)(LB + col + 4); f32x4 o0, o1;
;                         for (int i = 0; i < 4; ++i) { o0[i] = __logf(l0[i] + (1.f - l0[i]) * __builtin_amdgcn_rcpf(1.f + __expf(-v0[i]))); o1[i] = __logf(l1[i] + (1.f - l1[i]) * __builtin_amdgcn_rcpf(1.f + __expf(-v1[i]))); }
;                         *(u32x4*)(LOGF + row * 1024 + col) = pack8(o0, o1); }
.LBB0_383:
	s_andn2_b64 vcc, exec, s[14:15]
	s_cbranch_vccnz .LBB0_385
	v_add_u32_e32 v70, s33, v136
	v_ashrrev_i32_e32 v71, 31, v70
	v_lshl_add_u64 v[74:75], v[70:71], 2, s[40:41]
	global_load_dwordx4 v[70:73], v[74:75], off
	s_nop 0
	global_load_dwordx4 v[74:77], v[74:75], off offset:16
	v_mul_f32_e32 v78, 0xbfb8aa3b, v60
	v_mul_f32_e32 v79, 0xbfb8aa3b, v56
	v_exp_f32_e32 v78, v78
	v_mul_f32_e32 v80, 0xbfb8aa3b, v61
	v_exp_f32_e32 v79, v79
	v_mul_f32_e32 v81, 0xbfb8aa3b, v57
	v_exp_f32_e32 v80, v80
	v_exp_f32_e32 v81, v81
	v_mul_f32_e32 v82, 0xbfb8aa3b, v62
	v_add_f32_e32 v78, 1.0, v78
	v_exp_f32_e32 v82, v82
	v_add_f32_e32 v79, 1.0, v79
	v_rcp_f32_e32 v78, v78
	v_add_f32_e32 v80, 1.0, v80
	v_rcp_f32_e32 v79, v79
	v_add_f32_e32 v81, 1.0, v81
	v_rcp_f32_e32 v80, v80
	v_mul_f32_e32 v83, 0xbfb8aa3b, v58
	v_rcp_f32_e32 v81, v81
	v_exp_f32_e32 v83, v83
	v_add_f32_e32 v82, 1.0, v82
	v_rcp_f32_e32 v82, v82
	v_add_f32_e32 v83, 1.0, v83
	v_rcp_f32_e32 v83, v83
	s_waitcnt vmcnt(0)
	v_sub_f32_e32 v84, 1.0, v70
	v_sub_f32_e32 v85, 1.0, v74
	v_fma_f32 v70, v78, v84, v70
	v_sub_f32_e32 v86, 1.0, v71
	v_fma_f32 v74, v79, v85, v74
	v_cmp_gt_f32_e32 vcc, s82, v70
	v_sub_f32_e32 v87, 1.0, v75
	v_fma_f32 v71, v80, v86, v71
	v_cndmask_b32_e64 v78, 0, 32, vcc
	v_cmp_gt_f32_e64 s[14:15], s82, v74
	v_fma_f32 v75, v81, v87, v75
	v_cmp_gt_f32_e64 s[16:17], s82, v71
	v_cndmask_b32_e64 v79, 0, 32, s[14:15]
	v_ldexp_f32 v70, v70, v78
	v_sub_f32_e32 v88, 1.0, v72
	v_cndmask_b32_e64 v80, 0, 32, s[16:17]
	v_cmp_gt_f32_e64 s[18:19], s82, v75
	v_ldexp_f32 v74, v74, v79
	v_log_f32_e32 v70, v70
	v_fma_f32 v72, v82, v88, v72
	v_cndmask_b32_e64 v81, 0, 32, s[18:19]
	v_ldexp_f32 v71, v71, v80
	v_log_f32_e32 v74, v74
	v_cmp_gt_f32_e64 s[20:21], s82, v72
	v_ldexp_f32 v75, v75, v81
	v_log_f32_e32 v71, v71
	v_cndmask_b32_e64 v82, 0, 32, s[20:21]
	v_log_f32_e32 v75, v75
	v_sub_f32_e32 v89, 1.0, v76
	v_ldexp_f32 v72, v72, v82
	v_mul_f32_e32 v82, 0x3f317217, v70
	v_fma_f32 v76, v83, v89, v76
	v_mul_f32_e32 v83, 0x3f317217, v74
	v_fma_f32 v82, v70, s83, -v82
	v_mul_f32_e32 v84, 0x3f317217, v71
	v_fma_f32 v83, v74, s83, -v83
	v_fmac_f32_e32 v82, 0x3377d1cf, v70
	v_cndmask_b32_e32 v78, 0, v167, vcc
	v_mul_f32_e32 v85, 0x3f317217, v75
	v_fma_f32 v84, v71, s83, -v84
	v_fmac_f32_e32 v83, 0x3377d1cf, v74
	v_fmac_f32_e32 v82, 0x3f317217, v70
	v_cmp_lt_f32_e64 vcc, |v70|, s84
	v_fma_f32 v85, v75, s83, -v85
	v_fmac_f32_e32 v84, 0x3377d1cf, v71
	v_fmac_f32_e32 v83, 0x3f317217, v74
	v_cndmask_b32_e32 v70, v70, v82, vcc
	v_cmp_lt_f32_e64 vcc, |v74|, s84
	v_log_f32_e32 v72, v72
	v_fmac_f32_e32 v85, 0x3377d1cf, v75
	v_fmac_f32_e32 v84, 0x3f317217, v71
	v_cndmask_b32_e32 v74, v74, v83, vcc
	v_cmp_lt_f32_e64 vcc, |v71|, s84
	v_cndmask_b32_e64 v79, 0, v167, s[14:15]
	v_fmac_f32_e32 v85, 0x3f317217, v75
	v_cndmask_b32_e32 v71, v71, v84, vcc
	v_cmp_lt_f32_e64 vcc, |v75|, s84
	v_sub_f32_e32 v74, v74, v79
	v_mul_f32_e32 v79, 0xbfb8aa3b, v63
	v_cndmask_b32_e32 v75, v75, v85, vcc
	v_cmp_gt_f32_e32 vcc, s82, v76
	v_sub_f32_e32 v70, v70, v78
	v_exp_f32_e32 v79, v79
	v_cndmask_b32_e64 v78, 0, 32, vcc
	v_mul_f32_e32 v86, 0x3f317217, v72
	v_ldexp_f32 v76, v76, v78
	v_fma_f32 v86, v72, s83, -v86
	v_log_f32_e32 v76, v76
	v_fmac_f32_e32 v86, 0x3377d1cf, v72
	v_fmac_f32_e32 v86, 0x3f317217, v72
	v_cmp_lt_f32_e64 s[14:15], |v72|, s84
	v_add_f32_e32 v79, 1.0, v79
	v_cndmask_b32_e64 v78, 0, v167, s[20:21]
	v_cndmask_b32_e64 v72, v72, v86, s[14:15]
	v_rcp_f32_e32 v79, v79
	v_sub_f32_e32 v72, v72, v78
	v_mul_f32_e32 v78, 0x3f317217, v76
	v_cndmask_b32_e64 v80, 0, v167, s[16:17]
	v_fma_f32 v78, v76, s83, -v78
	v_sub_f32_e32 v71, v71, v80
	v_fmac_f32_e32 v78, 0x3377d1cf, v76
	v_sub_f32_e32 v80, 1.0, v73
	v_fmac_f32_e32 v78, 0x3f317217, v76
	v_cmp_lt_f32_e64 s[14:15], |v76|, s84
	v_fmac_f32_e32 v73, v79, v80
	v_sub_f32_e32 v80, 1.0, v77
	v_cndmask_b32_e64 v76, v76, v78, s[14:15]
	v_cndmask_b32_e32 v78, 0, v167, vcc
	v_cmp_gt_f32_e32 vcc, s82, v73
	v_sub_f32_e32 v76, v76, v78
	v_cndmask_b32_e64 v81, 0, v167, s[18:19]
	v_cndmask_b32_e64 v79, 0, 32, vcc
	v_ldexp_f32 v73, v73, v79
	v_mul_f32_e32 v79, 0xbfb8aa3b, v59
	v_exp_f32_e32 v79, v79
	v_log_f32_e32 v73, v73
	v_sub_f32_e32 v75, v75, v81
	v_cvt_pk_bf16_f32 v70, v70, v71
	v_add_f32_e32 v79, 1.0, v79
	v_rcp_f32_e32 v79, v79
	v_mul_f32_e32 v78, 0x3f317217, v73
	v_fma_f32 v78, v73, s83, -v78
	v_fmac_f32_e32 v78, 0x3377d1cf, v73
	v_fmac_f32_e32 v77, v79, v80
	v_cmp_gt_f32_e64 s[14:15], s82, v77
	v_fmac_f32_e32 v78, 0x3f317217, v73
	v_cmp_lt_f32_e64 s[16:17], |v73|, s84
	v_cndmask_b32_e64 v79, 0, 32, s[14:15]
	v_ldexp_f32 v77, v77, v79
	v_log_f32_e32 v77, v77
	v_cndmask_b32_e64 v73, v73, v78, s[16:17]
	v_cndmask_b32_e32 v78, 0, v167, vcc
	v_sub_f32_e32 v73, v73, v78
	v_mul_f32_e32 v78, 0x3f317217, v77
	v_fma_f32 v78, v77, s83, -v78
	v_fmac_f32_e32 v78, 0x3377d1cf, v77
	v_fmac_f32_e32 v78, 0x3f317217, v77
	v_cmp_lt_f32_e64 vcc, |v77|, s84
	v_cvt_pk_bf16_f32 v71, v72, v73
	v_cvt_pk_bf16_f32 v72, v74, v75
	v_lshl_add_u64 v[74:75], s[38:39], 0, v[64:65]
	s_nop 0
	v_cndmask_b32_e32 v77, v77, v78, vcc
	v_cndmask_b32_e64 v78, 0, v167, s[14:15]
	v_sub_f32_e32 v77, v77, v78
	v_cvt_pk_bf16_f32 v73, v76, v77
	v_lshl_add_u64 v[76:77], s[0:1], 0, v[136:137]
	v_lshl_add_u64 v[74:75], v[76:77], 1, v[74:75]
	global_store_dwordx4 v[74:75], v[70:73], off offset:-2048 sc1

;     __device__ __forceinline__ static u32x4 pack8(const f32x4 a, const f32x4 b) { u32x4 w; w.x = cvt_pk_bf16(a[0], a[1]); w.y = cvt_pk_bf16(a[2], a[3]); w.z = cvt_pk_bf16(b[0], b[1]); w.w = cvt_pk_bf16(b[2], b[3]); return w; }
;     __device__ __forceinline__ static f32x4 silu4(const f32x4 v) { f32x4 o; for (int i = 0; i < 4; ++i) o[i] = v[i] * __builtin_amdgcn_rcpf(1.f + __expf(-v[i])); return o; }
;     __device__ __forceinline__ void operator()(const f32x4 (&acc)[2][2][4][2], const Unit& u, int wr, int wc, int fr, int fq) const {
;     ...
;                     if (pn < 4) { *(u32x4*)(QH + row * 1024 + pn * 256 + c256) = pack8(silu4(v0), silu4(v1)); }
;                     else if (pn < 8) { const int col = (pn - 4) * 256 + c256; const f32x4 l0 = *(const f32x4*)(LB + col), l1 = *(const f32x4*)(LB + col + 4); f32x4 o0, o1;
;                         for (int i = 0; i < 4; ++i) { o0[i] = __logf(l0[i] + (1.f - l0[i]) * __builtin_amdgcn_rcpf(1.f + __expf(-v0[i]))); o1[i] = __logf(l1[i] + (1.f - l1[i]) * __builtin_amdgcn_rcpf(1.f + __expf(-v1[i]))); }
;                         *(u32x4*)(LOGF + row * 1024 + col) = pack8(o0, o1); }
;                     else if (pn < 12) { *(u32x4*)(VH + row * 1024 + (pn - 8) * 256 + c256) = pack8(v0, v1); }
;                     else if (pn < 16) { *(u32x4*)(GH + row * 1024 + (pn - 12) * 256 + c256) = pack8(silu4(v0), silu4(v1)); }
;                     else if (pn < 20) { const float sc = 0.125f * 1.4426950408889634f; *(u32x4*)(QN + row * 1024 + (pn - 16) * 256 + c256) = pack8(v0 * sc, v1 * sc); }
;                     else if (pn < 26) { *(u32x4*)(KV6 + (size_t)(pn - 20) * ((size_t)16384 * 256) + row * 256 + c256) = pack8(v0, v1); }
;                     else if (c256 < 64) { f32x4 o0, o1; for (int i = 0; i < 4; ++i) { o0[i] = __builtin_amdgcn_rcpf(1.f + __expf(-v0[i])); o1[i] = __builtin_amdgcn_rcpf(1.f + __expf(-v1[i])); }
;                         *(f32x4*)(GATE + row * 64 + c256) = o0; *(f32x4*)(GATE + row * 64 + c256 + 4) = o1; } } }
.LBB0_386:
	v_mul_f32_e32 v72, 0xbfb8aa3b, v60
	v_mul_f32_e32 v73, 0xbfb8aa3b, v61
	v_mul_f32_e32 v74, 0xbfb8aa3b, v62
	v_exp_f32_e32 v72, v72
	v_exp_f32_e32 v73, v73
	v_exp_f32_e32 v74, v74
	v_mul_f32_e32 v75, 0xbfb8aa3b, v63
	v_add_f32_e32 v72, 1.0, v72
	v_add_f32_e32 v73, 1.0, v73
	v_add_f32_e32 v74, 1.0, v74
	v_rcp_f32_e32 v72, v72
	v_rcp_f32_e32 v73, v73
	v_rcp_f32_e32 v74, v74
	v_exp_f32_e32 v75, v75
	v_mul_f32_e32 v60, v60, v72
	v_mul_f32_e32 v61, v61, v73
	v_mul_f32_e32 v62, v62, v74
	v_add_f32_e32 v72, 1.0, v75
	v_mul_f32_e32 v73, 0xbfb8aa3b, v56
	v_mul_f32_e32 v74, 0xbfb8aa3b, v57
	v_rcp_f32_e32 v72, v72
	v_exp_f32_e32 v73, v73
	v_exp_f32_e32 v74, v74
	v_mul_f32_e32 v75, 0xbfb8aa3b, v59
	v_mul_f32_e32 v63, v63, v72
	v_add_f32_e32 v72, 1.0, v73
	v_add_f32_e32 v73, 1.0, v74
	v_mul_f32_e32 v74, 0xbfb8aa3b, v58
	v_exp_f32_e32 v75, v75
	v_exp_f32_e32 v74, v74
	v_rcp_f32_e32 v72, v72
	v_rcp_f32_e32 v73, v73
	v_add_f32_e32 v75, 1.0, v75
	v_add_f32_e32 v74, 1.0, v74
	v_rcp_f32_e32 v75, v75
	v_rcp_f32_e32 v74, v74
	v_mul_f32_e32 v72, v56, v72
	v_cvt_pk_bf16_f32 v56, v60, v61
	v_mul_f32_e32 v59, v59, v75
	v_lshl_add_u64 v[60:61], v[136:137], 1, v[70:71]
	v_mul_f32_e32 v73, v57, v73
	v_mul_f32_e32 v74, v58, v74
	v_cvt_pk_bf16_f32 v57, v62, v63
	v_cvt_pk_bf16_f32 v58, v72, v73
	v_cvt_pk_bf16_f32 v59, v74, v59
	global_store_dwordx4 v[60:61], v[56:59], off sc1
	s_and_b64 vcc, exec, s[12:13]
	s_mov_b64 s[14:15], -1
	s_cbranch_vccnz .LBB0_205
.LBB0_387:
	s_and_b64 vcc, exec, s[10:11]
	s_cbranch_vccnz .LBB0_407
	s_andn2_b64 vcc, exec, s[62:63]
	s_cbranch_vccnz .LBB0_404
	s_andn2_b64 vcc, exec, s[60:61]
	s_cbranch_vccnz .LBB0_401
	s_andn2_b64 vcc, exec, s[58:59]
	s_cbranch_vccnz .LBB0_398
	s_andn2_b64 vcc, exec, s[56:57]
	s_cbranch_vccnz .LBB0_395
	s_and_saveexec_b64 s[14:15], s[6:7]
	s_cbranch_execz .LBB0_394
	v_mul_f32_e32 v57, 0xbfb8aa3b, v48
	v_exp_f32_e32 v57, v57
	v_mul_f32_e32 v58, 0xbfb8aa3b, v53
	v_mul_f32_e32 v59, 0xbfb8aa3b, v49
	v_exp_f32_e32 v58, v58
	v_exp_f32_e32 v59, v59
	v_add_f32_e32 v57, 1.0, v57
	v_rcp_f32_e32 v60, v57
	v_add_f32_e32 v57, 1.0, v58
	v_add_f32_e32 v58, 1.0, v59
	v_mul_f32_e32 v59, 0xbfb8aa3b, v54
	v_mul_f32_e32 v61, 0xbfb8aa3b, v50
	v_exp_f32_e32 v59, v59
	v_exp_f32_e32 v62, v61
	v_mul_f32_e32 v56, 0xbfb8aa3b, v52
	v_rcp_f32_e32 v61, v58
	v_add_f32_e32 v58, 1.0, v59
	v_add_f32_e32 v59, 1.0, v62
	v_mul_f32_e32 v62, 0xbfb8aa3b, v55
	v_exp_f32_e32 v56, v56
	v_exp_f32_e32 v63, v62
	v_mul_f32_e32 v62, 0xbfb8aa3b, v51
	v_exp_f32_e32 v72, v62
	v_add_f32_e32 v56, 1.0, v56
	v_rcp_f32_e32 v62, v59
	v_add_f32_e32 v59, 1.0, v63
	v_rcp_f32_e32 v56, v56
	v_rcp_f32_e32 v57, v57
	v_rcp_f32_e32 v58, v58
	v_rcp_f32_e32 v59, v59
	v_add_f32_e32 v63, 1.0, v72
	v_rcp_f32_e32 v63, v63
	v_lshl_add_u64 v[68:69], v[68:69], 2, v[142:143]
	global_store_dwordx4 v[68:69], v[56:59], off sc1
	global_store_dwordx4 v[68:69], v[60:63], off offset:16 sc1

;     __device__ __forceinline__ static u32x4 pack8(const f32x4 a, const f32x4 b) { u32x4 w; w.x = cvt_pk_bf16(a[0], a[1]); w.y = cvt_pk_bf16(a[2], a[3]); w.z = cvt_pk_bf16(b[0], b[1]); w.w = cvt_pk_bf16(b[2], b[3]); return w; }
;     __device__ __forceinline__ void operator()(const f32x4 (&acc)[2][2][4][2], const Unit& u, int wr, int wc, int fr, int fq) const {
;     ...
;                     else if (pn < 26) { *(u32x4*)(KV6 + (size_t)(pn - 20) * ((size_t)16384 * 256) + row * 256 + c256) = pack8(v0, v1); }
.LBB0_395:
	s_andn2_b64 vcc, exec, s[14:15]
	s_cbranch_vccnz .LBB0_397
	s_add_u32 s14, s73, s2
	s_addc_u32 s15, s74, s3
	v_lshl_add_u64 v[60:61], s[14:15], 0, v[66:67]
	v_lshl_add_u64 v[60:61], v[136:137], 1, v[60:61]
	v_cvt_pk_bf16_f32 v56, v52, v53
	v_cvt_pk_bf16_f32 v57, v54, v55
	v_cvt_pk_bf16_f32 v58, v48, v49
	v_cvt_pk_bf16_f32 v59, v50, v51
	global_store_dwordx4 v[60:61], v[56:59], off offset:256 sc1

;     __device__ __forceinline__ static u32x4 pack8(const f32x4 a, const f32x4 b) { u32x4 w; w.x = cvt_pk_bf16(a[0], a[1]); w.y = cvt_pk_bf16(a[2], a[3]); w.z = cvt_pk_bf16(b[0], b[1]); w.w = cvt_pk_bf16(b[2], b[3]); return w; }
;     __device__ __forceinline__ void operator()(const f32x4 (&acc)[2][2][4][2], const Unit& u, int wr, int wc, int fr, int fq) const {
;     ...
;                     else if (pn < 20) { const float sc = 0.125f * 1.4426950408889634f; *(u32x4*)(QN + row * 1024 + (pn - 16) * 256 + c256) = pack8(v0 * sc, v1 * sc); }
.LBB0_398:
	s_andn2_b64 vcc, exec, s[14:15]
	s_cbranch_vccnz .LBB0_400
	v_pk_mul_f32 v[58:59], v[54:55], s[46:47] op_sel_hi:[1,0]
	v_pk_mul_f32 v[56:57], v[52:53], s[46:47] op_sel_hi:[1,0]
	v_pk_mul_f32 v[60:61], v[50:51], s[46:47] op_sel_hi:[1,0]
	v_pk_mul_f32 v[62:63], v[48:49], s[46:47] op_sel_hi:[1,0]
	v_cvt_pk_bf16_f32 v56, v56, v57
	v_cvt_pk_bf16_f32 v57, v58, v59
	s_nop 0
	v_cvt_pk_bf16_f32 v58, v62, v63
	v_cvt_pk_bf16_f32 v59, v60, v61
	v_lshl_add_u64 v[60:61], s[36:37], 0, v[64:65]
	v_lshl_add_u64 v[60:61], s[24:25], 1, v[60:61]
	v_lshl_add_u64 v[60:61], v[138:139], 1, v[60:61]
	v_add_co_u32_e32 v60, vcc, 0xffffe000, v60
	s_nop 1
	v_addc_co_u32_e32 v61, vcc, -1, v61, vcc
	global_store_dwordx4 v[60:61], v[56:59], off sc1

;     __device__ __forceinline__ static u32x4 pack8(const f32x4 a, const f32x4 b) { u32x4 w; w.x = cvt_pk_bf16(a[0], a[1]); w.y = cvt_pk_bf16(a[2], a[3]); w.z = cvt_pk_bf16(b[0], b[1]); w.w = cvt_pk_bf16(b[2], b[3]); return w; }
;     __device__ __forceinline__ static f32x4 silu4(const f32x4 v) { f32x4 o; for (int i = 0; i < 4; ++i) o[i] = v[i] * __builtin_amdgcn_rcpf(1.f + __expf(-v[i])); return o; }
;     __device__ __forceinline__ void operator()(const f32x4 (&acc)[2][2][4][2], const Unit& u, int wr, int wc, int fr, int fq) const {
;     ...
;                     else if (pn < 16) { *(u32x4*)(GH + row * 1024 + (pn - 12) * 256 + c256) = pack8(silu4(v0), silu4(v1)); }
.LBB0_401:
	s_andn2_b64 vcc, exec, s[14:15]
	s_cbranch_vccnz .LBB0_403
	v_mul_f32_e32 v56, 0xbfb8aa3b, v52
	v_mul_f32_e32 v57, 0xbfb8aa3b, v53
	v_mul_f32_e32 v58, 0xbfb8aa3b, v54
	v_mul_f32_e32 v60, 0xbfb8aa3b, v48
	v_mul_f32_e32 v61, 0xbfb8aa3b, v49
	v_exp_f32_e32 v56, v56
	v_exp_f32_e32 v57, v57
	v_exp_f32_e32 v58, v58
	v_mul_f32_e32 v59, 0xbfb8aa3b, v55
	v_exp_f32_e32 v60, v60
	v_exp_f32_e32 v61, v61
	v_exp_f32_e32 v59, v59
	v_add_f32_e32 v56, 1.0, v56
	v_add_f32_e32 v57, 1.0, v57
	v_add_f32_e32 v58, 1.0, v58
	v_add_f32_e32 v60, 1.0, v60
	v_add_f32_e32 v61, 1.0, v61
	v_rcp_f32_e32 v56, v56
	v_rcp_f32_e32 v57, v57
	v_rcp_f32_e32 v58, v58
	v_add_f32_e32 v59, 1.0, v59
	v_rcp_f32_e32 v60, v60
	v_mul_f32_e32 v62, 0xbfb8aa3b, v50
	v_mul_f32_e32 v63, 0xbfb8aa3b, v51
	v_rcp_f32_e32 v61, v61
	v_rcp_f32_e32 v59, v59
	v_exp_f32_e32 v62, v62
	v_exp_f32_e32 v63, v63
	v_mul_f32_e32 v56, v52, v56
	v_mul_f32_e32 v57, v53, v57
	v_mul_f32_e32 v58, v54, v58
	v_mul_f32_e32 v60, v48, v60
	v_mul_f32_e32 v61, v49, v61
	v_mul_f32_e32 v59, v55, v59
	v_add_f32_e32 v62, 1.0, v62
	v_add_f32_e32 v63, 1.0, v63
	v_cvt_pk_bf16_f32 v56, v56, v57
	v_cvt_pk_bf16_f32 v57, v58, v59
	v_cvt_pk_bf16_f32 v58, v60, v61
	v_lshl_add_u64 v[60:61], s[34:35], 0, v[64:65]
	v_rcp_f32_e32 v62, v62
	v_rcp_f32_e32 v63, v63
	v_lshl_add_u64 v[60:61], s[24:25], 1, v[60:61]
	v_lshl_add_u64 v[60:61], v[138:139], 1, v[60:61]
	v_add_co_u32_e32 v60, vcc, 0xfffff000, v60
	v_mul_f32_e32 v62, v50, v62
	s_nop 0
	v_addc_co_u32_e32 v61, vcc, -1, v61, vcc
	v_mul_f32_e32 v63, v51, v63
	v_cvt_pk_bf16_f32 v59, v62, v63
	global_store_dwordx4 v[60:61], v[56:59], off offset:-2048 sc1

;     __device__ __forceinline__ static u32x4 pack8(const f32x4 a, const f32x4 b) { u32x4 w; w.x = cvt_pk_bf16(a[0], a[1]); w.y = cvt_pk_bf16(a[2], a[3]); w.z = cvt_pk_bf16(b[0], b[1]); w.w = cvt_pk_bf16(b[2], b[3]); return w; }
;     __device__ __forceinline__ void operator()(const f32x4 (&acc)[2][2][4][2], const Unit& u, int wr, int wc, int fr, int fq) const {
;     ...
;                     else if (pn < 12) { *(u32x4*)(VH + row * 1024 + (pn - 8) * 256 + c256) = pack8(v0, v1); }
.LBB0_404:
	s_andn2_b64 vcc, exec, s[14:15]
	s_cbranch_vccnz .LBB0_406
	v_lshl_add_u64 v[60:61], s[30:31], 0, v[64:65]
	v_lshl_add_u64 v[60:61], s[24:25], 1, v[60:61]
	v_lshl_add_u64 v[60:61], v[136:137], 1, v[60:61]
	v_cvt_pk_bf16_f32 v56, v52, v53
	v_cvt_pk_bf16_f32 v57, v54, v55
	v_cvt_pk_bf16_f32 v58, v48, v49
	v_cvt_pk_bf16_f32 v59, v50, v51
	global_store_dwordx4 v[60:61], v[56:59], off offset:-3840 sc1

;     __device__ __forceinline__ static u32x4 pack8(const f32x4 a, const f32x4 b) { u32x4 w; w.x = cvt_pk_bf16(a[0], a[1]); w.y = cvt_pk_bf16(a[2], a[3]); w.z = cvt_pk_bf16(b[0], b[1]); w.w = cvt_pk_bf16(b[2], b[3]); return w; }
;     __device__ __forceinline__ void operator()(const f32x4 (&acc)[2][2][4][2], const Unit& u, int wr, int wc, int fr, int fq) const {
;     ...
;                     else if (pn < 8) { const int col = (pn - 4) * 256 + c256; const f32x4 l0 = *(const f32x4*)(LB + col), l1 = *(const f32x4*)(LB + col + 4); f32x4 o0, o1;
;                         for (int i = 0; i < 4; ++i) { o0[i] = __logf(l0[i] + (1.f - l0[i]) * __builtin_amdgcn_rcpf(1.f + __expf(-v0[i]))); o1[i] = __logf(l1[i] + (1.f - l1[i]) * __builtin_amdgcn_rcpf(1.f + __expf(-v1[i]))); }
;                         *(u32x4*)(LOGF + row * 1024 + col) = pack8(o0, o1); }
.LBB0_407:
	s_andn2_b64 vcc, exec, s[14:15]
	s_cbranch_vccnz .LBB0_409
	v_add_u32_e32 v56, s33, v138
	v_ashrrev_i32_e32 v57, 31, v56
	v_lshl_add_u64 v[60:61], v[56:57], 2, s[40:41]
	global_load_dwordx4 v[56:59], v[60:61], off
	s_nop 0
	global_load_dwordx4 v[60:63], v[60:61], off offset:16
	v_mul_f32_e32 v66, 0xbfb8aa3b, v52
	v_mul_f32_e32 v67, 0xbfb8aa3b, v48
	v_exp_f32_e32 v66, v66
	v_mul_f32_e32 v68, 0xbfb8aa3b, v53
	v_exp_f32_e32 v67, v67
	v_mul_f32_e32 v69, 0xbfb8aa3b, v49
	v_exp_f32_e32 v68, v68
	v_exp_f32_e32 v69, v69
	v_mul_f32_e32 v72, 0xbfb8aa3b, v54
	v_add_f32_e32 v66, 1.0, v66
	v_exp_f32_e32 v72, v72
	v_add_f32_e32 v67, 1.0, v67
	v_rcp_f32_e32 v66, v66
	v_add_f32_e32 v68, 1.0, v68
	v_rcp_f32_e32 v67, v67
	v_add_f32_e32 v69, 1.0, v69
	v_rcp_f32_e32 v68, v68
	v_mul_f32_e32 v73, 0xbfb8aa3b, v50
	v_rcp_f32_e32 v69, v69
	v_exp_f32_e32 v73, v73
	v_add_f32_e32 v72, 1.0, v72
	v_rcp_f32_e32 v72, v72
	v_add_f32_e32 v73, 1.0, v73
	v_rcp_f32_e32 v73, v73
	s_waitcnt vmcnt(0)
	v_sub_f32_e32 v74, 1.0, v56
	v_sub_f32_e32 v75, 1.0, v60
	v_fma_f32 v56, v66, v74, v56
	v_sub_f32_e32 v76, 1.0, v57
	v_fma_f32 v60, v67, v75, v60
	v_cmp_gt_f32_e32 vcc, s82, v56
	v_sub_f32_e32 v77, 1.0, v61
	v_fma_f32 v57, v68, v76, v57
	v_cndmask_b32_e64 v66, 0, 32, vcc
	v_cmp_gt_f32_e64 s[14:15], s82, v60
	v_fma_f32 v61, v69, v77, v61
	v_cmp_gt_f32_e64 s[16:17], s82, v57
	v_cndmask_b32_e64 v67, 0, 32, s[14:15]
	v_ldexp_f32 v56, v56, v66
	v_sub_f32_e32 v78, 1.0, v58
	v_cndmask_b32_e64 v68, 0, 32, s[16:17]
	v_cmp_gt_f32_e64 s[18:19], s82, v61
	v_ldexp_f32 v60, v60, v67
	v_log_f32_e32 v56, v56
	v_fma_f32 v58, v72, v78, v58
	v_cndmask_b32_e64 v69, 0, 32, s[18:19]
	v_ldexp_f32 v57, v57, v68
	v_log_f32_e32 v60, v60
	v_cmp_gt_f32_e64 s[20:21], s82, v58
	v_ldexp_f32 v61, v61, v69
	v_log_f32_e32 v57, v57
	v_cndmask_b32_e64 v72, 0, 32, s[20:21]
	v_log_f32_e32 v61, v61
	v_sub_f32_e32 v79, 1.0, v62
	v_ldexp_f32 v58, v58, v72
	v_mul_f32_e32 v72, 0x3f317217, v56
	v_fma_f32 v62, v73, v79, v62
	v_mul_f32_e32 v73, 0x3f317217, v60
	v_fma_f32 v72, v56, s83, -v72
	v_mul_f32_e32 v74, 0x3f317217, v57
	v_fma_f32 v73, v60, s83, -v73
	v_fmac_f32_e32 v72, 0x3377d1cf, v56
	v_cndmask_b32_e32 v66, 0, v167, vcc
	v_mul_f32_e32 v75, 0x3f317217, v61
	v_fma_f32 v74, v57, s83, -v74
	v_fmac_f32_e32 v73, 0x3377d1cf, v60
	v_fmac_f32_e32 v72, 0x3f317217, v56
	v_cmp_lt_f32_e64 vcc, |v56|, s84
	v_fma_f32 v75, v61, s83, -v75
	v_fmac_f32_e32 v74, 0x3377d1cf, v57
	v_fmac_f32_e32 v73, 0x3f317217, v60
	v_cndmask_b32_e32 v56, v56, v72, vcc
	v_cmp_lt_f32_e64 vcc, |v60|, s84
	v_log_f32_e32 v58, v58
	v_fmac_f32_e32 v75, 0x3377d1cf, v61
	v_fmac_f32_e32 v74, 0x3f317217, v57
	v_cndmask_b32_e32 v60, v60, v73, vcc
	v_cmp_lt_f32_e64 vcc, |v57|, s84
	v_cndmask_b32_e64 v67, 0, v167, s[14:15]
	v_fmac_f32_e32 v75, 0x3f317217, v61
	v_cndmask_b32_e32 v57, v57, v74, vcc
	v_cmp_lt_f32_e64 vcc, |v61|, s84
	v_sub_f32_e32 v60, v60, v67
	v_mul_f32_e32 v67, 0xbfb8aa3b, v55
	v_cndmask_b32_e32 v61, v61, v75, vcc
	v_cmp_gt_f32_e32 vcc, s82, v62
	v_sub_f32_e32 v56, v56, v66
	v_exp_f32_e32 v67, v67
	v_cndmask_b32_e64 v66, 0, 32, vcc
	v_mul_f32_e32 v76, 0x3f317217, v58
	v_ldexp_f32 v62, v62, v66
	v_fma_f32 v76, v58, s83, -v76
	v_log_f32_e32 v62, v62
	v_fmac_f32_e32 v76, 0x3377d1cf, v58
	v_fmac_f32_e32 v76, 0x3f317217, v58
	v_cmp_lt_f32_e64 s[14:15], |v58|, s84
	v_add_f32_e32 v67, 1.0, v67
	v_cndmask_b32_e64 v66, 0, v167, s[20:21]
	v_cndmask_b32_e64 v58, v58, v76, s[14:15]
	v_rcp_f32_e32 v67, v67
	v_sub_f32_e32 v58, v58, v66
	v_mul_f32_e32 v66, 0x3f317217, v62
	v_cndmask_b32_e64 v68, 0, v167, s[16:17]
	v_fma_f32 v66, v62, s83, -v66
	v_sub_f32_e32 v57, v57, v68
	v_fmac_f32_e32 v66, 0x3377d1cf, v62
	v_sub_f32_e32 v68, 1.0, v59
	v_fmac_f32_e32 v66, 0x3f317217, v62
	v_cmp_lt_f32_e64 s[14:15], |v62|, s84
	v_fmac_f32_e32 v59, v67, v68
	v_sub_f32_e32 v68, 1.0, v63
	v_cndmask_b32_e64 v62, v62, v66, s[14:15]
	v_cndmask_b32_e32 v66, 0, v167, vcc
	v_cmp_gt_f32_e32 vcc, s82, v59
	v_sub_f32_e32 v62, v62, v66
	v_cndmask_b32_e64 v69, 0, v167, s[18:19]
	v_cndmask_b32_e64 v67, 0, 32, vcc
	v_ldexp_f32 v59, v59, v67
	v_mul_f32_e32 v67, 0xbfb8aa3b, v51
	v_exp_f32_e32 v67, v67
	v_log_f32_e32 v59, v59
	v_sub_f32_e32 v61, v61, v69
	v_cvt_pk_bf16_f32 v56, v56, v57
	v_add_f32_e32 v67, 1.0, v67
	v_rcp_f32_e32 v67, v67
	v_mul_f32_e32 v66, 0x3f317217, v59
	v_fma_f32 v66, v59, s83, -v66
	v_fmac_f32_e32 v66, 0x3377d1cf, v59
	v_fmac_f32_e32 v63, v67, v68
	v_cmp_gt_f32_e64 s[14:15], s82, v63
	v_fmac_f32_e32 v66, 0x3f317217, v59
	v_cmp_lt_f32_e64 s[16:17], |v59|, s84
	v_cndmask_b32_e64 v67, 0, 32, s[14:15]
	v_ldexp_f32 v63, v63, v67
	v_log_f32_e32 v63, v63
	v_cndmask_b32_e64 v59, v59, v66, s[16:17]
	v_cndmask_b32_e32 v66, 0, v167, vcc
	v_sub_f32_e32 v59, v59, v66
	v_mul_f32_e32 v66, 0x3f317217, v63
	v_fma_f32 v66, v63, s83, -v66
	v_fmac_f32_e32 v66, 0x3377d1cf, v63
	v_fmac_f32_e32 v66, 0x3f317217, v63
	v_cmp_lt_f32_e64 vcc, |v63|, s84
	v_cvt_pk_bf16_f32 v57, v58, v59
	v_cvt_pk_bf16_f32 v58, v60, v61
	v_lshl_add_u64 v[60:61], s[38:39], 0, v[64:65]
	s_nop 0
	v_cndmask_b32_e32 v63, v63, v66, vcc
	v_cndmask_b32_e64 v66, 0, v167, s[14:15]
	v_sub_f32_e32 v63, v63, v66
	v_cvt_pk_bf16_f32 v59, v62, v63
	v_lshl_add_u64 v[62:63], s[0:1], 0, v[138:139]
	v_lshl_add_u64 v[60:61], v[62:63], 1, v[60:61]
	global_store_dwordx4 v[60:61], v[56:59], off offset:-2048 sc1

;     __device__ __forceinline__ static u32x4 pack8(const f32x4 a, const f32x4 b) { u32x4 w; w.x = cvt_pk_bf16(a[0], a[1]); w.y = cvt_pk_bf16(a[2], a[3]); w.z = cvt_pk_bf16(b[0], b[1]); w.w = cvt_pk_bf16(b[2], b[3]); return w; }
;     __device__ __forceinline__ static f32x4 silu4(const f32x4 v) { f32x4 o; for (int i = 0; i < 4; ++i) o[i] = v[i] * __builtin_amdgcn_rcpf(1.f + __expf(-v[i])); return o; }
;     __device__ __forceinline__ void operator()(const f32x4 (&acc)[2][2][4][2], const Unit& u, int wr, int wc, int fr, int fq) const {
;     ...
;                 for (int bj = 0; bj < 2; ++bj) { const int c256 = bj * HALF + cl; f32x4 v0 = acc[ai][bj][m][0], v1 = acc[ai][bj][m][1];
;                     if (pn < 4) { *(u32x4*)(QH + row * 1024 + pn * 256 + c256) = pack8(silu4(v0), silu4(v1)); }
;                     else if (pn < 8) { const int col = (pn - 4) * 256 + c256; const f32x4 l0 = *(const f32x4*)(LB + col), l1 = *(const f32x4*)(LB + col + 4); f32x4 o0, o1;
;                         for (int i = 0; i < 4; ++i) { o0[i] = __logf(l0[i] + (1.f - l0[i]) * __builtin_amdgcn_rcpf(1.f + __expf(-v0[i]))); o1[i] = __logf(l1[i] + (1.f - l1[i]) * __builtin_amdgcn_rcpf(1.f + __expf(-v1[i]))); }
;                         *(u32x4*)(LOGF + row * 1024 + col) = pack8(o0, o1); }
;                     else if (pn < 12) { *(u32x4*)(VH + row * 1024 + (pn - 8) * 256 + c256) = pack8(v0, v1); }
;                     else if (pn < 16) { *(u32x4*)(GH + row * 1024 + (pn - 12) * 256 + c256) = pack8(silu4(v0), silu4(v1)); }
;                     else if (pn < 20) { const float sc = 0.125f * 1.4426950408889634f; *(u32x4*)(QN + row * 1024 + (pn - 16) * 256 + c256) = pack8(v0 * sc, v1 * sc); }
;                     else if (pn < 26) { *(u32x4*)(KV6 + (size_t)(pn - 20) * ((size_t)16384 * 256) + row * 256 + c256) = pack8(v0, v1); }
;                     else if (c256 < 64) { f32x4 o0, o1; for (int i = 0; i < 4; ++i) { o0[i] = __builtin_amdgcn_rcpf(1.f + __expf(-v0[i])); o1[i] = __builtin_amdgcn_rcpf(1.f + __expf(-v1[i])); }
;                         *(f32x4*)(GATE + row * 64 + c256) = o0; *(f32x4*)(GATE + row * 64 + c256 + 4) = o1; } } }
.LBB0_410:
	s_and_b64 vcc, exec, s[10:11]
	s_cbranch_vccnz .LBB0_430
	s_andn2_b64 vcc, exec, s[62:63]
	s_cbranch_vccnz .LBB0_427
	s_andn2_b64 vcc, exec, s[60:61]
	s_cbranch_vccnz .LBB0_424
	s_andn2_b64 vcc, exec, s[58:59]
	s_cbranch_vccnz .LBB0_421
	s_andn2_b64 vcc, exec, s[56:57]
	s_cbranch_vccnz .LBB0_418
	s_and_saveexec_b64 s[14:15], s[4:5]
	s_cbranch_execz .LBB0_417
	v_mul_f32_e32 v55, 0xbfb8aa3b, v40
	v_exp_f32_e32 v55, v55
	v_mul_f32_e32 v56, 0xbfb8aa3b, v45
	v_mul_f32_e32 v57, 0xbfb8aa3b, v41
	v_exp_f32_e32 v56, v56
	v_exp_f32_e32 v57, v57
	v_add_f32_e32 v55, 1.0, v55
	v_rcp_f32_e32 v58, v55
	v_add_f32_e32 v55, 1.0, v56
	v_add_f32_e32 v56, 1.0, v57
	v_mul_f32_e32 v57, 0xbfb8aa3b, v46
	v_mul_f32_e32 v59, 0xbfb8aa3b, v42
	v_exp_f32_e32 v57, v57
	v_exp_f32_e32 v60, v59
	v_mul_f32_e32 v54, 0xbfb8aa3b, v44
	v_rcp_f32_e32 v59, v56
	v_add_f32_e32 v56, 1.0, v57
	v_add_f32_e32 v57, 1.0, v60
	v_mul_f32_e32 v60, 0xbfb8aa3b, v47
	v_exp_f32_e32 v54, v54
	v_exp_f32_e32 v61, v60
	v_mul_f32_e32 v60, 0xbfb8aa3b, v43
	v_exp_f32_e32 v62, v60
	v_add_f32_e32 v54, 1.0, v54
	v_rcp_f32_e32 v60, v57
	v_add_f32_e32 v57, 1.0, v61
	v_rcp_f32_e32 v54, v54
	v_rcp_f32_e32 v55, v55
	v_rcp_f32_e32 v56, v56
	v_rcp_f32_e32 v57, v57
	v_add_f32_e32 v61, 1.0, v62
	v_rcp_f32_e32 v61, v61
	v_lshl_add_u64 v[62:63], v[52:53], 2, v[140:141]
	global_store_dwordx4 v[62:63], v[54:57], off sc1
	global_store_dwordx4 v[62:63], v[58:61], off offset:16 sc1

;     __device__ __forceinline__ static u32x4 pack8(const f32x4 a, const f32x4 b) { u32x4 w; w.x = cvt_pk_bf16(a[0], a[1]); w.y = cvt_pk_bf16(a[2], a[3]); w.z = cvt_pk_bf16(b[0], b[1]); w.w = cvt_pk_bf16(b[2], b[3]); return w; }
;     __device__ __forceinline__ void operator()(const f32x4 (&acc)[2][2][4][2], const Unit& u, int wr, int wc, int fr, int fq) const {
;     ...
;                     else if (pn < 26) { *(u32x4*)(KV6 + (size_t)(pn - 20) * ((size_t)16384 * 256) + row * 256 + c256) = pack8(v0, v1); }
.LBB0_418:
	s_andn2_b64 vcc, exec, s[14:15]
	s_cbranch_vccnz .LBB0_420
	s_add_u32 s14, s73, s2
	s_addc_u32 s15, s74, s3
	v_lshl_add_u64 v[58:59], s[14:15], 0, v[50:51]
	v_lshl_add_u64 v[58:59], v[136:137], 1, v[58:59]
	v_cvt_pk_bf16_f32 v54, v44, v45
	v_cvt_pk_bf16_f32 v55, v46, v47
	v_cvt_pk_bf16_f32 v56, v40, v41
	v_cvt_pk_bf16_f32 v57, v42, v43
	global_store_dwordx4 v[58:59], v[54:57], off sc1

;     __device__ __forceinline__ static u32x4 pack8(const f32x4 a, const f32x4 b) { u32x4 w; w.x = cvt_pk_bf16(a[0], a[1]); w.y = cvt_pk_bf16(a[2], a[3]); w.z = cvt_pk_bf16(b[0], b[1]); w.w = cvt_pk_bf16(b[2], b[3]); return w; }
;     __device__ __forceinline__ void operator()(const f32x4 (&acc)[2][2][4][2], const Unit& u, int wr, int wc, int fr, int fq) const {
;     ...
;                     else if (pn < 20) { const float sc = 0.125f * 1.4426950408889634f; *(u32x4*)(QN + row * 1024 + (pn - 16) * 256 + c256) = pack8(v0 * sc, v1 * sc); }
.LBB0_421:
	s_andn2_b64 vcc, exec, s[14:15]
	s_cbranch_vccnz .LBB0_423
	v_pk_mul_f32 v[56:57], v[46:47], s[46:47] op_sel_hi:[1,0]
	v_pk_mul_f32 v[54:55], v[44:45], s[46:47] op_sel_hi:[1,0]
	v_pk_mul_f32 v[58:59], v[42:43], s[46:47] op_sel_hi:[1,0]
	v_pk_mul_f32 v[60:61], v[40:41], s[46:47] op_sel_hi:[1,0]
	v_cvt_pk_bf16_f32 v54, v54, v55
	v_cvt_pk_bf16_f32 v55, v56, v57
	s_nop 0
	v_cvt_pk_bf16_f32 v56, v60, v61
	v_cvt_pk_bf16_f32 v57, v58, v59
	v_lshl_add_u64 v[58:59], s[36:37], 0, v[48:49]
	v_lshl_add_u64 v[58:59], s[24:25], 1, v[58:59]
	v_lshl_add_u64 v[58:59], v[136:137], 1, v[58:59]
	v_add_co_u32_e32 v58, vcc, 0xffffe000, v58
	s_nop 1
	v_addc_co_u32_e32 v59, vcc, -1, v59, vcc
	global_store_dwordx4 v[58:59], v[54:57], off sc1

;     __device__ __forceinline__ static u32x4 pack8(const f32x4 a, const f32x4 b) { u32x4 w; w.x = cvt_pk_bf16(a[0], a[1]); w.y = cvt_pk_bf16(a[2], a[3]); w.z = cvt_pk_bf16(b[0], b[1]); w.w = cvt_pk_bf16(b[2], b[3]); return w; }
;     __device__ __forceinline__ static f32x4 silu4(const f32x4 v) { f32x4 o; for (int i = 0; i < 4; ++i) o[i] = v[i] * __builtin_amdgcn_rcpf(1.f + __expf(-v[i])); return o; }
;     __device__ __forceinline__ void operator()(const f32x4 (&acc)[2][2][4][2], const Unit& u, int wr, int wc, int fr, int fq) const {
;     ...
;                     else if (pn < 16) { *(u32x4*)(GH + row * 1024 + (pn - 12) * 256 + c256) = pack8(silu4(v0), silu4(v1)); }
.LBB0_424:
	s_andn2_b64 vcc, exec, s[14:15]
	s_cbranch_vccnz .LBB0_426
	v_mul_f32_e32 v54, 0xbfb8aa3b, v44
	v_mul_f32_e32 v55, 0xbfb8aa3b, v45
	v_mul_f32_e32 v56, 0xbfb8aa3b, v46
	v_mul_f32_e32 v58, 0xbfb8aa3b, v40
	v_mul_f32_e32 v59, 0xbfb8aa3b, v41
	v_exp_f32_e32 v54, v54
	v_exp_f32_e32 v55, v55
	v_exp_f32_e32 v56, v56
	v_mul_f32_e32 v57, 0xbfb8aa3b, v47
	v_exp_f32_e32 v58, v58
	v_exp_f32_e32 v59, v59
	v_exp_f32_e32 v57, v57
	v_add_f32_e32 v54, 1.0, v54
	v_add_f32_e32 v55, 1.0, v55
	v_add_f32_e32 v56, 1.0, v56
	v_add_f32_e32 v58, 1.0, v58
	v_add_f32_e32 v59, 1.0, v59
	v_rcp_f32_e32 v54, v54
	v_rcp_f32_e32 v55, v55
	v_rcp_f32_e32 v56, v56
	v_add_f32_e32 v57, 1.0, v57
	v_rcp_f32_e32 v58, v58
	v_mul_f32_e32 v60, 0xbfb8aa3b, v42
	v_mul_f32_e32 v61, 0xbfb8aa3b, v43
	v_rcp_f32_e32 v59, v59
	v_rcp_f32_e32 v57, v57
	v_exp_f32_e32 v60, v60
	v_exp_f32_e32 v61, v61
	v_mul_f32_e32 v54, v44, v54
	v_mul_f32_e32 v55, v45, v55
	v_mul_f32_e32 v56, v46, v56
	v_mul_f32_e32 v58, v40, v58
	v_mul_f32_e32 v59, v41, v59
	v_mul_f32_e32 v57, v47, v57
	v_add_f32_e32 v60, 1.0, v60
	v_add_f32_e32 v61, 1.0, v61
	v_cvt_pk_bf16_f32 v54, v54, v55
	v_cvt_pk_bf16_f32 v55, v56, v57
	v_cvt_pk_bf16_f32 v56, v58, v59
	v_lshl_add_u64 v[58:59], s[34:35], 0, v[48:49]
	v_rcp_f32_e32 v60, v60
	v_rcp_f32_e32 v61, v61
	v_lshl_add_u64 v[58:59], s[24:25], 1, v[58:59]
	v_lshl_add_u64 v[58:59], v[136:137], 1, v[58:59]
	v_add_co_u32_e32 v58, vcc, 0xfffff000, v58
	v_mul_f32_e32 v60, v42, v60
	s_nop 0
	v_addc_co_u32_e32 v59, vcc, -1, v59, vcc
	v_mul_f32_e32 v61, v43, v61
	v_cvt_pk_bf16_f32 v57, v60, v61
	global_store_dwordx4 v[58:59], v[54:57], off offset:-2048 sc1

;     __device__ __forceinline__ static u32x4 pack8(const f32x4 a, const f32x4 b) { u32x4 w; w.x = cvt_pk_bf16(a[0], a[1]); w.y = cvt_pk_bf16(a[2], a[3]); w.z = cvt_pk_bf16(b[0], b[1]); w.w = cvt_pk_bf16(b[2], b[3]); return w; }
;     __device__ __forceinline__ void operator()(const f32x4 (&acc)[2][2][4][2], const Unit& u, int wr, int wc, int fr, int fq) const {
;     ...
;                     else if (pn < 12) { *(u32x4*)(VH + row * 1024 + (pn - 8) * 256 + c256) = pack8(v0, v1); }
.LBB0_427:
	s_andn2_b64 vcc, exec, s[14:15]
	s_cbranch_vccnz .LBB0_429
	v_lshl_add_u64 v[58:59], s[30:31], 0, v[48:49]
	v_lshl_add_u64 v[58:59], s[24:25], 1, v[58:59]
	v_lshl_add_u64 v[58:59], v[136:137], 1, v[58:59]
	v_cvt_pk_bf16_f32 v54, v44, v45
	v_cvt_pk_bf16_f32 v55, v46, v47
	v_cvt_pk_bf16_f32 v56, v40, v41
	v_cvt_pk_bf16_f32 v57, v42, v43
	global_store_dwordx4 v[58:59], v[54:57], off offset:-4096 sc1

;     __device__ __forceinline__ static u32x4 pack8(const f32x4 a, const f32x4 b) { u32x4 w; w.x = cvt_pk_bf16(a[0], a[1]); w.y = cvt_pk_bf16(a[2], a[3]); w.z = cvt_pk_bf16(b[0], b[1]); w.w = cvt_pk_bf16(b[2], b[3]); return w; }
;     __device__ __forceinline__ void operator()(const f32x4 (&acc)[2][2][4][2], const Unit& u, int wr, int wc, int fr, int fq) const {
;     ...
;                     else if (pn < 8) { const int col = (pn - 4) * 256 + c256; const f32x4 l0 = *(const f32x4*)(LB + col), l1 = *(const f32x4*)(LB + col + 4); f32x4 o0, o1;
;                         for (int i = 0; i < 4; ++i) { o0[i] = __logf(l0[i] + (1.f - l0[i]) * __builtin_amdgcn_rcpf(1.f + __expf(-v0[i]))); o1[i] = __logf(l1[i] + (1.f - l1[i]) * __builtin_amdgcn_rcpf(1.f + __expf(-v1[i]))); }
;                         *(u32x4*)(LOGF + row * 1024 + col) = pack8(o0, o1); }
.LBB0_430:
	s_andn2_b64 vcc, exec, s[14:15]
	s_cbranch_vccnz .LBB0_432
	v_add_u32_e32 v54, s33, v136
	v_ashrrev_i32_e32 v55, 31, v54
	v_lshl_add_u64 v[58:59], v[54:55], 2, s[40:41]
	global_load_dwordx4 v[54:57], v[58:59], off
	s_nop 0
	global_load_dwordx4 v[58:61], v[58:59], off offset:16
	v_mul_f32_e32 v62, 0xbfb8aa3b, v44
	v_mul_f32_e32 v63, 0xbfb8aa3b, v40
	v_exp_f32_e32 v62, v62
	v_mul_f32_e32 v64, 0xbfb8aa3b, v45
	v_exp_f32_e32 v63, v63
	v_mul_f32_e32 v65, 0xbfb8aa3b, v41
	v_exp_f32_e32 v64, v64
	v_exp_f32_e32 v65, v65
	v_mul_f32_e32 v66, 0xbfb8aa3b, v46
	v_add_f32_e32 v62, 1.0, v62
	v_exp_f32_e32 v66, v66
	v_add_f32_e32 v63, 1.0, v63
	v_rcp_f32_e32 v62, v62
	v_add_f32_e32 v64, 1.0, v64
	v_rcp_f32_e32 v63, v63
	v_add_f32_e32 v65, 1.0, v65
	v_rcp_f32_e32 v64, v64
	v_mul_f32_e32 v67, 0xbfb8aa3b, v42
	v_rcp_f32_e32 v65, v65
	v_exp_f32_e32 v67, v67
	v_add_f32_e32 v66, 1.0, v66
	v_rcp_f32_e32 v66, v66
	v_add_f32_e32 v67, 1.0, v67
	v_rcp_f32_e32 v67, v67
	s_waitcnt vmcnt(0)
	v_sub_f32_e32 v68, 1.0, v54
	v_sub_f32_e32 v69, 1.0, v58
	v_fma_f32 v54, v62, v68, v54
	v_sub_f32_e32 v70, 1.0, v55
	v_fma_f32 v58, v63, v69, v58
	v_cmp_gt_f32_e32 vcc, s82, v54
	v_sub_f32_e32 v71, 1.0, v59
	v_fma_f32 v55, v64, v70, v55
	v_cndmask_b32_e64 v62, 0, 32, vcc
	v_cmp_gt_f32_e64 s[14:15], s82, v58
	v_fma_f32 v59, v65, v71, v59
	v_cmp_gt_f32_e64 s[16:17], s82, v55
	v_cndmask_b32_e64 v63, 0, 32, s[14:15]
	v_ldexp_f32 v54, v54, v62
	v_sub_f32_e32 v72, 1.0, v56
	v_cndmask_b32_e64 v64, 0, 32, s[16:17]
	v_cmp_gt_f32_e64 s[18:19], s82, v59
	v_ldexp_f32 v58, v58, v63
	v_log_f32_e32 v54, v54
	v_fma_f32 v56, v66, v72, v56
	v_cndmask_b32_e64 v65, 0, 32, s[18:19]
	v_ldexp_f32 v55, v55, v64
	v_log_f32_e32 v58, v58
	v_cmp_gt_f32_e64 s[20:21], s82, v56
	v_ldexp_f32 v59, v59, v65
	v_log_f32_e32 v55, v55
	v_cndmask_b32_e64 v66, 0, 32, s[20:21]
	v_log_f32_e32 v59, v59
	v_sub_f32_e32 v73, 1.0, v60
	v_ldexp_f32 v56, v56, v66
	v_mul_f32_e32 v66, 0x3f317217, v54
	v_fma_f32 v60, v67, v73, v60
	v_mul_f32_e32 v67, 0x3f317217, v58
	v_fma_f32 v66, v54, s83, -v66
	v_mul_f32_e32 v68, 0x3f317217, v55
	v_fma_f32 v67, v58, s83, -v67
	v_fmac_f32_e32 v66, 0x3377d1cf, v54
	v_cndmask_b32_e32 v62, 0, v167, vcc
	v_mul_f32_e32 v69, 0x3f317217, v59
	v_fma_f32 v68, v55, s83, -v68
	v_fmac_f32_e32 v67, 0x3377d1cf, v58
	v_fmac_f32_e32 v66, 0x3f317217, v54
	v_cmp_lt_f32_e64 vcc, |v54|, s84
	v_fma_f32 v69, v59, s83, -v69
	v_fmac_f32_e32 v68, 0x3377d1cf, v55
	v_fmac_f32_e32 v67, 0x3f317217, v58
	v_cndmask_b32_e32 v54, v54, v66, vcc
	v_cmp_lt_f32_e64 vcc, |v58|, s84
	v_log_f32_e32 v56, v56
	v_fmac_f32_e32 v69, 0x3377d1cf, v59
	v_fmac_f32_e32 v68, 0x3f317217, v55
	v_cndmask_b32_e32 v58, v58, v67, vcc
	v_cmp_lt_f32_e64 vcc, |v55|, s84
	v_cndmask_b32_e64 v63, 0, v167, s[14:15]
	v_fmac_f32_e32 v69, 0x3f317217, v59
	v_cndmask_b32_e32 v55, v55, v68, vcc
	v_cmp_lt_f32_e64 vcc, |v59|, s84
	v_sub_f32_e32 v58, v58, v63
	v_mul_f32_e32 v63, 0xbfb8aa3b, v47
	v_cndmask_b32_e32 v59, v59, v69, vcc
	v_cmp_gt_f32_e32 vcc, s82, v60
	v_sub_f32_e32 v54, v54, v62
	v_exp_f32_e32 v63, v63
	v_cndmask_b32_e64 v62, 0, 32, vcc
	v_mul_f32_e32 v70, 0x3f317217, v56
	v_ldexp_f32 v60, v60, v62
	v_fma_f32 v70, v56, s83, -v70
	v_log_f32_e32 v60, v60
	v_fmac_f32_e32 v70, 0x3377d1cf, v56
	v_fmac_f32_e32 v70, 0x3f317217, v56
	v_cmp_lt_f32_e64 s[14:15], |v56|, s84
	v_add_f32_e32 v63, 1.0, v63
	v_cndmask_b32_e64 v62, 0, v167, s[20:21]
	v_cndmask_b32_e64 v56, v56, v70, s[14:15]
	v_rcp_f32_e32 v63, v63
	v_sub_f32_e32 v56, v56, v62
	v_mul_f32_e32 v62, 0x3f317217, v60
	v_cndmask_b32_e64 v64, 0, v167, s[16:17]
	v_fma_f32 v62, v60, s83, -v62
	v_sub_f32_e32 v55, v55, v64
	v_fmac_f32_e32 v62, 0x3377d1cf, v60
	v_sub_f32_e32 v64, 1.0, v57
	v_fmac_f32_e32 v62, 0x3f317217, v60
	v_cmp_lt_f32_e64 s[14:15], |v60|, s84
	v_fmac_f32_e32 v57, v63, v64
	v_sub_f32_e32 v64, 1.0, v61
	v_cndmask_b32_e64 v60, v60, v62, s[14:15]
	v_cndmask_b32_e32 v62, 0, v167, vcc
	v_cmp_gt_f32_e32 vcc, s82, v57
	v_sub_f32_e32 v60, v60, v62
	v_cndmask_b32_e64 v65, 0, v167, s[18:19]
	v_cndmask_b32_e64 v63, 0, 32, vcc
	v_ldexp_f32 v57, v57, v63
	v_mul_f32_e32 v63, 0xbfb8aa3b, v43
	v_exp_f32_e32 v63, v63
	v_log_f32_e32 v57, v57
	v_sub_f32_e32 v59, v59, v65
	v_cvt_pk_bf16_f32 v54, v54, v55
	v_add_f32_e32 v63, 1.0, v63
	v_rcp_f32_e32 v63, v63
	v_mul_f32_e32 v62, 0x3f317217, v57
	v_fma_f32 v62, v57, s83, -v62
	v_fmac_f32_e32 v62, 0x3377d1cf, v57
	v_fmac_f32_e32 v61, v63, v64
	v_cmp_gt_f32_e64 s[14:15], s82, v61
	v_fmac_f32_e32 v62, 0x3f317217, v57
	v_cmp_lt_f32_e64 s[16:17], |v57|, s84
	v_cndmask_b32_e64 v63, 0, 32, s[14:15]
	v_ldexp_f32 v61, v61, v63
	v_log_f32_e32 v61, v61
	v_cndmask_b32_e64 v57, v57, v62, s[16:17]
	v_cndmask_b32_e32 v62, 0, v167, vcc
	v_sub_f32_e32 v57, v57, v62
	v_mul_f32_e32 v62, 0x3f317217, v61
	v_fma_f32 v62, v61, s83, -v62
	v_fmac_f32_e32 v62, 0x3377d1cf, v61
	v_fmac_f32_e32 v62, 0x3f317217, v61
	v_cmp_lt_f32_e64 vcc, |v61|, s84
	v_cvt_pk_bf16_f32 v55, v56, v57
	v_cvt_pk_bf16_f32 v56, v58, v59
	v_lshl_add_u64 v[58:59], s[38:39], 0, v[48:49]
	s_nop 0
	v_cndmask_b32_e32 v61, v61, v62, vcc
	v_cndmask_b32_e64 v62, 0, v167, s[14:15]
	v_sub_f32_e32 v61, v61, v62
	v_cvt_pk_bf16_f32 v57, v60, v61
	v_lshl_add_u64 v[60:61], s[0:1], 0, v[136:137]
	v_lshl_add_u64 v[58:59], v[60:61], 1, v[58:59]
	global_store_dwordx4 v[58:59], v[54:57], off offset:-2048 sc1

;     __device__ __forceinline__ static u32x4 pack8(const f32x4 a, const f32x4 b) { u32x4 w; w.x = cvt_pk_bf16(a[0], a[1]); w.y = cvt_pk_bf16(a[2], a[3]); w.z = cvt_pk_bf16(b[0], b[1]); w.w = cvt_pk_bf16(b[2], b[3]); return w; }
;     __device__ __forceinline__ static f32x4 silu4(const f32x4 v) { f32x4 o; for (int i = 0; i < 4; ++i) o[i] = v[i] * __builtin_amdgcn_rcpf(1.f + __expf(-v[i])); return o; }
;     __device__ __forceinline__ void operator()(const f32x4 (&acc)[2][2][4][2], const Unit& u, int wr, int wc, int fr, int fq) const {
;     ...
;                     if (pn < 4) { *(u32x4*)(QH + row * 1024 + pn * 256 + c256) = pack8(silu4(v0), silu4(v1)); }
;                     else if (pn < 8) { const int col = (pn - 4) * 256 + c256; const f32x4 l0 = *(const f32x4*)(LB + col), l1 = *(const f32x4*)(LB + col + 4); f32x4 o0, o1;
;                         for (int i = 0; i < 4; ++i) { o0[i] = __logf(l0[i] + (1.f - l0[i]) * __builtin_amdgcn_rcpf(1.f + __expf(-v0[i]))); o1[i] = __logf(l1[i] + (1.f - l1[i]) * __builtin_amdgcn_rcpf(1.f + __expf(-v1[i]))); }
;                         *(u32x4*)(LOGF + row * 1024 + col) = pack8(o0, o1); }
;                     else if (pn < 12) { *(u32x4*)(VH + row * 1024 + (pn - 8) * 256 + c256) = pack8(v0, v1); }
;                     else if (pn < 16) { *(u32x4*)(GH + row * 1024 + (pn - 12) * 256 + c256) = pack8(silu4(v0), silu4(v1)); }
;                     else if (pn < 20) { const float sc = 0.125f * 1.4426950408889634f; *(u32x4*)(QN + row * 1024 + (pn - 16) * 256 + c256) = pack8(v0 * sc, v1 * sc); }
;                     else if (pn < 26) { *(u32x4*)(KV6 + (size_t)(pn - 20) * ((size_t)16384 * 256) + row * 256 + c256) = pack8(v0, v1); }
;                     else if (c256 < 64) { f32x4 o0, o1; for (int i = 0; i < 4; ++i) { o0[i] = __builtin_amdgcn_rcpf(1.f + __expf(-v0[i])); o1[i] = __builtin_amdgcn_rcpf(1.f + __expf(-v1[i])); }
;                         *(f32x4*)(GATE + row * 64 + c256) = o0; *(f32x4*)(GATE + row * 64 + c256 + 4) = o1; } } }
.LBB0_433:
	v_mul_f32_e32 v56, 0xbfb8aa3b, v44
	v_mul_f32_e32 v57, 0xbfb8aa3b, v45
	v_mul_f32_e32 v58, 0xbfb8aa3b, v46
	v_exp_f32_e32 v56, v56
	v_exp_f32_e32 v57, v57
	v_exp_f32_e32 v58, v58
	v_mul_f32_e32 v59, 0xbfb8aa3b, v47
	v_add_f32_e32 v56, 1.0, v56
	v_add_f32_e32 v57, 1.0, v57
	v_add_f32_e32 v58, 1.0, v58
	v_rcp_f32_e32 v56, v56
	v_rcp_f32_e32 v57, v57
	v_rcp_f32_e32 v58, v58
	v_exp_f32_e32 v59, v59
	v_mul_f32_e32 v44, v44, v56
	v_mul_f32_e32 v45, v45, v57
	v_mul_f32_e32 v46, v46, v58
	v_add_f32_e32 v56, 1.0, v59
	v_mul_f32_e32 v57, 0xbfb8aa3b, v40
	v_mul_f32_e32 v58, 0xbfb8aa3b, v41
	v_rcp_f32_e32 v56, v56
	v_exp_f32_e32 v57, v57
	v_exp_f32_e32 v58, v58
	v_mul_f32_e32 v59, 0xbfb8aa3b, v43
	v_mul_f32_e32 v47, v47, v56
	v_add_f32_e32 v56, 1.0, v57
	v_add_f32_e32 v57, 1.0, v58
	v_mul_f32_e32 v58, 0xbfb8aa3b, v42
	v_exp_f32_e32 v59, v59
	v_exp_f32_e32 v58, v58
	v_rcp_f32_e32 v56, v56
	v_rcp_f32_e32 v57, v57
	v_add_f32_e32 v59, 1.0, v59
	v_add_f32_e32 v58, 1.0, v58
	v_rcp_f32_e32 v59, v59
	v_rcp_f32_e32 v58, v58
	v_mul_f32_e32 v56, v40, v56
	v_cvt_pk_bf16_f32 v40, v44, v45
	v_mul_f32_e32 v43, v43, v59
	v_lshl_add_u64 v[44:45], v[136:137], 1, v[54:55]
	v_mul_f32_e32 v57, v41, v57
	v_mul_f32_e32 v58, v42, v58
	v_cvt_pk_bf16_f32 v41, v46, v47
	v_cvt_pk_bf16_f32 v42, v56, v57
	v_cvt_pk_bf16_f32 v43, v58, v43
	global_store_dwordx4 v[44:45], v[40:43], off sc1
	s_and_b64 vcc, exec, s[12:13]
	s_mov_b64 s[14:15], -1
	s_cbranch_vccnz .LBB0_210
.LBB0_434:
	s_and_b64 vcc, exec, s[10:11]
	s_cbranch_vccnz .LBB0_454
	s_andn2_b64 vcc, exec, s[62:63]
	s_cbranch_vccnz .LBB0_451
	s_andn2_b64 vcc, exec, s[60:61]
	s_cbranch_vccnz .LBB0_448
	s_andn2_b64 vcc, exec, s[58:59]
	s_cbranch_vccnz .LBB0_445
	s_andn2_b64 vcc, exec, s[56:57]
	s_cbranch_vccnz .LBB0_442
	s_and_saveexec_b64 s[14:15], s[6:7]
	s_cbranch_execz .LBB0_441
	v_mul_f32_e32 v41, 0xbfb8aa3b, v32
	v_exp_f32_e32 v41, v41
	v_mul_f32_e32 v42, 0xbfb8aa3b, v37
	v_mul_f32_e32 v43, 0xbfb8aa3b, v33
	v_exp_f32_e32 v42, v42
	v_exp_f32_e32 v43, v43
	v_add_f32_e32 v41, 1.0, v41
	v_rcp_f32_e32 v44, v41
	v_add_f32_e32 v41, 1.0, v42
	v_add_f32_e32 v42, 1.0, v43
	v_mul_f32_e32 v43, 0xbfb8aa3b, v38
	v_mul_f32_e32 v45, 0xbfb8aa3b, v34
	v_exp_f32_e32 v43, v43
	v_exp_f32_e32 v46, v45
	v_mul_f32_e32 v40, 0xbfb8aa3b, v36
	v_rcp_f32_e32 v45, v42
	v_add_f32_e32 v42, 1.0, v43
	v_add_f32_e32 v43, 1.0, v46
	v_mul_f32_e32 v46, 0xbfb8aa3b, v39
	v_exp_f32_e32 v40, v40
	v_exp_f32_e32 v47, v46
	v_mul_f32_e32 v46, 0xbfb8aa3b, v35
	v_exp_f32_e32 v56, v46
	v_add_f32_e32 v40, 1.0, v40
	v_rcp_f32_e32 v46, v43
	v_add_f32_e32 v43, 1.0, v47
	v_rcp_f32_e32 v40, v40
	v_rcp_f32_e32 v41, v41
	v_rcp_f32_e32 v42, v42
	v_rcp_f32_e32 v43, v43
	v_add_f32_e32 v47, 1.0, v56
	v_rcp_f32_e32 v47, v47
	v_lshl_add_u64 v[52:53], v[52:53], 2, v[142:143]
	global_store_dwordx4 v[52:53], v[40:43], off sc1
	global_store_dwordx4 v[52:53], v[44:47], off offset:16 sc1

;     __device__ __forceinline__ static u32x4 pack8(const f32x4 a, const f32x4 b) { u32x4 w; w.x = cvt_pk_bf16(a[0], a[1]); w.y = cvt_pk_bf16(a[2], a[3]); w.z = cvt_pk_bf16(b[0], b[1]); w.w = cvt_pk_bf16(b[2], b[3]); return w; }
;     __device__ __forceinline__ void operator()(const f32x4 (&acc)[2][2][4][2], const Unit& u, int wr, int wc, int fr, int fq) const {
;     ...
;                     else if (pn < 26) { *(u32x4*)(KV6 + (size_t)(pn - 20) * ((size_t)16384 * 256) + row * 256 + c256) = pack8(v0, v1); }
.LBB0_442:
	s_andn2_b64 vcc, exec, s[14:15]
	s_cbranch_vccnz .LBB0_444
	s_add_u32 s14, s73, s2
	s_addc_u32 s15, s74, s3
	v_lshl_add_u64 v[44:45], s[14:15], 0, v[50:51]
	v_lshl_add_u64 v[44:45], v[136:137], 1, v[44:45]
	v_cvt_pk_bf16_f32 v40, v36, v37
	v_cvt_pk_bf16_f32 v41, v38, v39
	v_cvt_pk_bf16_f32 v42, v32, v33
	v_cvt_pk_bf16_f32 v43, v34, v35
	global_store_dwordx4 v[44:45], v[40:43], off offset:256 sc1

;     __device__ __forceinline__ static u32x4 pack8(const f32x4 a, const f32x4 b) { u32x4 w; w.x = cvt_pk_bf16(a[0], a[1]); w.y = cvt_pk_bf16(a[2], a[3]); w.z = cvt_pk_bf16(b[0], b[1]); w.w = cvt_pk_bf16(b[2], b[3]); return w; }
;     __device__ __forceinline__ void operator()(const f32x4 (&acc)[2][2][4][2], const Unit& u, int wr, int wc, int fr, int fq) const {
;     ...
;                     else if (pn < 20) { const float sc = 0.125f * 1.4426950408889634f; *(u32x4*)(QN + row * 1024 + (pn - 16) * 256 + c256) = pack8(v0 * sc, v1 * sc); }
.LBB0_445:
	s_andn2_b64 vcc, exec, s[14:15]
	s_cbranch_vccnz .LBB0_447
	v_pk_mul_f32 v[42:43], v[38:39], s[46:47] op_sel_hi:[1,0]
	v_pk_mul_f32 v[40:41], v[36:37], s[46:47] op_sel_hi:[1,0]
	v_pk_mul_f32 v[44:45], v[34:35], s[46:47] op_sel_hi:[1,0]
	v_pk_mul_f32 v[46:47], v[32:33], s[46:47] op_sel_hi:[1,0]
	v_cvt_pk_bf16_f32 v40, v40, v41
	v_cvt_pk_bf16_f32 v41, v42, v43
	s_nop 0
	v_cvt_pk_bf16_f32 v42, v46, v47
	v_cvt_pk_bf16_f32 v43, v44, v45
	v_lshl_add_u64 v[44:45], s[36:37], 0, v[48:49]
	v_lshl_add_u64 v[44:45], s[24:25], 1, v[44:45]
	v_lshl_add_u64 v[44:45], v[138:139], 1, v[44:45]
	v_add_co_u32_e32 v44, vcc, 0xffffe000, v44
	s_nop 1
	v_addc_co_u32_e32 v45, vcc, -1, v45, vcc
	global_store_dwordx4 v[44:45], v[40:43], off sc1

;     __device__ __forceinline__ static u32x4 pack8(const f32x4 a, const f32x4 b) { u32x4 w; w.x = cvt_pk_bf16(a[0], a[1]); w.y = cvt_pk_bf16(a[2], a[3]); w.z = cvt_pk_bf16(b[0], b[1]); w.w = cvt_pk_bf16(b[2], b[3]); return w; }
;     __device__ __forceinline__ static f32x4 silu4(const f32x4 v) { f32x4 o; for (int i = 0; i < 4; ++i) o[i] = v[i] * __builtin_amdgcn_rcpf(1.f + __expf(-v[i])); return o; }
;     __device__ __forceinline__ void operator()(const f32x4 (&acc)[2][2][4][2], const Unit& u, int wr, int wc, int fr, int fq) const {
;     ...
;                     else if (pn < 16) { *(u32x4*)(GH + row * 1024 + (pn - 12) * 256 + c256) = pack8(silu4(v0), silu4(v1)); }
.LBB0_448:
	s_andn2_b64 vcc, exec, s[14:15]
	s_cbranch_vccnz .LBB0_450
	v_mul_f32_e32 v40, 0xbfb8aa3b, v36
	v_mul_f32_e32 v41, 0xbfb8aa3b, v37
	v_mul_f32_e32 v42, 0xbfb8aa3b, v38
	v_mul_f32_e32 v44, 0xbfb8aa3b, v32
	v_mul_f32_e32 v45, 0xbfb8aa3b, v33
	v_exp_f32_e32 v40, v40
	v_exp_f32_e32 v41, v41
	v_exp_f32_e32 v42, v42
	v_mul_f32_e32 v43, 0xbfb8aa3b, v39
	v_exp_f32_e32 v44, v44
	v_exp_f32_e32 v45, v45
	v_exp_f32_e32 v43, v43
	v_add_f32_e32 v40, 1.0, v40
	v_add_f32_e32 v41, 1.0, v41
	v_add_f32_e32 v42, 1.0, v42
	v_add_f32_e32 v44, 1.0, v44
	v_add_f32_e32 v45, 1.0, v45
	v_rcp_f32_e32 v40, v40
	v_rcp_f32_e32 v41, v41
	v_rcp_f32_e32 v42, v42
	v_add_f32_e32 v43, 1.0, v43
	v_rcp_f32_e32 v44, v44
	v_mul_f32_e32 v46, 0xbfb8aa3b, v34
	v_mul_f32_e32 v47, 0xbfb8aa3b, v35
	v_rcp_f32_e32 v45, v45
	v_rcp_f32_e32 v43, v43
	v_exp_f32_e32 v46, v46
	v_exp_f32_e32 v47, v47
	v_mul_f32_e32 v40, v36, v40
	v_mul_f32_e32 v41, v37, v41
	v_mul_f32_e32 v42, v38, v42
	v_mul_f32_e32 v44, v32, v44
	v_mul_f32_e32 v45, v33, v45
	v_mul_f32_e32 v43, v39, v43
	v_add_f32_e32 v46, 1.0, v46
	v_add_f32_e32 v47, 1.0, v47
	v_cvt_pk_bf16_f32 v40, v40, v41
	v_cvt_pk_bf16_f32 v41, v42, v43
	v_cvt_pk_bf16_f32 v42, v44, v45
	v_lshl_add_u64 v[44:45], s[34:35], 0, v[48:49]
	v_rcp_f32_e32 v46, v46
	v_rcp_f32_e32 v47, v47
	v_lshl_add_u64 v[44:45], s[24:25], 1, v[44:45]
	v_lshl_add_u64 v[44:45], v[138:139], 1, v[44:45]
	v_add_co_u32_e32 v44, vcc, 0xfffff000, v44
	v_mul_f32_e32 v46, v34, v46
	s_nop 0
	v_addc_co_u32_e32 v45, vcc, -1, v45, vcc
	v_mul_f32_e32 v47, v35, v47
	v_cvt_pk_bf16_f32 v43, v46, v47
	global_store_dwordx4 v[44:45], v[40:43], off offset:-2048 sc1

;     __device__ __forceinline__ static u32x4 pack8(const f32x4 a, const f32x4 b) { u32x4 w; w.x = cvt_pk_bf16(a[0], a[1]); w.y = cvt_pk_bf16(a[2], a[3]); w.z = cvt_pk_bf16(b[0], b[1]); w.w = cvt_pk_bf16(b[2], b[3]); return w; }
;     __device__ __forceinline__ void operator()(const f32x4 (&acc)[2][2][4][2], const Unit& u, int wr, int wc, int fr, int fq) const {
;     ...
;                     else if (pn < 12) { *(u32x4*)(VH + row * 1024 + (pn - 8) * 256 + c256) = pack8(v0, v1); }
.LBB0_451:
	s_andn2_b64 vcc, exec, s[14:15]
	s_cbranch_vccnz .LBB0_453
	v_lshl_add_u64 v[44:45], s[30:31], 0, v[48:49]
	v_lshl_add_u64 v[44:45], s[24:25], 1, v[44:45]
	v_lshl_add_u64 v[44:45], v[136:137], 1, v[44:45]
	v_cvt_pk_bf16_f32 v40, v36, v37
	v_cvt_pk_bf16_f32 v41, v38, v39
	v_cvt_pk_bf16_f32 v42, v32, v33
	v_cvt_pk_bf16_f32 v43, v34, v35
	global_store_dwordx4 v[44:45], v[40:43], off offset:-3840 sc1

;     __device__ __forceinline__ static u32x4 pack8(const f32x4 a, const f32x4 b) { u32x4 w; w.x = cvt_pk_bf16(a[0], a[1]); w.y = cvt_pk_bf16(a[2], a[3]); w.z = cvt_pk_bf16(b[0], b[1]); w.w = cvt_pk_bf16(b[2], b[3]); return w; }
;     __device__ __forceinline__ void operator()(const f32x4 (&acc)[2][2][4][2], const Unit& u, int wr, int wc, int fr, int fq) const {
;     ...
;                     else if (pn < 8) { const int col = (pn - 4) * 256 + c256; const f32x4 l0 = *(const f32x4*)(LB + col), l1 = *(const f32x4*)(LB + col + 4); f32x4 o0, o1;
;                         for (int i = 0; i < 4; ++i) { o0[i] = __logf(l0[i] + (1.f - l0[i]) * __builtin_amdgcn_rcpf(1.f + __expf(-v0[i]))); o1[i] = __logf(l1[i] + (1.f - l1[i]) * __builtin_amdgcn_rcpf(1.f + __expf(-v1[i]))); }
;                         *(u32x4*)(LOGF + row * 1024 + col) = pack8(o0, o1); }
.LBB0_454:
	s_andn2_b64 vcc, exec, s[14:15]
	s_cbranch_vccnz .LBB0_456
	v_add_u32_e32 v40, s33, v138
	v_ashrrev_i32_e32 v41, 31, v40
	v_lshl_add_u64 v[44:45], v[40:41], 2, s[40:41]
	global_load_dwordx4 v[40:43], v[44:45], off
	s_nop 0
	global_load_dwordx4 v[44:47], v[44:45], off offset:16
	v_mul_f32_e32 v50, 0xbfb8aa3b, v36
	v_mul_f32_e32 v51, 0xbfb8aa3b, v32
	v_exp_f32_e32 v50, v50
	v_mul_f32_e32 v52, 0xbfb8aa3b, v37
	v_exp_f32_e32 v51, v51
	v_mul_f32_e32 v53, 0xbfb8aa3b, v33
	v_exp_f32_e32 v52, v52
	v_exp_f32_e32 v53, v53
	v_mul_f32_e32 v56, 0xbfb8aa3b, v38
	v_add_f32_e32 v50, 1.0, v50
	v_exp_f32_e32 v56, v56
	v_add_f32_e32 v51, 1.0, v51
	v_rcp_f32_e32 v50, v50
	v_add_f32_e32 v52, 1.0, v52
	v_rcp_f32_e32 v51, v51
	v_add_f32_e32 v53, 1.0, v53
	v_rcp_f32_e32 v52, v52
	v_mul_f32_e32 v57, 0xbfb8aa3b, v34
	v_rcp_f32_e32 v53, v53
	v_exp_f32_e32 v57, v57
	v_add_f32_e32 v56, 1.0, v56
	v_rcp_f32_e32 v56, v56
	v_add_f32_e32 v57, 1.0, v57
	v_rcp_f32_e32 v57, v57
	s_waitcnt vmcnt(0)
	v_sub_f32_e32 v58, 1.0, v40
	v_sub_f32_e32 v59, 1.0, v44
	v_fma_f32 v40, v50, v58, v40
	v_sub_f32_e32 v60, 1.0, v41
	v_fma_f32 v44, v51, v59, v44
	v_cmp_gt_f32_e32 vcc, s82, v40
	v_sub_f32_e32 v61, 1.0, v45
	v_fma_f32 v41, v52, v60, v41
	v_cndmask_b32_e64 v50, 0, 32, vcc
	v_cmp_gt_f32_e64 s[14:15], s82, v44
	v_fma_f32 v45, v53, v61, v45
	v_cmp_gt_f32_e64 s[16:17], s82, v41
	v_cndmask_b32_e64 v51, 0, 32, s[14:15]
	v_ldexp_f32 v40, v40, v50
	v_sub_f32_e32 v62, 1.0, v42
	v_cndmask_b32_e64 v52, 0, 32, s[16:17]
	v_cmp_gt_f32_e64 s[18:19], s82, v45
	v_ldexp_f32 v44, v44, v51
	v_log_f32_e32 v40, v40
	v_fma_f32 v42, v56, v62, v42
	v_cndmask_b32_e64 v53, 0, 32, s[18:19]
	v_ldexp_f32 v41, v41, v52
	v_log_f32_e32 v44, v44
	v_cmp_gt_f32_e64 s[20:21], s82, v42
	v_ldexp_f32 v45, v45, v53
	v_log_f32_e32 v41, v41
	v_cndmask_b32_e64 v56, 0, 32, s[20:21]
	v_log_f32_e32 v45, v45
	v_sub_f32_e32 v63, 1.0, v46
	v_ldexp_f32 v42, v42, v56
	v_mul_f32_e32 v56, 0x3f317217, v40
	v_fma_f32 v46, v57, v63, v46
	v_mul_f32_e32 v57, 0x3f317217, v44
	v_fma_f32 v56, v40, s83, -v56
	v_mul_f32_e32 v58, 0x3f317217, v41
	v_fma_f32 v57, v44, s83, -v57
	v_fmac_f32_e32 v56, 0x3377d1cf, v40
	v_cndmask_b32_e32 v50, 0, v167, vcc
	v_mul_f32_e32 v59, 0x3f317217, v45
	v_fma_f32 v58, v41, s83, -v58
	v_fmac_f32_e32 v57, 0x3377d1cf, v44
	v_fmac_f32_e32 v56, 0x3f317217, v40
	v_cmp_lt_f32_e64 vcc, |v40|, s84
	v_fma_f32 v59, v45, s83, -v59
	v_fmac_f32_e32 v58, 0x3377d1cf, v41
	v_fmac_f32_e32 v57, 0x3f317217, v44
	v_cndmask_b32_e32 v40, v40, v56, vcc
	v_cmp_lt_f32_e64 vcc, |v44|, s84
	v_log_f32_e32 v42, v42
	v_fmac_f32_e32 v59, 0x3377d1cf, v45
	v_fmac_f32_e32 v58, 0x3f317217, v41
	v_cndmask_b32_e32 v44, v44, v57, vcc
	v_cmp_lt_f32_e64 vcc, |v41|, s84
	v_cndmask_b32_e64 v51, 0, v167, s[14:15]
	v_fmac_f32_e32 v59, 0x3f317217, v45
	v_cndmask_b32_e32 v41, v41, v58, vcc
	v_cmp_lt_f32_e64 vcc, |v45|, s84
	v_sub_f32_e32 v44, v44, v51
	v_mul_f32_e32 v51, 0xbfb8aa3b, v39
	v_cndmask_b32_e32 v45, v45, v59, vcc
	v_cmp_gt_f32_e32 vcc, s82, v46
	v_sub_f32_e32 v40, v40, v50
	v_exp_f32_e32 v51, v51
	v_cndmask_b32_e64 v50, 0, 32, vcc
	v_mul_f32_e32 v60, 0x3f317217, v42
	v_ldexp_f32 v46, v46, v50
	v_fma_f32 v60, v42, s83, -v60
	v_log_f32_e32 v46, v46
	v_fmac_f32_e32 v60, 0x3377d1cf, v42
	v_fmac_f32_e32 v60, 0x3f317217, v42
	v_cmp_lt_f32_e64 s[14:15], |v42|, s84
	v_add_f32_e32 v51, 1.0, v51
	v_cndmask_b32_e64 v50, 0, v167, s[20:21]
	v_cndmask_b32_e64 v42, v42, v60, s[14:15]
	v_rcp_f32_e32 v51, v51
	v_sub_f32_e32 v42, v42, v50
	v_mul_f32_e32 v50, 0x3f317217, v46
	v_cndmask_b32_e64 v52, 0, v167, s[16:17]
	v_fma_f32 v50, v46, s83, -v50
	v_sub_f32_e32 v41, v41, v52
	v_fmac_f32_e32 v50, 0x3377d1cf, v46
	v_sub_f32_e32 v52, 1.0, v43
	v_fmac_f32_e32 v50, 0x3f317217, v46
	v_cmp_lt_f32_e64 s[14:15], |v46|, s84
	v_fmac_f32_e32 v43, v51, v52
	v_sub_f32_e32 v52, 1.0, v47
	v_cndmask_b32_e64 v46, v46, v50, s[14:15]
	v_cndmask_b32_e32 v50, 0, v167, vcc
	v_cmp_gt_f32_e32 vcc, s82, v43
	v_sub_f32_e32 v46, v46, v50
	v_cndmask_b32_e64 v53, 0, v167, s[18:19]
	v_cndmask_b32_e64 v51, 0, 32, vcc
	v_ldexp_f32 v43, v43, v51
	v_mul_f32_e32 v51, 0xbfb8aa3b, v35
	v_exp_f32_e32 v51, v51
	v_log_f32_e32 v43, v43
	v_sub_f32_e32 v45, v45, v53
	v_cvt_pk_bf16_f32 v40, v40, v41
	v_add_f32_e32 v51, 1.0, v51
	v_rcp_f32_e32 v51, v51
	v_mul_f32_e32 v50, 0x3f317217, v43
	v_fma_f32 v50, v43, s83, -v50
	v_fmac_f32_e32 v50, 0x3377d1cf, v43
	v_fmac_f32_e32 v47, v51, v52
	v_cmp_gt_f32_e64 s[14:15], s82, v47
	v_fmac_f32_e32 v50, 0x3f317217, v43
	v_cmp_lt_f32_e64 s[16:17], |v43|, s84
	v_cndmask_b32_e64 v51, 0, 32, s[14:15]
	v_ldexp_f32 v47, v47, v51
	v_log_f32_e32 v47, v47
	v_cndmask_b32_e64 v43, v43, v50, s[16:17]
	v_cndmask_b32_e32 v50, 0, v167, vcc
	v_sub_f32_e32 v43, v43, v50
	v_mul_f32_e32 v50, 0x3f317217, v47
	v_fma_f32 v50, v47, s83, -v50
	v_fmac_f32_e32 v50, 0x3377d1cf, v47
	v_fmac_f32_e32 v50, 0x3f317217, v47
	v_cmp_lt_f32_e64 vcc, |v47|, s84
	v_cvt_pk_bf16_f32 v41, v42, v43
	v_cvt_pk_bf16_f32 v42, v44, v45
	v_lshl_add_u64 v[44:45], s[38:39], 0, v[48:49]
	s_nop 0
	v_cndmask_b32_e32 v47, v47, v50, vcc
	v_cndmask_b32_e64 v50, 0, v167, s[14:15]
	v_sub_f32_e32 v47, v47, v50
	v_cvt_pk_bf16_f32 v43, v46, v47
	v_lshl_add_u64 v[46:47], s[0:1], 0, v[138:139]
	v_lshl_add_u64 v[44:45], v[46:47], 1, v[44:45]
	global_store_dwordx4 v[44:45], v[40:43], off offset:-2048 sc1

;     __device__ __forceinline__ static u32x4 pack8(const f32x4 a, const f32x4 b) { u32x4 w; w.x = cvt_pk_bf16(a[0], a[1]); w.y = cvt_pk_bf16(a[2], a[3]); w.z = cvt_pk_bf16(b[0], b[1]); w.w = cvt_pk_bf16(b[2], b[3]); return w; }
;     __device__ __forceinline__ static f32x4 silu4(const f32x4 v) { f32x4 o; for (int i = 0; i < 4; ++i) o[i] = v[i] * __builtin_amdgcn_rcpf(1.f + __expf(-v[i])); return o; }
;     __device__ __forceinline__ void operator()(const f32x4 (&acc)[2][2][4][2], const Unit& u, int wr, int wc, int fr, int fq) const {
;     ...
;                 for (int bj = 0; bj < 2; ++bj) { const int c256 = bj * HALF + cl; f32x4 v0 = acc[ai][bj][m][0], v1 = acc[ai][bj][m][1];
;                     if (pn < 4) { *(u32x4*)(QH + row * 1024 + pn * 256 + c256) = pack8(silu4(v0), silu4(v1)); }
;                     else if (pn < 8) { const int col = (pn - 4) * 256 + c256; const f32x4 l0 = *(const f32x4*)(LB + col), l1 = *(const f32x4*)(LB + col + 4); f32x4 o0, o1;
;                         for (int i = 0; i < 4; ++i) { o0[i] = __logf(l0[i] + (1.f - l0[i]) * __builtin_amdgcn_rcpf(1.f + __expf(-v0[i]))); o1[i] = __logf(l1[i] + (1.f - l1[i]) * __builtin_amdgcn_rcpf(1.f + __expf(-v1[i]))); }
;                         *(u32x4*)(LOGF + row * 1024 + col) = pack8(o0, o1); }
;                     else if (pn < 12) { *(u32x4*)(VH + row * 1024 + (pn - 8) * 256 + c256) = pack8(v0, v1); }
;                     else if (pn < 16) { *(u32x4*)(GH + row * 1024 + (pn - 12) * 256 + c256) = pack8(silu4(v0), silu4(v1)); }
;                     else if (pn < 20) { const float sc = 0.125f * 1.4426950408889634f; *(u32x4*)(QN + row * 1024 + (pn - 16) * 256 + c256) = pack8(v0 * sc, v1 * sc); }
;                     else if (pn < 26) { *(u32x4*)(KV6 + (size_t)(pn - 20) * ((size_t)16384 * 256) + row * 256 + c256) = pack8(v0, v1); }
;                     else if (c256 < 64) { f32x4 o0, o1; for (int i = 0; i < 4; ++i) { o0[i] = __builtin_amdgcn_rcpf(1.f + __expf(-v0[i])); o1[i] = __builtin_amdgcn_rcpf(1.f + __expf(-v1[i])); }
;                         *(f32x4*)(GATE + row * 64 + c256) = o0; *(f32x4*)(GATE + row * 64 + c256 + 4) = o1; } } }
.LBB0_457:
	s_and_b64 vcc, exec, s[10:11]
	s_cbranch_vccnz .LBB0_477
	s_andn2_b64 vcc, exec, s[62:63]
	s_cbranch_vccnz .LBB0_474
	s_andn2_b64 vcc, exec, s[60:61]
	s_cbranch_vccnz .LBB0_471
	s_andn2_b64 vcc, exec, s[58:59]
	s_cbranch_vccnz .LBB0_468
	s_andn2_b64 vcc, exec, s[56:57]
	s_cbranch_vccnz .LBB0_465
	s_and_saveexec_b64 s[14:15], s[4:5]
	s_cbranch_execz .LBB0_464
	v_mul_f32_e32 v39, 0xbfb8aa3b, v24
	v_exp_f32_e32 v39, v39
	v_mul_f32_e32 v40, 0xbfb8aa3b, v29
	v_mul_f32_e32 v41, 0xbfb8aa3b, v25
	v_exp_f32_e32 v40, v40
	v_exp_f32_e32 v41, v41
	v_add_f32_e32 v39, 1.0, v39
	v_rcp_f32_e32 v42, v39
	v_add_f32_e32 v39, 1.0, v40
	v_add_f32_e32 v40, 1.0, v41
	v_mul_f32_e32 v41, 0xbfb8aa3b, v30
	v_mul_f32_e32 v43, 0xbfb8aa3b, v26
	v_exp_f32_e32 v41, v41
	v_exp_f32_e32 v44, v43
	v_mul_f32_e32 v38, 0xbfb8aa3b, v28
	v_rcp_f32_e32 v43, v40
	v_add_f32_e32 v40, 1.0, v41
	v_add_f32_e32 v41, 1.0, v44
	v_mul_f32_e32 v44, 0xbfb8aa3b, v31
	v_exp_f32_e32 v38, v38
	v_exp_f32_e32 v45, v44
	v_mul_f32_e32 v44, 0xbfb8aa3b, v27
	v_exp_f32_e32 v46, v44
	v_add_f32_e32 v38, 1.0, v38
	v_rcp_f32_e32 v44, v41
	v_add_f32_e32 v41, 1.0, v45
	v_rcp_f32_e32 v38, v38
	v_rcp_f32_e32 v39, v39
	v_rcp_f32_e32 v40, v40
	v_rcp_f32_e32 v41, v41
	v_add_f32_e32 v45, 1.0, v46
	v_rcp_f32_e32 v45, v45
	v_lshl_add_u64 v[46:47], v[36:37], 2, v[140:141]
	global_store_dwordx4 v[46:47], v[38:41], off sc1
	global_store_dwordx4 v[46:47], v[42:45], off offset:16 sc1

;     __device__ __forceinline__ static u32x4 pack8(const f32x4 a, const f32x4 b) { u32x4 w; w.x = cvt_pk_bf16(a[0], a[1]); w.y = cvt_pk_bf16(a[2], a[3]); w.z = cvt_pk_bf16(b[0], b[1]); w.w = cvt_pk_bf16(b[2], b[3]); return w; }
;     __device__ __forceinline__ void operator()(const f32x4 (&acc)[2][2][4][2], const Unit& u, int wr, int wc, int fr, int fq) const {
;     ...
;                     else if (pn < 26) { *(u32x4*)(KV6 + (size_t)(pn - 20) * ((size_t)16384 * 256) + row * 256 + c256) = pack8(v0, v1); }
.LBB0_465:
	s_andn2_b64 vcc, exec, s[14:15]
	s_cbranch_vccnz .LBB0_467
	s_add_u32 s14, s73, s2
	s_addc_u32 s15, s74, s3
	v_lshl_add_u64 v[42:43], s[14:15], 0, v[34:35]
	v_lshl_add_u64 v[42:43], v[136:137], 1, v[42:43]
	v_cvt_pk_bf16_f32 v38, v28, v29
	v_cvt_pk_bf16_f32 v39, v30, v31
	v_cvt_pk_bf16_f32 v40, v24, v25
	v_cvt_pk_bf16_f32 v41, v26, v27
	global_store_dwordx4 v[42:43], v[38:41], off sc1

;     __device__ __forceinline__ static u32x4 pack8(const f32x4 a, const f32x4 b) { u32x4 w; w.x = cvt_pk_bf16(a[0], a[1]); w.y = cvt_pk_bf16(a[2], a[3]); w.z = cvt_pk_bf16(b[0], b[1]); w.w = cvt_pk_bf16(b[2], b[3]); return w; }
;     __device__ __forceinline__ void operator()(const f32x4 (&acc)[2][2][4][2], const Unit& u, int wr, int wc, int fr, int fq) const {
;     ...
;                     else if (pn < 20) { const float sc = 0.125f * 1.4426950408889634f; *(u32x4*)(QN + row * 1024 + (pn - 16) * 256 + c256) = pack8(v0 * sc, v1 * sc); }
.LBB0_468:
	s_andn2_b64 vcc, exec, s[14:15]
	s_cbranch_vccnz .LBB0_470
	v_pk_mul_f32 v[40:41], v[30:31], s[46:47] op_sel_hi:[1,0]
	v_pk_mul_f32 v[38:39], v[28:29], s[46:47] op_sel_hi:[1,0]
	v_pk_mul_f32 v[42:43], v[26:27], s[46:47] op_sel_hi:[1,0]
	v_pk_mul_f32 v[44:45], v[24:25], s[46:47] op_sel_hi:[1,0]
	v_cvt_pk_bf16_f32 v38, v38, v39
	v_cvt_pk_bf16_f32 v39, v40, v41
	s_nop 0
	v_cvt_pk_bf16_f32 v40, v44, v45
	v_cvt_pk_bf16_f32 v41, v42, v43
	v_lshl_add_u64 v[42:43], s[36:37], 0, v[32:33]
	v_lshl_add_u64 v[42:43], s[24:25], 1, v[42:43]
	v_lshl_add_u64 v[42:43], v[136:137], 1, v[42:43]
	v_add_co_u32_e32 v42, vcc, 0xffffe000, v42
	s_nop 1
	v_addc_co_u32_e32 v43, vcc, -1, v43, vcc
	global_store_dwordx4 v[42:43], v[38:41], off sc1

;     __device__ __forceinline__ static u32x4 pack8(const f32x4 a, const f32x4 b) { u32x4 w; w.x = cvt_pk_bf16(a[0], a[1]); w.y = cvt_pk_bf16(a[2], a[3]); w.z = cvt_pk_bf16(b[0], b[1]); w.w = cvt_pk_bf16(b[2], b[3]); return w; }
;     __device__ __forceinline__ static f32x4 silu4(const f32x4 v) { f32x4 o; for (int i = 0; i < 4; ++i) o[i] = v[i] * __builtin_amdgcn_rcpf(1.f + __expf(-v[i])); return o; }
;     __device__ __forceinline__ void operator()(const f32x4 (&acc)[2][2][4][2], const Unit& u, int wr, int wc, int fr, int fq) const {
;     ...
;                     else if (pn < 16) { *(u32x4*)(GH + row * 1024 + (pn - 12) * 256 + c256) = pack8(silu4(v0), silu4(v1)); }
.LBB0_471:
	s_andn2_b64 vcc, exec, s[14:15]
	s_cbranch_vccnz .LBB0_473
	v_mul_f32_e32 v38, 0xbfb8aa3b, v28
	v_mul_f32_e32 v39, 0xbfb8aa3b, v29
	v_mul_f32_e32 v40, 0xbfb8aa3b, v30
	v_mul_f32_e32 v42, 0xbfb8aa3b, v24
	v_mul_f32_e32 v43, 0xbfb8aa3b, v25
	v_exp_f32_e32 v38, v38
	v_exp_f32_e32 v39, v39
	v_exp_f32_e32 v40, v40
	v_mul_f32_e32 v41, 0xbfb8aa3b, v31
	v_exp_f32_e32 v42, v42
	v_exp_f32_e32 v43, v43
	v_exp_f32_e32 v41, v41
	v_add_f32_e32 v38, 1.0, v38
	v_add_f32_e32 v39, 1.0, v39
	v_add_f32_e32 v40, 1.0, v40
	v_add_f32_e32 v42, 1.0, v42
	v_add_f32_e32 v43, 1.0, v43
	v_rcp_f32_e32 v38, v38
	v_rcp_f32_e32 v39, v39
	v_rcp_f32_e32 v40, v40
	v_add_f32_e32 v41, 1.0, v41
	v_rcp_f32_e32 v42, v42
	v_mul_f32_e32 v44, 0xbfb8aa3b, v26
	v_mul_f32_e32 v45, 0xbfb8aa3b, v27
	v_rcp_f32_e32 v43, v43
	v_rcp_f32_e32 v41, v41
	v_exp_f32_e32 v44, v44
	v_exp_f32_e32 v45, v45
	v_mul_f32_e32 v38, v28, v38
	v_mul_f32_e32 v39, v29, v39
	v_mul_f32_e32 v40, v30, v40
	v_mul_f32_e32 v42, v24, v42
	v_mul_f32_e32 v43, v25, v43
	v_mul_f32_e32 v41, v31, v41
	v_add_f32_e32 v44, 1.0, v44
	v_add_f32_e32 v45, 1.0, v45
	v_cvt_pk_bf16_f32 v38, v38, v39
	v_cvt_pk_bf16_f32 v39, v40, v41
	v_cvt_pk_bf16_f32 v40, v42, v43
	v_lshl_add_u64 v[42:43], s[34:35], 0, v[32:33]
	v_rcp_f32_e32 v44, v44
	v_rcp_f32_e32 v45, v45
	v_lshl_add_u64 v[42:43], s[24:25], 1, v[42:43]
	v_lshl_add_u64 v[42:43], v[136:137], 1, v[42:43]
	v_add_co_u32_e32 v42, vcc, 0xfffff000, v42
	v_mul_f32_e32 v44, v26, v44
	s_nop 0
	v_addc_co_u32_e32 v43, vcc, -1, v43, vcc
	v_mul_f32_e32 v45, v27, v45
	v_cvt_pk_bf16_f32 v41, v44, v45
	global_store_dwordx4 v[42:43], v[38:41], off offset:-2048 sc1

;     __device__ __forceinline__ static u32x4 pack8(const f32x4 a, const f32x4 b) { u32x4 w; w.x = cvt_pk_bf16(a[0], a[1]); w.y = cvt_pk_bf16(a[2], a[3]); w.z = cvt_pk_bf16(b[0], b[1]); w.w = cvt_pk_bf16(b[2], b[3]); return w; }
;     __device__ __forceinline__ void operator()(const f32x4 (&acc)[2][2][4][2], const Unit& u, int wr, int wc, int fr, int fq) const {
;     ...
;                     else if (pn < 12) { *(u32x4*)(VH + row * 1024 + (pn - 8) * 256 + c256) = pack8(v0, v1); }
.LBB0_474:
	s_andn2_b64 vcc, exec, s[14:15]
	s_cbranch_vccnz .LBB0_476
	v_lshl_add_u64 v[42:43], s[30:31], 0, v[32:33]
	v_lshl_add_u64 v[42:43], s[24:25], 1, v[42:43]
	v_lshl_add_u64 v[42:43], v[136:137], 1, v[42:43]
	v_cvt_pk_bf16_f32 v38, v28, v29
	v_cvt_pk_bf16_f32 v39, v30, v31
	v_cvt_pk_bf16_f32 v40, v24, v25
	v_cvt_pk_bf16_f32 v41, v26, v27
	global_store_dwordx4 v[42:43], v[38:41], off offset:-4096 sc1

;     __device__ __forceinline__ static u32x4 pack8(const f32x4 a, const f32x4 b) { u32x4 w; w.x = cvt_pk_bf16(a[0], a[1]); w.y = cvt_pk_bf16(a[2], a[3]); w.z = cvt_pk_bf16(b[0], b[1]); w.w = cvt_pk_bf16(b[2], b[3]); return w; }
;     __device__ __forceinline__ void operator()(const f32x4 (&acc)[2][2][4][2], const Unit& u, int wr, int wc, int fr, int fq) const {
;     ...
;                     else if (pn < 8) { const int col = (pn - 4) * 256 + c256; const f32x4 l0 = *(const f32x4*)(LB + col), l1 = *(const f32x4*)(LB + col + 4); f32x4 o0, o1;
;                         for (int i = 0; i < 4; ++i) { o0[i] = __logf(l0[i] + (1.f - l0[i]) * __builtin_amdgcn_rcpf(1.f + __expf(-v0[i]))); o1[i] = __logf(l1[i] + (1.f - l1[i]) * __builtin_amdgcn_rcpf(1.f + __expf(-v1[i]))); }
;                         *(u32x4*)(LOGF + row * 1024 + col) = pack8(o0, o1); }
.LBB0_477:
	s_andn2_b64 vcc, exec, s[14:15]
	s_cbranch_vccnz .LBB0_479
	v_add_u32_e32 v38, s33, v136
	v_ashrrev_i32_e32 v39, 31, v38
	v_lshl_add_u64 v[42:43], v[38:39], 2, s[40:41]
	global_load_dwordx4 v[38:41], v[42:43], off
	s_nop 0
	global_load_dwordx4 v[42:45], v[42:43], off offset:16
	v_mul_f32_e32 v46, 0xbfb8aa3b, v28
	v_mul_f32_e32 v47, 0xbfb8aa3b, v24
	v_exp_f32_e32 v46, v46
	v_mul_f32_e32 v48, 0xbfb8aa3b, v29
	v_exp_f32_e32 v47, v47
	v_mul_f32_e32 v49, 0xbfb8aa3b, v25
	v_exp_f32_e32 v48, v48
	v_exp_f32_e32 v49, v49
	v_mul_f32_e32 v50, 0xbfb8aa3b, v30
	v_add_f32_e32 v46, 1.0, v46
	v_exp_f32_e32 v50, v50
	v_add_f32_e32 v47, 1.0, v47
	v_rcp_f32_e32 v46, v46
	v_add_f32_e32 v48, 1.0, v48
	v_rcp_f32_e32 v47, v47
	v_add_f32_e32 v49, 1.0, v49
	v_rcp_f32_e32 v48, v48
	v_mul_f32_e32 v51, 0xbfb8aa3b, v26
	v_rcp_f32_e32 v49, v49
	v_exp_f32_e32 v51, v51
	v_add_f32_e32 v50, 1.0, v50
	v_rcp_f32_e32 v50, v50
	v_add_f32_e32 v51, 1.0, v51
	v_rcp_f32_e32 v51, v51
	s_waitcnt vmcnt(0)
	v_sub_f32_e32 v52, 1.0, v38
	v_sub_f32_e32 v53, 1.0, v42
	v_fma_f32 v38, v46, v52, v38
	v_sub_f32_e32 v54, 1.0, v39
	v_fma_f32 v42, v47, v53, v42
	v_cmp_gt_f32_e32 vcc, s82, v38
	v_sub_f32_e32 v55, 1.0, v43
	v_fma_f32 v39, v48, v54, v39
	v_cndmask_b32_e64 v46, 0, 32, vcc
	v_cmp_gt_f32_e64 s[14:15], s82, v42
	v_fma_f32 v43, v49, v55, v43
	v_cmp_gt_f32_e64 s[16:17], s82, v39
	v_cndmask_b32_e64 v47, 0, 32, s[14:15]
	v_ldexp_f32 v38, v38, v46
	v_sub_f32_e32 v56, 1.0, v40
	v_cndmask_b32_e64 v48, 0, 32, s[16:17]
	v_cmp_gt_f32_e64 s[18:19], s82, v43
	v_ldexp_f32 v42, v42, v47
	v_log_f32_e32 v38, v38
	v_fma_f32 v40, v50, v56, v40
	v_cndmask_b32_e64 v49, 0, 32, s[18:19]
	v_ldexp_f32 v39, v39, v48
	v_log_f32_e32 v42, v42
	v_cmp_gt_f32_e64 s[20:21], s82, v40
	v_ldexp_f32 v43, v43, v49
	v_log_f32_e32 v39, v39
	v_cndmask_b32_e64 v50, 0, 32, s[20:21]
	v_log_f32_e32 v43, v43
	v_sub_f32_e32 v57, 1.0, v44
	v_ldexp_f32 v40, v40, v50
	v_mul_f32_e32 v50, 0x3f317217, v38
	v_fma_f32 v44, v51, v57, v44
	v_mul_f32_e32 v51, 0x3f317217, v42
	v_fma_f32 v50, v38, s83, -v50
	v_mul_f32_e32 v52, 0x3f317217, v39
	v_fma_f32 v51, v42, s83, -v51
	v_fmac_f32_e32 v50, 0x3377d1cf, v38
	v_cndmask_b32_e32 v46, 0, v167, vcc
	v_mul_f32_e32 v53, 0x3f317217, v43
	v_fma_f32 v52, v39, s83, -v52
	v_fmac_f32_e32 v51, 0x3377d1cf, v42
	v_fmac_f32_e32 v50, 0x3f317217, v38
	v_cmp_lt_f32_e64 vcc, |v38|, s84
	v_fma_f32 v53, v43, s83, -v53
	v_fmac_f32_e32 v52, 0x3377d1cf, v39
	v_fmac_f32_e32 v51, 0x3f317217, v42
	v_cndmask_b32_e32 v38, v38, v50, vcc
	v_cmp_lt_f32_e64 vcc, |v42|, s84
	v_log_f32_e32 v40, v40
	v_fmac_f32_e32 v53, 0x3377d1cf, v43
	v_fmac_f32_e32 v52, 0x3f317217, v39
	v_cndmask_b32_e32 v42, v42, v51, vcc
	v_cmp_lt_f32_e64 vcc, |v39|, s84
	v_cndmask_b32_e64 v47, 0, v167, s[14:15]
	v_fmac_f32_e32 v53, 0x3f317217, v43
	v_cndmask_b32_e32 v39, v39, v52, vcc
	v_cmp_lt_f32_e64 vcc, |v43|, s84
	v_sub_f32_e32 v42, v42, v47
	v_mul_f32_e32 v47, 0xbfb8aa3b, v31
	v_cndmask_b32_e32 v43, v43, v53, vcc
	v_cmp_gt_f32_e32 vcc, s82, v44
	v_sub_f32_e32 v38, v38, v46
	v_exp_f32_e32 v47, v47
	v_cndmask_b32_e64 v46, 0, 32, vcc
	v_mul_f32_e32 v54, 0x3f317217, v40
	v_ldexp_f32 v44, v44, v46
	v_fma_f32 v54, v40, s83, -v54
	v_log_f32_e32 v44, v44
	v_fmac_f32_e32 v54, 0x3377d1cf, v40
	v_fmac_f32_e32 v54, 0x3f317217, v40
	v_cmp_lt_f32_e64 s[14:15], |v40|, s84
	v_add_f32_e32 v47, 1.0, v47
	v_cndmask_b32_e64 v46, 0, v167, s[20:21]
	v_cndmask_b32_e64 v40, v40, v54, s[14:15]
	v_rcp_f32_e32 v47, v47
	v_sub_f32_e32 v40, v40, v46
	v_mul_f32_e32 v46, 0x3f317217, v44
	v_cndmask_b32_e64 v48, 0, v167, s[16:17]
	v_fma_f32 v46, v44, s83, -v46
	v_sub_f32_e32 v39, v39, v48
	v_fmac_f32_e32 v46, 0x3377d1cf, v44
	v_sub_f32_e32 v48, 1.0, v41
	v_fmac_f32_e32 v46, 0x3f317217, v44
	v_cmp_lt_f32_e64 s[14:15], |v44|, s84
	v_fmac_f32_e32 v41, v47, v48
	v_sub_f32_e32 v48, 1.0, v45
	v_cndmask_b32_e64 v44, v44, v46, s[14:15]
	v_cndmask_b32_e32 v46, 0, v167, vcc
	v_cmp_gt_f32_e32 vcc, s82, v41
	v_sub_f32_e32 v44, v44, v46
	v_cndmask_b32_e64 v49, 0, v167, s[18:19]
	v_cndmask_b32_e64 v47, 0, 32, vcc
	v_ldexp_f32 v41, v41, v47
	v_mul_f32_e32 v47, 0xbfb8aa3b, v27
	v_exp_f32_e32 v47, v47
	v_log_f32_e32 v41, v41
	v_sub_f32_e32 v43, v43, v49
	v_cvt_pk_bf16_f32 v38, v38, v39
	v_add_f32_e32 v47, 1.0, v47
	v_rcp_f32_e32 v47, v47
	v_mul_f32_e32 v46, 0x3f317217, v41
	v_fma_f32 v46, v41, s83, -v46
	v_fmac_f32_e32 v46, 0x3377d1cf, v41
	v_fmac_f32_e32 v45, v47, v48
	v_cmp_gt_f32_e64 s[14:15], s82, v45
	v_fmac_f32_e32 v46, 0x3f317217, v41
	v_cmp_lt_f32_e64 s[16:17], |v41|, s84
	v_cndmask_b32_e64 v47, 0, 32, s[14:15]
	v_ldexp_f32 v45, v45, v47
	v_log_f32_e32 v45, v45
	v_cndmask_b32_e64 v41, v41, v46, s[16:17]
	v_cndmask_b32_e32 v46, 0, v167, vcc
	v_sub_f32_e32 v41, v41, v46
	v_mul_f32_e32 v46, 0x3f317217, v45
	v_fma_f32 v46, v45, s83, -v46
	v_fmac_f32_e32 v46, 0x3377d1cf, v45
	v_fmac_f32_e32 v46, 0x3f317217, v45
	v_cmp_lt_f32_e64 vcc, |v45|, s84
	v_cvt_pk_bf16_f32 v39, v40, v41
	v_cvt_pk_bf16_f32 v40, v42, v43
	v_lshl_add_u64 v[42:43], s[38:39], 0, v[32:33]
	s_nop 0
	v_cndmask_b32_e32 v45, v45, v46, vcc
	v_cndmask_b32_e64 v46, 0, v167, s[14:15]
	v_sub_f32_e32 v45, v45, v46
	v_cvt_pk_bf16_f32 v41, v44, v45
	v_lshl_add_u64 v[44:45], s[0:1], 0, v[136:137]
	v_lshl_add_u64 v[42:43], v[44:45], 1, v[42:43]
	global_store_dwordx4 v[42:43], v[38:41], off offset:-2048 sc1

;     __device__ __forceinline__ static u32x4 pack8(const f32x4 a, const f32x4 b) { u32x4 w; w.x = cvt_pk_bf16(a[0], a[1]); w.y = cvt_pk_bf16(a[2], a[3]); w.z = cvt_pk_bf16(b[0], b[1]); w.w = cvt_pk_bf16(b[2], b[3]); return w; }
;     __device__ __forceinline__ static f32x4 silu4(const f32x4 v) { f32x4 o; for (int i = 0; i < 4; ++i) o[i] = v[i] * __builtin_amdgcn_rcpf(1.f + __expf(-v[i])); return o; }
;     __device__ __forceinline__ void operator()(const f32x4 (&acc)[2][2][4][2], const Unit& u, int wr, int wc, int fr, int fq) const {
;     ...
;                     if (pn < 4) { *(u32x4*)(QH + row * 1024 + pn * 256 + c256) = pack8(silu4(v0), silu4(v1)); }
;                     else if (pn < 8) { const int col = (pn - 4) * 256 + c256; const f32x4 l0 = *(const f32x4*)(LB + col), l1 = *(const f32x4*)(LB + col + 4); f32x4 o0, o1;
;                         for (int i = 0; i < 4; ++i) { o0[i] = __logf(l0[i] + (1.f - l0[i]) * __builtin_amdgcn_rcpf(1.f + __expf(-v0[i]))); o1[i] = __logf(l1[i] + (1.f - l1[i]) * __builtin_amdgcn_rcpf(1.f + __expf(-v1[i]))); }
;                         *(u32x4*)(LOGF + row * 1024 + col) = pack8(o0, o1); }
;                     else if (pn < 12) { *(u32x4*)(VH + row * 1024 + (pn - 8) * 256 + c256) = pack8(v0, v1); }
;                     else if (pn < 16) { *(u32x4*)(GH + row * 1024 + (pn - 12) * 256 + c256) = pack8(silu4(v0), silu4(v1)); }
;                     else if (pn < 20) { const float sc = 0.125f * 1.4426950408889634f; *(u32x4*)(QN + row * 1024 + (pn - 16) * 256 + c256) = pack8(v0 * sc, v1 * sc); }
;                     else if (pn < 26) { *(u32x4*)(KV6 + (size_t)(pn - 20) * ((size_t)16384 * 256) + row * 256 + c256) = pack8(v0, v1); }
;                     else if (c256 < 64) { f32x4 o0, o1; for (int i = 0; i < 4; ++i) { o0[i] = __builtin_amdgcn_rcpf(1.f + __expf(-v0[i])); o1[i] = __builtin_amdgcn_rcpf(1.f + __expf(-v1[i])); }
;                         *(f32x4*)(GATE + row * 64 + c256) = o0; *(f32x4*)(GATE + row * 64 + c256 + 4) = o1; } } }
.LBB0_480:
	v_mul_f32_e32 v40, 0xbfb8aa3b, v28
	v_mul_f32_e32 v41, 0xbfb8aa3b, v29
	v_mul_f32_e32 v42, 0xbfb8aa3b, v30
	v_exp_f32_e32 v40, v40
	v_exp_f32_e32 v41, v41
	v_exp_f32_e32 v42, v42
	v_mul_f32_e32 v43, 0xbfb8aa3b, v31
	v_add_f32_e32 v40, 1.0, v40
	v_add_f32_e32 v41, 1.0, v41
	v_add_f32_e32 v42, 1.0, v42
	v_rcp_f32_e32 v40, v40
	v_rcp_f32_e32 v41, v41
	v_rcp_f32_e32 v42, v42
	v_exp_f32_e32 v43, v43
	v_mul_f32_e32 v28, v28, v40
	v_mul_f32_e32 v29, v29, v41
	v_mul_f32_e32 v30, v30, v42
	v_add_f32_e32 v40, 1.0, v43
	v_mul_f32_e32 v41, 0xbfb8aa3b, v24
	v_mul_f32_e32 v42, 0xbfb8aa3b, v25
	v_rcp_f32_e32 v40, v40
	v_exp_f32_e32 v41, v41
	v_exp_f32_e32 v42, v42
	v_mul_f32_e32 v43, 0xbfb8aa3b, v27
	v_mul_f32_e32 v31, v31, v40
	v_add_f32_e32 v40, 1.0, v41
	v_add_f32_e32 v41, 1.0, v42
	v_mul_f32_e32 v42, 0xbfb8aa3b, v26
	v_exp_f32_e32 v43, v43
	v_exp_f32_e32 v42, v42
	v_rcp_f32_e32 v40, v40
	v_rcp_f32_e32 v41, v41
	v_add_f32_e32 v43, 1.0, v43
	v_add_f32_e32 v42, 1.0, v42
	v_rcp_f32_e32 v43, v43
	v_rcp_f32_e32 v42, v42
	v_mul_f32_e32 v40, v24, v40
	v_cvt_pk_bf16_f32 v24, v28, v29
	v_mul_f32_e32 v27, v27, v43
	v_lshl_add_u64 v[28:29], v[136:137], 1, v[38:39]
	v_mul_f32_e32 v41, v25, v41
	v_mul_f32_e32 v42, v26, v42
	v_cvt_pk_bf16_f32 v25, v30, v31
	v_cvt_pk_bf16_f32 v26, v40, v41
	v_cvt_pk_bf16_f32 v27, v42, v27
	global_store_dwordx4 v[28:29], v[24:27], off sc1
	s_and_b64 vcc, exec, s[12:13]
	s_mov_b64 s[14:15], -1
	s_cbranch_vccnz .LBB0_215
.LBB0_481:
	s_and_b64 vcc, exec, s[10:11]
	s_cbranch_vccnz .LBB0_501
	s_andn2_b64 vcc, exec, s[62:63]
	s_cbranch_vccnz .LBB0_498
	s_andn2_b64 vcc, exec, s[60:61]
	s_cbranch_vccnz .LBB0_495
	s_andn2_b64 vcc, exec, s[58:59]
	s_cbranch_vccnz .LBB0_492
	s_andn2_b64 vcc, exec, s[56:57]
	s_cbranch_vccnz .LBB0_489
	s_and_saveexec_b64 s[14:15], s[6:7]
	s_cbranch_execz .LBB0_488
	v_mul_f32_e32 v25, 0xbfb8aa3b, v16
	v_exp_f32_e32 v25, v25
	v_mul_f32_e32 v26, 0xbfb8aa3b, v21
	v_mul_f32_e32 v27, 0xbfb8aa3b, v17
	v_exp_f32_e32 v26, v26
	v_exp_f32_e32 v27, v27
	v_add_f32_e32 v25, 1.0, v25
	v_rcp_f32_e32 v28, v25
	v_add_f32_e32 v25, 1.0, v26
	v_add_f32_e32 v26, 1.0, v27
	v_mul_f32_e32 v27, 0xbfb8aa3b, v22
	v_mul_f32_e32 v29, 0xbfb8aa3b, v18
	v_exp_f32_e32 v27, v27
	v_exp_f32_e32 v30, v29
	v_mul_f32_e32 v24, 0xbfb8aa3b, v20
	v_rcp_f32_e32 v29, v26
	v_add_f32_e32 v26, 1.0, v27
	v_add_f32_e32 v27, 1.0, v30
	v_mul_f32_e32 v30, 0xbfb8aa3b, v23
	v_exp_f32_e32 v24, v24
	v_exp_f32_e32 v31, v30
	v_mul_f32_e32 v30, 0xbfb8aa3b, v19
	v_exp_f32_e32 v40, v30
	v_add_f32_e32 v24, 1.0, v24
	v_rcp_f32_e32 v30, v27
	v_add_f32_e32 v27, 1.0, v31
	v_rcp_f32_e32 v24, v24
	v_rcp_f32_e32 v25, v25
	v_rcp_f32_e32 v26, v26
	v_rcp_f32_e32 v27, v27
	v_add_f32_e32 v31, 1.0, v40
	v_rcp_f32_e32 v31, v31
	v_lshl_add_u64 v[36:37], v[36:37], 2, v[142:143]
	global_store_dwordx4 v[36:37], v[24:27], off sc1
	global_store_dwordx4 v[36:37], v[28:31], off offset:16 sc1

;     __device__ __forceinline__ static u32x4 pack8(const f32x4 a, const f32x4 b) { u32x4 w; w.x = cvt_pk_bf16(a[0], a[1]); w.y = cvt_pk_bf16(a[2], a[3]); w.z = cvt_pk_bf16(b[0], b[1]); w.w = cvt_pk_bf16(b[2], b[3]); return w; }
;     __device__ __forceinline__ void operator()(const f32x4 (&acc)[2][2][4][2], const Unit& u, int wr, int wc, int fr, int fq) const {
;     ...
;                     else if (pn < 26) { *(u32x4*)(KV6 + (size_t)(pn - 20) * ((size_t)16384 * 256) + row * 256 + c256) = pack8(v0, v1); }
.LBB0_489:
	s_andn2_b64 vcc, exec, s[14:15]
	s_cbranch_vccnz .LBB0_491
	s_add_u32 s14, s73, s2
	s_addc_u32 s15, s74, s3
	v_lshl_add_u64 v[28:29], s[14:15], 0, v[34:35]
	v_lshl_add_u64 v[28:29], v[136:137], 1, v[28:29]
	v_cvt_pk_bf16_f32 v24, v20, v21
	v_cvt_pk_bf16_f32 v25, v22, v23
	v_cvt_pk_bf16_f32 v26, v16, v17
	v_cvt_pk_bf16_f32 v27, v18, v19
	global_store_dwordx4 v[28:29], v[24:27], off offset:256 sc1

;     __device__ __forceinline__ static u32x4 pack8(const f32x4 a, const f32x4 b) { u32x4 w; w.x = cvt_pk_bf16(a[0], a[1]); w.y = cvt_pk_bf16(a[2], a[3]); w.z = cvt_pk_bf16(b[0], b[1]); w.w = cvt_pk_bf16(b[2], b[3]); return w; }
;     __device__ __forceinline__ void operator()(const f32x4 (&acc)[2][2][4][2], const Unit& u, int wr, int wc, int fr, int fq) const {
;     ...
;                     else if (pn < 20) { const float sc = 0.125f * 1.4426950408889634f; *(u32x4*)(QN + row * 1024 + (pn - 16) * 256 + c256) = pack8(v0 * sc, v1 * sc); }
.LBB0_492:
	s_andn2_b64 vcc, exec, s[14:15]
	s_cbranch_vccnz .LBB0_494
	v_pk_mul_f32 v[26:27], v[22:23], s[46:47] op_sel_hi:[1,0]
	v_pk_mul_f32 v[24:25], v[20:21], s[46:47] op_sel_hi:[1,0]
	v_pk_mul_f32 v[28:29], v[18:19], s[46:47] op_sel_hi:[1,0]
	v_pk_mul_f32 v[30:31], v[16:17], s[46:47] op_sel_hi:[1,0]
	v_cvt_pk_bf16_f32 v24, v24, v25
	v_cvt_pk_bf16_f32 v25, v26, v27
	s_nop 0
	v_cvt_pk_bf16_f32 v26, v30, v31
	v_cvt_pk_bf16_f32 v27, v28, v29
	v_lshl_add_u64 v[28:29], s[36:37], 0, v[32:33]
	v_lshl_add_u64 v[28:29], s[24:25], 1, v[28:29]
	v_lshl_add_u64 v[28:29], v[138:139], 1, v[28:29]
	v_add_co_u32_e32 v28, vcc, 0xffffe000, v28
	s_nop 1
	v_addc_co_u32_e32 v29, vcc, -1, v29, vcc
	global_store_dwordx4 v[28:29], v[24:27], off sc1

;     __device__ __forceinline__ static u32x4 pack8(const f32x4 a, const f32x4 b) { u32x4 w; w.x = cvt_pk_bf16(a[0], a[1]); w.y = cvt_pk_bf16(a[2], a[3]); w.z = cvt_pk_bf16(b[0], b[1]); w.w = cvt_pk_bf16(b[2], b[3]); return w; }
;     __device__ __forceinline__ static f32x4 silu4(const f32x4 v) { f32x4 o; for (int i = 0; i < 4; ++i) o[i] = v[i] * __builtin_amdgcn_rcpf(1.f + __expf(-v[i])); return o; }
;     __device__ __forceinline__ void operator()(const f32x4 (&acc)[2][2][4][2], const Unit& u, int wr, int wc, int fr, int fq) const {
;     ...
;                     else if (pn < 16) { *(u32x4*)(GH + row * 1024 + (pn - 12) * 256 + c256) = pack8(silu4(v0), silu4(v1)); }
.LBB0_495:
	s_andn2_b64 vcc, exec, s[14:15]
	s_cbranch_vccnz .LBB0_497
	v_mul_f32_e32 v24, 0xbfb8aa3b, v20
	v_mul_f32_e32 v25, 0xbfb8aa3b, v21
	v_mul_f32_e32 v26, 0xbfb8aa3b, v22
	v_mul_f32_e32 v28, 0xbfb8aa3b, v16
	v_mul_f32_e32 v29, 0xbfb8aa3b, v17
	v_exp_f32_e32 v24, v24
	v_exp_f32_e32 v25, v25
	v_exp_f32_e32 v26, v26
	v_mul_f32_e32 v27, 0xbfb8aa3b, v23
	v_exp_f32_e32 v28, v28
	v_exp_f32_e32 v29, v29
	v_exp_f32_e32 v27, v27
	v_add_f32_e32 v24, 1.0, v24
	v_add_f32_e32 v25, 1.0, v25
	v_add_f32_e32 v26, 1.0, v26
	v_add_f32_e32 v28, 1.0, v28
	v_add_f32_e32 v29, 1.0, v29
	v_rcp_f32_e32 v24, v24
	v_rcp_f32_e32 v25, v25
	v_rcp_f32_e32 v26, v26
	v_add_f32_e32 v27, 1.0, v27
	v_rcp_f32_e32 v28, v28
	v_mul_f32_e32 v30, 0xbfb8aa3b, v18
	v_mul_f32_e32 v31, 0xbfb8aa3b, v19
	v_rcp_f32_e32 v29, v29
	v_rcp_f32_e32 v27, v27
	v_exp_f32_e32 v30, v30
	v_exp_f32_e32 v31, v31
	v_mul_f32_e32 v24, v20, v24
	v_mul_f32_e32 v25, v21, v25
	v_mul_f32_e32 v26, v22, v26
	v_mul_f32_e32 v28, v16, v28
	v_mul_f32_e32 v29, v17, v29
	v_mul_f32_e32 v27, v23, v27
	v_add_f32_e32 v30, 1.0, v30
	v_add_f32_e32 v31, 1.0, v31
	v_cvt_pk_bf16_f32 v24, v24, v25
	v_cvt_pk_bf16_f32 v25, v26, v27
	v_cvt_pk_bf16_f32 v26, v28, v29
	v_lshl_add_u64 v[28:29], s[34:35], 0, v[32:33]
	v_rcp_f32_e32 v30, v30
	v_rcp_f32_e32 v31, v31
	v_lshl_add_u64 v[28:29], s[24:25], 1, v[28:29]
	v_lshl_add_u64 v[28:29], v[138:139], 1, v[28:29]
	v_add_co_u32_e32 v28, vcc, 0xfffff000, v28
	v_mul_f32_e32 v30, v18, v30
	s_nop 0
	v_addc_co_u32_e32 v29, vcc, -1, v29, vcc
	v_mul_f32_e32 v31, v19, v31
	v_cvt_pk_bf16_f32 v27, v30, v31
	global_store_dwordx4 v[28:29], v[24:27], off offset:-2048 sc1

;     __device__ __forceinline__ static u32x4 pack8(const f32x4 a, const f32x4 b) { u32x4 w; w.x = cvt_pk_bf16(a[0], a[1]); w.y = cvt_pk_bf16(a[2], a[3]); w.z = cvt_pk_bf16(b[0], b[1]); w.w = cvt_pk_bf16(b[2], b[3]); return w; }
;     __device__ __forceinline__ void operator()(const f32x4 (&acc)[2][2][4][2], const Unit& u, int wr, int wc, int fr, int fq) const {
;     ...
;                     else if (pn < 12) { *(u32x4*)(VH + row * 1024 + (pn - 8) * 256 + c256) = pack8(v0, v1); }
.LBB0_498:
	s_andn2_b64 vcc, exec, s[14:15]
	s_cbranch_vccnz .LBB0_500
	v_lshl_add_u64 v[28:29], s[30:31], 0, v[32:33]
	v_lshl_add_u64 v[28:29], s[24:25], 1, v[28:29]
	v_lshl_add_u64 v[28:29], v[136:137], 1, v[28:29]
	v_cvt_pk_bf16_f32 v24, v20, v21
	v_cvt_pk_bf16_f32 v25, v22, v23
	v_cvt_pk_bf16_f32 v26, v16, v17
	v_cvt_pk_bf16_f32 v27, v18, v19
	global_store_dwordx4 v[28:29], v[24:27], off offset:-3840 sc1

;     __device__ __forceinline__ static u32x4 pack8(const f32x4 a, const f32x4 b) { u32x4 w; w.x = cvt_pk_bf16(a[0], a[1]); w.y = cvt_pk_bf16(a[2], a[3]); w.z = cvt_pk_bf16(b[0], b[1]); w.w = cvt_pk_bf16(b[2], b[3]); return w; }
;     __device__ __forceinline__ void operator()(const f32x4 (&acc)[2][2][4][2], const Unit& u, int wr, int wc, int fr, int fq) const {
;     ...
;                     else if (pn < 8) { const int col = (pn - 4) * 256 + c256; const f32x4 l0 = *(const f32x4*)(LB + col), l1 = *(const f32x4*)(LB + col + 4); f32x4 o0, o1;
;                         for (int i = 0; i < 4; ++i) { o0[i] = __logf(l0[i] + (1.f - l0[i]) * __builtin_amdgcn_rcpf(1.f + __expf(-v0[i]))); o1[i] = __logf(l1[i] + (1.f - l1[i]) * __builtin_amdgcn_rcpf(1.f + __expf(-v1[i]))); }
;                         *(u32x4*)(LOGF + row * 1024 + col) = pack8(o0, o1); }
.LBB0_501:
	s_andn2_b64 vcc, exec, s[14:15]
	s_cbranch_vccnz .LBB0_503
	v_add_u32_e32 v24, s33, v138
	v_ashrrev_i32_e32 v25, 31, v24
	v_lshl_add_u64 v[28:29], v[24:25], 2, s[40:41]
	global_load_dwordx4 v[24:27], v[28:29], off
	s_nop 0
	global_load_dwordx4 v[28:31], v[28:29], off offset:16
	v_mul_f32_e32 v34, 0xbfb8aa3b, v20
	v_mul_f32_e32 v35, 0xbfb8aa3b, v16
	v_exp_f32_e32 v34, v34
	v_mul_f32_e32 v36, 0xbfb8aa3b, v21
	v_exp_f32_e32 v35, v35
	v_mul_f32_e32 v37, 0xbfb8aa3b, v17
	v_exp_f32_e32 v36, v36
	v_exp_f32_e32 v37, v37
	v_mul_f32_e32 v40, 0xbfb8aa3b, v22
	v_add_f32_e32 v34, 1.0, v34
	v_exp_f32_e32 v40, v40
	v_add_f32_e32 v35, 1.0, v35
	v_rcp_f32_e32 v34, v34
	v_add_f32_e32 v36, 1.0, v36
	v_rcp_f32_e32 v35, v35
	v_add_f32_e32 v37, 1.0, v37
	v_rcp_f32_e32 v36, v36
	v_mul_f32_e32 v41, 0xbfb8aa3b, v18
	v_rcp_f32_e32 v37, v37
	v_exp_f32_e32 v41, v41
	v_add_f32_e32 v40, 1.0, v40
	v_rcp_f32_e32 v40, v40
	v_add_f32_e32 v41, 1.0, v41
	v_rcp_f32_e32 v41, v41
	s_waitcnt vmcnt(0)
	v_sub_f32_e32 v42, 1.0, v24
	v_sub_f32_e32 v43, 1.0, v28
	v_fma_f32 v24, v34, v42, v24
	v_sub_f32_e32 v44, 1.0, v25
	v_fma_f32 v28, v35, v43, v28
	v_cmp_gt_f32_e32 vcc, s82, v24
	v_sub_f32_e32 v45, 1.0, v29
	v_fma_f32 v25, v36, v44, v25
	v_cndmask_b32_e64 v34, 0, 32, vcc
	v_cmp_gt_f32_e64 s[14:15], s82, v28
	v_fma_f32 v29, v37, v45, v29
	v_cmp_gt_f32_e64 s[16:17], s82, v25
	v_cndmask_b32_e64 v35, 0, 32, s[14:15]
	v_ldexp_f32 v24, v24, v34
	v_sub_f32_e32 v46, 1.0, v26
	v_cndmask_b32_e64 v36, 0, 32, s[16:17]
	v_cmp_gt_f32_e64 s[18:19], s82, v29
	v_ldexp_f32 v28, v28, v35
	v_log_f32_e32 v24, v24
	v_fma_f32 v26, v40, v46, v26
	v_cndmask_b32_e64 v37, 0, 32, s[18:19]
	v_ldexp_f32 v25, v25, v36
	v_log_f32_e32 v28, v28
	v_cmp_gt_f32_e64 s[20:21], s82, v26
	v_ldexp_f32 v29, v29, v37
	v_log_f32_e32 v25, v25
	v_cndmask_b32_e64 v40, 0, 32, s[20:21]
	v_log_f32_e32 v29, v29
	v_sub_f32_e32 v47, 1.0, v30
	v_ldexp_f32 v26, v26, v40
	v_mul_f32_e32 v40, 0x3f317217, v24
	v_fma_f32 v30, v41, v47, v30
	v_mul_f32_e32 v41, 0x3f317217, v28
	v_fma_f32 v40, v24, s83, -v40
	v_mul_f32_e32 v42, 0x3f317217, v25
	v_fma_f32 v41, v28, s83, -v41
	v_fmac_f32_e32 v40, 0x3377d1cf, v24
	v_cndmask_b32_e32 v34, 0, v167, vcc
	v_mul_f32_e32 v43, 0x3f317217, v29
	v_fma_f32 v42, v25, s83, -v42
	v_fmac_f32_e32 v41, 0x3377d1cf, v28
	v_fmac_f32_e32 v40, 0x3f317217, v24
	v_cmp_lt_f32_e64 vcc, |v24|, s84
	v_fma_f32 v43, v29, s83, -v43
	v_fmac_f32_e32 v42, 0x3377d1cf, v25
	v_fmac_f32_e32 v41, 0x3f317217, v28
	v_cndmask_b32_e32 v24, v24, v40, vcc
	v_cmp_lt_f32_e64 vcc, |v28|, s84
	v_log_f32_e32 v26, v26
	v_fmac_f32_e32 v43, 0x3377d1cf, v29
	v_fmac_f32_e32 v42, 0x3f317217, v25
	v_cndmask_b32_e32 v28, v28, v41, vcc
	v_cmp_lt_f32_e64 vcc, |v25|, s84
	v_cndmask_b32_e64 v35, 0, v167, s[14:15]
	v_fmac_f32_e32 v43, 0x3f317217, v29
	v_cndmask_b32_e32 v25, v25, v42, vcc
	v_cmp_lt_f32_e64 vcc, |v29|, s84
	v_sub_f32_e32 v28, v28, v35
	v_mul_f32_e32 v35, 0xbfb8aa3b, v23
	v_cndmask_b32_e32 v29, v29, v43, vcc
	v_cmp_gt_f32_e32 vcc, s82, v30
	v_sub_f32_e32 v24, v24, v34
	v_exp_f32_e32 v35, v35
	v_cndmask_b32_e64 v34, 0, 32, vcc
	v_mul_f32_e32 v44, 0x3f317217, v26
	v_ldexp_f32 v30, v30, v34
	v_fma_f32 v44, v26, s83, -v44
	v_log_f32_e32 v30, v30
	v_fmac_f32_e32 v44, 0x3377d1cf, v26
	v_fmac_f32_e32 v44, 0x3f317217, v26
	v_cmp_lt_f32_e64 s[14:15], |v26|, s84
	v_add_f32_e32 v35, 1.0, v35
	v_cndmask_b32_e64 v34, 0, v167, s[20:21]
	v_cndmask_b32_e64 v26, v26, v44, s[14:15]
	v_rcp_f32_e32 v35, v35
	v_sub_f32_e32 v26, v26, v34
	v_mul_f32_e32 v34, 0x3f317217, v30
	v_cndmask_b32_e64 v36, 0, v167, s[16:17]
	v_fma_f32 v34, v30, s83, -v34
	v_sub_f32_e32 v25, v25, v36
	v_fmac_f32_e32 v34, 0x3377d1cf, v30
	v_sub_f32_e32 v36, 1.0, v27
	v_fmac_f32_e32 v34, 0x3f317217, v30
	v_cmp_lt_f32_e64 s[14:15], |v30|, s84
	v_fmac_f32_e32 v27, v35, v36
	v_sub_f32_e32 v36, 1.0, v31
	v_cndmask_b32_e64 v30, v30, v34, s[14:15]
	v_cndmask_b32_e32 v34, 0, v167, vcc
	v_cmp_gt_f32_e32 vcc, s82, v27
	v_sub_f32_e32 v30, v30, v34
	v_cndmask_b32_e64 v37, 0, v167, s[18:19]
	v_cndmask_b32_e64 v35, 0, 32, vcc
	v_ldexp_f32 v27, v27, v35
	v_mul_f32_e32 v35, 0xbfb8aa3b, v19
	v_exp_f32_e32 v35, v35
	v_log_f32_e32 v27, v27
	v_sub_f32_e32 v29, v29, v37
	v_cvt_pk_bf16_f32 v24, v24, v25
	v_add_f32_e32 v35, 1.0, v35
	v_rcp_f32_e32 v35, v35
	v_mul_f32_e32 v34, 0x3f317217, v27
	v_fma_f32 v34, v27, s83, -v34
	v_fmac_f32_e32 v34, 0x3377d1cf, v27
	v_fmac_f32_e32 v31, v35, v36
	v_cmp_gt_f32_e64 s[14:15], s82, v31
	v_fmac_f32_e32 v34, 0x3f317217, v27
	v_cmp_lt_f32_e64 s[16:17], |v27|, s84
	v_cndmask_b32_e64 v35, 0, 32, s[14:15]
	v_ldexp_f32 v31, v31, v35
	v_log_f32_e32 v31, v31
	v_cndmask_b32_e64 v27, v27, v34, s[16:17]
	v_cndmask_b32_e32 v34, 0, v167, vcc
	v_sub_f32_e32 v27, v27, v34
	v_mul_f32_e32 v34, 0x3f317217, v31
	v_fma_f32 v34, v31, s83, -v34
	v_fmac_f32_e32 v34, 0x3377d1cf, v31
	v_fmac_f32_e32 v34, 0x3f317217, v31
	v_cmp_lt_f32_e64 vcc, |v31|, s84
	v_cvt_pk_bf16_f32 v25, v26, v27
	v_cvt_pk_bf16_f32 v26, v28, v29
	v_lshl_add_u64 v[28:29], s[38:39], 0, v[32:33]
	s_nop 0
	v_cndmask_b32_e32 v31, v31, v34, vcc
	v_cndmask_b32_e64 v34, 0, v167, s[14:15]
	v_sub_f32_e32 v31, v31, v34
	v_cvt_pk_bf16_f32 v27, v30, v31
	v_lshl_add_u64 v[30:31], s[0:1], 0, v[138:139]
	v_lshl_add_u64 v[28:29], v[30:31], 1, v[28:29]
	global_store_dwordx4 v[28:29], v[24:27], off offset:-2048 sc1

;     __device__ __forceinline__ static u32x4 pack8(const f32x4 a, const f32x4 b) { u32x4 w; w.x = cvt_pk_bf16(a[0], a[1]); w.y = cvt_pk_bf16(a[2], a[3]); w.z = cvt_pk_bf16(b[0], b[1]); w.w = cvt_pk_bf16(b[2], b[3]); return w; }
;     __device__ __forceinline__ static f32x4 silu4(const f32x4 v) { f32x4 o; for (int i = 0; i < 4; ++i) o[i] = v[i] * __builtin_amdgcn_rcpf(1.f + __expf(-v[i])); return o; }
;     __device__ __forceinline__ void operator()(const f32x4 (&acc)[2][2][4][2], const Unit& u, int wr, int wc, int fr, int fq) const {
;     ...
;                 for (int bj = 0; bj < 2; ++bj) { const int c256 = bj * HALF + cl; f32x4 v0 = acc[ai][bj][m][0], v1 = acc[ai][bj][m][1];
;                     if (pn < 4) { *(u32x4*)(QH + row * 1024 + pn * 256 + c256) = pack8(silu4(v0), silu4(v1)); }
;                     else if (pn < 8) { const int col = (pn - 4) * 256 + c256; const f32x4 l0 = *(const f32x4*)(LB + col), l1 = *(const f32x4*)(LB + col + 4); f32x4 o0, o1;
;                         for (int i = 0; i < 4; ++i) { o0[i] = __logf(l0[i] + (1.f - l0[i]) * __builtin_amdgcn_rcpf(1.f + __expf(-v0[i]))); o1[i] = __logf(l1[i] + (1.f - l1[i]) * __builtin_amdgcn_rcpf(1.f + __expf(-v1[i]))); }
;                         *(u32x4*)(LOGF + row * 1024 + col) = pack8(o0, o1); }
;                     else if (pn < 12) { *(u32x4*)(VH + row * 1024 + (pn - 8) * 256 + c256) = pack8(v0, v1); }
;                     else if (pn < 16) { *(u32x4*)(GH + row * 1024 + (pn - 12) * 256 + c256) = pack8(silu4(v0), silu4(v1)); }
;                     else if (pn < 20) { const float sc = 0.125f * 1.4426950408889634f; *(u32x4*)(QN + row * 1024 + (pn - 16) * 256 + c256) = pack8(v0 * sc, v1 * sc); }
;                     else if (pn < 26) { *(u32x4*)(KV6 + (size_t)(pn - 20) * ((size_t)16384 * 256) + row * 256 + c256) = pack8(v0, v1); }
;                     else if (c256 < 64) { f32x4 o0, o1; for (int i = 0; i < 4; ++i) { o0[i] = __builtin_amdgcn_rcpf(1.f + __expf(-v0[i])); o1[i] = __builtin_amdgcn_rcpf(1.f + __expf(-v1[i])); }
;                         *(f32x4*)(GATE + row * 64 + c256) = o0; *(f32x4*)(GATE + row * 64 + c256 + 4) = o1; } } }
.LBB0_504:
	s_and_b64 vcc, exec, s[10:11]
	s_cbranch_vccnz .LBB0_524
	s_andn2_b64 vcc, exec, s[62:63]
	s_cbranch_vccnz .LBB0_521
	s_andn2_b64 vcc, exec, s[60:61]
	s_cbranch_vccnz .LBB0_518
	s_andn2_b64 vcc, exec, s[58:59]
	s_cbranch_vccnz .LBB0_515
	s_andn2_b64 vcc, exec, s[56:57]
	s_cbranch_vccnz .LBB0_512
	s_and_saveexec_b64 s[14:15], s[4:5]
	s_cbranch_execz .LBB0_511
	v_mul_f32_e32 v23, 0xbfb8aa3b, v8
	v_exp_f32_e32 v23, v23
	v_mul_f32_e32 v24, 0xbfb8aa3b, v13
	v_mul_f32_e32 v25, 0xbfb8aa3b, v9
	v_exp_f32_e32 v24, v24
	v_exp_f32_e32 v25, v25
	v_add_f32_e32 v23, 1.0, v23
	v_rcp_f32_e32 v26, v23
	v_add_f32_e32 v23, 1.0, v24
	v_add_f32_e32 v24, 1.0, v25
	v_mul_f32_e32 v25, 0xbfb8aa3b, v14
	v_mul_f32_e32 v27, 0xbfb8aa3b, v10
	v_exp_f32_e32 v25, v25
	v_exp_f32_e32 v28, v27
	v_mul_f32_e32 v22, 0xbfb8aa3b, v12
	v_rcp_f32_e32 v27, v24
	v_add_f32_e32 v24, 1.0, v25
	v_add_f32_e32 v25, 1.0, v28
	v_mul_f32_e32 v28, 0xbfb8aa3b, v15
	v_exp_f32_e32 v22, v22
	v_exp_f32_e32 v29, v28
	v_mul_f32_e32 v28, 0xbfb8aa3b, v11
	v_exp_f32_e32 v30, v28
	v_add_f32_e32 v22, 1.0, v22
	v_rcp_f32_e32 v28, v25
	v_add_f32_e32 v25, 1.0, v29
	v_rcp_f32_e32 v22, v22
	v_rcp_f32_e32 v23, v23
	v_rcp_f32_e32 v24, v24
	v_rcp_f32_e32 v25, v25
	v_add_f32_e32 v29, 1.0, v30
	v_rcp_f32_e32 v29, v29
	v_lshl_add_u64 v[30:31], v[20:21], 2, v[140:141]
	global_store_dwordx4 v[30:31], v[22:25], off sc1
	global_store_dwordx4 v[30:31], v[26:29], off offset:16 sc1

;     __device__ __forceinline__ static u32x4 pack8(const f32x4 a, const f32x4 b) { u32x4 w; w.x = cvt_pk_bf16(a[0], a[1]); w.y = cvt_pk_bf16(a[2], a[3]); w.z = cvt_pk_bf16(b[0], b[1]); w.w = cvt_pk_bf16(b[2], b[3]); return w; }
;     __device__ __forceinline__ void operator()(const f32x4 (&acc)[2][2][4][2], const Unit& u, int wr, int wc, int fr, int fq) const {
;     ...
;                     else if (pn < 26) { *(u32x4*)(KV6 + (size_t)(pn - 20) * ((size_t)16384 * 256) + row * 256 + c256) = pack8(v0, v1); }
.LBB0_512:
	s_andn2_b64 vcc, exec, s[14:15]
	s_cbranch_vccnz .LBB0_514
	s_add_u32 s14, s73, s2
	s_addc_u32 s15, s74, s3
	v_lshl_add_u64 v[26:27], s[14:15], 0, v[18:19]
	v_lshl_add_u64 v[26:27], v[136:137], 1, v[26:27]
	v_cvt_pk_bf16_f32 v22, v12, v13
	v_cvt_pk_bf16_f32 v23, v14, v15
	v_cvt_pk_bf16_f32 v24, v8, v9
	v_cvt_pk_bf16_f32 v25, v10, v11
	global_store_dwordx4 v[26:27], v[22:25], off sc1

;     __device__ __forceinline__ static u32x4 pack8(const f32x4 a, const f32x4 b) { u32x4 w; w.x = cvt_pk_bf16(a[0], a[1]); w.y = cvt_pk_bf16(a[2], a[3]); w.z = cvt_pk_bf16(b[0], b[1]); w.w = cvt_pk_bf16(b[2], b[3]); return w; }
;     __device__ __forceinline__ void operator()(const f32x4 (&acc)[2][2][4][2], const Unit& u, int wr, int wc, int fr, int fq) const {
;     ...
;                     else if (pn < 20) { const float sc = 0.125f * 1.4426950408889634f; *(u32x4*)(QN + row * 1024 + (pn - 16) * 256 + c256) = pack8(v0 * sc, v1 * sc); }
.LBB0_515:
	s_andn2_b64 vcc, exec, s[14:15]
	s_cbranch_vccnz .LBB0_517
	v_pk_mul_f32 v[24:25], v[14:15], s[46:47] op_sel_hi:[1,0]
	v_pk_mul_f32 v[22:23], v[12:13], s[46:47] op_sel_hi:[1,0]
	v_pk_mul_f32 v[26:27], v[10:11], s[46:47] op_sel_hi:[1,0]
	v_pk_mul_f32 v[28:29], v[8:9], s[46:47] op_sel_hi:[1,0]
	v_cvt_pk_bf16_f32 v22, v22, v23
	v_cvt_pk_bf16_f32 v23, v24, v25
	s_nop 0
	v_cvt_pk_bf16_f32 v24, v28, v29
	v_cvt_pk_bf16_f32 v25, v26, v27
	v_lshl_add_u64 v[26:27], s[36:37], 0, v[16:17]
	v_lshl_add_u64 v[26:27], s[24:25], 1, v[26:27]
	v_lshl_add_u64 v[26:27], v[136:137], 1, v[26:27]
	v_add_co_u32_e32 v26, vcc, 0xffffe000, v26
	s_nop 1
	v_addc_co_u32_e32 v27, vcc, -1, v27, vcc
	global_store_dwordx4 v[26:27], v[22:25], off sc1

;     __device__ __forceinline__ static u32x4 pack8(const f32x4 a, const f32x4 b) { u32x4 w; w.x = cvt_pk_bf16(a[0], a[1]); w.y = cvt_pk_bf16(a[2], a[3]); w.z = cvt_pk_bf16(b[0], b[1]); w.w = cvt_pk_bf16(b[2], b[3]); return w; }
;     __device__ __forceinline__ static f32x4 silu4(const f32x4 v) { f32x4 o; for (int i = 0; i < 4; ++i) o[i] = v[i] * __builtin_amdgcn_rcpf(1.f + __expf(-v[i])); return o; }
;     __device__ __forceinline__ void operator()(const f32x4 (&acc)[2][2][4][2], const Unit& u, int wr, int wc, int fr, int fq) const {
;     ...
;                     else if (pn < 16) { *(u32x4*)(GH + row * 1024 + (pn - 12) * 256 + c256) = pack8(silu4(v0), silu4(v1)); }
.LBB0_518:
	s_andn2_b64 vcc, exec, s[14:15]
	s_cbranch_vccnz .LBB0_520
	v_mul_f32_e32 v22, 0xbfb8aa3b, v12
	v_mul_f32_e32 v23, 0xbfb8aa3b, v13
	v_mul_f32_e32 v24, 0xbfb8aa3b, v14
	v_mul_f32_e32 v26, 0xbfb8aa3b, v8
	v_mul_f32_e32 v27, 0xbfb8aa3b, v9
	v_exp_f32_e32 v22, v22
	v_exp_f32_e32 v23, v23
	v_exp_f32_e32 v24, v24
	v_mul_f32_e32 v25, 0xbfb8aa3b, v15
	v_exp_f32_e32 v26, v26
	v_exp_f32_e32 v27, v27
	v_exp_f32_e32 v25, v25
	v_add_f32_e32 v22, 1.0, v22
	v_add_f32_e32 v23, 1.0, v23
	v_add_f32_e32 v24, 1.0, v24
	v_add_f32_e32 v26, 1.0, v26
	v_add_f32_e32 v27, 1.0, v27
	v_rcp_f32_e32 v22, v22
	v_rcp_f32_e32 v23, v23
	v_rcp_f32_e32 v24, v24
	v_add_f32_e32 v25, 1.0, v25
	v_rcp_f32_e32 v26, v26
	v_mul_f32_e32 v28, 0xbfb8aa3b, v10
	v_mul_f32_e32 v29, 0xbfb8aa3b, v11
	v_rcp_f32_e32 v27, v27
	v_rcp_f32_e32 v25, v25
	v_exp_f32_e32 v28, v28
	v_exp_f32_e32 v29, v29
	v_mul_f32_e32 v22, v12, v22
	v_mul_f32_e32 v23, v13, v23
	v_mul_f32_e32 v24, v14, v24
	v_mul_f32_e32 v26, v8, v26
	v_mul_f32_e32 v27, v9, v27
	v_mul_f32_e32 v25, v15, v25
	v_add_f32_e32 v28, 1.0, v28
	v_add_f32_e32 v29, 1.0, v29
	v_cvt_pk_bf16_f32 v22, v22, v23
	v_cvt_pk_bf16_f32 v23, v24, v25
	v_cvt_pk_bf16_f32 v24, v26, v27
	v_lshl_add_u64 v[26:27], s[34:35], 0, v[16:17]
	v_rcp_f32_e32 v28, v28
	v_rcp_f32_e32 v29, v29
	v_lshl_add_u64 v[26:27], s[24:25], 1, v[26:27]
	v_lshl_add_u64 v[26:27], v[136:137], 1, v[26:27]
	v_add_co_u32_e32 v26, vcc, 0xfffff000, v26
	v_mul_f32_e32 v28, v10, v28
	s_nop 0
	v_addc_co_u32_e32 v27, vcc, -1, v27, vcc
	v_mul_f32_e32 v29, v11, v29
	v_cvt_pk_bf16_f32 v25, v28, v29
	global_store_dwordx4 v[26:27], v[22:25], off offset:-2048 sc1

;     __device__ __forceinline__ static u32x4 pack8(const f32x4 a, const f32x4 b) { u32x4 w; w.x = cvt_pk_bf16(a[0], a[1]); w.y = cvt_pk_bf16(a[2], a[3]); w.z = cvt_pk_bf16(b[0], b[1]); w.w = cvt_pk_bf16(b[2], b[3]); return w; }
;     __device__ __forceinline__ void operator()(const f32x4 (&acc)[2][2][4][2], const Unit& u, int wr, int wc, int fr, int fq) const {
;     ...
;                     else if (pn < 12) { *(u32x4*)(VH + row * 1024 + (pn - 8) * 256 + c256) = pack8(v0, v1); }
.LBB0_521:
	s_andn2_b64 vcc, exec, s[14:15]
	s_cbranch_vccnz .LBB0_523
	v_lshl_add_u64 v[26:27], s[30:31], 0, v[16:17]
	v_lshl_add_u64 v[26:27], s[24:25], 1, v[26:27]
	v_lshl_add_u64 v[26:27], v[136:137], 1, v[26:27]
	v_cvt_pk_bf16_f32 v22, v12, v13
	v_cvt_pk_bf16_f32 v23, v14, v15
	v_cvt_pk_bf16_f32 v24, v8, v9
	v_cvt_pk_bf16_f32 v25, v10, v11
	global_store_dwordx4 v[26:27], v[22:25], off offset:-4096 sc1

;     __device__ __forceinline__ static u32x4 pack8(const f32x4 a, const f32x4 b) { u32x4 w; w.x = cvt_pk_bf16(a[0], a[1]); w.y = cvt_pk_bf16(a[2], a[3]); w.z = cvt_pk_bf16(b[0], b[1]); w.w = cvt_pk_bf16(b[2], b[3]); return w; }
;     __device__ __forceinline__ void operator()(const f32x4 (&acc)[2][2][4][2], const Unit& u, int wr, int wc, int fr, int fq) const {
;     ...
;                     else if (pn < 8) { const int col = (pn - 4) * 256 + c256; const f32x4 l0 = *(const f32x4*)(LB + col), l1 = *(const f32x4*)(LB + col + 4); f32x4 o0, o1;
;                         for (int i = 0; i < 4; ++i) { o0[i] = __logf(l0[i] + (1.f - l0[i]) * __builtin_amdgcn_rcpf(1.f + __expf(-v0[i]))); o1[i] = __logf(l1[i] + (1.f - l1[i]) * __builtin_amdgcn_rcpf(1.f + __expf(-v1[i]))); }
;                         *(u32x4*)(LOGF + row * 1024 + col) = pack8(o0, o1); }
.LBB0_524:
	s_andn2_b64 vcc, exec, s[14:15]
	s_cbranch_vccnz .LBB0_526
	v_add_u32_e32 v22, s33, v136
	v_ashrrev_i32_e32 v23, 31, v22
	v_lshl_add_u64 v[26:27], v[22:23], 2, s[40:41]
	global_load_dwordx4 v[22:25], v[26:27], off
	s_nop 0
	global_load_dwordx4 v[26:29], v[26:27], off offset:16
	v_mul_f32_e32 v30, 0xbfb8aa3b, v12
	v_mul_f32_e32 v31, 0xbfb8aa3b, v8
	v_exp_f32_e32 v30, v30
	v_mul_f32_e32 v32, 0xbfb8aa3b, v13
	v_exp_f32_e32 v31, v31
	v_mul_f32_e32 v33, 0xbfb8aa3b, v9
	v_exp_f32_e32 v32, v32
	v_exp_f32_e32 v33, v33
	v_mul_f32_e32 v34, 0xbfb8aa3b, v14
	v_add_f32_e32 v30, 1.0, v30
	v_exp_f32_e32 v34, v34
	v_add_f32_e32 v31, 1.0, v31
	v_rcp_f32_e32 v30, v30
	v_add_f32_e32 v32, 1.0, v32
	v_rcp_f32_e32 v31, v31
	v_add_f32_e32 v33, 1.0, v33
	v_rcp_f32_e32 v32, v32
	v_mul_f32_e32 v35, 0xbfb8aa3b, v10
	v_rcp_f32_e32 v33, v33
	v_exp_f32_e32 v35, v35
	v_add_f32_e32 v34, 1.0, v34
	v_rcp_f32_e32 v34, v34
	v_add_f32_e32 v35, 1.0, v35
	v_rcp_f32_e32 v35, v35
	s_waitcnt vmcnt(0)
	v_sub_f32_e32 v36, 1.0, v22
	v_sub_f32_e32 v37, 1.0, v26
	v_fma_f32 v22, v30, v36, v22
	v_sub_f32_e32 v38, 1.0, v23
	v_fma_f32 v26, v31, v37, v26
	v_cmp_gt_f32_e32 vcc, s82, v22
	v_sub_f32_e32 v39, 1.0, v27
	v_fma_f32 v23, v32, v38, v23
	v_cndmask_b32_e64 v30, 0, 32, vcc
	v_cmp_gt_f32_e64 s[14:15], s82, v26
	v_fma_f32 v27, v33, v39, v27
	v_cmp_gt_f32_e64 s[16:17], s82, v23
	v_cndmask_b32_e64 v31, 0, 32, s[14:15]
	v_ldexp_f32 v22, v22, v30
	v_sub_f32_e32 v40, 1.0, v24
	v_cndmask_b32_e64 v32, 0, 32, s[16:17]
	v_cmp_gt_f32_e64 s[18:19], s82, v27
	v_ldexp_f32 v26, v26, v31
	v_log_f32_e32 v22, v22
	v_fma_f32 v24, v34, v40, v24
	v_cndmask_b32_e64 v33, 0, 32, s[18:19]
	v_ldexp_f32 v23, v23, v32
	v_log_f32_e32 v26, v26
	v_cmp_gt_f32_e64 s[20:21], s82, v24
	v_ldexp_f32 v27, v27, v33
	v_log_f32_e32 v23, v23
	v_cndmask_b32_e64 v34, 0, 32, s[20:21]
	v_log_f32_e32 v27, v27
	v_sub_f32_e32 v41, 1.0, v28
	v_ldexp_f32 v24, v24, v34
	v_mul_f32_e32 v34, 0x3f317217, v22
	v_fma_f32 v28, v35, v41, v28
	v_mul_f32_e32 v35, 0x3f317217, v26
	v_fma_f32 v34, v22, s83, -v34
	v_mul_f32_e32 v36, 0x3f317217, v23
	v_fma_f32 v35, v26, s83, -v35
	v_fmac_f32_e32 v34, 0x3377d1cf, v22
	v_cndmask_b32_e32 v30, 0, v167, vcc
	v_mul_f32_e32 v37, 0x3f317217, v27
	v_fma_f32 v36, v23, s83, -v36
	v_fmac_f32_e32 v35, 0x3377d1cf, v26
	v_fmac_f32_e32 v34, 0x3f317217, v22
	v_cmp_lt_f32_e64 vcc, |v22|, s84
	v_fma_f32 v37, v27, s83, -v37
	v_fmac_f32_e32 v36, 0x3377d1cf, v23
	v_fmac_f32_e32 v35, 0x3f317217, v26
	v_cndmask_b32_e32 v22, v22, v34, vcc
	v_cmp_lt_f32_e64 vcc, |v26|, s84
	v_log_f32_e32 v24, v24
	v_fmac_f32_e32 v37, 0x3377d1cf, v27
	v_fmac_f32_e32 v36, 0x3f317217, v23
	v_cndmask_b32_e32 v26, v26, v35, vcc
	v_cmp_lt_f32_e64 vcc, |v23|, s84
	v_cndmask_b32_e64 v31, 0, v167, s[14:15]
	v_fmac_f32_e32 v37, 0x3f317217, v27
	v_cndmask_b32_e32 v23, v23, v36, vcc
	v_cmp_lt_f32_e64 vcc, |v27|, s84
	v_sub_f32_e32 v26, v26, v31
	v_mul_f32_e32 v31, 0xbfb8aa3b, v15
	v_cndmask_b32_e32 v27, v27, v37, vcc
	v_cmp_gt_f32_e32 vcc, s82, v28
	v_sub_f32_e32 v22, v22, v30
	v_exp_f32_e32 v31, v31
	v_cndmask_b32_e64 v30, 0, 32, vcc
	v_mul_f32_e32 v38, 0x3f317217, v24
	v_ldexp_f32 v28, v28, v30
	v_fma_f32 v38, v24, s83, -v38
	v_log_f32_e32 v28, v28
	v_fmac_f32_e32 v38, 0x3377d1cf, v24
	v_fmac_f32_e32 v38, 0x3f317217, v24
	v_cmp_lt_f32_e64 s[14:15], |v24|, s84
	v_add_f32_e32 v31, 1.0, v31
	v_cndmask_b32_e64 v30, 0, v167, s[20:21]
	v_cndmask_b32_e64 v24, v24, v38, s[14:15]
	v_rcp_f32_e32 v31, v31
	v_sub_f32_e32 v24, v24, v30
	v_mul_f32_e32 v30, 0x3f317217, v28
	v_cndmask_b32_e64 v32, 0, v167, s[16:17]
	v_fma_f32 v30, v28, s83, -v30
	v_sub_f32_e32 v23, v23, v32
	v_fmac_f32_e32 v30, 0x3377d1cf, v28
	v_sub_f32_e32 v32, 1.0, v25
	v_fmac_f32_e32 v30, 0x3f317217, v28
	v_cmp_lt_f32_e64 s[14:15], |v28|, s84
	v_fmac_f32_e32 v25, v31, v32
	v_sub_f32_e32 v32, 1.0, v29
	v_cndmask_b32_e64 v28, v28, v30, s[14:15]
	v_cndmask_b32_e32 v30, 0, v167, vcc
	v_cmp_gt_f32_e32 vcc, s82, v25
	v_sub_f32_e32 v28, v28, v30
	v_cndmask_b32_e64 v33, 0, v167, s[18:19]
	v_cndmask_b32_e64 v31, 0, 32, vcc
	v_ldexp_f32 v25, v25, v31
	v_mul_f32_e32 v31, 0xbfb8aa3b, v11
	v_exp_f32_e32 v31, v31
	v_log_f32_e32 v25, v25
	v_sub_f32_e32 v27, v27, v33
	v_cvt_pk_bf16_f32 v22, v22, v23
	v_add_f32_e32 v31, 1.0, v31
	v_rcp_f32_e32 v31, v31
	v_mul_f32_e32 v30, 0x3f317217, v25
	v_fma_f32 v30, v25, s83, -v30
	v_fmac_f32_e32 v30, 0x3377d1cf, v25
	v_fmac_f32_e32 v29, v31, v32
	v_cmp_gt_f32_e64 s[14:15], s82, v29
	v_fmac_f32_e32 v30, 0x3f317217, v25
	v_cmp_lt_f32_e64 s[16:17], |v25|, s84
	v_cndmask_b32_e64 v31, 0, 32, s[14:15]
	v_ldexp_f32 v29, v29, v31
	v_log_f32_e32 v29, v29
	v_cndmask_b32_e64 v25, v25, v30, s[16:17]
	v_cndmask_b32_e32 v30, 0, v167, vcc
	v_sub_f32_e32 v25, v25, v30
	v_mul_f32_e32 v30, 0x3f317217, v29
	v_fma_f32 v30, v29, s83, -v30
	v_fmac_f32_e32 v30, 0x3377d1cf, v29
	v_fmac_f32_e32 v30, 0x3f317217, v29
	v_cmp_lt_f32_e64 vcc, |v29|, s84
	v_cvt_pk_bf16_f32 v23, v24, v25
	v_cvt_pk_bf16_f32 v24, v26, v27
	v_lshl_add_u64 v[26:27], s[38:39], 0, v[16:17]
	s_nop 0
	v_cndmask_b32_e32 v29, v29, v30, vcc
	v_cndmask_b32_e64 v30, 0, v167, s[14:15]
	v_sub_f32_e32 v29, v29, v30
	v_cvt_pk_bf16_f32 v25, v28, v29
	v_lshl_add_u64 v[28:29], s[0:1], 0, v[136:137]
	v_lshl_add_u64 v[26:27], v[28:29], 1, v[26:27]
	global_store_dwordx4 v[26:27], v[22:25], off offset:-2048 sc1

;     __device__ __forceinline__ static u32x4 pack8(const f32x4 a, const f32x4 b) { u32x4 w; w.x = cvt_pk_bf16(a[0], a[1]); w.y = cvt_pk_bf16(a[2], a[3]); w.z = cvt_pk_bf16(b[0], b[1]); w.w = cvt_pk_bf16(b[2], b[3]); return w; }
;     __device__ __forceinline__ static f32x4 silu4(const f32x4 v) { f32x4 o; for (int i = 0; i < 4; ++i) o[i] = v[i] * __builtin_amdgcn_rcpf(1.f + __expf(-v[i])); return o; }
;     __device__ __forceinline__ void operator()(const f32x4 (&acc)[2][2][4][2], const Unit& u, int wr, int wc, int fr, int fq) const {
;     ...
;                     if (pn < 4) { *(u32x4*)(QH + row * 1024 + pn * 256 + c256) = pack8(silu4(v0), silu4(v1)); }
;                     else if (pn < 8) { const int col = (pn - 4) * 256 + c256; const f32x4 l0 = *(const f32x4*)(LB + col), l1 = *(const f32x4*)(LB + col + 4); f32x4 o0, o1;
;                         for (int i = 0; i < 4; ++i) { o0[i] = __logf(l0[i] + (1.f - l0[i]) * __builtin_amdgcn_rcpf(1.f + __expf(-v0[i]))); o1[i] = __logf(l1[i] + (1.f - l1[i]) * __builtin_amdgcn_rcpf(1.f + __expf(-v1[i]))); }
;                         *(u32x4*)(LOGF + row * 1024 + col) = pack8(o0, o1); }
;                     else if (pn < 12) { *(u32x4*)(VH + row * 1024 + (pn - 8) * 256 + c256) = pack8(v0, v1); }
;                     else if (pn < 16) { *(u32x4*)(GH + row * 1024 + (pn - 12) * 256 + c256) = pack8(silu4(v0), silu4(v1)); }
;                     else if (pn < 20) { const float sc = 0.125f * 1.4426950408889634f; *(u32x4*)(QN + row * 1024 + (pn - 16) * 256 + c256) = pack8(v0 * sc, v1 * sc); }
;                     else if (pn < 26) { *(u32x4*)(KV6 + (size_t)(pn - 20) * ((size_t)16384 * 256) + row * 256 + c256) = pack8(v0, v1); }
;                     else if (c256 < 64) { f32x4 o0, o1; for (int i = 0; i < 4; ++i) { o0[i] = __builtin_amdgcn_rcpf(1.f + __expf(-v0[i])); o1[i] = __builtin_amdgcn_rcpf(1.f + __expf(-v1[i])); }
;                         *(f32x4*)(GATE + row * 64 + c256) = o0; *(f32x4*)(GATE + row * 64 + c256 + 4) = o1; } } }
.LBB0_527:
	v_mul_f32_e32 v24, 0xbfb8aa3b, v12
	v_mul_f32_e32 v25, 0xbfb8aa3b, v13
	v_mul_f32_e32 v26, 0xbfb8aa3b, v14
	v_exp_f32_e32 v24, v24
	v_exp_f32_e32 v25, v25
	v_exp_f32_e32 v26, v26
	v_mul_f32_e32 v27, 0xbfb8aa3b, v15
	v_add_f32_e32 v24, 1.0, v24
	v_add_f32_e32 v25, 1.0, v25
	v_add_f32_e32 v26, 1.0, v26
	v_rcp_f32_e32 v24, v24
	v_rcp_f32_e32 v25, v25
	v_rcp_f32_e32 v26, v26
	v_exp_f32_e32 v27, v27
	v_mul_f32_e32 v12, v12, v24
	v_mul_f32_e32 v13, v13, v25
	v_mul_f32_e32 v14, v14, v26
	v_add_f32_e32 v24, 1.0, v27
	v_mul_f32_e32 v25, 0xbfb8aa3b, v8
	v_mul_f32_e32 v26, 0xbfb8aa3b, v9
	v_rcp_f32_e32 v24, v24
	v_exp_f32_e32 v25, v25
	v_exp_f32_e32 v26, v26
	v_mul_f32_e32 v27, 0xbfb8aa3b, v11
	v_mul_f32_e32 v15, v15, v24
	v_add_f32_e32 v24, 1.0, v25
	v_add_f32_e32 v25, 1.0, v26
	v_mul_f32_e32 v26, 0xbfb8aa3b, v10
	v_exp_f32_e32 v27, v27
	v_exp_f32_e32 v26, v26
	v_rcp_f32_e32 v24, v24
	v_rcp_f32_e32 v25, v25
	v_add_f32_e32 v27, 1.0, v27
	v_add_f32_e32 v26, 1.0, v26
	v_rcp_f32_e32 v27, v27
	v_rcp_f32_e32 v26, v26
	v_mul_f32_e32 v24, v8, v24
	v_cvt_pk_bf16_f32 v8, v12, v13
	v_mul_f32_e32 v11, v11, v27
	v_lshl_add_u64 v[12:13], v[136:137], 1, v[22:23]
	v_mul_f32_e32 v25, v9, v25
	v_mul_f32_e32 v26, v10, v26
	v_cvt_pk_bf16_f32 v9, v14, v15
	v_cvt_pk_bf16_f32 v10, v24, v25
	v_cvt_pk_bf16_f32 v11, v26, v11
	global_store_dwordx4 v[12:13], v[8:11], off sc1
	s_and_b64 vcc, exec, s[12:13]
	s_mov_b64 s[12:13], -1
	s_cbranch_vccnz .LBB0_220
.LBB0_528:
	s_and_b64 vcc, exec, s[10:11]
	s_mov_b64 s[10:11], -1
	s_cbranch_vccnz .LBB0_548
	s_andn2_b64 vcc, exec, s[62:63]
	s_cbranch_vccnz .LBB0_545
	s_andn2_b64 vcc, exec, s[60:61]
	s_cbranch_vccnz .LBB0_542
	s_andn2_b64 vcc, exec, s[58:59]
	s_cbranch_vccnz .LBB0_539
	s_andn2_b64 vcc, exec, s[56:57]
	s_cbranch_vccnz .LBB0_536
	s_and_saveexec_b64 s[10:11], s[6:7]
	s_cbranch_execz .LBB0_535
	v_mul_f32_e32 v9, 0xbfb8aa3b, v0
	v_exp_f32_e32 v9, v9
	v_mul_f32_e32 v10, 0xbfb8aa3b, v5
	v_mul_f32_e32 v11, 0xbfb8aa3b, v1
	v_exp_f32_e32 v10, v10
	v_exp_f32_e32 v11, v11
	v_add_f32_e32 v9, 1.0, v9
	v_rcp_f32_e32 v12, v9
	v_add_f32_e32 v9, 1.0, v10
	v_add_f32_e32 v10, 1.0, v11
	v_mul_f32_e32 v11, 0xbfb8aa3b, v6
	v_mul_f32_e32 v13, 0xbfb8aa3b, v2
	v_exp_f32_e32 v11, v11
	v_exp_f32_e32 v14, v13
	v_mul_f32_e32 v8, 0xbfb8aa3b, v4
	v_rcp_f32_e32 v13, v10
	v_add_f32_e32 v10, 1.0, v11
	v_add_f32_e32 v11, 1.0, v14
	v_mul_f32_e32 v14, 0xbfb8aa3b, v7
	v_exp_f32_e32 v8, v8
	v_exp_f32_e32 v15, v14
	v_mul_f32_e32 v14, 0xbfb8aa3b, v3
	v_exp_f32_e32 v24, v14
	v_add_f32_e32 v8, 1.0, v8
	v_rcp_f32_e32 v14, v11
	v_add_f32_e32 v11, 1.0, v15
	v_rcp_f32_e32 v8, v8
	v_rcp_f32_e32 v9, v9
	v_rcp_f32_e32 v10, v10
	v_rcp_f32_e32 v11, v11
	v_add_f32_e32 v15, 1.0, v24
	v_rcp_f32_e32 v15, v15
	v_lshl_add_u64 v[20:21], v[20:21], 2, v[142:143]
	global_store_dwordx4 v[20:21], v[8:11], off sc1
	global_store_dwordx4 v[20:21], v[12:15], off offset:16 sc1

;     __device__ __forceinline__ static u32x4 pack8(const f32x4 a, const f32x4 b) { u32x4 w; w.x = cvt_pk_bf16(a[0], a[1]); w.y = cvt_pk_bf16(a[2], a[3]); w.z = cvt_pk_bf16(b[0], b[1]); w.w = cvt_pk_bf16(b[2], b[3]); return w; }
;     __device__ __forceinline__ void operator()(const f32x4 (&acc)[2][2][4][2], const Unit& u, int wr, int wc, int fr, int fq) const {
;     ...
;                     else if (pn < 26) { *(u32x4*)(KV6 + (size_t)(pn - 20) * ((size_t)16384 * 256) + row * 256 + c256) = pack8(v0, v1); }
.LBB0_536:
	s_andn2_b64 vcc, exec, s[10:11]
	s_cbranch_vccnz .LBB0_538
	s_add_u32 s2, s73, s2
	s_addc_u32 s3, s74, s3
	v_lshl_add_u64 v[12:13], s[2:3], 0, v[18:19]
	v_lshl_add_u64 v[12:13], v[136:137], 1, v[12:13]
	v_cvt_pk_bf16_f32 v8, v4, v5
	v_cvt_pk_bf16_f32 v9, v6, v7
	v_cvt_pk_bf16_f32 v10, v0, v1
	v_cvt_pk_bf16_f32 v11, v2, v3
	global_store_dwordx4 v[12:13], v[8:11], off offset:256 sc1

;     __device__ __forceinline__ static u32x4 pack8(const f32x4 a, const f32x4 b) { u32x4 w; w.x = cvt_pk_bf16(a[0], a[1]); w.y = cvt_pk_bf16(a[2], a[3]); w.z = cvt_pk_bf16(b[0], b[1]); w.w = cvt_pk_bf16(b[2], b[3]); return w; }
;     __device__ __forceinline__ void operator()(const f32x4 (&acc)[2][2][4][2], const Unit& u, int wr, int wc, int fr, int fq) const {
;     ...
;                     else if (pn < 20) { const float sc = 0.125f * 1.4426950408889634f; *(u32x4*)(QN + row * 1024 + (pn - 16) * 256 + c256) = pack8(v0 * sc, v1 * sc); }
.LBB0_539:
	s_andn2_b64 vcc, exec, s[10:11]
	s_cbranch_vccnz .LBB0_541
	v_pk_mul_f32 v[10:11], v[6:7], s[46:47] op_sel_hi:[1,0]
	v_pk_mul_f32 v[8:9], v[4:5], s[46:47] op_sel_hi:[1,0]
	v_pk_mul_f32 v[12:13], v[2:3], s[46:47] op_sel_hi:[1,0]
	v_pk_mul_f32 v[14:15], v[0:1], s[46:47] op_sel_hi:[1,0]
	v_cvt_pk_bf16_f32 v8, v8, v9
	v_cvt_pk_bf16_f32 v9, v10, v11
	s_nop 0
	v_cvt_pk_bf16_f32 v10, v14, v15
	v_cvt_pk_bf16_f32 v11, v12, v13
	v_lshl_add_u64 v[12:13], s[36:37], 0, v[16:17]
	v_lshl_add_u64 v[12:13], s[24:25], 1, v[12:13]
	v_lshl_add_u64 v[12:13], v[138:139], 1, v[12:13]
	v_add_co_u32_e32 v12, vcc, 0xffffe000, v12
	s_nop 1
	v_addc_co_u32_e32 v13, vcc, -1, v13, vcc
	global_store_dwordx4 v[12:13], v[8:11], off sc1

;     __device__ __forceinline__ static u32x4 pack8(const f32x4 a, const f32x4 b) { u32x4 w; w.x = cvt_pk_bf16(a[0], a[1]); w.y = cvt_pk_bf16(a[2], a[3]); w.z = cvt_pk_bf16(b[0], b[1]); w.w = cvt_pk_bf16(b[2], b[3]); return w; }
;     __device__ __forceinline__ static f32x4 silu4(const f32x4 v) { f32x4 o; for (int i = 0; i < 4; ++i) o[i] = v[i] * __builtin_amdgcn_rcpf(1.f + __expf(-v[i])); return o; }
;     __device__ __forceinline__ void operator()(const f32x4 (&acc)[2][2][4][2], const Unit& u, int wr, int wc, int fr, int fq) const {
;     ...
;                     else if (pn < 16) { *(u32x4*)(GH + row * 1024 + (pn - 12) * 256 + c256) = pack8(silu4(v0), silu4(v1)); }
.LBB0_542:
	s_andn2_b64 vcc, exec, s[10:11]
	s_cbranch_vccnz .LBB0_544
	v_mul_f32_e32 v8, 0xbfb8aa3b, v4
	v_mul_f32_e32 v9, 0xbfb8aa3b, v5
	v_mul_f32_e32 v10, 0xbfb8aa3b, v6
	v_mul_f32_e32 v12, 0xbfb8aa3b, v0
	v_mul_f32_e32 v13, 0xbfb8aa3b, v1
	v_exp_f32_e32 v8, v8
	v_exp_f32_e32 v9, v9
	v_exp_f32_e32 v10, v10
	v_mul_f32_e32 v11, 0xbfb8aa3b, v7
	v_exp_f32_e32 v12, v12
	v_exp_f32_e32 v13, v13
	v_exp_f32_e32 v11, v11
	v_add_f32_e32 v8, 1.0, v8
	v_add_f32_e32 v9, 1.0, v9
	v_add_f32_e32 v10, 1.0, v10
	v_add_f32_e32 v12, 1.0, v12
	v_add_f32_e32 v13, 1.0, v13
	v_rcp_f32_e32 v8, v8
	v_rcp_f32_e32 v9, v9
	v_rcp_f32_e32 v10, v10
	v_add_f32_e32 v11, 1.0, v11
	v_rcp_f32_e32 v12, v12
	v_mul_f32_e32 v14, 0xbfb8aa3b, v2
	v_mul_f32_e32 v15, 0xbfb8aa3b, v3
	v_rcp_f32_e32 v13, v13
	v_rcp_f32_e32 v11, v11
	v_exp_f32_e32 v14, v14
	v_exp_f32_e32 v15, v15
	v_mul_f32_e32 v8, v4, v8
	v_mul_f32_e32 v9, v5, v9
	v_mul_f32_e32 v10, v6, v10
	v_mul_f32_e32 v12, v0, v12
	v_mul_f32_e32 v13, v1, v13
	v_mul_f32_e32 v11, v7, v11
	v_add_f32_e32 v14, 1.0, v14
	v_add_f32_e32 v15, 1.0, v15
	v_cvt_pk_bf16_f32 v8, v8, v9
	v_cvt_pk_bf16_f32 v9, v10, v11
	v_cvt_pk_bf16_f32 v10, v12, v13
	v_lshl_add_u64 v[12:13], s[34:35], 0, v[16:17]
	v_rcp_f32_e32 v14, v14
	v_rcp_f32_e32 v15, v15
	v_lshl_add_u64 v[12:13], s[24:25], 1, v[12:13]
	v_lshl_add_u64 v[12:13], v[138:139], 1, v[12:13]
	v_add_co_u32_e32 v12, vcc, 0xfffff000, v12
	v_mul_f32_e32 v14, v2, v14
	s_nop 0
	v_addc_co_u32_e32 v13, vcc, -1, v13, vcc
	v_mul_f32_e32 v15, v3, v15
	v_cvt_pk_bf16_f32 v11, v14, v15
	global_store_dwordx4 v[12:13], v[8:11], off offset:-2048 sc1

;     __device__ __forceinline__ static u32x4 pack8(const f32x4 a, const f32x4 b) { u32x4 w; w.x = cvt_pk_bf16(a[0], a[1]); w.y = cvt_pk_bf16(a[2], a[3]); w.z = cvt_pk_bf16(b[0], b[1]); w.w = cvt_pk_bf16(b[2], b[3]); return w; }
;     __device__ __forceinline__ void operator()(const f32x4 (&acc)[2][2][4][2], const Unit& u, int wr, int wc, int fr, int fq) const {
;     ...
;                     else if (pn < 12) { *(u32x4*)(VH + row * 1024 + (pn - 8) * 256 + c256) = pack8(v0, v1); }
.LBB0_545:
	s_andn2_b64 vcc, exec, s[10:11]
	s_cbranch_vccnz .LBB0_547
	v_lshl_add_u64 v[12:13], s[30:31], 0, v[16:17]
	v_lshl_add_u64 v[12:13], s[24:25], 1, v[12:13]
	v_lshl_add_u64 v[12:13], v[136:137], 1, v[12:13]
	v_cvt_pk_bf16_f32 v8, v4, v5
	v_cvt_pk_bf16_f32 v9, v6, v7
	v_cvt_pk_bf16_f32 v10, v0, v1
	v_cvt_pk_bf16_f32 v11, v2, v3
	global_store_dwordx4 v[12:13], v[8:11], off offset:-3840 sc1

;     __device__ __forceinline__ static u32x4 pack8(const f32x4 a, const f32x4 b) { u32x4 w; w.x = cvt_pk_bf16(a[0], a[1]); w.y = cvt_pk_bf16(a[2], a[3]); w.z = cvt_pk_bf16(b[0], b[1]); w.w = cvt_pk_bf16(b[2], b[3]); return w; }
;     __device__ __forceinline__ void operator()(const f32x4 (&acc)[2][2][4][2], const Unit& u, int wr, int wc, int fr, int fq) const {
;     ...
;                     else if (pn < 8) { const int col = (pn - 4) * 256 + c256; const f32x4 l0 = *(const f32x4*)(LB + col), l1 = *(const f32x4*)(LB + col + 4); f32x4 o0, o1;
;                         for (int i = 0; i < 4; ++i) { o0[i] = __logf(l0[i] + (1.f - l0[i]) * __builtin_amdgcn_rcpf(1.f + __expf(-v0[i]))); o1[i] = __logf(l1[i] + (1.f - l1[i]) * __builtin_amdgcn_rcpf(1.f + __expf(-v1[i]))); }
;                         *(u32x4*)(LOGF + row * 1024 + col) = pack8(o0, o1); }
.LBB0_548:
	s_andn2_b64 vcc, exec, s[10:11]
	s_cbranch_vccnz .LBB0_550
	v_add_u32_e32 v8, s33, v138
	v_ashrrev_i32_e32 v9, 31, v8
	v_lshl_add_u64 v[12:13], v[8:9], 2, s[40:41]
	global_load_dwordx4 v[8:11], v[12:13], off
	s_nop 0
	global_load_dwordx4 v[12:15], v[12:13], off offset:16
	v_mul_f32_e32 v18, 0xbfb8aa3b, v4
	v_mul_f32_e32 v19, 0xbfb8aa3b, v0
	v_exp_f32_e32 v18, v18
	v_mul_f32_e32 v20, 0xbfb8aa3b, v5
	v_exp_f32_e32 v19, v19
	v_mul_f32_e32 v21, 0xbfb8aa3b, v1
	v_exp_f32_e32 v20, v20
	v_exp_f32_e32 v21, v21
	v_mul_f32_e32 v24, 0xbfb8aa3b, v6
	v_add_f32_e32 v18, 1.0, v18
	v_exp_f32_e32 v24, v24
	v_add_f32_e32 v19, 1.0, v19
	v_rcp_f32_e32 v18, v18
	v_add_f32_e32 v20, 1.0, v20
	v_rcp_f32_e32 v19, v19
	v_add_f32_e32 v21, 1.0, v21
	v_rcp_f32_e32 v20, v20
	v_mul_f32_e32 v25, 0xbfb8aa3b, v2
	v_rcp_f32_e32 v21, v21
	v_exp_f32_e32 v25, v25
	v_add_f32_e32 v24, 1.0, v24
	v_rcp_f32_e32 v24, v24
	v_add_f32_e32 v25, 1.0, v25
	v_rcp_f32_e32 v25, v25
	s_waitcnt vmcnt(0)
	v_sub_f32_e32 v26, 1.0, v8
	v_sub_f32_e32 v27, 1.0, v12
	v_fma_f32 v8, v18, v26, v8
	v_sub_f32_e32 v28, 1.0, v9
	v_fma_f32 v12, v19, v27, v12
	v_cmp_gt_f32_e32 vcc, s82, v8
	v_sub_f32_e32 v29, 1.0, v13
	v_fma_f32 v9, v20, v28, v9
	v_cndmask_b32_e64 v18, 0, 32, vcc
	v_cmp_gt_f32_e64 s[10:11], s82, v12
	v_fma_f32 v13, v21, v29, v13
	v_cmp_gt_f32_e64 s[12:13], s82, v9
	v_cndmask_b32_e64 v19, 0, 32, s[10:11]
	v_ldexp_f32 v8, v8, v18
	v_sub_f32_e32 v30, 1.0, v10
	v_cndmask_b32_e64 v20, 0, 32, s[12:13]
	v_cmp_gt_f32_e64 s[14:15], s82, v13
	v_ldexp_f32 v12, v12, v19
	v_log_f32_e32 v8, v8
	v_fma_f32 v10, v24, v30, v10
	v_cndmask_b32_e64 v21, 0, 32, s[14:15]
	v_ldexp_f32 v9, v9, v20
	v_log_f32_e32 v12, v12
	v_cmp_gt_f32_e64 s[16:17], s82, v10
	v_ldexp_f32 v13, v13, v21
	v_log_f32_e32 v9, v9
	v_cndmask_b32_e64 v24, 0, 32, s[16:17]
	v_log_f32_e32 v13, v13
	v_sub_f32_e32 v31, 1.0, v14
	v_ldexp_f32 v10, v10, v24
	v_mul_f32_e32 v24, 0x3f317217, v8
	v_fma_f32 v14, v25, v31, v14
	v_mul_f32_e32 v25, 0x3f317217, v12
	v_fma_f32 v24, v8, s83, -v24
	v_mul_f32_e32 v26, 0x3f317217, v9
	v_fma_f32 v25, v12, s83, -v25
	v_fmac_f32_e32 v24, 0x3377d1cf, v8
	v_cndmask_b32_e32 v18, 0, v167, vcc
	v_mul_f32_e32 v27, 0x3f317217, v13
	v_fma_f32 v26, v9, s83, -v26
	v_fmac_f32_e32 v25, 0x3377d1cf, v12
	v_fmac_f32_e32 v24, 0x3f317217, v8
	v_cmp_lt_f32_e64 vcc, |v8|, s84
	v_fma_f32 v27, v13, s83, -v27
	v_fmac_f32_e32 v26, 0x3377d1cf, v9
	v_fmac_f32_e32 v25, 0x3f317217, v12
	v_cndmask_b32_e32 v8, v8, v24, vcc
	v_cmp_lt_f32_e64 vcc, |v12|, s84
	v_log_f32_e32 v10, v10
	v_fmac_f32_e32 v27, 0x3377d1cf, v13
	v_fmac_f32_e32 v26, 0x3f317217, v9
	v_cndmask_b32_e32 v12, v12, v25, vcc
	v_cmp_lt_f32_e64 vcc, |v9|, s84
	v_cndmask_b32_e64 v19, 0, v167, s[10:11]
	v_fmac_f32_e32 v27, 0x3f317217, v13
	v_cndmask_b32_e32 v9, v9, v26, vcc
	v_cmp_lt_f32_e64 vcc, |v13|, s84
	v_sub_f32_e32 v12, v12, v19
	v_mul_f32_e32 v19, 0xbfb8aa3b, v7
	v_cndmask_b32_e32 v13, v13, v27, vcc
	v_cmp_gt_f32_e32 vcc, s82, v14
	v_sub_f32_e32 v8, v8, v18
	v_exp_f32_e32 v19, v19
	v_cndmask_b32_e64 v18, 0, 32, vcc
	v_mul_f32_e32 v28, 0x3f317217, v10
	v_ldexp_f32 v14, v14, v18
	v_fma_f32 v28, v10, s83, -v28
	v_log_f32_e32 v14, v14
	v_fmac_f32_e32 v28, 0x3377d1cf, v10
	v_fmac_f32_e32 v28, 0x3f317217, v10
	v_cmp_lt_f32_e64 s[10:11], |v10|, s84
	v_add_f32_e32 v19, 1.0, v19
	v_cndmask_b32_e64 v18, 0, v167, s[16:17]
	v_cndmask_b32_e64 v10, v10, v28, s[10:11]
	v_rcp_f32_e32 v19, v19
	v_sub_f32_e32 v10, v10, v18
	v_mul_f32_e32 v18, 0x3f317217, v14
	v_cndmask_b32_e64 v20, 0, v167, s[12:13]
	v_fma_f32 v18, v14, s83, -v18
	v_sub_f32_e32 v9, v9, v20
	v_fmac_f32_e32 v18, 0x3377d1cf, v14
	v_sub_f32_e32 v20, 1.0, v11
	v_fmac_f32_e32 v18, 0x3f317217, v14
	v_cmp_lt_f32_e64 s[10:11], |v14|, s84
	v_fmac_f32_e32 v11, v19, v20
	v_sub_f32_e32 v20, 1.0, v15
	v_cndmask_b32_e64 v14, v14, v18, s[10:11]
	v_cndmask_b32_e32 v18, 0, v167, vcc
	v_cmp_gt_f32_e32 vcc, s82, v11
	v_sub_f32_e32 v14, v14, v18
	v_cndmask_b32_e64 v21, 0, v167, s[14:15]
	v_cndmask_b32_e64 v19, 0, 32, vcc
	v_ldexp_f32 v11, v11, v19
	v_mul_f32_e32 v19, 0xbfb8aa3b, v3
	v_exp_f32_e32 v19, v19
	v_log_f32_e32 v11, v11
	v_sub_f32_e32 v13, v13, v21
	v_cvt_pk_bf16_f32 v8, v8, v9
	v_add_f32_e32 v19, 1.0, v19
	v_rcp_f32_e32 v19, v19
	v_mul_f32_e32 v18, 0x3f317217, v11
	v_fma_f32 v18, v11, s83, -v18
	v_fmac_f32_e32 v18, 0x3377d1cf, v11
	v_fmac_f32_e32 v15, v19, v20
	v_cmp_gt_f32_e64 s[10:11], s82, v15
	v_fmac_f32_e32 v18, 0x3f317217, v11
	v_cmp_lt_f32_e64 s[12:13], |v11|, s84
	v_cndmask_b32_e64 v19, 0, 32, s[10:11]
	v_ldexp_f32 v15, v15, v19
	v_log_f32_e32 v15, v15
	v_cndmask_b32_e64 v11, v11, v18, s[12:13]
	v_cndmask_b32_e32 v18, 0, v167, vcc
	v_sub_f32_e32 v11, v11, v18
	v_mul_f32_e32 v18, 0x3f317217, v15
	v_fma_f32 v18, v15, s83, -v18
	v_fmac_f32_e32 v18, 0x3377d1cf, v15
	v_fmac_f32_e32 v18, 0x3f317217, v15
	v_cmp_lt_f32_e64 vcc, |v15|, s84
	v_cvt_pk_bf16_f32 v9, v10, v11
	v_cvt_pk_bf16_f32 v10, v12, v13
	v_lshl_add_u64 v[12:13], s[38:39], 0, v[16:17]
	s_nop 0
	v_cndmask_b32_e32 v15, v15, v18, vcc
	v_cndmask_b32_e64 v18, 0, v167, s[10:11]
	v_sub_f32_e32 v15, v15, v18
	v_cvt_pk_bf16_f32 v11, v14, v15
	v_lshl_add_u64 v[14:15], s[0:1], 0, v[138:139]
	v_lshl_add_u64 v[12:13], v[14:15], 1, v[12:13]
	global_store_dwordx4 v[12:13], v[8:11], off offset:-2048 sc1

;     __device__ __forceinline__ static u32x4 pack8(const f32x4 a, const f32x4 b) { u32x4 w; w.x = cvt_pk_bf16(a[0], a[1]); w.y = cvt_pk_bf16(a[2], a[3]); w.z = cvt_pk_bf16(b[0], b[1]); w.w = cvt_pk_bf16(b[2], b[3]); return w; }
;     __device__ __forceinline__ static f32x4 silu4(const f32x4 v) { f32x4 o; for (int i = 0; i < 4; ++i) o[i] = v[i] * __builtin_amdgcn_rcpf(1.f + __expf(-v[i])); return o; }
;     __device__ __forceinline__ void operator()(const f32x4 (&acc)[2][2][4][2], const Unit& u, int wr, int wc, int fr, int fq) const {
;     ...
;                     if (pn < 4) { *(u32x4*)(QH + row * 1024 + pn * 256 + c256) = pack8(silu4(v0), silu4(v1)); }
.LBB0_551:
	s_nop 0
	v_mul_f32_e32 v8, 0xbfb8aa3b, v4
	v_mul_f32_e32 v9, 0xbfb8aa3b, v5
	v_mul_f32_e32 v10, 0xbfb8aa3b, v6
	v_exp_f32_e32 v8, v8
	v_exp_f32_e32 v9, v9
	v_exp_f32_e32 v10, v10
	v_mul_f32_e32 v11, 0xbfb8aa3b, v7
	v_add_f32_e32 v8, 1.0, v8
	v_add_f32_e32 v9, 1.0, v9
	v_add_f32_e32 v10, 1.0, v10
	v_rcp_f32_e32 v8, v8
	v_rcp_f32_e32 v9, v9
	v_rcp_f32_e32 v10, v10
	v_exp_f32_e32 v11, v11
	v_mul_f32_e32 v4, v4, v8
	v_mul_f32_e32 v5, v5, v9
	v_mul_f32_e32 v6, v6, v10
	v_add_f32_e32 v8, 1.0, v11
	v_mul_f32_e32 v9, 0xbfb8aa3b, v0
	v_mul_f32_e32 v10, 0xbfb8aa3b, v1
	v_rcp_f32_e32 v8, v8
	v_exp_f32_e32 v9, v9
	v_exp_f32_e32 v10, v10
	v_mul_f32_e32 v11, 0xbfb8aa3b, v3
	v_mul_f32_e32 v7, v7, v8
	v_add_f32_e32 v8, 1.0, v9
	v_add_f32_e32 v9, 1.0, v10
	v_mul_f32_e32 v10, 0xbfb8aa3b, v2
	v_exp_f32_e32 v11, v11
	v_exp_f32_e32 v10, v10
	v_rcp_f32_e32 v8, v8
	v_rcp_f32_e32 v9, v9
	v_add_f32_e32 v11, 1.0, v11
	v_add_f32_e32 v10, 1.0, v10
	v_rcp_f32_e32 v11, v11
	v_rcp_f32_e32 v10, v10
	v_mul_f32_e32 v8, v0, v8
	v_cvt_pk_bf16_f32 v0, v4, v5
	v_mul_f32_e32 v3, v3, v11
	v_lshl_add_u64 v[4:5], v[136:137], 1, v[22:23]
	v_mul_f32_e32 v9, v1, v9
	v_mul_f32_e32 v10, v2, v10
	v_cvt_pk_bf16_f32 v1, v6, v7
	v_cvt_pk_bf16_f32 v2, v8, v9
	v_cvt_pk_bf16_f32 v3, v10, v3
	global_store_dwordx4 v[4:5], v[0:3], off offset:256 sc1
	s_andn2_b64 vcc, exec, s[8:9]
	s_mov_b64 s[0:1], -1
	s_cbranch_vccnz .LBB0_128

.LBB0_741:
	s_or_b64 exec, exec, s[6:7]
	s_lshl_b32 s0, s77, 2
	s_or_b32 s1, s0, 3
	v_mov_b32_e32 v175, v173
	s_lshl_b32 s0, s70, 6
	v_mov_b32_e32 v115, 0
	v_permlane32_swap_b32_e32 v173, v175
	s_cmp_ge_i32 s0, s1
	v_mov_b32_e32 v114, v115
	v_mov_b32_e32 v117, v115
	v_mov_b32_e32 v116, v115
	v_mov_b32_e32 v119, v115
	v_mov_b32_e32 v118, v115
	v_mov_b32_e32 v121, v115
	v_mov_b32_e32 v120, v115
	v_mov_b32_e32 v123, v115
	v_mov_b32_e32 v122, v115
	v_mov_b32_e32 v125, v115
	v_mov_b32_e32 v124, v115
	v_mov_b32_e32 v127, v115
	v_mov_b32_e32 v126, v115
	v_mov_b32_e32 v129, v115
	v_mov_b32_e32 v128, v115
	v_mov_b32_e32 v99, v115
	v_mov_b32_e32 v98, v115
	v_mov_b32_e32 v101, v115
	v_mov_b32_e32 v100, v115
	v_mov_b32_e32 v103, v115
	v_mov_b32_e32 v102, v115
	v_mov_b32_e32 v105, v115
	v_mov_b32_e32 v104, v115
	v_mov_b32_e32 v109, v115
	v_mov_b32_e32 v108, v115
	v_mov_b32_e32 v111, v115
	v_mov_b32_e32 v110, v115
	v_mov_b32_e32 v113, v115
	v_mov_b32_e32 v112, v115
	v_mov_b32_e32 v107, v115
	v_mov_b32_e32 v106, v115
	s_waitcnt lgkmcnt(0)
	s_barrier
	s_cbranch_scc1 .LBB0_745
	s_mul_i32 s1, s70, 0x2400
	s_add_i32 s1, s1, 0
	v_add3_u32 v32, s1, v97, v168
	ds_read_b128 v[64:67], v32
	ds_read_b128 v[68:71], v32 offset:32
	ds_read_b128 v[72:75], v32 offset:4608
	ds_read_b128 v[76:79], v32 offset:4640
	ds_read_b128 v[80:83], v32 offset:64
	ds_read_b128 v[84:87], v32 offset:96
	ds_read_b128 v[88:91], v32 offset:4672
	ds_read_b128 v[92:95], v32 offset:4704
	v_or_b32_e32 v32, s0, v229
	v_sub_u32_e32 v32, v133, v32
	s_add_i32 s0, s80, 0x48e
	v_cmp_lt_i32_e32 vcc, 27, v32
	v_cmp_lt_i32_e64 s[6:7], 26, v32
	v_cmp_lt_i32_e64 s[8:9], 25, v32
	v_cmp_lt_i32_e64 s[10:11], 24, v32
	v_cmp_lt_i32_e64 s[12:13], 19, v32
	v_cmp_lt_i32_e64 s[14:15], 18, v32
	v_cmp_lt_i32_e64 s[16:17], 17, v32
	v_cmp_lt_i32_e64 s[18:19], 16, v32
	v_cmp_lt_i32_e64 s[20:21], 11, v32
	v_cmp_lt_i32_e64 s[22:23], 10, v32
	v_cmp_lt_i32_e64 s[24:25], 9, v32
	v_cmp_lt_i32_e64 s[26:27], 8, v32
	v_cmp_lt_i32_e64 s[28:29], 3, v32
	v_cmp_lt_i32_e64 s[30:31], 2, v32
	v_cmp_lt_i32_e64 s[34:35], 1, v32
	v_cmp_lt_i32_e64 s[36:37], 0, v32
	v_cmp_lt_i32_e64 s[38:39], 59, v32
	v_cmp_lt_i32_e64 s[40:41], 58, v32
	v_cmp_lt_i32_e64 s[42:43], 57, v32
	v_cmp_lt_i32_e64 s[44:45], 56, v32
	v_cmp_lt_i32_e64 s[46:47], 51, v32
	v_cmp_lt_i32_e64 s[48:49], 50, v32
	v_cmp_lt_i32_e64 s[50:51], 49, v32
	v_cmp_lt_i32_e64 s[52:53], 48, v32
	v_cmp_lt_i32_e64 s[54:55], 43, v32
	v_cmp_lt_i32_e64 s[56:57], 42, v32
	v_cmp_lt_i32_e64 s[58:59], 41, v32
	v_cmp_lt_i32_e64 s[60:61], 40, v32
	v_cmp_lt_i32_e64 s[62:63], 35, v32
	v_cmp_lt_i32_e64 s[64:65], 34, v32
	v_cmp_lt_i32_e64 s[66:67], 33, v32
	v_cmp_lt_i32_e64 s[68:69], 32, v32
	v_add_u32_e32 v32, s0, v132
	s_add_i32 s0, s76, s2
	v_add_u32_e32 v33, s0, v172
	v_sub_u32_e32 v32, v32, v33
	v_med3_i32 v32, v32, 0, v223
	s_add_i32 s0, s80, 0x47e
	v_lshl_or_b32 v141, v32, 2, v226
	v_add_u32_e32 v32, s0, v132
	v_sub_u32_e32 v32, v32, v33
	v_med3_i32 v32, v32, 0, v223
	s_add_i32 s0, s80, 0x46e
	v_lshl_or_b32 v142, v32, 2, v226
	v_add_u32_e32 v32, s0, v132
	v_sub_u32_e32 v32, v32, v33
	v_med3_i32 v32, v32, 0, v223
	s_add_i32 s0, s80, 0x45e
	v_lshl_or_b32 v143, v32, 2, v226
	v_add_u32_e32 v32, s0, v132
	v_sub_u32_e32 v32, v32, v33
	v_med3_i32 v32, v32, 0, v223
	s_add_i32 s0, s80, 0x40e
	v_lshl_or_b32 v160, v32, 2, v226
	v_add_u32_e32 v32, s0, v132
	v_sub_u32_e32 v32, v32, v33
	v_med3_i32 v32, v32, 0, v223
	s_add_i32 s0, s80, 0x3fe
	v_lshl_or_b32 v161, v32, 2, v226
	v_add_u32_e32 v32, s0, v132
	v_sub_u32_e32 v32, v32, v33
	v_med3_i32 v32, v32, 0, v223
	s_add_i32 s0, s80, 0x3ee
	v_lshl_or_b32 v162, v32, 2, v226
	v_add_u32_e32 v32, s0, v132
	v_sub_u32_e32 v32, v32, v33
	v_med3_i32 v32, v32, 0, v223
	s_add_i32 s0, s80, 0x3de
	v_lshl_or_b32 v163, v32, 2, v226
	v_add_u32_e32 v32, s0, v132
	v_sub_u32_e32 v32, v32, v33
	v_med3_i32 v32, v32, 0, v223
	s_add_i32 s0, s80, 0x38e
	v_lshl_or_b32 v164, v32, 2, v226
	v_add_u32_e32 v32, s0, v132
	v_sub_u32_e32 v32, v32, v33
	v_med3_i32 v32, v32, 0, v223
	s_add_i32 s0, s80, 0x37e
	v_lshl_or_b32 v165, v32, 2, v226
	v_add_u32_e32 v32, s0, v132
	v_sub_u32_e32 v32, v32, v33
	v_med3_i32 v32, v32, 0, v223
	s_add_i32 s0, s80, 0x36e
	v_lshl_or_b32 v166, v32, 2, v226
	v_add_u32_e32 v32, s0, v132
	v_sub_u32_e32 v32, v32, v33
	v_med3_i32 v32, v32, 0, v223
	s_add_i32 s0, s80, 0x35e
	v_lshl_or_b32 v167, v32, 2, v226
	v_add_u32_e32 v32, s0, v132
	v_sub_u32_e32 v32, v32, v33
	v_med3_i32 v32, v32, 0, v223
	s_add_i32 s0, s80, 0x30e
	v_lshl_or_b32 v174, v32, 2, v226
	v_add_u32_e32 v32, s0, v132
	v_sub_u32_e32 v32, v32, v33
	v_med3_i32 v32, v32, 0, v223
	s_add_i32 s0, s80, 0x2fe
	v_lshl_or_b32 v176, v32, 2, v226
	v_add_u32_e32 v32, s0, v132
	v_sub_u32_e32 v32, v32, v33
	v_med3_i32 v32, v32, 0, v223
	s_add_i32 s0, s80, 0x2ee
	v_lshl_or_b32 v177, v32, 2, v226
	v_add_u32_e32 v32, s0, v132
	v_sub_u32_e32 v32, v32, v33
	v_med3_i32 v32, v32, 0, v223
	s_add_i32 s0, s80, 0x2de
	v_lshl_or_b32 v178, v32, 2, v226
	v_add_u32_e32 v32, s0, v132
	v_sub_u32_e32 v32, v32, v33
	v_med3_i32 v32, v32, 0, v223
	s_add_i32 s0, s80, 0x28e
	v_lshl_or_b32 v179, v32, 2, v226
	v_add_u32_e32 v32, s0, v132
	v_sub_u32_e32 v32, v32, v33
	v_med3_i32 v32, v32, 0, v223
	s_add_i32 s0, s80, 0x27e
	v_lshl_or_b32 v180, v32, 2, v226
	v_add_u32_e32 v32, s0, v132
	v_sub_u32_e32 v32, v32, v33
	v_med3_i32 v32, v32, 0, v223
	s_add_i32 s0, s80, 0x26e
	v_lshl_or_b32 v181, v32, 2, v226
	v_add_u32_e32 v32, s0, v132
	v_sub_u32_e32 v32, v32, v33
	v_med3_i32 v32, v32, 0, v223
	s_add_i32 s0, s80, 0x25e
	v_lshl_or_b32 v182, v32, 2, v226
	v_add_u32_e32 v32, s0, v132
	v_sub_u32_e32 v32, v32, v33
	v_med3_i32 v32, v32, 0, v223
	s_add_i32 s0, s80, 0x20e
	v_lshl_or_b32 v183, v32, 2, v226
	v_add_u32_e32 v32, s0, v132
	v_sub_u32_e32 v32, v32, v33
	v_med3_i32 v32, v32, 0, v223
	s_add_i32 s0, s80, 0x1fe
	v_lshl_or_b32 v184, v32, 2, v226
	v_add_u32_e32 v32, s0, v132
	v_sub_u32_e32 v32, v32, v33
	v_med3_i32 v32, v32, 0, v223
	s_add_i32 s0, s80, 0x1ee
	v_lshl_or_b32 v185, v32, 2, v226
	v_add_u32_e32 v32, s0, v132
	v_sub_u32_e32 v32, v32, v33
	v_med3_i32 v32, v32, 0, v223
	s_add_i32 s0, s80, 0x1de
	v_lshl_or_b32 v186, v32, 2, v226
	v_add_u32_e32 v32, s0, v132
	v_sub_u32_e32 v32, v32, v33
	v_med3_i32 v32, v32, 0, v223
	s_add_i32 s0, s80, 0x18e
	v_lshl_or_b32 v187, v32, 2, v226
	v_add_u32_e32 v32, s0, v132
	v_sub_u32_e32 v32, v32, v33
	v_med3_i32 v32, v32, 0, v223
	s_add_i32 s0, s80, 0x17e
	v_lshl_or_b32 v188, v32, 2, v226
	v_add_u32_e32 v32, s0, v132
	v_sub_u32_e32 v32, v32, v33
	v_med3_i32 v32, v32, 0, v223
	s_add_i32 s0, s80, 0x16e
	v_lshl_or_b32 v189, v32, 2, v226
	v_add_u32_e32 v32, s0, v132
	v_sub_u32_e32 v32, v32, v33
	v_med3_i32 v32, v32, 0, v223
	s_add_i32 s0, s80, 0x15e
	v_lshl_or_b32 v190, v32, 2, v226
	v_add_u32_e32 v32, s0, v132
	v_sub_u32_e32 v32, v32, v33
	v_med3_i32 v32, v32, 0, v223
	s_add_i32 s0, s80, 0x10e
	v_lshl_or_b32 v191, v32, 2, v226
	v_add_u32_e32 v32, s0, v132
	v_sub_u32_e32 v32, v32, v33
	v_med3_i32 v32, v32, 0, v223
	s_add_i32 s0, s80, 0xfe
	v_lshl_or_b32 v192, v32, 2, v226
	v_add_u32_e32 v32, s0, v132
	v_sub_u32_e32 v32, v32, v33
	v_med3_i32 v32, v32, 0, v223
	s_add_i32 s0, s80, 0xee
	v_lshl_or_b32 v193, v32, 2, v226
	v_add_u32_e32 v32, s0, v132
	v_sub_u32_e32 v32, v32, v33
	v_med3_i32 v32, v32, 0, v223
	s_add_i32 s0, s80, 0xde
	v_lshl_or_b32 v194, v32, 2, v226
	v_add_u32_e32 v32, s0, v132
	v_sub_u32_e32 v32, v32, v33
	v_med3_i32 v32, v32, 0, v223
	v_lshl_or_b32 v195, v32, 2, v226
	s_and_b32 s0, s33, 1
	v_lshlrev_b32_e32 v32, 3, v172
	v_lshl_or_b32 v196, s0, 8, v32
	v_and_b32_e32 v32, 32, v96
	v_lshrrev_b32_e32 v32, 1, v32
	v_mov_b32_e32 v33, v169
	v_readlane_b32 s0, v248, 58
	v_lshl_add_u64 v[32:33], v[130:131], 0, v[32:33]
	v_readlane_b32 s1, v248, 59
	v_mov_b32_e32 v106, 0
	s_mov_b64 s[72:73], 0
	v_lshl_add_u64 v[130:131], s[0:1], 0, v[32:33]
	v_lshl_add_u64 v[214:215], v[130:131], 0, s[72:73]
	global_load_dwordx4 v[210:213], v[214:215], off offset:-64
	global_load_dwordx4 v[198:201], v[214:215], off offset:-32
	global_load_dwordx4 v[202:205], v[214:215], off
	global_load_dwordx4 v[206:209], v[214:215], off offset:32
	v_mov_b32_e32 v107, v106
	v_mov_b32_e32 v112, v106
	v_mov_b32_e32 v113, v106
	v_mov_b32_e32 v110, v106
	v_mov_b32_e32 v111, v106
	v_mov_b32_e32 v108, v106
	v_mov_b32_e32 v109, v106
	v_mov_b32_e32 v104, v106
	v_mov_b32_e32 v105, v106
	v_mov_b32_e32 v102, v106
	v_mov_b32_e32 v103, v106
	v_mov_b32_e32 v100, v106
	v_mov_b32_e32 v101, v106
	v_mov_b32_e32 v98, v106
	v_mov_b32_e32 v99, v106
	v_mov_b32_e32 v128, v106
	v_mov_b32_e32 v129, v106
	v_mov_b32_e32 v126, v106
	v_mov_b32_e32 v127, v106
	v_mov_b32_e32 v124, v106
	v_mov_b32_e32 v125, v106
	v_mov_b32_e32 v122, v106
	v_mov_b32_e32 v123, v106
	v_mov_b32_e32 v120, v106
	v_mov_b32_e32 v121, v106
	v_mov_b32_e32 v118, v106
	v_mov_b32_e32 v119, v106
	v_mov_b32_e32 v116, v106
	v_mov_b32_e32 v117, v106
	v_mov_b32_e32 v114, v106
	v_mov_b32_e32 v115, v106
.LBB0_743:
	v_add_u32_e32 v132, 0, v196
	v_add_u32_e32 v132, 0x12400, v132
	v_add_u32_e32 v197, 0, v195
	ds_read_b64 v[132:133], v132
	ds_read_b32 v197, v197
	s_add_u32 s72, s72, 0x80
	s_addc_u32 s73, s73, 0
	v_add_u32_e32 v195, 0x400, v195
	v_add_u32_e32 v196, 0x200, v196
	s_cmpk_lg_i32 s72, 0x200
	s_waitcnt vmcnt(3) lgkmcnt(9)
	v_mfma_f32_32x32x16_bf16 v[48:63], v[64:67], v[210:213], 0
	s_waitcnt vmcnt(2) lgkmcnt(8)
	v_mfma_f32_32x32x16_bf16 v[48:63], v[68:71], v[198:201], v[48:63]
	s_waitcnt vmcnt(1) lgkmcnt(5)
	v_mfma_f32_32x32x16_bf16 v[48:63], v[80:83], v[202:205], v[48:63]
	v_mfma_f32_32x32x16_bf16 v[32:47], v[72:75], v[210:213], 0
	s_waitcnt vmcnt(0) lgkmcnt(4)
	v_mfma_f32_32x32x16_bf16 v[48:63], v[84:87], v[206:209], v[48:63]
	v_mfma_f32_32x32x16_bf16 v[32:47], v[76:79], v[198:201], v[32:47]
	s_waitcnt lgkmcnt(0)
	s_nop 9
	v_add_f32_e32 v48, v48, v197
	v_add_u32_e32 v197, 0, v194
	ds_read_b32 v197, v197
	v_sub_f32_e32 v48, v48, v132
	v_exp_f32_e32 v48, v48
	v_add_u32_e32 v194, 0x400, v194
	s_waitcnt lgkmcnt(0)
	v_add_f32_e32 v49, v49, v197
	v_mfma_f32_32x32x16_bf16 v[32:47], v[88:91], v[202:205], v[32:47]
	v_sub_f32_e32 v49, v49, v132
	v_exp_f32_e32 v49, v49
	v_add_u32_e32 v197, 0, v193
	ds_read_b32 v197, v197
	v_add_u32_e32 v193, 0x400, v193
	v_pk_mul_f32 v[48:49], v[132:133], v[48:49] op_sel:[1,0]
	v_mfma_f32_32x32x16_bf16 v[32:47], v[92:95], v[206:209], v[32:47]
	s_cbranch_scc0 .Limp_nopf
	v_lshl_add_u64 v[214:215], v[130:131], 0, s[72:73]
	global_load_dwordx4 v[210:213], v[214:215], off offset:-64
	global_load_dwordx4 v[198:201], v[214:215], off offset:-32
	global_load_dwordx4 v[202:205], v[214:215], off
	global_load_dwordx4 v[206:209], v[214:215], off offset:32
.Limp_nopf:
	v_cndmask_b32_e64 v49, 0, v49, s[34:35]
	v_cndmask_b32_e64 v48, 0, v48, s[36:37]
	v_add_f32_e64 v128, v128, v48
	v_add_f32_e64 v129, v129, v49
	v_add_u32_e32 v48, 0, v179
	ds_read_b32 v48, v48
	s_waitcnt lgkmcnt(1)
	v_add_f32_e32 v50, v50, v197
	v_add_u32_e32 v197, 0, v192
	ds_read_b32 v197, v197
	v_sub_f32_e32 v50, v50, v132
	s_waitcnt lgkmcnt(1)
	v_add_f32_e32 v32, v32, v48
	v_add_u32_e32 v48, 0, v178
	ds_read_b32 v48, v48
	s_waitcnt lgkmcnt(1)
	v_add_f32_e32 v51, v51, v197
	v_add_u32_e32 v197, 0, v191
	ds_read_b32 v197, v197
	v_sub_f32_e32 v51, v51, v132
	s_waitcnt lgkmcnt(1)
	v_add_f32_e32 v33, v33, v48
	v_add_u32_e32 v48, 0, v177
	ds_read_b32 v48, v48
	s_waitcnt lgkmcnt(1)
	v_add_f32_e32 v52, v52, v197
	v_add_u32_e32 v197, 0, v190
	ds_read_b32 v197, v197
	v_sub_f32_e32 v52, v52, v132
	s_waitcnt lgkmcnt(1)
	v_add_f32_e32 v34, v34, v48
	v_add_u32_e32 v48, 0, v176
	ds_read_b32 v48, v48
	s_waitcnt lgkmcnt(1)
	v_add_f32_e32 v53, v53, v197
	v_add_u32_e32 v197, 0, v189
	ds_read_b32 v197, v197
	v_sub_f32_e32 v53, v53, v132
	s_waitcnt lgkmcnt(1)
	v_add_f32_e32 v35, v35, v48
	v_add_u32_e32 v48, 0, v174
	ds_read_b32 v48, v48
	s_waitcnt lgkmcnt(1)
	v_add_f32_e32 v54, v54, v197
	v_add_u32_e32 v197, 0, v188
	ds_read_b32 v197, v197
	v_sub_f32_e32 v54, v54, v132
	s_waitcnt lgkmcnt(1)
	v_add_f32_e32 v36, v36, v48
	v_add_u32_e32 v48, 0, v167
	ds_read_b32 v48, v48
	s_waitcnt lgkmcnt(1)
	v_add_f32_e32 v55, v55, v197
	v_add_u32_e32 v197, 0, v187
	ds_read_b32 v197, v197
	v_sub_f32_e32 v55, v55, v132
	s_waitcnt lgkmcnt(1)
	v_add_f32_e32 v37, v37, v48
	v_add_u32_e32 v48, 0, v166
	ds_read_b32 v48, v48
	s_waitcnt lgkmcnt(1)
	v_add_f32_e32 v56, v56, v197
	v_add_u32_e32 v197, 0, v186
	ds_read_b32 v197, v197
	v_sub_f32_e32 v56, v56, v132
	s_waitcnt lgkmcnt(1)
	v_add_f32_e32 v38, v38, v48
	v_add_u32_e32 v48, 0, v165
	ds_read_b32 v48, v48
	s_waitcnt lgkmcnt(1)
	v_add_f32_e32 v57, v57, v197
	v_add_u32_e32 v197, 0, v185
	ds_read_b32 v197, v197
	v_sub_f32_e32 v57, v57, v132
	s_waitcnt lgkmcnt(1)
	v_add_f32_e32 v39, v39, v48
	v_add_u32_e32 v48, 0, v164
	ds_read_b32 v48, v48
	s_waitcnt lgkmcnt(1)
	v_add_f32_e32 v58, v58, v197
	v_add_u32_e32 v197, 0, v184
	ds_read_b32 v197, v197
	v_sub_f32_e32 v58, v58, v132
	s_waitcnt lgkmcnt(1)
	v_add_f32_e32 v40, v40, v48
	v_add_u32_e32 v48, 0, v163
	ds_read_b32 v48, v48
	s_waitcnt lgkmcnt(1)
	v_add_f32_e32 v59, v59, v197
	v_add_u32_e32 v197, 0, v183
	ds_read_b32 v197, v197
	v_sub_f32_e32 v59, v59, v132
	s_waitcnt lgkmcnt(1)
	v_add_f32_e32 v41, v41, v48
	v_add_u32_e32 v48, 0, v162
	ds_read_b32 v48, v48
	s_waitcnt lgkmcnt(1)
	v_add_f32_e32 v60, v60, v197
	v_add_u32_e32 v197, 0, v182
	ds_read_b32 v197, v197
	v_sub_f32_e32 v60, v60, v132
	s_waitcnt lgkmcnt(1)
	v_add_f32_e32 v42, v42, v48
	v_add_u32_e32 v48, 0, v161
	ds_read_b32 v48, v48
	s_waitcnt lgkmcnt(1)
	v_add_f32_e32 v61, v61, v197
	v_add_u32_e32 v197, 0, v181
	ds_read_b32 v197, v197
	v_sub_f32_e32 v61, v61, v132
	s_waitcnt lgkmcnt(1)
	v_add_f32_e32 v43, v43, v48
	v_add_u32_e32 v48, 0, v160
	ds_read_b32 v48, v48
	s_waitcnt lgkmcnt(1)
	v_add_f32_e32 v62, v62, v197
	v_add_u32_e32 v197, 0, v180
	ds_read_b32 v197, v197
	v_sub_f32_e32 v62, v62, v132
	s_waitcnt lgkmcnt(1)
	v_add_f32_e32 v44, v44, v48
	v_add_u32_e32 v48, 0, v143
	ds_read_b32 v48, v48
	s_waitcnt lgkmcnt(1)
	v_add_f32_e32 v63, v63, v197
	v_sub_f32_e32 v63, v63, v132
	v_sub_f32_e32 v32, v32, v132
	v_sub_f32_e32 v33, v33, v132
	s_waitcnt lgkmcnt(0)
	v_add_f32_e32 v45, v45, v48
	v_add_u32_e32 v48, 0, v142
	ds_read_b32 v48, v48
	v_sub_f32_e32 v34, v34, v132
	v_sub_f32_e32 v35, v35, v132
	v_sub_f32_e32 v36, v36, v132
	v_sub_f32_e32 v37, v37, v132
	s_waitcnt lgkmcnt(0)
	v_add_f32_e32 v46, v46, v48
	v_add_u32_e32 v48, 0, v141
	ds_read_b32 v48, v48
	v_sub_f32_e32 v38, v38, v132
	v_sub_f32_e32 v39, v39, v132
	v_sub_f32_e32 v40, v40, v132
	v_sub_f32_e32 v41, v41, v132
	s_waitcnt lgkmcnt(0)
	v_add_f32_e32 v47, v47, v48
	v_sub_f32_e32 v42, v42, v132
	v_sub_f32_e32 v43, v43, v132
	v_sub_f32_e32 v44, v44, v132
	v_sub_f32_e32 v45, v45, v132
	v_sub_f32_e32 v46, v46, v132
	v_sub_f32_e32 v47, v47, v132
	v_exp_f32_e32 v50, v50
	v_exp_f32_e32 v51, v51
	v_exp_f32_e32 v52, v52
	v_exp_f32_e32 v53, v53
	v_exp_f32_e32 v54, v54
	v_exp_f32_e32 v55, v55
	v_exp_f32_e32 v56, v56
	v_exp_f32_e32 v57, v57
	v_exp_f32_e32 v58, v58
	v_exp_f32_e32 v59, v59
	v_exp_f32_e32 v60, v60
	v_exp_f32_e32 v61, v61
	v_exp_f32_e32 v62, v62
	v_exp_f32_e32 v63, v63
	v_exp_f32_e32 v32, v32
	v_exp_f32_e32 v33, v33
	v_exp_f32_e32 v34, v34
	v_exp_f32_e32 v35, v35
	v_exp_f32_e32 v36, v36
	v_exp_f32_e32 v37, v37
	v_exp_f32_e32 v38, v38
	v_exp_f32_e32 v39, v39
	v_exp_f32_e32 v40, v40
	v_exp_f32_e32 v41, v41
	v_exp_f32_e32 v42, v42
	v_exp_f32_e32 v43, v43
	v_exp_f32_e32 v44, v44
	v_exp_f32_e32 v45, v45
	v_exp_f32_e32 v46, v46
	v_exp_f32_e32 v47, v47
	v_pk_mul_f32 v[62:63], v[132:133], v[62:63] op_sel:[1,0]
	v_pk_mul_f32 v[60:61], v[132:133], v[60:61] op_sel:[1,0]
	v_pk_mul_f32 v[58:59], v[132:133], v[58:59] op_sel:[1,0]
	v_pk_mul_f32 v[56:57], v[132:133], v[56:57] op_sel:[1,0]
	v_pk_mul_f32 v[54:55], v[132:133], v[54:55] op_sel:[1,0]
	v_pk_mul_f32 v[52:53], v[132:133], v[52:53] op_sel:[1,0]
	v_pk_mul_f32 v[50:51], v[132:133], v[50:51] op_sel:[1,0]
	v_pk_mul_f32 v[46:47], v[132:133], v[46:47] op_sel:[1,0]
	v_pk_mul_f32 v[44:45], v[132:133], v[44:45] op_sel:[1,0]
	v_pk_mul_f32 v[42:43], v[132:133], v[42:43] op_sel:[1,0]
	v_pk_mul_f32 v[40:41], v[132:133], v[40:41] op_sel:[1,0]
	v_pk_mul_f32 v[38:39], v[132:133], v[38:39] op_sel:[1,0]
	v_pk_mul_f32 v[36:37], v[132:133], v[36:37] op_sel:[1,0]
	v_pk_mul_f32 v[34:35], v[132:133], v[34:35] op_sel:[1,0]
	v_pk_mul_f32 v[32:33], v[132:133], v[32:33] op_sel:[1,0]
	v_cndmask_b32_e64 v51, 0, v51, s[28:29]
	v_cndmask_b32_e64 v50, 0, v50, s[30:31]
	v_cndmask_b32_e64 v53, 0, v53, s[24:25]
	v_cndmask_b32_e64 v52, 0, v52, s[26:27]
	v_cndmask_b32_e64 v55, 0, v55, s[20:21]
	v_cndmask_b32_e64 v54, 0, v54, s[22:23]
	v_cndmask_b32_e64 v57, 0, v57, s[16:17]
	v_cndmask_b32_e64 v56, 0, v56, s[18:19]
	v_cndmask_b32_e64 v59, 0, v59, s[12:13]
	v_cndmask_b32_e64 v58, 0, v58, s[14:15]
	v_cndmask_b32_e64 v61, 0, v61, s[8:9]
	v_cndmask_b32_e64 v60, 0, v60, s[10:11]
	v_cndmask_b32_e64 v62, 0, v62, s[6:7]
	v_cndmask_b32_e32 v63, 0, v63, vcc
	v_cndmask_b32_e64 v33, 0, v33, s[66:67]
	v_cndmask_b32_e64 v32, 0, v32, s[68:69]
	v_cndmask_b32_e64 v35, 0, v35, s[62:63]
	v_cndmask_b32_e64 v34, 0, v34, s[64:65]
	v_cndmask_b32_e64 v37, 0, v37, s[58:59]
	v_cndmask_b32_e64 v36, 0, v36, s[60:61]
	v_cndmask_b32_e64 v39, 0, v39, s[54:55]
	v_cndmask_b32_e64 v38, 0, v38, s[56:57]
	v_cndmask_b32_e64 v41, 0, v41, s[50:51]
	v_cndmask_b32_e64 v40, 0, v40, s[52:53]
	v_cndmask_b32_e64 v43, 0, v43, s[46:47]
	v_cndmask_b32_e64 v42, 0, v42, s[48:49]
	v_cndmask_b32_e64 v45, 0, v45, s[42:43]
	v_cndmask_b32_e64 v44, 0, v44, s[44:45]
	v_cndmask_b32_e64 v46, 0, v46, s[40:41]
	v_cndmask_b32_e64 v47, 0, v47, s[38:39]
	v_pk_add_f32 v[114:115], v[114:115], v[62:63]
	v_pk_add_f32 v[116:117], v[116:117], v[60:61]
	v_pk_add_f32 v[118:119], v[118:119], v[58:59]
	v_pk_add_f32 v[120:121], v[120:121], v[56:57]
	v_pk_add_f32 v[122:123], v[122:123], v[54:55]
	v_pk_add_f32 v[124:125], v[124:125], v[52:53]
	v_pk_add_f32 v[126:127], v[126:127], v[50:51]
	v_pk_add_f32 v[98:99], v[98:99], v[46:47]
	v_pk_add_f32 v[100:101], v[100:101], v[44:45]
	v_pk_add_f32 v[102:103], v[102:103], v[42:43]
	v_pk_add_f32 v[104:105], v[104:105], v[40:41]
	v_pk_add_f32 v[108:109], v[108:109], v[38:39]
	v_pk_add_f32 v[110:111], v[110:111], v[36:37]
	v_pk_add_f32 v[112:113], v[112:113], v[34:35]
	v_pk_add_f32 v[106:107], v[106:107], v[32:33]
	v_add_u32_e32 v141, 0x400, v141
	v_add_u32_e32 v142, 0x400, v142
	v_add_u32_e32 v143, 0x400, v143
	v_add_u32_e32 v160, 0x400, v160
	v_add_u32_e32 v161, 0x400, v161
	v_add_u32_e32 v162, 0x400, v162
	v_add_u32_e32 v163, 0x400, v163
	v_add_u32_e32 v164, 0x400, v164
	v_add_u32_e32 v165, 0x400, v165
	v_add_u32_e32 v166, 0x400, v166
	v_add_u32_e32 v167, 0x400, v167
	v_add_u32_e32 v174, 0x400, v174
	v_add_u32_e32 v176, 0x400, v176
	v_add_u32_e32 v177, 0x400, v177
	v_add_u32_e32 v178, 0x400, v178
	v_add_u32_e32 v179, 0x400, v179
	v_add_u32_e32 v180, 0x400, v180
	v_add_u32_e32 v181, 0x400, v181
	v_add_u32_e32 v182, 0x400, v182
	v_add_u32_e32 v183, 0x400, v183
	v_add_u32_e32 v184, 0x400, v184
	v_add_u32_e32 v185, 0x400, v185
	v_add_u32_e32 v186, 0x400, v186
	v_add_u32_e32 v187, 0x400, v187
	v_add_u32_e32 v188, 0x400, v188
	v_add_u32_e32 v189, 0x400, v189
	v_add_u32_e32 v190, 0x400, v190
	v_add_u32_e32 v191, 0x400, v191
	v_add_u32_e32 v192, 0x400, v192
	s_cbranch_scc1 .LBB0_743
	s_movk_i32 s16, 0x90

.LBB0_764:
	s_lshl_b32 s6, 1, s3
	s_or_b32 s18, s6, s8
	s_or_b32 s19, s6, s13
	s_or_b32 s20, s6, s12
	s_or_b32 s21, s6, s11
	s_or_b32 s22, s6, s10
	s_or_b32 s23, s6, s2
	s_or_b32 s24, s6, s1
	s_or_b32 s25, s6, s0
	v_cmp_le_u32_e64 s[34:35], s18, v37
	v_cmp_le_u32_e64 s[36:37], s19, v36
	v_cmp_le_u32_e64 s[38:39], s20, v34
	v_cmp_le_u32_e64 s[40:41], s21, v35
	v_cmp_le_u32_e64 s[42:43], s22, v41
	v_cmp_le_u32_e64 s[44:45], s23, v40
	v_cmp_le_u32_e64 s[46:47], s24, v38
	v_cmp_le_u32_e64 s[48:49], s25, v39
	s_bcnt1_i32_b64 s4, s[34:35]
	s_cmp_gt_u32 s4, 15
	s_cselect_b32 s8, s18, s8
	s_bcnt1_i32_b64 s4, s[36:37]
	s_cmp_gt_u32 s4, 15
	s_cselect_b32 s13, s19, s13
	s_bcnt1_i32_b64 s4, s[38:39]
	s_cmp_gt_u32 s4, 15
	s_cselect_b32 s12, s20, s12
	s_bcnt1_i32_b64 s4, s[40:41]
	s_cmp_gt_u32 s4, 15
	s_cselect_b32 s11, s21, s11
	s_bcnt1_i32_b64 s4, s[42:43]
	s_cmp_gt_u32 s4, 15
	s_cselect_b32 s10, s22, s10
	s_bcnt1_i32_b64 s4, s[44:45]
	s_cmp_gt_u32 s4, 15
	s_cselect_b32 s2, s23, s2
	s_bcnt1_i32_b64 s4, s[46:47]
	s_cmp_gt_u32 s4, 15
	s_cselect_b32 s1, s24, s1
	s_bcnt1_i32_b64 s4, s[48:49]
	s_cmp_gt_u32 s4, 15
	s_cselect_b32 s0, s25, s0
	s_add_i32 s3, s3, -1
	s_cmp_lg_u32 s3, -1
	s_cbranch_scc1 .LBB0_764
	v_lshlrev_b64 v[32:33], v139, -1
	v_not_b32_e32 v32, v32
	v_cmp_lt_u32_e64 s[6:7], s8, v37
	v_cmp_eq_u32_e64 s[8:9], s8, v37
	v_not_b32_e32 v33, v33
	v_cndmask_b32_e64 v42, 0, 1, s[6:7]
	v_and_b32_e32 v43, s8, v32
	s_bcnt1_i32_b64 s6, s[6:7]
	v_and_b32_e32 v37, s9, v33
	v_bcnt_u32_b32 v43, v43, 0
	s_sub_i32 s6, 16, s6
	v_bcnt_u32_b32 v37, v37, v43
	v_cmp_gt_i32_e64 s[6:7], s6, v37
	v_cmp_ge_u32_e64 s[4:5], s77, v139
	s_lshl_b32 s3, s33, 6
	v_cndmask_b32_e64 v37, 0, 1, s[6:7]
	v_cndmask_b32_e64 v37, v42, v37, s[8:9]
	v_and_b32_e32 v37, 1, v37
	v_cmp_eq_u32_e64 s[6:7], 1, v37
	s_and_b64 s[6:7], s[6:7], s[4:5]
	s_nop 0
	v_cndmask_b32_e64 v37, 0, 1, s[6:7]
	v_cmp_ne_u32_e64 s[8:9], 0, v37
	s_and_saveexec_b64 s[6:7], vcc
	s_add_i32 s14, s3, 0
	s_add_i32 s14, s14, 0x1ac00
	v_mov_b32_e32 v37, s14
	v_mov_b64_e32 v[42:43], s[8:9]
	ds_write_b64 v37, v[42:43]
	s_or_b64 exec, exec, s[6:7]
	v_cmp_eq_u32_e64 s[8:9], s13, v36
	v_cmp_lt_u32_e64 s[6:7], s13, v36
	s_nop 0
	v_and_b32_e32 v42, s8, v32
	v_cndmask_b32_e64 v37, 0, 1, s[6:7]
	s_bcnt1_i32_b64 s6, s[6:7]
	v_and_b32_e32 v36, s9, v33
	v_bcnt_u32_b32 v42, v42, 0
	s_sub_i32 s6, 16, s6
	v_bcnt_u32_b32 v36, v36, v42
	v_cmp_gt_i32_e64 s[6:7], s6, v36
	s_nop 1
	v_cndmask_b32_e64 v36, 0, 1, s[6:7]
	v_cndmask_b32_e64 v36, v37, v36, s[8:9]
	v_and_b32_e32 v36, 1, v36
	v_cmp_eq_u32_e64 s[6:7], 1, v36
	s_and_b64 s[6:7], s[6:7], s[4:5]
	s_nop 0
	v_cndmask_b32_e64 v36, 0, 1, s[6:7]
	v_cmp_ne_u32_e64 s[8:9], 0, v36
	s_and_saveexec_b64 s[6:7], vcc
	s_add_i32 s13, s3, 0
	s_add_i32 s13, s13, 0x1ac08
	v_mov_b32_e32 v36, s13
	v_mov_b64_e32 v[42:43], s[8:9]
	ds_write_b64 v36, v[42:43]
	s_or_b64 exec, exec, s[6:7]
	v_cmp_eq_u32_e64 s[8:9], s12, v34
	v_cmp_lt_u32_e64 s[6:7], s12, v34
	s_nop 0
	v_and_b32_e32 v37, s8, v32
	v_cndmask_b32_e64 v36, 0, 1, s[6:7]
	s_bcnt1_i32_b64 s6, s[6:7]
	v_and_b32_e32 v34, s9, v33
	v_bcnt_u32_b32 v37, v37, 0
	s_sub_i32 s6, 16, s6
	v_bcnt_u32_b32 v34, v34, v37
	v_cmp_gt_i32_e64 s[6:7], s6, v34
	s_nop 1
	v_cndmask_b32_e64 v34, 0, 1, s[6:7]
	v_cndmask_b32_e64 v34, v36, v34, s[8:9]
	v_and_b32_e32 v34, 1, v34
	v_cmp_eq_u32_e64 s[6:7], 1, v34
	s_and_b64 s[6:7], s[6:7], s[4:5]
	s_nop 0
	v_cndmask_b32_e64 v34, 0, 1, s[6:7]
	v_cmp_ne_u32_e64 s[8:9], 0, v34
	s_and_saveexec_b64 s[6:7], vcc
	s_add_i32 s12, s3, 0
	s_add_i32 s12, s12, 0x1ac10
	v_mov_b32_e32 v34, s12
	v_mov_b64_e32 v[36:37], s[8:9]
	ds_write_b64 v34, v[36:37]
	s_or_b64 exec, exec, s[6:7]
	v_cmp_eq_u32_e64 s[8:9], s11, v35
	v_cmp_lt_u32_e64 s[6:7], s11, v35
	s_nop 0
	v_and_b32_e32 v36, s8, v32
	v_cndmask_b32_e64 v34, 0, 1, s[6:7]
	s_bcnt1_i32_b64 s6, s[6:7]
	v_and_b32_e32 v35, s9, v33
	v_bcnt_u32_b32 v36, v36, 0
	s_sub_i32 s6, 16, s6
	v_bcnt_u32_b32 v35, v35, v36
	v_cmp_gt_i32_e64 s[6:7], s6, v35
	s_nop 1
	v_cndmask_b32_e64 v35, 0, 1, s[6:7]
	v_cndmask_b32_e64 v34, v34, v35, s[8:9]
	v_and_b32_e32 v34, 1, v34
	v_cmp_eq_u32_e64 s[6:7], 1, v34
	s_and_b64 s[6:7], s[6:7], s[4:5]
	s_nop 0
	v_cndmask_b32_e64 v34, 0, 1, s[6:7]
	v_cmp_ne_u32_e64 s[8:9], 0, v34
	s_and_saveexec_b64 s[6:7], vcc
	s_add_i32 s11, s3, 0
	s_add_i32 s11, s11, 0x1ac18
	v_mov_b32_e32 v34, s11
	v_mov_b64_e32 v[36:37], s[8:9]
	ds_write_b64 v34, v[36:37]
	s_or_b64 exec, exec, s[6:7]
	v_cmp_eq_u32_e64 s[8:9], s10, v41
	v_cmp_lt_u32_e64 s[6:7], s10, v41
	s_nop 0
	v_and_b32_e32 v36, s8, v32
	v_cndmask_b32_e64 v34, 0, 1, s[6:7]
	s_bcnt1_i32_b64 s6, s[6:7]
	v_and_b32_e32 v35, s9, v33
	v_bcnt_u32_b32 v36, v36, 0
	s_sub_i32 s6, 16, s6
	v_bcnt_u32_b32 v35, v35, v36
	v_cmp_gt_i32_e64 s[6:7], s6, v35
	s_nop 1
	v_cndmask_b32_e64 v35, 0, 1, s[6:7]
	v_cndmask_b32_e64 v34, v34, v35, s[8:9]
	v_and_b32_e32 v34, 1, v34
	v_cmp_eq_u32_e64 s[6:7], 1, v34
	s_and_b64 s[6:7], s[6:7], s[4:5]
	s_nop 0
	v_cndmask_b32_e64 v34, 0, 1, s[6:7]
	v_cmp_ne_u32_e64 s[8:9], 0, v34
	s_and_saveexec_b64 s[6:7], vcc
	s_add_i32 s10, s3, 0
	s_add_i32 s10, s10, 0x1ac20
	v_mov_b32_e32 v34, s10
	v_mov_b64_e32 v[36:37], s[8:9]
	ds_write_b64 v34, v[36:37]
	s_or_b64 exec, exec, s[6:7]
	v_cmp_eq_u32_e64 s[8:9], s2, v40
	v_cmp_lt_u32_e64 s[6:7], s2, v40
	s_bcnt1_i32_b64 s2, s[6:7]
	v_and_b32_e32 v36, s8, v32
	v_and_b32_e32 v35, s9, v33
	v_bcnt_u32_b32 v36, v36, 0
	s_sub_i32 s2, 16, s2
	v_bcnt_u32_b32 v35, v35, v36
	v_cndmask_b32_e64 v34, 0, 1, s[6:7]
	v_cmp_gt_i32_e64 s[6:7], s2, v35
	s_nop 1
	v_cndmask_b32_e64 v35, 0, 1, s[6:7]
	v_cndmask_b32_e64 v34, v34, v35, s[8:9]
	v_and_b32_e32 v34, 1, v34
	v_cmp_eq_u32_e64 s[6:7], 1, v34
	s_and_b64 s[6:7], s[6:7], s[4:5]
	s_nop 0
	v_cndmask_b32_e64 v34, 0, 1, s[6:7]
	v_cmp_ne_u32_e64 s[8:9], 0, v34
	s_and_saveexec_b64 s[6:7], vcc
	s_add_i32 s2, s3, 0
	s_add_i32 s2, s2, 0x1ac28
	v_mov_b32_e32 v34, s2
	v_mov_b64_e32 v[36:37], s[8:9]
	ds_write_b64 v34, v[36:37]
	s_or_b64 exec, exec, s[6:7]
	v_cmp_eq_u32_e64 s[8:9], s1, v38
	v_cmp_lt_u32_e64 s[6:7], s1, v38
	s_bcnt1_i32_b64 s1, s[6:7]
	v_and_b32_e32 v36, s8, v32
	v_and_b32_e32 v35, s9, v33
	v_bcnt_u32_b32 v36, v36, 0
	s_sub_i32 s1, 16, s1
	v_bcnt_u32_b32 v35, v35, v36
	v_cndmask_b32_e64 v34, 0, 1, s[6:7]
	v_cmp_gt_i32_e64 s[6:7], s1, v35
	s_nop 1
	v_cndmask_b32_e64 v35, 0, 1, s[6:7]
	v_cndmask_b32_e64 v34, v34, v35, s[8:9]
	v_and_b32_e32 v34, 1, v34
	v_cmp_eq_u32_e64 s[6:7], 1, v34
	s_and_b64 s[6:7], s[6:7], s[4:5]
	s_nop 0
	v_cndmask_b32_e64 v34, 0, 1, s[6:7]
	v_cmp_ne_u32_e64 s[8:9], 0, v34
	s_and_saveexec_b64 s[6:7], vcc
	s_add_i32 s1, s3, 0
	s_add_i32 s1, s1, 0x1ac30
	v_mov_b32_e32 v34, s1
	v_mov_b64_e32 v[36:37], s[8:9]
	ds_write_b64 v34, v[36:37]
	s_or_b64 exec, exec, s[6:7]
	v_cmp_eq_u32_e64 s[8:9], s0, v39
	v_cmp_lt_u32_e64 s[6:7], s0, v39
	s_bcnt1_i32_b64 s0, s[6:7]
	v_and_b32_e32 v32, s8, v32
	v_and_b32_e32 v33, s9, v33
	v_bcnt_u32_b32 v32, v32, 0
	s_sub_i32 s0, 16, s0
	v_bcnt_u32_b32 v32, v33, v32
	v_cndmask_b32_e64 v34, 0, 1, s[6:7]
	v_cmp_gt_i32_e64 s[6:7], s0, v32
	s_nop 1
	v_cndmask_b32_e64 v32, 0, 1, s[6:7]
	v_cndmask_b32_e64 v32, v34, v32, s[8:9]
	v_and_b32_e32 v32, 1, v32
	v_cmp_eq_u32_e64 s[6:7], 1, v32
	s_and_b64 s[0:1], s[6:7], s[4:5]
	v_cndmask_b32_e64 v32, 0, 1, s[0:1]
	v_cmp_ne_u32_e64 s[6:7], 0, v32
	s_and_saveexec_b64 s[4:5], vcc
	s_add_i32 s0, s3, 0
	s_add_i32 s0, s0, 0x1ac38
	v_mov_b32_e32 v32, s0
	v_mov_b64_e32 v[34:35], s[6:7]
	ds_write_b64 v32, v[34:35]
	s_or_b64 exec, exec, s[4:5]
	v_ashrrev_i32_e32 v34, 3, v96
	v_ashrrev_i32_e32 v35, 31, v34
	v_lshl_add_u64 v[122:123], s[94:95], 0, v[34:35]
	v_readlane_b32 s0, v248, 50
	v_lshlrev_b64 v[36:37], 9, v[122:123]
	v_readlane_b32 s1, v248, 51
	v_and_b32_e32 v40, 56, v137
	v_readlane_b32 s2, v248, 52
	v_lshl_add_u32 v32, v138, 2, 0
	v_lshl_add_u64 v[38:39], s[0:1], 0, v[36:37]
	v_lshlrev_b32_e32 v120, 1, v40
	v_mov_b32_e32 v121, v169
	v_readlane_b32 s3, v248, 53
	v_add_u32_e32 v32, 0x1ac00, v32
	v_lshl_add_u64 v[38:39], v[38:39], 0, v[120:121]
	v_lshl_add_u64 v[36:37], s[2:3], 0, v[36:37]
	s_waitcnt lgkmcnt(0)
	s_barrier
	ds_read_b64 v[32:33], v32
	s_waitcnt lgkmcnt(0)
	s_barrier
	v_lshl_add_u64 v[36:37], v[36:37], 0, v[120:121]
	global_load_dwordx4 v[112:115], v[38:39], off
	global_load_dwordx4 v[116:119], v[36:37], off
	ds_bpermute_b32 v36, v217, v32
	ds_bpermute_b32 v37, v217, v33
	v_lshl_add_u64 v[124:125], s[0:1], 0, v[120:121]
	v_readlane_b32 s0, v248, 19
	v_readlane_b32 s1, v248, 20
	s_waitcnt lgkmcnt(1)
	v_or_b32_e32 v32, v36, v32
	s_waitcnt lgkmcnt(0)
	v_or_b32_e32 v33, v37, v33
	ds_bpermute_b32 v36, v218, v32
	ds_bpermute_b32 v37, v218, v33
	v_lshl_add_u64 v[176:177], s[0:1], 0, v[34:35]
	s_mov_b32 s4, s87
	s_lshl_b64 s[6:7], 1, s77
	s_waitcnt lgkmcnt(1)
	v_or_b32_e32 v32, v36, v32
	s_waitcnt lgkmcnt(0)
	v_or_b32_e32 v33, v37, v33
	ds_bpermute_b32 v36, v219, v32
	ds_bpermute_b32 v37, v219, v33
	v_lshlrev_b32_e32 v39, 10, v96
	v_lshlrev_b32_e32 v38, 4, v96
	v_and_b32_e32 v39, 0x1000, v39
	s_waitcnt lgkmcnt(1)
	v_or_b32_e32 v32, v36, v32
	s_waitcnt lgkmcnt(0)
	v_or_b32_e32 v33, v37, v33
	ds_bpermute_b32 v36, v220, v32
	ds_bpermute_b32 v37, v220, v33
	v_mul_lo_u32 v40, v34, s16
	v_and_b32_e32 v41, 0x70, v38
	v_lshlrev_b32_e32 v42, 6, v34
	s_waitcnt lgkmcnt(1)
	v_or_b32_e32 v32, v36, v32
	s_waitcnt lgkmcnt(0)
	v_or_b32_e32 v33, v37, v33
	ds_bpermute_b32 v36, v221, v32
	ds_bpermute_b32 v37, v221, v33
	v_and_b32_e32 v38, 48, v38
	v_add_u32_e32 v39, 0, v39
	v_add3_u32 v174, 0, v40, v41
	s_waitcnt lgkmcnt(1)
	v_or_b32_e32 v32, v36, v32
	s_waitcnt lgkmcnt(0)
	v_or_b32_e32 v33, v37, v33
	ds_bpermute_b32 v36, v222, v32
	ds_bpermute_b32 v37, v222, v33
	v_lshl_add_u64 v[126:127], s[2:3], 0, v[120:121]
	v_add3_u32 v232, v39, v42, v38
	s_waitcnt vmcnt(1)
	ds_write_b128 v174, v[112:115]
	s_waitcnt vmcnt(0)
	ds_write_b128 v232, v[116:119] offset:18432
	s_waitcnt lgkmcnt(3)
	v_or_b32_e32 v32, v36, v32
	s_waitcnt lgkmcnt(2)
	v_or_b32_e32 v33, v37, v33
	v_readfirstlane_b32 s0, v32
	v_readfirstlane_b32 s5, v33
	s_ashr_i32 s1, s0, 31
	s_or_b64 s[0:1], s[4:5], s[0:1]
	s_andn2_b64 s[72:73], s[0:1], s[6:7]
	s_cmp_eq_u64 s[72:73], 0
	s_flbit_i32_b64 s0, s[72:73]
	s_cselect_b64 s[90:91], -1, 0
	s_cmp_lg_u64 s[72:73], 0
	s_cselect_b64 s[92:93], -1, 0
	s_xor_b32 s79, s0, 63
	s_and_b64 vcc, exec, s[90:91]
	s_waitcnt lgkmcnt(0)
	s_barrier
	s_cbranch_vccnz .LBB0_783
	s_lshl_b32 s86, s79, 6
	v_lshl_add_u64 v[32:33], v[176:177], 0, s[86:87]
	v_lshlrev_b64 v[32:33], 9, v[32:33]
	v_lshl_add_u64 v[34:35], v[124:125], 0, v[32:33]
	v_lshl_add_u64 v[32:33], v[126:127], 0, v[32:33]
	global_load_dwordx4 v[112:115], v[34:35], off
	global_load_dwordx4 v[116:119], v[32:33], off

; __device__ __forceinline__ unsigned cvt_pk_bf16(float lo, float hi) { unsigned r; asm volatile("v_cvt_pk_bf16_f32 %0, %1, %2" : "=v"(r) : "v"(lo), "v"(hi)); return r; }
;     template <class Tp> __device__ __forceinline__ Tp* w(size_t off) const { return (Tp*)(ws + off); }
;     __device__ __forceinline__ void operator()(const f32x4 (&acc)[2][2][4][2], const Unit& u, int wr, int wc, int fr, int fq) const {
;     ...
;                 for (int n = 0; n < 2; ++n)
; #pragma unroll
;                     for (int i = 0; i < 4; ++i) { const float gv = acc[ai][0][m][n][i], uv = acc[ai][1][m][n][i]; h[n * 4 + i] = gv * __builtin_amdgcn_rcpf(1.f + __expf(-gv)) * uv; }
;                 u32x4 w; w.x = cvt_pk_bf16(h[0], h[1]); w.y = cvt_pk_bf16(h[2], h[3]); w.z = cvt_pk_bf16(h[4], h[5]); w.w = cvt_pk_bf16(h[6], h[7]);
;                 *(u32x4*)rowp = w; }
.LBB0_1142:
	v_mul_f32_e32 v210, 0xbfb8aa3b, v174
	v_lshl_add_u32 v208, s49, 8, v217
	v_exp_f32_e32 v210, v210
	v_mul_f32_e32 v211, 0xbfb8aa3b, v175
	v_ashrrev_i32_e32 v209, 31, v208
	v_mul_f32_e32 v193, 0xbfb8aa3b, v180
	v_mul_f32_e32 v195, 0xbfb8aa3b, v181
	v_exp_f32_e32 v211, v211
	v_exp_f32_e32 v193, v193
	v_exp_f32_e32 v195, v195
	v_lshlrev_b64 v[206:207], 11, v[208:209]
	v_mul_f32_e32 v199, 0xbfb8aa3b, v182
	v_mul_f32_e32 v203, 0xbfb8aa3b, v183
	v_mul_f32_e32 v205, 0xbfb8aa3b, v172
	v_mul_f32_e32 v209, 0xbfb8aa3b, v173
	v_exp_f32_e32 v199, v199
	v_exp_f32_e32 v203, v203
	v_exp_f32_e32 v205, v205
	v_exp_f32_e32 v209, v209
	v_add_f32_e32 v210, 1.0, v210
	v_rcp_f32_e32 v210, v210
	v_add_f32_e32 v211, 1.0, v211
	v_add_f32_e32 v193, 1.0, v193
	v_add_f32_e32 v195, 1.0, v195
	v_rcp_f32_e32 v211, v211
	v_rcp_f32_e32 v193, v193
	v_rcp_f32_e32 v195, v195
	v_add_f32_e32 v199, 1.0, v199
	v_add_f32_e32 v203, 1.0, v203
	v_add_f32_e32 v205, 1.0, v205
	v_add_f32_e32 v209, 1.0, v209
	v_rcp_f32_e32 v199, v199
	v_rcp_f32_e32 v203, v203
	v_rcp_f32_e32 v205, v205
	v_rcp_f32_e32 v209, v209
	s_lshl_b32 s10, s50, 7
	v_mul_f32_e32 v210, v174, v210
	s_and_b32 s10, s10, 0x380
	v_mul_f32_e32 v212, v134, v210
	v_mul_f32_e32 v210, v175, v211
	v_lshl_add_u64 v[206:207], s[22:23], 0, v[206:207]
	v_mul_f32_e32 v193, v180, v193
	v_mul_f32_e32 v195, v181, v195
	v_mul_f32_e32 v213, v135, v210
	v_add_lshl_u32 v210, v222, s10, 1
	v_mov_b32_e32 v211, v197
	v_mul_f32_e32 v193, v140, v193
	v_mul_f32_e32 v195, v141, v195
	v_mul_f32_e32 v199, v182, v199
	v_mul_f32_e32 v203, v183, v203
	v_mul_f32_e32 v205, v172, v205
	v_mul_f32_e32 v209, v173, v209
	v_lshl_add_u64 v[206:207], v[206:207], 0, v[210:211]
	v_cvt_pk_bf16_f32 v226, v193, v195
	v_mul_f32_e32 v199, v142, v199
	v_mul_f32_e32 v203, v143, v203
	v_mul_f32_e32 v205, v132, v205
	v_mul_f32_e32 v209, v133, v209
	v_cvt_pk_bf16_f32 v227, v199, v203
	v_cvt_pk_bf16_f32 v228, v205, v209
	v_cvt_pk_bf16_f32 v229, v212, v213
	global_store_dwordx4 v[206:207], v[226:229], off sc1
	v_mul_f32_e32 v193, 0xbfb8aa3b, v164
	v_mul_f32_e32 v195, 0xbfb8aa3b, v165
	v_mul_f32_e32 v226, 0xbfb8aa3b, v163
	v_exp_f32_e32 v193, v193
	v_exp_f32_e32 v195, v195
	v_mul_f32_e32 v199, 0xbfb8aa3b, v166
	v_mul_f32_e32 v203, 0xbfb8aa3b, v167
	v_mul_f32_e32 v205, 0xbfb8aa3b, v160
	v_mul_f32_e32 v209, 0xbfb8aa3b, v161
	v_mul_f32_e32 v225, 0xbfb8aa3b, v162
	v_exp_f32_e32 v226, v226
	v_exp_f32_e32 v199, v199
	v_exp_f32_e32 v203, v203
	v_exp_f32_e32 v205, v205
	v_exp_f32_e32 v209, v209
	v_exp_f32_e32 v225, v225
	v_add_f32_e32 v193, 1.0, v193
	v_add_f32_e32 v195, 1.0, v195
	v_add_f32_e32 v226, 1.0, v226
	v_rcp_f32_e32 v193, v193
	v_rcp_f32_e32 v195, v195
	v_add_f32_e32 v199, 1.0, v199
	v_add_f32_e32 v203, 1.0, v203
	v_add_f32_e32 v205, 1.0, v205
	v_add_f32_e32 v209, 1.0, v209
	v_add_f32_e32 v225, 1.0, v225
	v_rcp_f32_e32 v226, v226
	v_or_b32_e32 v212, 16, v208
	v_rcp_f32_e32 v199, v199
	v_rcp_f32_e32 v203, v203
	v_rcp_f32_e32 v205, v205
	v_rcp_f32_e32 v209, v209
	v_rcp_f32_e32 v225, v225
	v_ashrrev_i32_e32 v213, 31, v212
	v_lshlrev_b64 v[212:213], 11, v[212:213]
	v_lshl_add_u64 v[212:213], s[22:23], 0, v[212:213]
	v_mul_f32_e32 v193, v164, v193
	v_mul_f32_e32 v195, v165, v195
	v_mul_f32_e32 v226, v163, v226
	v_mul_f32_e32 v193, v124, v193
	v_mul_f32_e32 v195, v125, v195
	v_mul_f32_e32 v199, v166, v199
	v_mul_f32_e32 v203, v167, v203
	v_mul_f32_e32 v205, v160, v205
	v_mul_f32_e32 v209, v161, v209
	v_mul_f32_e32 v225, v162, v225
	v_mul_f32_e32 v229, v119, v226
	v_lshl_add_u64 v[212:213], v[212:213], 0, v[210:211]
	v_cvt_pk_bf16_f32 v226, v193, v195
	v_mul_f32_e32 v199, v126, v199
	v_mul_f32_e32 v203, v127, v203
	v_mul_f32_e32 v205, v116, v205
	v_mul_f32_e32 v209, v117, v209
	v_mul_f32_e32 v225, v118, v225
	v_cvt_pk_bf16_f32 v227, v199, v203
	v_cvt_pk_bf16_f32 v228, v205, v209
	v_cvt_pk_bf16_f32 v229, v225, v229
	global_store_dwordx4 v[212:213], v[226:229], off sc1
	v_mul_f32_e32 v193, 0xbfb8aa3b, v156
	v_mul_f32_e32 v195, 0xbfb8aa3b, v157
	v_mul_f32_e32 v226, 0xbfb8aa3b, v155
	v_mul_f32_e32 v199, 0xbfb8aa3b, v158
	v_mul_f32_e32 v203, 0xbfb8aa3b, v159
	v_mul_f32_e32 v205, 0xbfb8aa3b, v152
	v_mul_f32_e32 v209, 0xbfb8aa3b, v153
	v_mul_f32_e32 v225, 0xbfb8aa3b, v154
	v_exp_f32_e32 v226, v226
	v_exp_f32_e32 v193, v193
	v_exp_f32_e32 v195, v195
	v_exp_f32_e32 v199, v199
	v_exp_f32_e32 v203, v203
	v_exp_f32_e32 v205, v205
	v_exp_f32_e32 v209, v209
	v_exp_f32_e32 v225, v225
	v_add_f32_e32 v226, 1.0, v226
	v_add_f32_e32 v193, 1.0, v193
	v_add_f32_e32 v195, 1.0, v195
	v_add_f32_e32 v199, 1.0, v199
	v_add_f32_e32 v203, 1.0, v203
	v_add_f32_e32 v205, 1.0, v205
	v_add_f32_e32 v209, 1.0, v209
	v_add_f32_e32 v225, 1.0, v225
	v_rcp_f32_e32 v226, v226
	v_or_b32_e32 v212, 32, v208
	v_rcp_f32_e32 v193, v193
	v_rcp_f32_e32 v195, v195
	v_rcp_f32_e32 v199, v199
	v_rcp_f32_e32 v203, v203
	v_rcp_f32_e32 v205, v205
	v_rcp_f32_e32 v209, v209
	v_rcp_f32_e32 v225, v225
	v_ashrrev_i32_e32 v213, 31, v212
	v_lshlrev_b64 v[212:213], 11, v[212:213]
	v_lshl_add_u64 v[212:213], s[22:23], 0, v[212:213]
	v_mul_f32_e32 v226, v155, v226
	v_mul_f32_e32 v193, v156, v193
	v_mul_f32_e32 v195, v157, v195
	v_mul_f32_e32 v199, v158, v199
	v_mul_f32_e32 v203, v159, v203
	v_mul_f32_e32 v205, v152, v205
	v_mul_f32_e32 v209, v153, v209
	v_mul_f32_e32 v225, v154, v225
	v_mul_f32_e32 v229, v107, v226
	v_lshl_add_u64 v[212:213], v[212:213], 0, v[210:211]
	v_mul_f32_e32 v193, v108, v193
	v_mul_f32_e32 v195, v109, v195
	v_mul_f32_e32 v199, v110, v199
	v_mul_f32_e32 v203, v111, v203
	v_mul_f32_e32 v205, v104, v205
	v_mul_f32_e32 v209, v105, v209
	v_mul_f32_e32 v225, v106, v225
	v_cvt_pk_bf16_f32 v226, v193, v195
; __device__ __forceinline__ unsigned cvt_pk_bf16(float lo, float hi) { unsigned r; asm volatile("v_cvt_pk_bf16_f32 %0, %1, %2" : "=v"(r) : "v"(lo), "v"(hi)); return r; }
;     template <class Tp> __device__ __forceinline__ Tp* w(size_t off) const { return (Tp*)(ws + off); }
;     __device__ __forceinline__ void operator()(const f32x4 (&acc)[2][2][4][2], const Unit& u, int wr, int wc, int fr, int fq) const {
;         const int row0 = u.pm * BM + wr * 64 + fr, col0 = (u.pn & 7) * 128 + wc * 32 + 8 * fq;
; #pragma unroll
;         for (int ai = 0; ai < 2; ++ai)
; #pragma unroll
;             for (int m = 0; m < 4; ++m) { bf16_t* rowp = HID + (size_t)(row0 + ai * HALF + m * 16) * 1024 + col0;
;                 float h[8];
; #pragma unroll
;                 for (int n = 0; n < 2; ++n)
; #pragma unroll
;                     for (int i = 0; i < 4; ++i) { const float gv = acc[ai][0][m][n][i], uv = acc[ai][1][m][n][i]; h[n * 4 + i] = gv * __builtin_amdgcn_rcpf(1.f + __expf(-gv)) * uv; }
;                 u32x4 w; w.x = cvt_pk_bf16(h[0], h[1]); w.y = cvt_pk_bf16(h[2], h[3]); w.z = cvt_pk_bf16(h[4], h[5]); w.w = cvt_pk_bf16(h[6], h[7]);
;                 *(u32x4*)rowp = w; }
	v_cvt_pk_bf16_f32 v227, v199, v203
	v_cvt_pk_bf16_f32 v228, v205, v209
	v_cvt_pk_bf16_f32 v229, v225, v229
	global_store_dwordx4 v[212:213], v[226:229], off sc1
	v_mul_f32_e32 v212, 0xbfb8aa3b, v145
	v_exp_f32_e32 v212, v212
	v_mul_f32_e32 v213, 0xbfb8aa3b, v146
	v_mul_f32_e32 v193, 0xbfb8aa3b, v148
	v_mul_f32_e32 v195, 0xbfb8aa3b, v149
	v_exp_f32_e32 v213, v213
	v_mul_f32_e32 v225, 0xbfb8aa3b, v147
	v_exp_f32_e32 v193, v193
	v_exp_f32_e32 v195, v195
	v_mul_f32_e32 v199, 0xbfb8aa3b, v150
	v_mul_f32_e32 v203, 0xbfb8aa3b, v151
	v_mul_f32_e32 v205, 0xbfb8aa3b, v144
	v_exp_f32_e32 v225, v225
	v_exp_f32_e32 v199, v199
	v_exp_f32_e32 v203, v203
	v_exp_f32_e32 v205, v205
	v_add_f32_e32 v212, 1.0, v212
	v_rcp_f32_e32 v212, v212
	v_add_f32_e32 v213, 1.0, v213
	v_add_f32_e32 v193, 1.0, v193
	v_add_f32_e32 v195, 1.0, v195
	v_rcp_f32_e32 v213, v213
	v_add_f32_e32 v225, 1.0, v225
	v_rcp_f32_e32 v193, v193
	v_rcp_f32_e32 v195, v195
	v_add_f32_e32 v199, 1.0, v199
	v_add_f32_e32 v203, 1.0, v203
	v_add_f32_e32 v205, 1.0, v205
	v_rcp_f32_e32 v225, v225
	v_or_b32_e32 v208, 48, v208
	v_rcp_f32_e32 v199, v199
	v_rcp_f32_e32 v203, v203
	v_rcp_f32_e32 v205, v205
	v_ashrrev_i32_e32 v209, 31, v208
	v_mul_f32_e32 v212, v145, v212
	v_lshlrev_b64 v[208:209], 11, v[208:209]
	v_mul_f32_e32 v226, v97, v212
	v_mul_f32_e32 v212, v146, v213
	v_lshl_add_u64 v[208:209], s[22:23], 0, v[208:209]
	v_mul_f32_e32 v193, v148, v193
	v_mul_f32_e32 v195, v149, v195
	v_mul_f32_e32 v227, v98, v212
	v_mul_f32_e32 v212, v147, v225
	v_mul_f32_e32 v193, v100, v193
	v_mul_f32_e32 v195, v101, v195
	v_mul_f32_e32 v199, v150, v199
	v_mul_f32_e32 v203, v151, v203
	v_mul_f32_e32 v205, v144, v205
	v_mul_f32_e32 v225, v99, v212
	v_lshl_add_u64 v[212:213], v[208:209], 0, v[210:211]
	v_cvt_pk_bf16_f32 v208, v193, v195
	v_mul_f32_e32 v199, v102, v199
	v_mul_f32_e32 v203, v103, v203
	v_mul_f32_e32 v205, v96, v205
	v_cvt_pk_bf16_f32 v209, v199, v203
	v_cvt_pk_bf16_f32 v210, v205, v226
	v_cvt_pk_bf16_f32 v211, v227, v225
	global_store_dwordx4 v[212:213], v[208:211], off sc1
	v_mul_f32_e32 v193, 0xbfb8aa3b, v92
	v_mul_f32_e32 v195, 0xbfb8aa3b, v93
	v_mul_f32_e32 v208, 0xbfb8aa3b, v89
	v_exp_f32_e32 v208, v208
	v_mul_f32_e32 v209, 0xbfb8aa3b, v90
	v_mul_f32_e32 v199, 0xbfb8aa3b, v94
	v_mul_f32_e32 v203, 0xbfb8aa3b, v95
	v_mul_f32_e32 v205, 0xbfb8aa3b, v88
	v_exp_f32_e32 v209, v209
	v_mul_f32_e32 v210, 0xbfb8aa3b, v91
	v_exp_f32_e32 v193, v193
	v_exp_f32_e32 v195, v195
	v_exp_f32_e32 v199, v199
	v_exp_f32_e32 v203, v203
	v_exp_f32_e32 v205, v205
	v_exp_f32_e32 v210, v210
	v_add_f32_e32 v208, 1.0, v208
	v_rcp_f32_e32 v208, v208
	v_add_f32_e32 v209, 1.0, v209
	v_add_f32_e32 v193, 1.0, v193
	v_add_f32_e32 v195, 1.0, v195
	v_add_f32_e32 v199, 1.0, v199
	v_add_f32_e32 v203, 1.0, v203
	v_add_f32_e32 v205, 1.0, v205
	v_rcp_f32_e32 v209, v209
	v_add_f32_e32 v210, 1.0, v210
	v_rcp_f32_e32 v193, v193
	v_rcp_f32_e32 v195, v195
	v_rcp_f32_e32 v199, v199
	v_rcp_f32_e32 v203, v203
	v_rcp_f32_e32 v205, v205
	v_rcp_f32_e32 v210, v210
	v_mul_f32_e32 v208, v89, v208
	v_mul_f32_e32 v211, v57, v208
	v_mul_f32_e32 v208, v90, v209
	v_mul_f32_e32 v193, v92, v193
	v_mul_f32_e32 v195, v93, v195
	v_mul_f32_e32 v199, v94, v199
	v_mul_f32_e32 v203, v95, v203
	v_mul_f32_e32 v205, v88, v205
	v_mul_f32_e32 v212, v58, v208
	v_mul_f32_e32 v208, v91, v210
	v_mul_f32_e32 v193, v60, v193
	v_mul_f32_e32 v195, v61, v195
	v_mul_f32_e32 v199, v62, v199
	v_mul_f32_e32 v203, v63, v203
	v_mul_f32_e32 v205, v56, v205
	v_mul_f32_e32 v213, v59, v208
	v_cvt_pk_bf16_f32 v208, v193, v195
	v_cvt_pk_bf16_f32 v209, v199, v203
	v_cvt_pk_bf16_f32 v210, v205, v211
	v_cvt_pk_bf16_f32 v211, v212, v213
	v_add_co_u32_e32 v212, vcc, s62, v206
	v_mul_f32_e32 v193, 0xbfb8aa3b, v84
	s_nop 0
	v_addc_co_u32_e32 v213, vcc, 0, v207, vcc
	global_store_dwordx4 v[212:213], v[208:211], off sc1
	v_mul_f32_e32 v195, 0xbfb8aa3b, v85
	v_mul_f32_e32 v199, 0xbfb8aa3b, v86
	v_mul_f32_e32 v208, 0xbfb8aa3b, v81
	v_exp_f32_e32 v208, v208
	v_mul_f32_e32 v209, 0xbfb8aa3b, v82
	v_mul_f32_e32 v203, 0xbfb8aa3b, v87
	v_mul_f32_e32 v205, 0xbfb8aa3b, v80
	v_exp_f32_e32 v209, v209
	v_mul_f32_e32 v210, 0xbfb8aa3b, v83
	v_exp_f32_e32 v193, v193
	v_exp_f32_e32 v195, v195
	v_exp_f32_e32 v199, v199
	v_exp_f32_e32 v203, v203
	v_exp_f32_e32 v205, v205
	v_exp_f32_e32 v210, v210
	v_add_f32_e32 v208, 1.0, v208
	v_rcp_f32_e32 v208, v208
	v_add_f32_e32 v209, 1.0, v209
	v_add_f32_e32 v193, 1.0, v193
	v_add_f32_e32 v195, 1.0, v195
	v_add_f32_e32 v199, 1.0, v199
	v_add_f32_e32 v203, 1.0, v203
	v_add_f32_e32 v205, 1.0, v205
; __device__ __forceinline__ unsigned cvt_pk_bf16(float lo, float hi) { unsigned r; asm volatile("v_cvt_pk_bf16_f32 %0, %1, %2" : "=v"(r) : "v"(lo), "v"(hi)); return r; }
;     template <class Tp> __device__ __forceinline__ Tp* w(size_t off) const { return (Tp*)(ws + off); }
;     __device__ __forceinline__ void operator()(const f32x4 (&acc)[2][2][4][2], const Unit& u, int wr, int wc, int fr, int fq) const {
;         const int row0 = u.pm * BM + wr * 64 + fr, col0 = (u.pn & 7) * 128 + wc * 32 + 8 * fq;
; #pragma unroll
;         for (int ai = 0; ai < 2; ++ai)
; #pragma unroll
;             for (int m = 0; m < 4; ++m) { bf16_t* rowp = HID + (size_t)(row0 + ai * HALF + m * 16) * 1024 + col0;
;                 float h[8];
; #pragma unroll
;                 for (int n = 0; n < 2; ++n)
; #pragma unroll
;                     for (int i = 0; i < 4; ++i) { const float gv = acc[ai][0][m][n][i], uv = acc[ai][1][m][n][i]; h[n * 4 + i] = gv * __builtin_amdgcn_rcpf(1.f + __expf(-gv)) * uv; }
;                 u32x4 w; w.x = cvt_pk_bf16(h[0], h[1]); w.y = cvt_pk_bf16(h[2], h[3]); w.z = cvt_pk_bf16(h[4], h[5]); w.w = cvt_pk_bf16(h[6], h[7]);
;                 *(u32x4*)rowp = w; }
	v_rcp_f32_e32 v209, v209
	v_add_f32_e32 v210, 1.0, v210
	v_rcp_f32_e32 v193, v193
	v_rcp_f32_e32 v195, v195
	v_rcp_f32_e32 v199, v199
	v_rcp_f32_e32 v203, v203
	v_rcp_f32_e32 v205, v205
	v_rcp_f32_e32 v210, v210
	v_mul_f32_e32 v208, v81, v208
	v_mul_f32_e32 v211, v49, v208
	v_mul_f32_e32 v208, v82, v209
	v_mul_f32_e32 v193, v84, v193
	v_mul_f32_e32 v195, v85, v195
	v_mul_f32_e32 v199, v86, v199
	v_mul_f32_e32 v203, v87, v203
	v_mul_f32_e32 v205, v80, v205
	v_mul_f32_e32 v212, v50, v208
	v_mul_f32_e32 v208, v83, v210
	v_mul_f32_e32 v193, v52, v193
	v_mul_f32_e32 v195, v53, v195
	v_mul_f32_e32 v199, v54, v199
	v_mul_f32_e32 v203, v55, v203
	v_mul_f32_e32 v205, v48, v205
	v_mul_f32_e32 v213, v51, v208
	v_cvt_pk_bf16_f32 v208, v193, v195
	v_cvt_pk_bf16_f32 v209, v199, v203
	v_cvt_pk_bf16_f32 v210, v205, v211
	v_cvt_pk_bf16_f32 v211, v212, v213
	v_add_co_u32_e32 v212, vcc, s63, v206
	v_mul_f32_e32 v193, 0xbfb8aa3b, v76
	s_nop 0
	v_addc_co_u32_e32 v213, vcc, 0, v207, vcc
	global_store_dwordx4 v[212:213], v[208:211], off sc1
	v_mul_f32_e32 v195, 0xbfb8aa3b, v77
	v_mul_f32_e32 v199, 0xbfb8aa3b, v78
	v_mul_f32_e32 v208, 0xbfb8aa3b, v73
	v_exp_f32_e32 v208, v208
	v_mul_f32_e32 v209, 0xbfb8aa3b, v74
	v_mul_f32_e32 v203, 0xbfb8aa3b, v79
	v_mul_f32_e32 v205, 0xbfb8aa3b, v72
	v_exp_f32_e32 v209, v209
	v_mul_f32_e32 v210, 0xbfb8aa3b, v75
	v_exp_f32_e32 v193, v193
	v_exp_f32_e32 v195, v195
	v_exp_f32_e32 v199, v199
	v_exp_f32_e32 v203, v203
	v_exp_f32_e32 v205, v205
	v_exp_f32_e32 v210, v210
	v_add_f32_e32 v208, 1.0, v208
	v_rcp_f32_e32 v208, v208
	v_add_f32_e32 v209, 1.0, v209
	v_add_f32_e32 v193, 1.0, v193
	v_add_f32_e32 v195, 1.0, v195
	v_add_f32_e32 v199, 1.0, v199
	v_add_f32_e32 v203, 1.0, v203
	v_add_f32_e32 v205, 1.0, v205
	v_rcp_f32_e32 v209, v209
	v_add_f32_e32 v210, 1.0, v210
	v_rcp_f32_e32 v193, v193
	v_rcp_f32_e32 v195, v195
	v_rcp_f32_e32 v199, v199
	v_rcp_f32_e32 v203, v203
	v_rcp_f32_e32 v205, v205
	v_rcp_f32_e32 v210, v210
	v_mul_f32_e32 v208, v73, v208
	v_mul_f32_e32 v211, v37, v208
	v_mul_f32_e32 v208, v74, v209
	v_mul_f32_e32 v193, v76, v193
	v_mul_f32_e32 v195, v77, v195
	v_mul_f32_e32 v199, v78, v199
	v_mul_f32_e32 v203, v79, v203
	v_mul_f32_e32 v205, v72, v205
	v_mul_f32_e32 v212, v38, v208
	v_mul_f32_e32 v208, v75, v210
	v_mul_f32_e32 v193, v40, v193
	v_mul_f32_e32 v195, v41, v195
	v_mul_f32_e32 v199, v42, v199
	v_mul_f32_e32 v203, v43, v203
	v_mul_f32_e32 v205, v36, v205
	v_mul_f32_e32 v213, v39, v208
	v_cvt_pk_bf16_f32 v208, v193, v195
	v_cvt_pk_bf16_f32 v209, v199, v203
	v_cvt_pk_bf16_f32 v210, v205, v211
	v_cvt_pk_bf16_f32 v211, v212, v213
	v_add_co_u32_e32 v212, vcc, s64, v206
	v_mul_f32_e32 v193, 0xbfb8aa3b, v68
	s_nop 0
	v_addc_co_u32_e32 v213, vcc, 0, v207, vcc
	global_store_dwordx4 v[212:213], v[208:211], off sc1
	v_mul_f32_e32 v195, 0xbfb8aa3b, v69
	v_mul_f32_e32 v199, 0xbfb8aa3b, v70
	v_mul_f32_e32 v208, 0xbfb8aa3b, v65
	v_exp_f32_e32 v208, v208
	v_mul_f32_e32 v209, 0xbfb8aa3b, v66
	v_mul_f32_e32 v203, 0xbfb8aa3b, v71
	v_mul_f32_e32 v205, 0xbfb8aa3b, v64
	v_exp_f32_e32 v209, v209
	v_mul_f32_e32 v210, 0xbfb8aa3b, v67
	v_exp_f32_e32 v193, v193
	v_exp_f32_e32 v195, v195
	v_exp_f32_e32 v199, v199
	v_exp_f32_e32 v203, v203
	v_exp_f32_e32 v205, v205
	v_exp_f32_e32 v210, v210
	v_add_f32_e32 v208, 1.0, v208
	v_rcp_f32_e32 v208, v208
	v_add_f32_e32 v209, 1.0, v209
	v_add_f32_e32 v193, 1.0, v193
	v_add_f32_e32 v195, 1.0, v195
	v_add_f32_e32 v199, 1.0, v199
	v_add_f32_e32 v203, 1.0, v203
	v_add_f32_e32 v205, 1.0, v205
	v_rcp_f32_e32 v209, v209
	v_add_f32_e32 v210, 1.0, v210
	v_rcp_f32_e32 v193, v193
	v_rcp_f32_e32 v195, v195
	v_rcp_f32_e32 v199, v199
	v_rcp_f32_e32 v203, v203
	v_rcp_f32_e32 v205, v205
	v_rcp_f32_e32 v210, v210
	v_mul_f32_e32 v208, v65, v208
	v_mul_f32_e32 v211, v25, v208
	v_mul_f32_e32 v208, v66, v209
	v_add_co_u32_e32 v206, vcc, 0x58000, v206
	v_mul_f32_e32 v193, v68, v193
	v_mul_f32_e32 v195, v69, v195
	v_mul_f32_e32 v199, v70, v199
	v_mul_f32_e32 v203, v71, v203
	v_mul_f32_e32 v205, v64, v205
	v_mul_f32_e32 v212, v26, v208
	v_mul_f32_e32 v208, v67, v210
	v_addc_co_u32_e32 v207, vcc, 0, v207, vcc
	v_mul_f32_e32 v193, v32, v193
	v_mul_f32_e32 v195, v33, v195
	v_mul_f32_e32 v199, v34, v199
	v_mul_f32_e32 v203, v35, v203
	v_mul_f32_e32 v205, v24, v205
	v_mul_f32_e32 v213, v27, v208
	v_cvt_pk_bf16_f32 v208, v193, v195
	v_cvt_pk_bf16_f32 v209, v199, v203
	v_cvt_pk_bf16_f32 v210, v205, v211
	v_cvt_pk_bf16_f32 v211, v212, v213
	global_store_dwordx4 v[206:207], v[208:211], off sc1
	s_and_b64 vcc, exec, s[6:7]
	s_cbranch_vccnz .LBB0_1057

; __device__ __forceinline__ unsigned cvt_pk_bf16(float lo, float hi) { unsigned r; asm volatile("v_cvt_pk_bf16_f32 %0, %1, %2" : "=v"(r) : "v"(lo), "v"(hi)); return r; }
;     template <class Tp> __device__ __forceinline__ Tp* w(size_t off) const { return (Tp*)(ws + off); }
;     __device__ __forceinline__ void operator()(const f32x4 (&acc)[2][2][4][2], const Unit& u, int wr, int wc, int fr, int fq) const {
;         const int e = u.pn >> 3, lim = offs[e] + cnts[e], lb = e * 16384 - offs[e];
;         const int row0 = u.pm * BM + wr * 64 + fr, col0 = (u.pn & 7) * BM + wc * 32 + 8 * fq;
; #pragma unroll
;         for (int ai = 0; ai < 2; ++ai)
; #pragma unroll
;             for (int m = 0; m < 4; ++m) { const int p = row0 + ai * HALF + m * 16;
;                 if (p < lim) { const float w = wrow[lb + p]; bf16_t* rowp = Y2 + (size_t)tsi[lb + p] * 2048 + col0;
; #pragma unroll
;                     for (int bj = 0; bj < 2; ++bj) { const f32x4 v0 = acc[ai][bj][m][0] * w, v1 = acc[ai][bj][m][1] * w;
;                         u32x4 o; o.x = cvt_pk_bf16(v0[0], v0[1]); o.y = cvt_pk_bf16(v0[2], v0[3]); o.z = cvt_pk_bf16(v1[0], v1[1]); o.w = cvt_pk_bf16(v1[2], v1[3]);
;                         *(u32x4*)(rowp + bj * HALF) = o; } } }
;     }
.LBB0_1326:
	s_ashr_i32 s10, s56, 3
	s_lshl_b32 s11, s10, 2
	s_add_i32 s11, s11, 0
	s_add_i32 s12, s11, 0x20000
	s_add_i32 s11, s11, 0x20200
	v_mov_b32_e32 v2, s12
	v_mov_b32_e32 v3, s11
	ds_read_b32 v2, v2
	ds_read_b32 v3, v3
	s_lshl_b32 s10, s10, 14
	v_lshl_add_u32 v203, s55, 8, v219
	s_waitcnt lgkmcnt(0)
	v_sub_u32_e32 v199, s10, v2
	s_lshl_b32 s10, s56, 8
	s_and_b32 s10, s10, 0x700
	v_add_u32_e32 v201, v3, v2
	v_or_b32_e32 v2, s10, v224
	v_cmp_lt_i32_e32 vcc, v203, v201
	v_lshlrev_b32_e32 v2, 1, v2
	s_and_saveexec_b64 s[10:11], vcc
	s_cbranch_execz .LBB0_1328
	v_add_u32_e32 v208, v199, v203
	v_ashrrev_i32_e32 v209, 31, v208
	v_lshlrev_b64 v[208:209], 2, v[208:209]
	v_lshl_add_u64 v[210:211], s[30:31], 0, v[208:209]
	v_lshl_add_u64 v[208:209], s[28:29], 0, v[208:209]
	global_load_dword v208, v[208:209], off
	s_nop 0
	global_load_dword v210, v[210:211], off
	v_mov_b32_e32 v3, v1
	s_waitcnt vmcnt(0)
	v_ashrrev_i32_e32 v209, 31, v208
	v_pk_mul_f32 v[212:213], v[186:187], v[210:211] op_sel_hi:[1,0]
	v_lshlrev_b64 v[240:241], 12, v[208:209]
	v_pk_mul_f32 v[226:227], v[184:185], v[210:211] op_sel_hi:[1,0]
	v_pk_mul_f32 v[228:229], v[178:179], v[210:211] op_sel_hi:[1,0]
	v_cvt_pk_bf16_f32 v208, v226, v227
	v_cvt_pk_bf16_f32 v209, v212, v213
	v_lshl_add_u64 v[212:213], s[26:27], 0, v[240:241]
	v_pk_mul_f32 v[230:231], v[176:177], v[210:211] op_sel_hi:[1,0]
	v_pk_mul_f32 v[232:233], v[146:147], v[210:211] op_sel_hi:[1,0]
	v_pk_mul_f32 v[234:235], v[144:145], v[210:211] op_sel_hi:[1,0]
	v_pk_mul_f32 v[236:237], v[138:139], v[210:211] op_sel_hi:[1,0]
	v_pk_mul_f32 v[238:239], v[136:137], v[210:211] op_sel_hi:[1,0]
	v_cvt_pk_bf16_f32 v210, v230, v231
	v_cvt_pk_bf16_f32 v211, v228, v229
	v_lshl_add_u64 v[212:213], v[212:213], 0, v[2:3]
	global_store_dwordx4 v[212:213], v[208:211], off sc1
	s_nop 1
	v_cvt_pk_bf16_f32 v208, v234, v235
	v_cvt_pk_bf16_f32 v209, v232, v233
	v_cvt_pk_bf16_f32 v210, v238, v239
	v_cvt_pk_bf16_f32 v211, v236, v237
	global_store_dwordx4 v[212:213], v[208:211], off offset:256 sc1
.LBB0_1328:
	s_or_b64 exec, exec, s[10:11]
	v_or_b32_e32 v3, 16, v203
	v_cmp_lt_i32_e32 vcc, v3, v201
	s_and_saveexec_b64 s[10:11], vcc
	s_cbranch_execz .LBB0_1330
	v_add_u32_e32 v208, v199, v3
	v_ashrrev_i32_e32 v209, 31, v208
	v_lshlrev_b64 v[208:209], 2, v[208:209]
	v_lshl_add_u64 v[210:211], s[30:31], 0, v[208:209]
	v_lshl_add_u64 v[208:209], s[28:29], 0, v[208:209]
	global_load_dword v208, v[208:209], off
	s_nop 0
	global_load_dword v210, v[210:211], off
	v_mov_b32_e32 v3, v1
	s_waitcnt vmcnt(0)
	v_ashrrev_i32_e32 v209, 31, v208
	v_pk_mul_f32 v[212:213], v[170:171], v[210:211] op_sel_hi:[1,0]
	v_lshlrev_b64 v[240:241], 12, v[208:209]
	v_pk_mul_f32 v[226:227], v[168:169], v[210:211] op_sel_hi:[1,0]
	v_pk_mul_f32 v[228:229], v[166:167], v[210:211] op_sel_hi:[1,0]
	v_cvt_pk_bf16_f32 v208, v226, v227
	v_cvt_pk_bf16_f32 v209, v212, v213
	v_lshl_add_u64 v[212:213], s[26:27], 0, v[240:241]
	v_pk_mul_f32 v[230:231], v[164:165], v[210:211] op_sel_hi:[1,0]
	v_pk_mul_f32 v[232:233], v[130:131], v[210:211] op_sel_hi:[1,0]
	v_pk_mul_f32 v[234:235], v[128:129], v[210:211] op_sel_hi:[1,0]
	v_pk_mul_f32 v[236:237], v[122:123], v[210:211] op_sel_hi:[1,0]
	v_pk_mul_f32 v[238:239], v[120:121], v[210:211] op_sel_hi:[1,0]
	v_cvt_pk_bf16_f32 v210, v230, v231
	v_cvt_pk_bf16_f32 v211, v228, v229
	v_lshl_add_u64 v[212:213], v[212:213], 0, v[2:3]
	global_store_dwordx4 v[212:213], v[208:211], off sc1
	s_nop 1
	v_cvt_pk_bf16_f32 v208, v234, v235
	v_cvt_pk_bf16_f32 v209, v232, v233
	v_cvt_pk_bf16_f32 v210, v238, v239
	v_cvt_pk_bf16_f32 v211, v236, v237
	global_store_dwordx4 v[212:213], v[208:211], off offset:256 sc1
.LBB0_1330:
	s_or_b64 exec, exec, s[10:11]
	v_or_b32_e32 v3, 32, v203
	v_cmp_lt_i32_e32 vcc, v3, v201
	s_and_saveexec_b64 s[10:11], vcc
	s_cbranch_execz .LBB0_1332
	v_add_u32_e32 v208, v199, v3
	v_ashrrev_i32_e32 v209, 31, v208
	v_lshlrev_b64 v[208:209], 2, v[208:209]
	v_lshl_add_u64 v[210:211], s[30:31], 0, v[208:209]
	v_lshl_add_u64 v[208:209], s[28:29], 0, v[208:209]
	global_load_dword v208, v[208:209], off
	s_nop 0
	global_load_dword v210, v[210:211], off
	v_mov_b32_e32 v3, v1
	s_waitcnt vmcnt(0)
	v_ashrrev_i32_e32 v209, 31, v208
	v_pk_mul_f32 v[212:213], v[162:163], v[210:211] op_sel_hi:[1,0]
	v_lshlrev_b64 v[240:241], 12, v[208:209]
	v_pk_mul_f32 v[226:227], v[160:161], v[210:211] op_sel_hi:[1,0]
	v_pk_mul_f32 v[228:229], v[158:159], v[210:211] op_sel_hi:[1,0]
	v_cvt_pk_bf16_f32 v208, v226, v227
	v_cvt_pk_bf16_f32 v209, v212, v213
	v_lshl_add_u64 v[212:213], s[26:27], 0, v[240:241]
	v_pk_mul_f32 v[230:231], v[156:157], v[210:211] op_sel_hi:[1,0]
	v_pk_mul_f32 v[232:233], v[114:115], v[210:211] op_sel_hi:[1,0]
	v_pk_mul_f32 v[234:235], v[112:113], v[210:211] op_sel_hi:[1,0]
	v_pk_mul_f32 v[236:237], v[110:111], v[210:211] op_sel_hi:[1,0]
	v_pk_mul_f32 v[238:239], v[108:109], v[210:211] op_sel_hi:[1,0]
	v_cvt_pk_bf16_f32 v210, v230, v231
	v_cvt_pk_bf16_f32 v211, v228, v229
	v_lshl_add_u64 v[212:213], v[212:213], 0, v[2:3]
	global_store_dwordx4 v[212:213], v[208:211], off sc1
	s_nop 1
	v_cvt_pk_bf16_f32 v208, v234, v235
	v_cvt_pk_bf16_f32 v209, v232, v233
	v_cvt_pk_bf16_f32 v210, v238, v239
	v_cvt_pk_bf16_f32 v211, v236, v237
	global_store_dwordx4 v[212:213], v[208:211], off offset:256 sc1
; __device__ __forceinline__ unsigned cvt_pk_bf16(float lo, float hi) { unsigned r; asm volatile("v_cvt_pk_bf16_f32 %0, %1, %2" : "=v"(r) : "v"(lo), "v"(hi)); return r; }
;     template <class Tp> __device__ __forceinline__ Tp* w(size_t off) const { return (Tp*)(ws + off); }
;     __device__ __forceinline__ void operator()(const f32x4 (&acc)[2][2][4][2], const Unit& u, int wr, int wc, int fr, int fq) const {
;     ...
;             for (int m = 0; m < 4; ++m) { const int p = row0 + ai * HALF + m * 16;
;                 if (p < lim) { const float w = wrow[lb + p]; bf16_t* rowp = Y2 + (size_t)tsi[lb + p] * 2048 + col0;
; #pragma unroll
;                     for (int bj = 0; bj < 2; ++bj) { const f32x4 v0 = acc[ai][bj][m][0] * w, v1 = acc[ai][bj][m][1] * w;
;                         u32x4 o; o.x = cvt_pk_bf16(v0[0], v0[1]); o.y = cvt_pk_bf16(v0[2], v0[3]); o.z = cvt_pk_bf16(v1[0], v1[1]); o.w = cvt_pk_bf16(v1[2], v1[3]);
;                         *(u32x4*)(rowp + bj * HALF) = o; } } }
.LBB0_1332:
	s_or_b64 exec, exec, s[10:11]
	v_or_b32_e32 v3, 48, v203
	v_cmp_lt_i32_e32 vcc, v3, v201
	s_and_saveexec_b64 s[10:11], vcc
	s_cbranch_execz .LBB0_1334
	v_add_u32_e32 v208, v199, v3
	v_ashrrev_i32_e32 v209, 31, v208
	v_lshlrev_b64 v[208:209], 2, v[208:209]
	v_lshl_add_u64 v[210:211], s[30:31], 0, v[208:209]
	v_lshl_add_u64 v[208:209], s[28:29], 0, v[208:209]
	global_load_dword v208, v[208:209], off
	s_nop 0
	global_load_dword v210, v[210:211], off
	v_mov_b32_e32 v3, v1
	s_waitcnt vmcnt(0)
	v_ashrrev_i32_e32 v209, 31, v208
	v_pk_mul_f32 v[212:213], v[154:155], v[210:211] op_sel_hi:[1,0]
	v_lshlrev_b64 v[240:241], 12, v[208:209]
	v_pk_mul_f32 v[226:227], v[152:153], v[210:211] op_sel_hi:[1,0]
	v_pk_mul_f32 v[228:229], v[150:151], v[210:211] op_sel_hi:[1,0]
	v_cvt_pk_bf16_f32 v208, v226, v227
	v_cvt_pk_bf16_f32 v209, v212, v213
	v_lshl_add_u64 v[212:213], s[26:27], 0, v[240:241]
	v_pk_mul_f32 v[230:231], v[148:149], v[210:211] op_sel_hi:[1,0]
	v_pk_mul_f32 v[232:233], v[106:107], v[210:211] op_sel_hi:[1,0]
	v_pk_mul_f32 v[234:235], v[104:105], v[210:211] op_sel_hi:[1,0]
	v_pk_mul_f32 v[236:237], v[102:103], v[210:211] op_sel_hi:[1,0]
	v_pk_mul_f32 v[238:239], v[100:101], v[210:211] op_sel_hi:[1,0]
	v_cvt_pk_bf16_f32 v210, v230, v231
	v_cvt_pk_bf16_f32 v211, v228, v229
	v_lshl_add_u64 v[212:213], v[212:213], 0, v[2:3]
	global_store_dwordx4 v[212:213], v[208:211], off sc1
	s_nop 1
	v_cvt_pk_bf16_f32 v208, v234, v235
	v_cvt_pk_bf16_f32 v209, v232, v233
	v_cvt_pk_bf16_f32 v210, v238, v239
	v_cvt_pk_bf16_f32 v211, v236, v237
	global_store_dwordx4 v[212:213], v[208:211], off offset:256 sc1
.LBB0_1334:
	s_or_b64 exec, exec, s[10:11]
	v_add_u32_e32 v3, 0x80, v203
	v_cmp_lt_i32_e32 vcc, v3, v201
	s_and_saveexec_b64 s[10:11], vcc
	s_cbranch_execz .LBB0_1336
	v_add_u32_e32 v208, v199, v3
	v_ashrrev_i32_e32 v209, 31, v208
	v_lshlrev_b64 v[208:209], 2, v[208:209]
	v_lshl_add_u64 v[210:211], s[30:31], 0, v[208:209]
	v_lshl_add_u64 v[208:209], s[28:29], 0, v[208:209]
	global_load_dword v208, v[208:209], off
	s_nop 0
	global_load_dword v210, v[210:211], off
	v_mov_b32_e32 v3, v1
	s_waitcnt vmcnt(0)
	v_ashrrev_i32_e32 v209, 31, v208
	v_pk_mul_f32 v[212:213], v[98:99], v[210:211] op_sel_hi:[1,0]
	v_lshlrev_b64 v[240:241], 12, v[208:209]
	v_pk_mul_f32 v[226:227], v[96:97], v[210:211] op_sel_hi:[1,0]
	v_pk_mul_f32 v[228:229], v[94:95], v[210:211] op_sel_hi:[1,0]
	v_cvt_pk_bf16_f32 v208, v226, v227
	v_cvt_pk_bf16_f32 v209, v212, v213
	v_lshl_add_u64 v[212:213], s[26:27], 0, v[240:241]
	v_pk_mul_f32 v[230:231], v[92:93], v[210:211] op_sel_hi:[1,0]
	v_pk_mul_f32 v[232:233], v[66:67], v[210:211] op_sel_hi:[1,0]
	v_pk_mul_f32 v[234:235], v[64:65], v[210:211] op_sel_hi:[1,0]
	v_pk_mul_f32 v[236:237], v[62:63], v[210:211] op_sel_hi:[1,0]
	v_pk_mul_f32 v[238:239], v[60:61], v[210:211] op_sel_hi:[1,0]
	v_cvt_pk_bf16_f32 v210, v230, v231
	v_cvt_pk_bf16_f32 v211, v228, v229
	v_lshl_add_u64 v[212:213], v[212:213], 0, v[2:3]
	global_store_dwordx4 v[212:213], v[208:211], off sc1
	s_nop 1
	v_cvt_pk_bf16_f32 v208, v234, v235
	v_cvt_pk_bf16_f32 v209, v232, v233
	v_cvt_pk_bf16_f32 v210, v238, v239
	v_cvt_pk_bf16_f32 v211, v236, v237
	global_store_dwordx4 v[212:213], v[208:211], off offset:256 sc1
; __device__ __forceinline__ unsigned cvt_pk_bf16(float lo, float hi) { unsigned r; asm volatile("v_cvt_pk_bf16_f32 %0, %1, %2" : "=v"(r) : "v"(lo), "v"(hi)); return r; }
;     template <class Tp> __device__ __forceinline__ Tp* w(size_t off) const { return (Tp*)(ws + off); }
;     __device__ __forceinline__ void operator()(const f32x4 (&acc)[2][2][4][2], const Unit& u, int wr, int wc, int fr, int fq) const {
;     ...
;             for (int m = 0; m < 4; ++m) { const int p = row0 + ai * HALF + m * 16;
;                 if (p < lim) { const float w = wrow[lb + p]; bf16_t* rowp = Y2 + (size_t)tsi[lb + p] * 2048 + col0;
; #pragma unroll
;                     for (int bj = 0; bj < 2; ++bj) { const f32x4 v0 = acc[ai][bj][m][0] * w, v1 = acc[ai][bj][m][1] * w;
;                         u32x4 o; o.x = cvt_pk_bf16(v0[0], v0[1]); o.y = cvt_pk_bf16(v0[2], v0[3]); o.z = cvt_pk_bf16(v1[0], v1[1]); o.w = cvt_pk_bf16(v1[2], v1[3]);
;                         *(u32x4*)(rowp + bj * HALF) = o; } } }
.LBB0_1336:
	s_or_b64 exec, exec, s[10:11]
	v_add_u32_e32 v3, 0x90, v203
	v_cmp_lt_i32_e32 vcc, v3, v201
	s_and_saveexec_b64 s[10:11], vcc
	s_cbranch_execz .LBB0_1338
	v_add_u32_e32 v208, v199, v3
	v_ashrrev_i32_e32 v209, 31, v208
	v_lshlrev_b64 v[208:209], 2, v[208:209]
	v_lshl_add_u64 v[210:211], s[30:31], 0, v[208:209]
	v_lshl_add_u64 v[208:209], s[28:29], 0, v[208:209]
	global_load_dword v208, v[208:209], off
	s_nop 0
	global_load_dword v210, v[210:211], off
	v_mov_b32_e32 v3, v1
	s_waitcnt vmcnt(0)
	v_ashrrev_i32_e32 v209, 31, v208
	v_pk_mul_f32 v[212:213], v[90:91], v[210:211] op_sel_hi:[1,0]
	v_lshlrev_b64 v[240:241], 12, v[208:209]
	v_pk_mul_f32 v[226:227], v[88:89], v[210:211] op_sel_hi:[1,0]
	v_pk_mul_f32 v[228:229], v[86:87], v[210:211] op_sel_hi:[1,0]
	v_cvt_pk_bf16_f32 v208, v226, v227
	v_cvt_pk_bf16_f32 v209, v212, v213
	v_lshl_add_u64 v[212:213], s[26:27], 0, v[240:241]
	v_pk_mul_f32 v[230:231], v[84:85], v[210:211] op_sel_hi:[1,0]
	v_pk_mul_f32 v[232:233], v[54:55], v[210:211] op_sel_hi:[1,0]
	v_pk_mul_f32 v[234:235], v[52:53], v[210:211] op_sel_hi:[1,0]
	v_pk_mul_f32 v[236:237], v[50:51], v[210:211] op_sel_hi:[1,0]
	v_pk_mul_f32 v[238:239], v[48:49], v[210:211] op_sel_hi:[1,0]
	v_cvt_pk_bf16_f32 v210, v230, v231
	v_cvt_pk_bf16_f32 v211, v228, v229
	v_lshl_add_u64 v[212:213], v[212:213], 0, v[2:3]
	global_store_dwordx4 v[212:213], v[208:211], off sc1
	s_nop 1
	v_cvt_pk_bf16_f32 v208, v234, v235
	v_cvt_pk_bf16_f32 v209, v232, v233
	v_cvt_pk_bf16_f32 v210, v238, v239
	v_cvt_pk_bf16_f32 v211, v236, v237
	global_store_dwordx4 v[212:213], v[208:211], off offset:256 sc1
.LBB0_1338:
	s_or_b64 exec, exec, s[10:11]
	v_add_u32_e32 v3, 0xa0, v203
	v_cmp_lt_i32_e32 vcc, v3, v201
	s_and_saveexec_b64 s[10:11], vcc
	s_cbranch_execz .LBB0_1340
	v_add_u32_e32 v208, v199, v3
	v_ashrrev_i32_e32 v209, 31, v208
	v_lshlrev_b64 v[208:209], 2, v[208:209]
	v_lshl_add_u64 v[210:211], s[30:31], 0, v[208:209]
	v_lshl_add_u64 v[208:209], s[28:29], 0, v[208:209]
	global_load_dword v208, v[208:209], off
	s_nop 0
	global_load_dword v210, v[210:211], off
	v_mov_b32_e32 v3, v1
	s_waitcnt vmcnt(0)
	v_ashrrev_i32_e32 v209, 31, v208
	v_pk_mul_f32 v[212:213], v[82:83], v[210:211] op_sel_hi:[1,0]
	v_lshlrev_b64 v[240:241], 12, v[208:209]
	v_pk_mul_f32 v[226:227], v[80:81], v[210:211] op_sel_hi:[1,0]
	v_pk_mul_f32 v[228:229], v[78:79], v[210:211] op_sel_hi:[1,0]
	v_cvt_pk_bf16_f32 v208, v226, v227
	v_cvt_pk_bf16_f32 v209, v212, v213
	v_lshl_add_u64 v[212:213], s[26:27], 0, v[240:241]
	v_pk_mul_f32 v[230:231], v[76:77], v[210:211] op_sel_hi:[1,0]
	v_pk_mul_f32 v[232:233], v[46:47], v[210:211] op_sel_hi:[1,0]
	v_pk_mul_f32 v[234:235], v[44:45], v[210:211] op_sel_hi:[1,0]
	v_pk_mul_f32 v[236:237], v[42:43], v[210:211] op_sel_hi:[1,0]
	v_pk_mul_f32 v[238:239], v[40:41], v[210:211] op_sel_hi:[1,0]
	v_cvt_pk_bf16_f32 v210, v230, v231
	v_cvt_pk_bf16_f32 v211, v228, v229
	v_lshl_add_u64 v[212:213], v[212:213], 0, v[2:3]
	global_store_dwordx4 v[212:213], v[208:211], off sc1
	s_nop 1
	v_cvt_pk_bf16_f32 v208, v234, v235
	v_cvt_pk_bf16_f32 v209, v232, v233
	v_cvt_pk_bf16_f32 v210, v238, v239
	v_cvt_pk_bf16_f32 v211, v236, v237
	global_store_dwordx4 v[212:213], v[208:211], off offset:256 sc1
.LBB0_1340:
	s_or_b64 exec, exec, s[10:11]
	v_add_u32_e32 v3, 0xb0, v203
	v_cmp_lt_i32_e32 vcc, v3, v201
	s_and_saveexec_b64 s[10:11], vcc
	s_cbranch_execz .LBB0_1342
	v_add_u32_e32 v208, v199, v3
	v_ashrrev_i32_e32 v209, 31, v208
	v_lshlrev_b64 v[208:209], 2, v[208:209]
	v_lshl_add_u64 v[210:211], s[30:31], 0, v[208:209]
	v_lshl_add_u64 v[208:209], s[28:29], 0, v[208:209]
	global_load_dword v208, v[208:209], off
	s_nop 0
	global_load_dword v210, v[210:211], off
	v_mov_b32_e32 v3, v1
	s_waitcnt vmcnt(0)
	v_ashrrev_i32_e32 v209, 31, v208
	v_pk_mul_f32 v[212:213], v[74:75], v[210:211] op_sel_hi:[1,0]
	v_lshlrev_b64 v[240:241], 12, v[208:209]
	v_pk_mul_f32 v[226:227], v[72:73], v[210:211] op_sel_hi:[1,0]
	v_pk_mul_f32 v[228:229], v[70:71], v[210:211] op_sel_hi:[1,0]
	v_cvt_pk_bf16_f32 v208, v226, v227
	v_cvt_pk_bf16_f32 v209, v212, v213
	v_lshl_add_u64 v[212:213], s[26:27], 0, v[240:241]
	v_pk_mul_f32 v[230:231], v[68:69], v[210:211] op_sel_hi:[1,0]
	v_pk_mul_f32 v[232:233], v[38:39], v[210:211] op_sel_hi:[1,0]
	v_pk_mul_f32 v[234:235], v[36:37], v[210:211] op_sel_hi:[1,0]
	v_pk_mul_f32 v[236:237], v[34:35], v[210:211] op_sel_hi:[1,0]
	v_pk_mul_f32 v[238:239], v[32:33], v[210:211] op_sel_hi:[1,0]
	v_cvt_pk_bf16_f32 v210, v230, v231
	v_cvt_pk_bf16_f32 v211, v228, v229
	v_lshl_add_u64 v[2:3], v[212:213], 0, v[2:3]
	global_store_dwordx4 v[2:3], v[208:211], off sc1
	s_nop 1
	v_cvt_pk_bf16_f32 v208, v234, v235
	v_cvt_pk_bf16_f32 v209, v232, v233
	v_cvt_pk_bf16_f32 v210, v238, v239
	v_cvt_pk_bf16_f32 v211, v236, v237
	global_store_dwordx4 v[2:3], v[208:211], off offset:256 sc1
